# batch 3 plus write-through (sc1) policy on the 16-byte GEMM epilogue stores so the grid-barrier release has little dirty L2 data to write back
# baseline (speedup 1.0000x reference)
; DI unsigned pk4_fp8(float a, float b, float c, float d) { int r = 0; r = __builtin_amdgcn_cvt_pk_fp8_f32(sat8(a), sat8(b), r, false); r = __builtin_amdgcn_cvt_pk_fp8_f32(sat8(c), sat8(d), r, true); return (unsigned)r; }
; DI void store_pair8(unsigned char* base, size_t off0, size_t off1, const u32x2& w0, const u32x2& w1, bool oddq) {
;     const auto rx = __builtin_amdgcn_permlane16_swap(w0.x, w1.x, false, false), ry = __builtin_amdgcn_permlane16_swap(w0.y, w1.y, false, false);
;     u32x4 ww; ww.x = rx[0]; ww.y = ry[0]; ww.z = rx[1]; ww.w = ry[1];
;     *(u32x4*)(base + (oddq ? off1 - 8 : off0)) = ww;
; }
;     DI void operator()(const f32x4 (&acc)[2][2][4][2], const Unit& u, int wr, int wc, int fr, int fq) const {
;         const float s2 = sc * GATE8_SCALE; const bool oddq = (fq & 1) != 0;
; #pragma unroll
;         for (int ai = 0; ai < 2; ++ai)
; #pragma unroll
;             for (int p2 = 0; p2 < 2; ++p2) { const size_t row0 = (size_t)u.pm * 256 + 128 * ai + 64 * wr + 32 * p2 + fr;
; #pragma unroll
;                 for (int bj = 0; bj < 2; ++bj) { u32x2 w[2];
; #pragma unroll
;                     for (int r2 = 0; r2 < 2; ++r2) { const f32x4 a = acc[ai][bj][2 * p2 + r2][0] * s2, b = acc[ai][bj][2 * p2 + r2][1] * s2; w[r2].x = pk4_fp8(a[0], a[1], a[2], a[3]); w[r2].y = pk4_fp8(b[0], b[1], b[2], b[3]); }
;                     const size_t c = (size_t)(u.pn * 256 + bj * 128 + 32 * wc + 8 * fq);
;                     store_pair8(o, row0 * D + c, (row0 + 16) * D + c, w[0], w[1], oddq); } }
;     }
;     DI void operator()(const f32x4 (&acc)[2][2][4][2], const Unit& u, int wr, int wc, int fr, int fq) const {
;         Unit u2 = u;
;         if (u.pn < 2) { EpiScaled E{v, AW, sc}; E(acc, u2, wr, wc, fr, fq); }
;         else if (u.pn < 4) { u2.pn = u.pn - 2; EpiU E{ua, sc}; E(acc, u2, wr, wc, fr, fq); }
;         else { u2.pn = (u.pn - 4) & 3; EpiSig E{u.pn < 8 ? ga : gs, sc}; E(acc, u2, wr, wc, fr, fq); }
;     }
;     DI void operator()(const f32x4 (&acc)[2][2][4][2], const Unit& u, int wr, int wc, int fr, int fq) const {
;         if (u.pn < 4) a(acc, u, wr, wc, fr, fq); else { Unit u2 = u; u2.pn = u.pn - 4; b(acc, u2, wr, wc, fr, fq); }
.LBB0_247:
	s_mov_b32 s0, s51
	s_mov_b32 s1, -1
	s_ashr_i32 s23, s0, 2
	v_mbcnt_lo_u32_b32 v0, s1, 0
	v_mbcnt_hi_u32_b32 v0, s1, v0
	s_and_b32 s21, s0, 3
	s_cmp_gt_i32 s33, 3
	v_and_b32_e32 v142, 15, v0
	v_ashrrev_i32_e32 v143, 4, v0
	s_mov_b64 s[2:3], -1
	s_cbranch_scc0 .LBB0_257
	s_add_i32 s28, s33, -4
	s_cmp_gt_u32 s28, 1
	s_cbranch_scc0 .LBB0_254
	s_cmp_gt_u32 s28, 3
	s_cbranch_scc0 .LBB0_251
	s_cmp_lt_u32 s28, 8
	s_mov_b32 s0, 0x2ac00000
	s_cselect_b32 s0, s0, 0x2ec00000
	s_add_u32 s2, s6, s0
	s_addc_u32 s3, s7, 0
	s_ashr_i32 s19, s18, 31
	s_lshl_b64 s[0:1], s[18:19], 8
	s_lshl_b32 s19, s23, 6
	s_ashr_i32 s29, s19, 31
	s_add_u32 s0, s0, s19
	s_addc_u32 s1, s1, s29
	v_or_b32_e32 v132, s0, v142
	s_lshl_b32 s0, s33, 8
	v_mov_b32_e32 v133, s1
	s_and_b32 s0, s0, 0x300
	s_lshl_b32 s1, s21, 5
	s_or_b32 s0, s1, s0
	v_lshl_add_u32 v130, v143, 3, s0
	v_lshlrev_b64 v[132:133], 10, v[132:133]
	s_mov_b64 s[0:1], 0x3ff8
	v_lshl_add_u64 v[144:145], v[132:133], 0, s[0:1]
	s_mov_b32 s0, 0x3c800000
	v_pk_mul_f32 v[134:135], v[126:127], s[0:1] op_sel_hi:[1,0]
	v_pk_mul_f32 v[136:137], v[128:129], s[0:1] op_sel_hi:[1,0]
	v_pk_mul_f32 v[148:149], v[122:123], s[0:1] op_sel_hi:[1,0]
	v_med3_f32 v131, v134, s53, v204
	v_med3_f32 v135, v135, s53, v204
	v_mov_b32_e32 v134, v1
	v_cvt_pk_fp8_f32 v134, v131, v135
	v_med3_f32 v131, v136, s53, v204
	v_med3_f32 v136, v137, s53, v204
	v_med3_f32 v137, v148, s53, v204
	v_med3_f32 v148, v149, s53, v204
	v_mov_b32_e32 v135, v1
	v_cvt_pk_fp8_f32 v135, v137, v148
	v_pk_mul_f32 v[146:147], v[124:125], s[0:1] op_sel_hi:[1,0]
	v_cvt_pk_fp8_f32 v134, v131, v136 op_sel:[0,0,1]
	v_med3_f32 v131, v146, s53, v204
	v_med3_f32 v136, v147, s53, v204
	v_cvt_pk_fp8_f32 v135, v131, v136 op_sel:[0,0,1]
	v_pk_mul_f32 v[136:137], v[118:119], s[0:1] op_sel_hi:[1,0]
	v_pk_mul_f32 v[146:147], v[120:121], s[0:1] op_sel_hi:[1,0]
	v_pk_mul_f32 v[150:151], v[110:111], s[0:1] op_sel_hi:[1,0]
	v_med3_f32 v131, v136, s53, v204
	v_med3_f32 v137, v137, s53, v204
	v_mov_b32_e32 v136, v1
	v_cvt_pk_fp8_f32 v136, v131, v137
	v_med3_f32 v131, v146, s53, v204
	v_med3_f32 v146, v147, s53, v204
	v_med3_f32 v147, v150, s53, v204
	v_med3_f32 v150, v151, s53, v204
	v_mov_b32_e32 v137, v1
	v_cvt_pk_fp8_f32 v137, v147, v150
	v_pk_mul_f32 v[148:149], v[112:113], s[0:1] op_sel_hi:[1,0]
	v_cvt_pk_fp8_f32 v136, v131, v146 op_sel:[0,0,1]
	v_med3_f32 v131, v148, s53, v204
	v_med3_f32 v146, v149, s53, v204
	v_and_b32_e32 v0, 16, v0
	v_cvt_pk_fp8_f32 v137, v131, v146 op_sel:[0,0,1]
	v_cmp_eq_u32_e32 vcc, 0, v0
	v_ashrrev_i32_e32 v131, 31, v130
	v_permlane16_swap_b32_e32 v134, v136
	v_cndmask_b32_e32 v145, v145, v133, vcc
	v_cndmask_b32_e32 v144, v144, v132, vcc
	v_lshl_add_u64 v[144:145], s[2:3], 0, v[144:145]
	v_permlane16_swap_b32_e32 v135, v137
	v_lshl_add_u64 v[144:145], v[144:145], 0, v[130:131]
	global_store_dwordx4 v[144:145], v[134:137], off sc1
	v_pk_mul_f32 v[148:149], v[106:107], s[0:1] op_sel_hi:[1,0]
	v_pk_mul_f32 v[146:147], v[108:109], s[0:1] op_sel_hi:[1,0]
	v_pk_mul_f32 v[134:135], v[114:115], s[0:1] op_sel_hi:[1,0]
	v_pk_mul_f32 v[136:137], v[116:117], s[0:1] op_sel_hi:[1,0]
	v_med3_f32 v0, v134, s53, v204
	v_med3_f32 v135, v135, s53, v204
	v_mov_b32_e32 v134, v1
	v_cvt_pk_fp8_f32 v134, v0, v135
	v_med3_f32 v0, v136, s53, v204
	v_med3_f32 v136, v137, s53, v204
	v_med3_f32 v137, v148, s53, v204
	v_med3_f32 v148, v149, s53, v204
	v_mov_b32_e32 v135, v1
	v_cvt_pk_fp8_f32 v135, v137, v148
	v_cvt_pk_fp8_f32 v134, v0, v136 op_sel:[0,0,1]
	v_med3_f32 v0, v146, s53, v204
	v_med3_f32 v136, v147, s53, v204
	v_cvt_pk_fp8_f32 v135, v0, v136 op_sel:[0,0,1]
	v_pk_mul_f32 v[136:137], v[98:99], s[0:1] op_sel_hi:[1,0]
	v_pk_mul_f32 v[146:147], v[100:101], s[0:1] op_sel_hi:[1,0]
	v_pk_mul_f32 v[150:151], v[90:91], s[0:1] op_sel_hi:[1,0]
	v_med3_f32 v0, v136, s53, v204
	v_med3_f32 v137, v137, s53, v204
	v_mov_b32_e32 v136, v1
	v_cvt_pk_fp8_f32 v136, v0, v137
	v_med3_f32 v0, v146, s53, v204
	v_med3_f32 v146, v147, s53, v204
	v_med3_f32 v147, v150, s53, v204
	v_med3_f32 v150, v151, s53, v204
	v_mov_b32_e32 v137, v1
	v_cvt_pk_fp8_f32 v137, v147, v150
	v_pk_mul_f32 v[148:149], v[92:93], s[0:1] op_sel_hi:[1,0]
	v_cvt_pk_fp8_f32 v136, v0, v146 op_sel:[0,0,1]
	v_med3_f32 v0, v148, s53, v204
	v_med3_f32 v146, v149, s53, v204
	v_cvt_pk_fp8_f32 v137, v0, v146 op_sel:[0,0,1]
	v_permlane16_swap_b32_e32 v134, v136
	v_pk_mul_f32 v[148:149], v[94:95], s[0:1] op_sel_hi:[1,0]
	v_permlane16_swap_b32_e32 v135, v137
	global_store_dwordx4 v[144:145], v[134:137], off offset:128 sc1
	v_med3_f32 v148, v148, s53, v204
	v_med3_f32 v149, v149, s53, v204
	v_pk_mul_f32 v[134:135], v[102:103], s[0:1] op_sel_hi:[1,0]
	v_pk_mul_f32 v[136:137], v[104:105], s[0:1] op_sel_hi:[1,0]
	v_med3_f32 v150, v134, s53, v204
	v_med3_f32 v135, v135, s53, v204
	v_mov_b32_e32 v134, v1
	v_cvt_pk_fp8_f32 v134, v150, v135
	v_mov_b32_e32 v135, v1
	v_cvt_pk_fp8_f32 v135, v148, v149
	v_pk_mul_f32 v[146:147], v[96:97], s[0:1] op_sel_hi:[1,0]
	v_med3_f32 v136, v136, s53, v204
	v_med3_f32 v137, v137, s53, v204
	v_cvt_pk_fp8_f32 v134, v136, v137 op_sel:[0,0,1]
	v_med3_f32 v136, v146, s53, v204
	v_med3_f32 v137, v147, s53, v204
	v_cvt_pk_fp8_f32 v135, v136, v137 op_sel:[0,0,1]
	v_pk_mul_f32 v[136:137], v[86:87], s[0:1] op_sel_hi:[1,0]
	v_pk_mul_f32 v[150:151], v[78:79], s[0:1] op_sel_hi:[1,0]
	v_med3_f32 v152, v136, s53, v204
	v_med3_f32 v137, v137, s53, v204
	v_mov_b32_e32 v136, v1
	v_cvt_pk_fp8_f32 v136, v152, v137
	v_med3_f32 v150, v150, s53, v204
	v_med3_f32 v151, v151, s53, v204
	v_mov_b32_e32 v137, v1
	v_cvt_pk_fp8_f32 v137, v150, v151
	v_pk_mul_f32 v[146:147], v[88:89], s[0:1] op_sel_hi:[1,0]
; DI unsigned pk4_fp8(float a, float b, float c, float d) { int r = 0; r = __builtin_amdgcn_cvt_pk_fp8_f32(sat8(a), sat8(b), r, false); r = __builtin_amdgcn_cvt_pk_fp8_f32(sat8(c), sat8(d), r, true); return (unsigned)r; }
; DI void store_pair8(unsigned char* base, size_t off0, size_t off1, const u32x2& w0, const u32x2& w1, bool oddq) {
;     const auto rx = __builtin_amdgcn_permlane16_swap(w0.x, w1.x, false, false), ry = __builtin_amdgcn_permlane16_swap(w0.y, w1.y, false, false);
;     u32x4 ww; ww.x = rx[0]; ww.y = ry[0]; ww.z = rx[1]; ww.w = ry[1];
;     *(u32x4*)(base + (oddq ? off1 - 8 : off0)) = ww;
; }
;     DI void operator()(const f32x4 (&acc)[2][2][4][2], const Unit& u, int wr, int wc, int fr, int fq) const {
;         const float s2 = sc * GATE8_SCALE; const bool oddq = (fq & 1) != 0;
; #pragma unroll
;         for (int ai = 0; ai < 2; ++ai)
; #pragma unroll
;             for (int p2 = 0; p2 < 2; ++p2) { const size_t row0 = (size_t)u.pm * 256 + 128 * ai + 64 * wr + 32 * p2 + fr;
; #pragma unroll
;                 for (int bj = 0; bj < 2; ++bj) { u32x2 w[2];
; #pragma unroll
;                     for (int r2 = 0; r2 < 2; ++r2) { const f32x4 a = acc[ai][bj][2 * p2 + r2][0] * s2, b = acc[ai][bj][2 * p2 + r2][1] * s2; w[r2].x = pk4_fp8(a[0], a[1], a[2], a[3]); w[r2].y = pk4_fp8(b[0], b[1], b[2], b[3]); }
;                     const size_t c = (size_t)(u.pn * 256 + bj * 128 + 32 * wc + 8 * fq);
;                     store_pair8(o, row0 * D + c, (row0 + 16) * D + c, w[0], w[1], oddq); } }
;     }
	v_pk_mul_f32 v[148:149], v[80:81], s[0:1] op_sel_hi:[1,0]
	v_med3_f32 v146, v146, s53, v204
	v_med3_f32 v147, v147, s53, v204
	v_cvt_pk_fp8_f32 v136, v146, v147 op_sel:[0,0,1]
	v_med3_f32 v146, v148, s53, v204
	v_med3_f32 v147, v149, s53, v204
	s_mov_b64 s[30:31], 0xbff8
	v_cvt_pk_fp8_f32 v137, v146, v147 op_sel:[0,0,1]
	v_or_b32_e32 v0, 0x8000, v132
	v_lshl_add_u64 v[144:145], v[132:133], 0, s[30:31]
	v_cndmask_b32_e32 v145, v145, v133, vcc
	v_cndmask_b32_e32 v144, v144, v0, vcc
	v_lshl_add_u64 v[144:145], s[2:3], 0, v[144:145]
	v_permlane16_swap_b32_e32 v134, v136
	v_permlane16_swap_b32_e32 v135, v137
	v_lshl_add_u64 v[144:145], v[144:145], 0, v[130:131]
	global_store_dwordx4 v[144:145], v[134:137], off sc1
	v_pk_mul_f32 v[148:149], v[74:75], s[0:1] op_sel_hi:[1,0]
	v_pk_mul_f32 v[146:147], v[76:77], s[0:1] op_sel_hi:[1,0]
	v_pk_mul_f32 v[134:135], v[82:83], s[0:1] op_sel_hi:[1,0]
	v_pk_mul_f32 v[136:137], v[84:85], s[0:1] op_sel_hi:[1,0]
	v_med3_f32 v0, v134, s53, v204
	v_med3_f32 v135, v135, s53, v204
	v_mov_b32_e32 v134, v1
	v_cvt_pk_fp8_f32 v134, v0, v135
	v_med3_f32 v0, v136, s53, v204
	v_med3_f32 v136, v137, s53, v204
	v_med3_f32 v137, v148, s53, v204
	v_med3_f32 v148, v149, s53, v204
	v_mov_b32_e32 v135, v1
	v_cvt_pk_fp8_f32 v135, v137, v148
	v_cvt_pk_fp8_f32 v134, v0, v136 op_sel:[0,0,1]
	v_med3_f32 v0, v146, s53, v204
	v_med3_f32 v136, v147, s53, v204
	v_cvt_pk_fp8_f32 v135, v0, v136 op_sel:[0,0,1]
	v_pk_mul_f32 v[136:137], v[70:71], s[0:1] op_sel_hi:[1,0]
	v_pk_mul_f32 v[146:147], v[72:73], s[0:1] op_sel_hi:[1,0]
	v_pk_mul_f32 v[150:151], v[66:67], s[0:1] op_sel_hi:[1,0]
	v_med3_f32 v0, v136, s53, v204
	v_med3_f32 v137, v137, s53, v204
	v_mov_b32_e32 v136, v1
	v_cvt_pk_fp8_f32 v136, v0, v137
	v_med3_f32 v0, v146, s53, v204
	v_med3_f32 v146, v147, s53, v204
	v_med3_f32 v147, v150, s53, v204
	v_med3_f32 v150, v151, s53, v204
	v_mov_b32_e32 v137, v1
	v_cvt_pk_fp8_f32 v137, v147, v150
	v_pk_mul_f32 v[148:149], v[68:69], s[0:1] op_sel_hi:[1,0]
	v_cvt_pk_fp8_f32 v136, v0, v146 op_sel:[0,0,1]
	v_med3_f32 v0, v148, s53, v204
	v_med3_f32 v146, v149, s53, v204
	v_cvt_pk_fp8_f32 v137, v0, v146 op_sel:[0,0,1]
	v_permlane16_swap_b32_e32 v134, v136
	v_pk_mul_f32 v[146:147], v[58:59], s[0:1] op_sel_hi:[1,0]
	v_permlane16_swap_b32_e32 v135, v137
	global_store_dwordx4 v[144:145], v[134:137], off offset:128 sc1
	v_pk_mul_f32 v[144:145], v[60:61], s[0:1] op_sel_hi:[1,0]
	v_pk_mul_f32 v[148:149], v[46:47], s[0:1] op_sel_hi:[1,0]
	v_pk_mul_f32 v[134:135], v[62:63], s[0:1] op_sel_hi:[1,0]
	v_pk_mul_f32 v[136:137], v[64:65], s[0:1] op_sel_hi:[1,0]
	v_med3_f32 v0, v134, s53, v204
	v_med3_f32 v135, v135, s53, v204
	v_mov_b32_e32 v134, v1
	v_cvt_pk_fp8_f32 v134, v0, v135
	v_med3_f32 v0, v136, s53, v204
	v_med3_f32 v136, v137, s53, v204
	v_med3_f32 v137, v146, s53, v204
	v_med3_f32 v146, v147, s53, v204
	v_mov_b32_e32 v135, v1
	v_cvt_pk_fp8_f32 v135, v137, v146
	v_cvt_pk_fp8_f32 v134, v0, v136 op_sel:[0,0,1]
	v_med3_f32 v0, v144, s53, v204
	v_med3_f32 v136, v145, s53, v204
	v_cvt_pk_fp8_f32 v135, v0, v136 op_sel:[0,0,1]
	v_pk_mul_f32 v[136:137], v[54:55], s[0:1] op_sel_hi:[1,0]
	v_pk_mul_f32 v[144:145], v[56:57], s[0:1] op_sel_hi:[1,0]
	v_med3_f32 v0, v136, s53, v204
	v_med3_f32 v137, v137, s53, v204
	v_mov_b32_e32 v136, v1
	v_cvt_pk_fp8_f32 v136, v0, v137
	v_med3_f32 v0, v144, s53, v204
	v_med3_f32 v144, v145, s53, v204
	v_med3_f32 v145, v148, s53, v204
	v_med3_f32 v148, v149, s53, v204
	v_mov_b32_e32 v137, v1
	v_cvt_pk_fp8_f32 v137, v145, v148
	v_pk_mul_f32 v[146:147], v[48:49], s[0:1] op_sel_hi:[1,0]
	v_cvt_pk_fp8_f32 v136, v0, v144 op_sel:[0,0,1]
	v_med3_f32 v0, v146, s53, v204
	v_med3_f32 v144, v147, s53, v204
	v_cvt_pk_fp8_f32 v137, v0, v144 op_sel:[0,0,1]
	v_mov_b32_e32 v0, 0x23ff8
	v_mov_b32_e32 v144, 0x20000
	v_cndmask_b32_e32 v0, v0, v144, vcc
	v_lshl_add_u64 v[144:145], s[2:3], 0, v[132:133]
	v_lshl_add_u64 v[132:133], v[144:145], 0, v[0:1]
	v_permlane16_swap_b32_e32 v134, v136
	v_permlane16_swap_b32_e32 v135, v137
	v_lshl_add_u64 v[146:147], v[132:133], 0, v[130:131]
	v_pk_mul_f32 v[132:133], v[50:51], s[0:1] op_sel_hi:[1,0]
	global_store_dwordx4 v[146:147], v[134:137], off sc1
	v_pk_mul_f32 v[148:149], v[42:43], s[0:1] op_sel_hi:[1,0]
	v_med3_f32 v0, v132, s53, v204
	v_pk_mul_f32 v[134:135], v[52:53], s[0:1] op_sel_hi:[1,0]
	v_med3_f32 v133, v133, s53, v204
	v_mov_b32_e32 v132, v1
	v_cvt_pk_fp8_f32 v132, v0, v133
	v_med3_f32 v0, v134, s53, v204
	v_med3_f32 v134, v135, s53, v204
	v_med3_f32 v135, v148, s53, v204
	v_med3_f32 v148, v149, s53, v204
	v_mov_b32_e32 v133, v1
	v_cvt_pk_fp8_f32 v133, v135, v148
	v_pk_mul_f32 v[136:137], v[44:45], s[0:1] op_sel_hi:[1,0]
	v_cvt_pk_fp8_f32 v132, v0, v134 op_sel:[0,0,1]
	v_med3_f32 v0, v136, s53, v204
	v_med3_f32 v134, v137, s53, v204
	v_cvt_pk_fp8_f32 v133, v0, v134 op_sel:[0,0,1]
	v_pk_mul_f32 v[134:135], v[34:35], s[0:1] op_sel_hi:[1,0]
	v_pk_mul_f32 v[136:137], v[36:37], s[0:1] op_sel_hi:[1,0]
	v_pk_mul_f32 v[150:151], v[26:27], s[0:1] op_sel_hi:[1,0]
	v_med3_f32 v0, v134, s53, v204
	v_med3_f32 v135, v135, s53, v204
	v_mov_b32_e32 v134, v1
	v_cvt_pk_fp8_f32 v134, v0, v135
	v_med3_f32 v0, v136, s53, v204
	v_med3_f32 v136, v137, s53, v204
	v_med3_f32 v137, v150, s53, v204
	v_med3_f32 v150, v151, s53, v204
	v_mov_b32_e32 v135, v1
	v_cvt_pk_fp8_f32 v135, v137, v150
	v_pk_mul_f32 v[148:149], v[28:29], s[0:1] op_sel_hi:[1,0]
	v_cvt_pk_fp8_f32 v134, v0, v136 op_sel:[0,0,1]
	v_med3_f32 v0, v148, s53, v204
	v_med3_f32 v136, v149, s53, v204
	v_cvt_pk_fp8_f32 v135, v0, v136 op_sel:[0,0,1]
	v_permlane16_swap_b32_e32 v132, v134
	v_pk_mul_f32 v[136:137], v[32:33], s[0:1] op_sel_hi:[1,0]
	v_permlane16_swap_b32_e32 v133, v135
; DI unsigned pk4_fp8(float a, float b, float c, float d) { int r = 0; r = __builtin_amdgcn_cvt_pk_fp8_f32(sat8(a), sat8(b), r, false); r = __builtin_amdgcn_cvt_pk_fp8_f32(sat8(c), sat8(d), r, true); return (unsigned)r; }
; DI u32x4 pack8(const f32x4& a, const f32x4& b) { u32x4 w; w.x = pk2(a[0], a[1]); w.y = pk2(a[2], a[3]); w.z = pk2(b[0], b[1]); w.w = pk2(b[2], b[3]); return w; }
;     DI void operator()(const f32x4 (&acc)[2][2][4][2], const Unit& u, int wr, int wc, int fr, int fq) const {
;         EPI_ROWS_BEGIN
;             const int row = u.pm * 256 + rt;
; #pragma unroll
;             for (int bj = 0; bj < 2; ++bj) { const int ch = u.pn * 256 + bj * 128 + 32 * wc + 8 * fq; const int g = ch >> 4, c0 = ch & 15;
;                 *(u32x4*)(ua + ((size_t)g * CROWS + (row >> 5)) * UAK + (row & 31) * 16 + c0) = pack8(acc[ai][bj][m][0] * sc, acc[ai][bj][m][1] * sc); }
;         EPI_ROWS_END
;     }
;     DI void operator()(const f32x4 (&acc)[2][2][4][2], const Unit& u, int wr, int wc, int fr, int fq) const {
;         const float s2 = sc * GATE8_SCALE; const bool oddq = (fq & 1) != 0;
; #pragma unroll
;         for (int ai = 0; ai < 2; ++ai)
; #pragma unroll
;             for (int p2 = 0; p2 < 2; ++p2) { const size_t row0 = (size_t)u.pm * 256 + 128 * ai + 64 * wr + 32 * p2 + fr;
; #pragma unroll
;                 for (int bj = 0; bj < 2; ++bj) { u32x2 w[2];
; #pragma unroll
;                     for (int r2 = 0; r2 < 2; ++r2) { const f32x4 a = acc[ai][bj][2 * p2 + r2][0] * s2, b = acc[ai][bj][2 * p2 + r2][1] * s2; w[r2].x = pk4_fp8(a[0], a[1], a[2], a[3]); w[r2].y = pk4_fp8(b[0], b[1], b[2], b[3]); }
;                     const size_t c = (size_t)(u.pn * 256 + bj * 128 + 32 * wc + 8 * fq);
;                     store_pair8(o, row0 * D + c, (row0 + 16) * D + c, w[0], w[1], oddq); } }
	global_store_dwordx4 v[146:147], v[132:135], off offset:128 sc1
	v_pk_mul_f32 v[146:147], v[30:31], s[0:1] op_sel_hi:[1,0]
	v_pk_mul_f32 v[148:149], v[14:15], s[0:1] op_sel_hi:[1,0]
	v_pk_mul_f32 v[132:133], v[38:39], s[0:1] op_sel_hi:[1,0]
	v_pk_mul_f32 v[134:135], v[40:41], s[0:1] op_sel_hi:[1,0]
	v_med3_f32 v0, v132, s53, v204
	v_med3_f32 v133, v133, s53, v204
	v_mov_b32_e32 v132, v1
	v_cvt_pk_fp8_f32 v132, v0, v133
	v_med3_f32 v0, v134, s53, v204
	v_med3_f32 v134, v135, s53, v204
	v_med3_f32 v135, v146, s53, v204
	v_med3_f32 v146, v147, s53, v204
	v_mov_b32_e32 v133, v1
	v_cvt_pk_fp8_f32 v133, v135, v146
	v_cvt_pk_fp8_f32 v132, v0, v134 op_sel:[0,0,1]
	v_med3_f32 v0, v136, s53, v204
	v_med3_f32 v134, v137, s53, v204
	v_cvt_pk_fp8_f32 v133, v0, v134 op_sel:[0,0,1]
	v_pk_mul_f32 v[134:135], v[22:23], s[0:1] op_sel_hi:[1,0]
	v_pk_mul_f32 v[136:137], v[24:25], s[0:1] op_sel_hi:[1,0]
	v_med3_f32 v0, v134, s53, v204
	v_med3_f32 v135, v135, s53, v204
	v_mov_b32_e32 v134, v1
	v_cvt_pk_fp8_f32 v134, v0, v135
	v_med3_f32 v0, v136, s53, v204
	v_med3_f32 v136, v137, s53, v204
	v_med3_f32 v137, v148, s53, v204
	v_med3_f32 v148, v149, s53, v204
	v_mov_b32_e32 v135, v1
	v_cvt_pk_fp8_f32 v135, v137, v148
	v_pk_mul_f32 v[146:147], v[16:17], s[0:1] op_sel_hi:[1,0]
	v_cvt_pk_fp8_f32 v134, v0, v136 op_sel:[0,0,1]
	v_med3_f32 v0, v146, s53, v204
	v_med3_f32 v136, v147, s53, v204
	v_cvt_pk_fp8_f32 v135, v0, v136 op_sel:[0,0,1]
	v_mov_b32_e32 v0, 0x2bff8
	v_mov_b32_e32 v136, 0x28000
	v_cndmask_b32_e32 v0, v0, v136, vcc
	v_lshl_add_u64 v[136:137], v[144:145], 0, v[0:1]
	v_permlane16_swap_b32_e32 v132, v134
	v_permlane16_swap_b32_e32 v133, v135
	v_lshl_add_u64 v[136:137], v[136:137], 0, v[130:131]
	v_pk_mul_f32 v[130:131], v[18:19], s[0:1] op_sel_hi:[1,0]
	global_store_dwordx4 v[136:137], v[132:135], off sc1
	v_pk_mul_f32 v[144:145], v[10:11], s[0:1] op_sel_hi:[1,0]
	v_med3_f32 v0, v130, s53, v204
	v_pk_mul_f32 v[132:133], v[20:21], s[0:1] op_sel_hi:[1,0]
	v_med3_f32 v131, v131, s53, v204
	v_mov_b32_e32 v130, v1
	v_cvt_pk_fp8_f32 v130, v0, v131
	v_med3_f32 v0, v132, s53, v204
	v_med3_f32 v132, v133, s53, v204
	v_med3_f32 v133, v144, s53, v204
	v_med3_f32 v144, v145, s53, v204
	v_mov_b32_e32 v131, v1
	v_cvt_pk_fp8_f32 v131, v133, v144
	v_pk_mul_f32 v[134:135], v[12:13], s[0:1] op_sel_hi:[1,0]
	v_cvt_pk_fp8_f32 v130, v0, v132 op_sel:[0,0,1]
	v_med3_f32 v0, v134, s53, v204
	v_med3_f32 v132, v135, s53, v204
	v_cvt_pk_fp8_f32 v131, v0, v132 op_sel:[0,0,1]
	v_pk_mul_f32 v[132:133], v[6:7], s[0:1] op_sel_hi:[1,0]
	v_pk_mul_f32 v[134:135], v[8:9], s[0:1] op_sel_hi:[1,0]
	v_pk_mul_f32 v[146:147], v[2:3], s[0:1] op_sel_hi:[1,0]
	v_med3_f32 v0, v132, s53, v204
	v_med3_f32 v133, v133, s53, v204
	v_mov_b32_e32 v132, v1
	v_cvt_pk_fp8_f32 v132, v0, v133
	v_med3_f32 v0, v134, s53, v204
	v_med3_f32 v134, v135, s53, v204
	v_med3_f32 v135, v146, s53, v204
	v_med3_f32 v146, v147, s53, v204
	v_mov_b32_e32 v133, v1
	v_cvt_pk_fp8_f32 v133, v135, v146
	v_pk_mul_f32 v[144:145], v[4:5], s[0:1] op_sel_hi:[1,0]
	v_cvt_pk_fp8_f32 v132, v0, v134 op_sel:[0,0,1]
	v_med3_f32 v0, v144, s53, v204
	v_med3_f32 v134, v145, s53, v204
	v_cvt_pk_fp8_f32 v133, v0, v134 op_sel:[0,0,1]
	v_permlane16_swap_b32_e32 v130, v132
	s_mov_b64 s[2:3], 0
	v_permlane16_swap_b32_e32 v131, v133
	global_store_dwordx4 v[136:137], v[130:133], off offset:128 sc1
.LBB0_251:
	s_andn2_b64 vcc, exec, s[2:3]
	s_cbranch_vccnz .LBB0_253
	s_lshl_b32 s19, s21, 5
	v_lshlrev_b32_e32 v0, 4, v143
	s_lshl_b32 s29, s28, 8
	v_and_b32_e32 v0, 16, v0
	s_or_b32 s19, s29, s19
	v_lshl_add_u64 v[130:131], s[60:61], 0, v[0:1]
	v_lshlrev_b32_e32 v0, 5, v142
	s_addk_i32 s19, 0xfe00
	s_lshl_b32 s1, s23, 6
	s_lshl_b32 s0, s18, 8
	v_lshl_add_u64 v[134:135], v[130:131], 0, v[0:1]
	v_lshl_add_u32 v0, v143, 3, s19
	v_or_b32_e32 v156, s1, v142
	s_add_i32 s1, s1, s0
	v_ashrrev_i32_e32 v132, 4, v0
	s_ashr_i32 s2, s1, 5
	v_ashrrev_i32_e32 v133, 31, v132
	s_ashr_i32 s3, s2, 31
	v_pk_mul_f32 v[136:137], v[128:129], s[52:53] op_sel_hi:[1,0]
	v_pk_mul_f32 v[144:145], v[126:127], s[52:53] op_sel_hi:[1,0]
	v_lshlrev_b64 v[132:133], 10, v[132:133]
	v_pk_mul_f32 v[148:149], v[124:125], s[52:53] op_sel_hi:[1,0]
	v_pk_mul_f32 v[146:147], v[122:123], s[52:53] op_sel_hi:[1,0]
	v_cvt_pk_bf16_f32 v144, v144, v145
	v_cvt_pk_bf16_f32 v145, v136, v137
	v_lshl_add_u64 v[136:137], v[132:133], 0, s[2:3]
	s_movk_i32 s19, 0x500
	v_add_u32_e32 v0, 0x80, v0
	v_cvt_pk_bf16_f32 v146, v146, v147
	v_cvt_pk_bf16_f32 v147, v148, v149
	v_mad_u64_u32 v[148:149], s[30:31], v136, s19, v[134:135]
	v_ashrrev_i32_e32 v136, 4, v0
	v_mad_i32_i24 v149, v137, s19, v149
	v_ashrrev_i32_e32 v137, 31, v136
	global_store_dwordx4 v[148:149], v[144:147], off sc1
	v_pk_mul_f32 v[150:151], v[108:109], s[52:53] op_sel_hi:[1,0]
	v_lshlrev_b64 v[136:137], 10, v[136:137]
	v_pk_mul_f32 v[146:147], v[116:117], s[52:53] op_sel_hi:[1,0]
	v_pk_mul_f32 v[144:145], v[114:115], s[52:53] op_sel_hi:[1,0]
	v_pk_mul_f32 v[152:153], v[106:107], s[52:53] op_sel_hi:[1,0]
	v_cvt_pk_bf16_f32 v144, v144, v145
	v_cvt_pk_bf16_f32 v145, v146, v147
	v_cvt_pk_bf16_f32 v147, v150, v151
	v_lshl_add_u64 v[150:151], v[136:137], 0, s[2:3]
	v_cvt_pk_bf16_f32 v146, v152, v153
	v_mad_u64_u32 v[152:153], s[30:31], v150, s19, v[134:135]
	v_mad_i32_i24 v153, v151, s19, v153
	global_store_dwordx4 v[152:153], v[144:147], off sc1
	v_pk_mul_f32 v[150:151], v[112:113], s[52:53] op_sel_hi:[1,0]
	v_pk_mul_f32 v[154:155], v[110:111], s[52:53] op_sel_hi:[1,0]
	v_pk_mul_f32 v[146:147], v[120:121], s[52:53] op_sel_hi:[1,0]
	v_pk_mul_f32 v[144:145], v[118:119], s[52:53] op_sel_hi:[1,0]
	s_or_b32 s2, s2, 1
	v_cvt_pk_bf16_f32 v144, v144, v145
; DI u32x4 pack8(const f32x4& a, const f32x4& b) { u32x4 w; w.x = pk2(a[0], a[1]); w.y = pk2(a[2], a[3]); w.z = pk2(b[0], b[1]); w.w = pk2(b[2], b[3]); return w; }
;     DI void operator()(const f32x4 (&acc)[2][2][4][2], const Unit& u, int wr, int wc, int fr, int fq) const {
;         EPI_ROWS_BEGIN
;             const int row = u.pm * 256 + rt;
; #pragma unroll
;             for (int bj = 0; bj < 2; ++bj) { const int ch = u.pn * 256 + bj * 128 + 32 * wc + 8 * fq; const int g = ch >> 4, c0 = ch & 15;
;                 *(u32x4*)(ua + ((size_t)g * CROWS + (row >> 5)) * UAK + (row & 31) * 16 + c0) = pack8(acc[ai][bj][m][0] * sc, acc[ai][bj][m][1] * sc); }
;         EPI_ROWS_END
;     }
	v_cvt_pk_bf16_f32 v145, v146, v147
	v_cvt_pk_bf16_f32 v146, v154, v155
	v_cvt_pk_bf16_f32 v147, v150, v151
	global_store_dwordx4 v[148:149], v[144:147], off offset:512 sc1
	v_pk_mul_f32 v[148:149], v[92:93], s[52:53] op_sel_hi:[1,0]
	v_pk_mul_f32 v[150:151], v[90:91], s[52:53] op_sel_hi:[1,0]
	v_pk_mul_f32 v[146:147], v[100:101], s[52:53] op_sel_hi:[1,0]
	v_pk_mul_f32 v[144:145], v[98:99], s[52:53] op_sel_hi:[1,0]
	s_ashr_i32 s3, s2, 31
	v_cvt_pk_bf16_f32 v144, v144, v145
	v_cvt_pk_bf16_f32 v145, v146, v147
	v_cvt_pk_bf16_f32 v146, v150, v151
	v_cvt_pk_bf16_f32 v147, v148, v149
	global_store_dwordx4 v[152:153], v[144:147], off offset:512 sc1
	v_pk_mul_f32 v[148:149], v[96:97], s[52:53] op_sel_hi:[1,0]
	v_pk_mul_f32 v[150:151], v[94:95], s[52:53] op_sel_hi:[1,0]
	v_pk_mul_f32 v[146:147], v[104:105], s[52:53] op_sel_hi:[1,0]
	v_pk_mul_f32 v[144:145], v[102:103], s[52:53] op_sel_hi:[1,0]
	v_or_b32_e32 v0, 48, v156
	v_cvt_pk_bf16_f32 v144, v144, v145
	v_cvt_pk_bf16_f32 v145, v146, v147
	v_cvt_pk_bf16_f32 v147, v148, v149
	v_lshl_add_u64 v[148:149], v[132:133], 0, s[2:3]
	v_cvt_pk_bf16_f32 v146, v150, v151
	v_mad_u64_u32 v[150:151], s[30:31], v148, s19, v[134:135]
	v_mad_i32_i24 v151, v149, s19, v151
	global_store_dwordx4 v[150:151], v[144:147], off sc1
	v_pk_mul_f32 v[148:149], v[76:77], s[52:53] op_sel_hi:[1,0]
	v_pk_mul_f32 v[150:151], v[74:75], s[52:53] op_sel_hi:[1,0]
	v_pk_mul_f32 v[146:147], v[84:85], s[52:53] op_sel_hi:[1,0]
	v_pk_mul_f32 v[144:145], v[82:83], s[52:53] op_sel_hi:[1,0]
	v_pk_mul_f32 v[152:153], v[80:81], s[52:53] op_sel_hi:[1,0]
	v_cvt_pk_bf16_f32 v144, v144, v145
	v_cvt_pk_bf16_f32 v145, v146, v147
	v_cvt_pk_bf16_f32 v147, v148, v149
	v_lshl_add_u64 v[148:149], v[136:137], 0, s[2:3]
	v_cvt_pk_bf16_f32 v146, v150, v151
	v_mad_u64_u32 v[150:151], s[2:3], v148, s19, v[134:135]
	v_mad_i32_i24 v151, v149, s19, v151
	global_store_dwordx4 v[150:151], v[144:147], off sc1
	v_pk_mul_f32 v[154:155], v[78:79], s[52:53] op_sel_hi:[1,0]
	s_nop 0
	v_add_u32_e32 v144, s0, v0
	v_ashrrev_i32_e32 v148, 5, v144
	v_lshlrev_b32_e32 v0, 5, v0
	v_ashrrev_i32_e32 v149, 31, v148
	v_and_b32_e32 v0, 0x3e0, v0
	v_pk_mul_f32 v[146:147], v[88:89], s[52:53] op_sel_hi:[1,0]
	v_pk_mul_f32 v[144:145], v[86:87], s[52:53] op_sel_hi:[1,0]
	v_lshl_add_u64 v[150:151], v[130:131], 0, v[0:1]
	v_cvt_pk_bf16_f32 v144, v144, v145
	v_cvt_pk_bf16_f32 v145, v146, v147
	v_cvt_pk_bf16_f32 v147, v152, v153
	v_lshl_add_u64 v[152:153], v[132:133], 0, v[148:149]
	v_cvt_pk_bf16_f32 v146, v154, v155
	v_mad_u64_u32 v[154:155], s[2:3], v152, s19, v[150:151]
	v_lshl_add_u64 v[148:149], v[136:137], 0, v[148:149]
	v_mad_i32_i24 v155, v153, s19, v155
	v_mad_u64_u32 v[150:151], s[2:3], v148, s19, v[150:151]
	global_store_dwordx4 v[154:155], v[144:147], off sc1
	v_pk_mul_f32 v[152:153], v[68:69], s[52:53] op_sel_hi:[1,0]
	v_pk_mul_f32 v[154:155], v[66:67], s[52:53] op_sel_hi:[1,0]
	v_pk_mul_f32 v[146:147], v[72:73], s[52:53] op_sel_hi:[1,0]
	v_pk_mul_f32 v[144:145], v[70:71], s[52:53] op_sel_hi:[1,0]
	s_add_i32 s2, s1, 0x80
	v_cvt_pk_bf16_f32 v144, v144, v145
	v_cvt_pk_bf16_f32 v145, v146, v147
	v_cvt_pk_bf16_f32 v146, v154, v155
	v_cvt_pk_bf16_f32 v147, v152, v153
	v_mad_i32_i24 v151, v149, s19, v151
	s_ashr_i32 s2, s2, 5
	global_store_dwordx4 v[150:151], v[144:147], off sc1
	s_ashr_i32 s3, s2, 31
	v_pk_mul_f32 v[148:149], v[60:61], s[52:53] op_sel_hi:[1,0]
	v_pk_mul_f32 v[146:147], v[64:65], s[52:53] op_sel_hi:[1,0]
	v_pk_mul_f32 v[144:145], v[62:63], s[52:53] op_sel_hi:[1,0]
	v_pk_mul_f32 v[150:151], v[58:59], s[52:53] op_sel_hi:[1,0]
	v_cvt_pk_bf16_f32 v144, v144, v145
	v_cvt_pk_bf16_f32 v145, v146, v147
	v_cvt_pk_bf16_f32 v147, v148, v149
	v_lshl_add_u64 v[148:149], v[132:133], 0, s[2:3]
	v_cvt_pk_bf16_f32 v146, v150, v151
	v_mad_u64_u32 v[150:151], s[30:31], v148, s19, v[134:135]
	v_mad_i32_i24 v151, v149, s19, v151
	global_store_dwordx4 v[150:151], v[144:147], off sc1
	v_pk_mul_f32 v[148:149], v[44:45], s[52:53] op_sel_hi:[1,0]
	v_pk_mul_f32 v[150:151], v[42:43], s[52:53] op_sel_hi:[1,0]
	v_pk_mul_f32 v[146:147], v[52:53], s[52:53] op_sel_hi:[1,0]
	v_pk_mul_f32 v[144:145], v[50:51], s[52:53] op_sel_hi:[1,0]
	v_add_u32_e32 v0, 0x90, v156
	v_cvt_pk_bf16_f32 v144, v144, v145
	v_cvt_pk_bf16_f32 v145, v146, v147
	v_cvt_pk_bf16_f32 v147, v148, v149
; DI u32x4 pack8(const f32x4& a, const f32x4& b) { u32x4 w; w.x = pk2(a[0], a[1]); w.y = pk2(a[2], a[3]); w.z = pk2(b[0], b[1]); w.w = pk2(b[2], b[3]); return w; }
;     DI void operator()(const f32x4 (&acc)[2][2][4][2], const Unit& u, int wr, int wc, int fr, int fq) const {
;         EPI_ROWS_BEGIN
;             const int row = u.pm * 256 + rt;
; #pragma unroll
;             for (int bj = 0; bj < 2; ++bj) { const int ch = u.pn * 256 + bj * 128 + 32 * wc + 8 * fq; const int g = ch >> 4, c0 = ch & 15;
;                 *(u32x4*)(ua + ((size_t)g * CROWS + (row >> 5)) * UAK + (row & 31) * 16 + c0) = pack8(acc[ai][bj][m][0] * sc, acc[ai][bj][m][1] * sc); }
;         EPI_ROWS_END
;     }
	v_lshl_add_u64 v[148:149], v[136:137], 0, s[2:3]
	v_cvt_pk_bf16_f32 v146, v150, v151
	v_mad_u64_u32 v[150:151], s[2:3], v148, s19, v[134:135]
	v_mad_i32_i24 v151, v149, s19, v151
	global_store_dwordx4 v[150:151], v[144:147], off sc1
	v_pk_mul_f32 v[152:153], v[48:49], s[52:53] op_sel_hi:[1,0]
	v_pk_mul_f32 v[154:155], v[46:47], s[52:53] op_sel_hi:[1,0]
	v_add_u32_e32 v144, s0, v0
	v_ashrrev_i32_e32 v148, 5, v144
	v_lshlrev_b32_e32 v0, 5, v0
	v_ashrrev_i32_e32 v149, 31, v148
	v_and_b32_e32 v0, 0x3e0, v0
	v_pk_mul_f32 v[146:147], v[56:57], s[52:53] op_sel_hi:[1,0]
	v_pk_mul_f32 v[144:145], v[54:55], s[52:53] op_sel_hi:[1,0]
	v_lshl_add_u64 v[150:151], v[130:131], 0, v[0:1]
	v_cvt_pk_bf16_f32 v144, v144, v145
	v_cvt_pk_bf16_f32 v145, v146, v147
	v_cvt_pk_bf16_f32 v147, v152, v153
	v_lshl_add_u64 v[152:153], v[132:133], 0, v[148:149]
	v_cvt_pk_bf16_f32 v146, v154, v155
	v_mad_u64_u32 v[154:155], s[2:3], v152, s19, v[150:151]
	v_mad_i32_i24 v155, v153, s19, v155
	v_lshl_add_u64 v[148:149], v[136:137], 0, v[148:149]
	global_store_dwordx4 v[154:155], v[144:147], off sc1
	v_pk_mul_f32 v[152:153], v[28:29], s[52:53] op_sel_hi:[1,0]
	v_pk_mul_f32 v[154:155], v[26:27], s[52:53] op_sel_hi:[1,0]
	v_pk_mul_f32 v[146:147], v[36:37], s[52:53] op_sel_hi:[1,0]
	v_pk_mul_f32 v[144:145], v[34:35], s[52:53] op_sel_hi:[1,0]
	v_mad_u64_u32 v[150:151], s[2:3], v148, s19, v[150:151]
	s_addk_i32 s1, 0xa0
	v_cvt_pk_bf16_f32 v144, v144, v145
	v_cvt_pk_bf16_f32 v145, v146, v147
	v_cvt_pk_bf16_f32 v146, v154, v155
	v_cvt_pk_bf16_f32 v147, v152, v153
	v_mad_i32_i24 v151, v149, s19, v151
	s_ashr_i32 s2, s1, 5
	global_store_dwordx4 v[150:151], v[144:147], off sc1
	s_ashr_i32 s3, s2, 31
	v_pk_mul_f32 v[148:149], v[32:33], s[52:53] op_sel_hi:[1,0]
	v_pk_mul_f32 v[146:147], v[40:41], s[52:53] op_sel_hi:[1,0]
	v_pk_mul_f32 v[144:145], v[38:39], s[52:53] op_sel_hi:[1,0]
	v_pk_mul_f32 v[150:151], v[30:31], s[52:53] op_sel_hi:[1,0]
	v_cvt_pk_bf16_f32 v144, v144, v145
	v_cvt_pk_bf16_f32 v145, v146, v147
	v_cvt_pk_bf16_f32 v147, v148, v149
	v_lshl_add_u64 v[148:149], v[132:133], 0, s[2:3]
	v_cvt_pk_bf16_f32 v146, v150, v151
	v_mad_u64_u32 v[150:151], s[30:31], v148, s19, v[134:135]
	v_mad_i32_i24 v151, v149, s19, v151
	global_store_dwordx4 v[150:151], v[144:147], off sc1
	v_pk_mul_f32 v[148:149], v[12:13], s[52:53] op_sel_hi:[1,0]
	v_pk_mul_f32 v[150:151], v[10:11], s[52:53] op_sel_hi:[1,0]
	v_pk_mul_f32 v[146:147], v[20:21], s[52:53] op_sel_hi:[1,0]
	v_pk_mul_f32 v[144:145], v[18:19], s[52:53] op_sel_hi:[1,0]
	v_add_u32_e32 v0, 0xb0, v156
	v_cvt_pk_bf16_f32 v144, v144, v145
	v_cvt_pk_bf16_f32 v145, v146, v147
	v_cvt_pk_bf16_f32 v147, v148, v149
	v_lshl_add_u64 v[148:149], v[136:137], 0, s[2:3]
	v_mad_u64_u32 v[134:135], s[2:3], v148, s19, v[134:135]
	v_cvt_pk_bf16_f32 v146, v150, v151
	v_mad_i32_i24 v135, v149, s19, v135
	global_store_dwordx4 v[134:135], v[144:147], off sc1
	v_add_u32_e32 v134, s0, v0
	v_lshlrev_b32_e32 v0, 5, v0
	v_ashrrev_i32_e32 v134, 5, v134
	v_and_b32_e32 v0, 0x3e0, v0
	v_ashrrev_i32_e32 v135, 31, v134
	v_lshl_add_u64 v[148:149], v[130:131], 0, v[0:1]
	v_pk_mul_f32 v[130:131], v[24:25], s[52:53] op_sel_hi:[1,0]
	v_pk_mul_f32 v[144:145], v[22:23], s[52:53] op_sel_hi:[1,0]
	v_pk_mul_f32 v[150:151], v[16:17], s[52:53] op_sel_hi:[1,0]
	v_cvt_pk_bf16_f32 v144, v144, v145
	v_cvt_pk_bf16_f32 v145, v130, v131
	v_lshl_add_u64 v[130:131], v[132:133], 0, v[134:135]
	v_pk_mul_f32 v[146:147], v[14:15], s[52:53] op_sel_hi:[1,0]
	v_mad_u64_u32 v[132:133], s[0:1], v130, s19, v[148:149]
	v_cvt_pk_bf16_f32 v146, v146, v147
	v_cvt_pk_bf16_f32 v147, v150, v151
	v_mad_i32_i24 v133, v131, s19, v133
	v_lshl_add_u64 v[134:135], v[136:137], 0, v[134:135]
	global_store_dwordx4 v[132:133], v[144:147], off sc1
	v_pk_mul_f32 v[132:133], v[8:9], s[52:53] op_sel_hi:[1,0]
	v_pk_mul_f32 v[130:131], v[6:7], s[52:53] op_sel_hi:[1,0]
	v_pk_mul_f32 v[144:145], v[4:5], s[52:53] op_sel_hi:[1,0]
	v_pk_mul_f32 v[146:147], v[2:3], s[52:53] op_sel_hi:[1,0]
	v_mad_u64_u32 v[136:137], s[0:1], v134, s19, v[148:149]
	v_cvt_pk_bf16_f32 v130, v130, v131
	v_cvt_pk_bf16_f32 v131, v132, v133
	v_cvt_pk_bf16_f32 v132, v146, v147
	v_cvt_pk_bf16_f32 v133, v144, v145
	v_mad_i32_i24 v137, v135, s19, v137
	global_store_dwordx4 v[136:137], v[130:133], off sc1

; DI u32x4 pack8(const f32x4& a, const f32x4& b) { u32x4 w; w.x = pk2(a[0], a[1]); w.y = pk2(a[2], a[3]); w.z = pk2(b[0], b[1]); w.w = pk2(b[2], b[3]); return w; }
;     DI void operator()(const f32x4 (&acc)[2][2][4][2], const Unit& u, int wr, int wc, int fr, int fq) const {
;         EPI_ROWS_BEGIN
;             const size_t row = (size_t)u.pm * 256 + rt;
; #pragma unroll
;             for (int bj = 0; bj < 2; ++bj) *(u32x4*)(o + row * ldc + u.pn * 256 + bj * 128 + 32 * wc + 8 * fq) = pack8(acc[ai][bj][m][0] * sc, acc[ai][bj][m][1] * sc);
;         EPI_ROWS_END
;     }
;     DI void operator()(const f32x4 (&acc)[2][2][4][2], const Unit& u, int wr, int wc, int fr, int fq) const {
;     ...
;         if (u.pn < 2) { EpiScaled E{v, AW, sc}; E(acc, u2, wr, wc, fr, fq); }
.LBB0_254:
	s_andn2_b64 vcc, exec, s[2:3]
	s_cbranch_vccnz .LBB0_256
	v_lshl_or_b32 v130, s23, 6, v142
	s_ashr_i32 s19, s18, 31
	s_lshl_b64 s[2:3], s[18:19], 8
	v_ashrrev_i32_e32 v131, 31, v130
	v_lshl_add_u64 v[144:145], s[2:3], 0, v[130:131]
	v_lshlrev_b64 v[144:145], 10, v[144:145]
	v_lshlrev_b32_e32 v132, 3, v143
	v_lshl_add_u64 v[144:145], s[12:13], 0, v[144:145]
	s_lshl_b32 s58, s28, 9
	v_ashrrev_i32_e32 v133, 31, v132
	v_lshl_add_u64 v[144:145], v[144:145], 0, s[58:59]
	s_lshl_b32 s28, s21, 6
	s_mov_b32 s29, s59
	v_pk_mul_f32 v[136:137], v[128:129], s[52:53] op_sel_hi:[1,0]
	v_pk_mul_f32 v[134:135], v[126:127], s[52:53] op_sel_hi:[1,0]
	v_pk_mul_f32 v[146:147], v[124:125], s[52:53] op_sel_hi:[1,0]
	v_pk_mul_f32 v[148:149], v[122:123], s[52:53] op_sel_hi:[1,0]
	v_lshl_add_u64 v[144:145], v[144:145], 0, s[28:29]
	v_lshlrev_b64 v[132:133], 1, v[132:133]
	v_cvt_pk_bf16_f32 v134, v134, v135
	v_cvt_pk_bf16_f32 v135, v136, v137
	v_cvt_pk_bf16_f32 v136, v148, v149
	v_cvt_pk_bf16_f32 v137, v146, v147
	v_lshl_add_u64 v[144:145], v[144:145], 0, v[132:133]
	global_store_dwordx4 v[144:145], v[134:137], off sc1
	v_pk_mul_f32 v[146:147], v[108:109], s[52:53] op_sel_hi:[1,0]
	v_pk_mul_f32 v[148:149], v[106:107], s[52:53] op_sel_hi:[1,0]
	v_pk_mul_f32 v[136:137], v[116:117], s[52:53] op_sel_hi:[1,0]
	v_pk_mul_f32 v[134:135], v[114:115], s[52:53] op_sel_hi:[1,0]
	s_nop 0
	v_cvt_pk_bf16_f32 v134, v134, v135
	v_cvt_pk_bf16_f32 v135, v136, v137
	v_cvt_pk_bf16_f32 v136, v148, v149
	v_cvt_pk_bf16_f32 v137, v146, v147
	global_store_dwordx4 v[144:145], v[134:137], off offset:256 sc1
	v_pk_mul_f32 v[146:147], v[112:113], s[52:53] op_sel_hi:[1,0]
	v_pk_mul_f32 v[148:149], v[110:111], s[52:53] op_sel_hi:[1,0]
	v_or_b32_e32 v134, 16, v130
	v_ashrrev_i32_e32 v135, 31, v134
	v_lshl_add_u64 v[144:145], s[2:3], 0, v[134:135]
	v_lshlrev_b64 v[144:145], 10, v[144:145]
	v_lshl_add_u64 v[144:145], s[12:13], 0, v[144:145]
	v_lshl_add_u64 v[144:145], v[144:145], 0, s[58:59]
	v_pk_mul_f32 v[136:137], v[120:121], s[52:53] op_sel_hi:[1,0]
	v_pk_mul_f32 v[134:135], v[118:119], s[52:53] op_sel_hi:[1,0]
	v_lshl_add_u64 v[144:145], v[144:145], 0, s[28:29]
	v_cvt_pk_bf16_f32 v134, v134, v135
	v_cvt_pk_bf16_f32 v135, v136, v137
	v_cvt_pk_bf16_f32 v136, v148, v149
	v_cvt_pk_bf16_f32 v137, v146, v147
	v_lshl_add_u64 v[144:145], v[144:145], 0, v[132:133]
	global_store_dwordx4 v[144:145], v[134:137], off sc1
	v_pk_mul_f32 v[146:147], v[92:93], s[52:53] op_sel_hi:[1,0]
	v_pk_mul_f32 v[148:149], v[90:91], s[52:53] op_sel_hi:[1,0]
	v_pk_mul_f32 v[136:137], v[100:101], s[52:53] op_sel_hi:[1,0]
	v_pk_mul_f32 v[134:135], v[98:99], s[52:53] op_sel_hi:[1,0]
	s_nop 0
	v_cvt_pk_bf16_f32 v134, v134, v135
	v_cvt_pk_bf16_f32 v135, v136, v137
	v_cvt_pk_bf16_f32 v136, v148, v149
	v_cvt_pk_bf16_f32 v137, v146, v147
	global_store_dwordx4 v[144:145], v[134:137], off offset:256 sc1
	v_pk_mul_f32 v[146:147], v[96:97], s[52:53] op_sel_hi:[1,0]
	v_pk_mul_f32 v[148:149], v[94:95], s[52:53] op_sel_hi:[1,0]
	v_or_b32_e32 v134, 32, v130
	v_ashrrev_i32_e32 v135, 31, v134
	v_lshl_add_u64 v[144:145], s[2:3], 0, v[134:135]
	v_lshlrev_b64 v[144:145], 10, v[144:145]
	v_lshl_add_u64 v[144:145], s[12:13], 0, v[144:145]
	v_lshl_add_u64 v[144:145], v[144:145], 0, s[58:59]
	v_pk_mul_f32 v[136:137], v[104:105], s[52:53] op_sel_hi:[1,0]
	v_pk_mul_f32 v[134:135], v[102:103], s[52:53] op_sel_hi:[1,0]
	v_lshl_add_u64 v[144:145], v[144:145], 0, s[28:29]
	v_cvt_pk_bf16_f32 v134, v134, v135
	v_cvt_pk_bf16_f32 v135, v136, v137
	v_cvt_pk_bf16_f32 v136, v148, v149
	v_cvt_pk_bf16_f32 v137, v146, v147
	v_lshl_add_u64 v[144:145], v[144:145], 0, v[132:133]
	global_store_dwordx4 v[144:145], v[134:137], off sc1
	v_pk_mul_f32 v[146:147], v[76:77], s[52:53] op_sel_hi:[1,0]
	v_pk_mul_f32 v[148:149], v[74:75], s[52:53] op_sel_hi:[1,0]
	v_pk_mul_f32 v[136:137], v[84:85], s[52:53] op_sel_hi:[1,0]
	v_pk_mul_f32 v[134:135], v[82:83], s[52:53] op_sel_hi:[1,0]
	s_nop 0
	v_cvt_pk_bf16_f32 v134, v134, v135
	v_cvt_pk_bf16_f32 v135, v136, v137
	v_cvt_pk_bf16_f32 v136, v148, v149
	v_cvt_pk_bf16_f32 v137, v146, v147
	global_store_dwordx4 v[144:145], v[134:137], off offset:256 sc1
	v_pk_mul_f32 v[146:147], v[80:81], s[52:53] op_sel_hi:[1,0]
	v_pk_mul_f32 v[148:149], v[78:79], s[52:53] op_sel_hi:[1,0]
	v_or_b32_e32 v134, 48, v130
	v_ashrrev_i32_e32 v135, 31, v134
	v_lshl_add_u64 v[144:145], s[2:3], 0, v[134:135]
	v_lshlrev_b64 v[144:145], 10, v[144:145]
	v_lshl_add_u64 v[144:145], s[12:13], 0, v[144:145]
	v_lshl_add_u64 v[144:145], v[144:145], 0, s[58:59]
	v_pk_mul_f32 v[136:137], v[88:89], s[52:53] op_sel_hi:[1,0]
	v_pk_mul_f32 v[134:135], v[86:87], s[52:53] op_sel_hi:[1,0]
	v_lshl_add_u64 v[144:145], v[144:145], 0, s[28:29]
	v_cvt_pk_bf16_f32 v134, v134, v135
	v_cvt_pk_bf16_f32 v135, v136, v137
	v_cvt_pk_bf16_f32 v136, v148, v149
	v_cvt_pk_bf16_f32 v137, v146, v147
	v_lshl_add_u64 v[144:145], v[144:145], 0, v[132:133]
	global_store_dwordx4 v[144:145], v[134:137], off sc1
	v_pk_mul_f32 v[146:147], v[68:69], s[52:53] op_sel_hi:[1,0]
	v_pk_mul_f32 v[148:149], v[66:67], s[52:53] op_sel_hi:[1,0]
	v_pk_mul_f32 v[136:137], v[72:73], s[52:53] op_sel_hi:[1,0]
	v_pk_mul_f32 v[134:135], v[70:71], s[52:53] op_sel_hi:[1,0]
	s_nop 0
	v_cvt_pk_bf16_f32 v134, v134, v135
; DI u32x4 pack8(const f32x4& a, const f32x4& b) { u32x4 w; w.x = pk2(a[0], a[1]); w.y = pk2(a[2], a[3]); w.z = pk2(b[0], b[1]); w.w = pk2(b[2], b[3]); return w; }
;     DI void operator()(const f32x4 (&acc)[2][2][4][2], const Unit& u, int wr, int wc, int fr, int fq) const {
;         EPI_ROWS_BEGIN
;             const size_t row = (size_t)u.pm * 256 + rt;
; #pragma unroll
;             for (int bj = 0; bj < 2; ++bj) *(u32x4*)(o + row * ldc + u.pn * 256 + bj * 128 + 32 * wc + 8 * fq) = pack8(acc[ai][bj][m][0] * sc, acc[ai][bj][m][1] * sc);
;         EPI_ROWS_END
;     }
	v_cvt_pk_bf16_f32 v135, v136, v137
	v_cvt_pk_bf16_f32 v136, v148, v149
	v_cvt_pk_bf16_f32 v137, v146, v147
	global_store_dwordx4 v[144:145], v[134:137], off offset:256 sc1
	v_pk_mul_f32 v[146:147], v[60:61], s[52:53] op_sel_hi:[1,0]
	v_pk_mul_f32 v[148:149], v[58:59], s[52:53] op_sel_hi:[1,0]
	v_add_u32_e32 v134, 0x80, v130
	v_ashrrev_i32_e32 v135, 31, v134
	v_lshl_add_u64 v[144:145], s[2:3], 0, v[134:135]
	v_lshlrev_b64 v[144:145], 10, v[144:145]
	v_lshl_add_u64 v[144:145], s[12:13], 0, v[144:145]
	v_lshl_add_u64 v[144:145], v[144:145], 0, s[58:59]
	v_pk_mul_f32 v[136:137], v[64:65], s[52:53] op_sel_hi:[1,0]
	v_pk_mul_f32 v[134:135], v[62:63], s[52:53] op_sel_hi:[1,0]
	v_lshl_add_u64 v[144:145], v[144:145], 0, s[28:29]
	v_cvt_pk_bf16_f32 v134, v134, v135
	v_cvt_pk_bf16_f32 v135, v136, v137
	v_cvt_pk_bf16_f32 v136, v148, v149
	v_cvt_pk_bf16_f32 v137, v146, v147
	v_lshl_add_u64 v[144:145], v[144:145], 0, v[132:133]
	global_store_dwordx4 v[144:145], v[134:137], off sc1
	v_pk_mul_f32 v[146:147], v[44:45], s[52:53] op_sel_hi:[1,0]
	v_pk_mul_f32 v[148:149], v[42:43], s[52:53] op_sel_hi:[1,0]
	v_pk_mul_f32 v[136:137], v[52:53], s[52:53] op_sel_hi:[1,0]
	v_pk_mul_f32 v[134:135], v[50:51], s[52:53] op_sel_hi:[1,0]
	s_nop 0
	v_cvt_pk_bf16_f32 v134, v134, v135
	v_cvt_pk_bf16_f32 v135, v136, v137
	v_cvt_pk_bf16_f32 v136, v148, v149
	v_cvt_pk_bf16_f32 v137, v146, v147
	global_store_dwordx4 v[144:145], v[134:137], off offset:256 sc1
	v_pk_mul_f32 v[146:147], v[48:49], s[52:53] op_sel_hi:[1,0]
	v_pk_mul_f32 v[148:149], v[46:47], s[52:53] op_sel_hi:[1,0]
	v_add_u32_e32 v134, 0x90, v130
	v_ashrrev_i32_e32 v135, 31, v134
	v_lshl_add_u64 v[144:145], s[2:3], 0, v[134:135]
	v_lshlrev_b64 v[144:145], 10, v[144:145]
	v_lshl_add_u64 v[144:145], s[12:13], 0, v[144:145]
	v_lshl_add_u64 v[144:145], v[144:145], 0, s[58:59]
	v_pk_mul_f32 v[136:137], v[56:57], s[52:53] op_sel_hi:[1,0]
	v_pk_mul_f32 v[134:135], v[54:55], s[52:53] op_sel_hi:[1,0]
	v_lshl_add_u64 v[144:145], v[144:145], 0, s[28:29]
	v_cvt_pk_bf16_f32 v134, v134, v135
	v_cvt_pk_bf16_f32 v135, v136, v137
	v_cvt_pk_bf16_f32 v136, v148, v149
	v_cvt_pk_bf16_f32 v137, v146, v147
	v_lshl_add_u64 v[144:145], v[144:145], 0, v[132:133]
	global_store_dwordx4 v[144:145], v[134:137], off sc1
	v_pk_mul_f32 v[146:147], v[28:29], s[52:53] op_sel_hi:[1,0]
	v_pk_mul_f32 v[148:149], v[26:27], s[52:53] op_sel_hi:[1,0]
	v_pk_mul_f32 v[136:137], v[36:37], s[52:53] op_sel_hi:[1,0]
	v_pk_mul_f32 v[134:135], v[34:35], s[52:53] op_sel_hi:[1,0]
	s_nop 0
	v_cvt_pk_bf16_f32 v134, v134, v135
	v_cvt_pk_bf16_f32 v135, v136, v137
	v_cvt_pk_bf16_f32 v136, v148, v149
	v_cvt_pk_bf16_f32 v137, v146, v147
	global_store_dwordx4 v[144:145], v[134:137], off offset:256 sc1
	v_pk_mul_f32 v[146:147], v[32:33], s[52:53] op_sel_hi:[1,0]
	v_pk_mul_f32 v[148:149], v[30:31], s[52:53] op_sel_hi:[1,0]
	v_add_u32_e32 v134, 0xa0, v130
	v_ashrrev_i32_e32 v135, 31, v134
	v_lshl_add_u64 v[144:145], s[2:3], 0, v[134:135]
	v_lshlrev_b64 v[144:145], 10, v[144:145]
	v_lshl_add_u64 v[144:145], s[12:13], 0, v[144:145]
	v_add_u32_e32 v130, 0xb0, v130
	v_lshl_add_u64 v[144:145], v[144:145], 0, s[58:59]
	v_ashrrev_i32_e32 v131, 31, v130
	v_pk_mul_f32 v[136:137], v[40:41], s[52:53] op_sel_hi:[1,0]
	v_pk_mul_f32 v[134:135], v[38:39], s[52:53] op_sel_hi:[1,0]
	v_lshl_add_u64 v[144:145], v[144:145], 0, s[28:29]
	v_lshl_add_u64 v[130:131], s[2:3], 0, v[130:131]
	v_cvt_pk_bf16_f32 v134, v134, v135
	v_cvt_pk_bf16_f32 v135, v136, v137
	v_cvt_pk_bf16_f32 v136, v148, v149
	v_cvt_pk_bf16_f32 v137, v146, v147
	v_lshl_add_u64 v[144:145], v[144:145], 0, v[132:133]
	v_lshlrev_b64 v[130:131], 10, v[130:131]
	global_store_dwordx4 v[144:145], v[134:137], off sc1
	v_pk_mul_f32 v[146:147], v[12:13], s[52:53] op_sel_hi:[1,0]
	v_pk_mul_f32 v[148:149], v[10:11], s[52:53] op_sel_hi:[1,0]
	v_pk_mul_f32 v[136:137], v[20:21], s[52:53] op_sel_hi:[1,0]
	v_pk_mul_f32 v[134:135], v[18:19], s[52:53] op_sel_hi:[1,0]
	v_lshl_add_u64 v[130:131], s[12:13], 0, v[130:131]
	v_cvt_pk_bf16_f32 v134, v134, v135
	v_cvt_pk_bf16_f32 v135, v136, v137
	v_cvt_pk_bf16_f32 v136, v148, v149
	v_cvt_pk_bf16_f32 v137, v146, v147
	v_lshl_add_u64 v[130:131], v[130:131], 0, s[58:59]
	global_store_dwordx4 v[144:145], v[134:137], off offset:256 sc1
	v_pk_mul_f32 v[144:145], v[16:17], s[52:53] op_sel_hi:[1,0]
	v_pk_mul_f32 v[146:147], v[14:15], s[52:53] op_sel_hi:[1,0]
	v_pk_mul_f32 v[136:137], v[24:25], s[52:53] op_sel_hi:[1,0]
	v_pk_mul_f32 v[134:135], v[22:23], s[52:53] op_sel_hi:[1,0]
	v_lshl_add_u64 v[130:131], v[130:131], 0, s[28:29]
	v_cvt_pk_bf16_f32 v134, v134, v135
	v_cvt_pk_bf16_f32 v135, v136, v137
	v_cvt_pk_bf16_f32 v136, v146, v147
	v_cvt_pk_bf16_f32 v137, v144, v145
	v_lshl_add_u64 v[144:145], v[130:131], 0, v[132:133]
	global_store_dwordx4 v[144:145], v[134:137], off sc1
	v_pk_mul_f32 v[132:133], v[8:9], s[52:53] op_sel_hi:[1,0]
	v_pk_mul_f32 v[130:131], v[6:7], s[52:53] op_sel_hi:[1,0]
	v_pk_mul_f32 v[134:135], v[4:5], s[52:53] op_sel_hi:[1,0]
	v_pk_mul_f32 v[136:137], v[2:3], s[52:53] op_sel_hi:[1,0]
	v_cvt_pk_bf16_f32 v130, v130, v131
	v_cvt_pk_bf16_f32 v131, v132, v133
	v_cvt_pk_bf16_f32 v132, v136, v137
	v_cvt_pk_bf16_f32 v133, v134, v135
	global_store_dwordx4 v[144:145], v[130:133], off offset:256 sc1

; DI u32x4 pack8(const f32x4& a, const f32x4& b) { u32x4 w; w.x = pk2(a[0], a[1]); w.y = pk2(a[2], a[3]); w.z = pk2(b[0], b[1]); w.w = pk2(b[2], b[3]); return w; }
;     DI void operator()(const f32x4 (&acc)[2][2][4][2], const Unit& u, int wr, int wc, int fr, int fq) const {
;         const int c0 = u.pn * 256 + 32 * wc + 8 * fq; const int ln = fq * 16 + fr;
;         EPI_ROWS_BEGIN
;             const size_t row = (size_t)u.pm * 256 + rt;
; #pragma unroll
;             for (int bj = 0; bj < 2; ++bj) *(u32x4*)(k + row * AW + c0 + bj * 128) = pack8(acc[ai][bj][m][0] * sc, acc[ai][bj][m][1] * sc);
;         EPI_ROWS_END
;     DI void operator()(const f32x4 (&acc)[2][2][4][2], const Unit& u, int wr, int wc, int fr, int fq) const {
;         Unit u2 = u; u2.pn = u.pn & 1;
;         if (u.pn < 2) { EpiScaled E{q, AW, sc * (0.125f * LOG2E_C)}; E(acc, u2, wr, wc, fr, fq); }
;         else { EpiK E{k, kmean, sc}; E(acc, u2, wr, wc, fr, fq); }
;     }
.LBB0_257:
	s_andn2_b64 vcc, exec, s[2:3]
	s_cbranch_vccnz .LBB0_270
	s_and_b32 s30, s33, 1
	s_cmp_gt_i32 s33, 1
	v_lshlrev_b32_e32 v132, 3, v143
	s_mov_b64 s[2:3], -1
	v_lshl_or_b32 v130, s23, 6, v142
	s_cbranch_scc0 .LBB0_268
	s_lshl_b32 s0, s30, 8
	s_lshl_b32 s1, s21, 5
	s_or_b32 s0, s1, s0
	s_ashr_i32 s19, s18, 31
	v_add_u32_e32 v134, s0, v132
	s_lshl_b64 s[0:1], s[18:19], 18
	v_ashrrev_i32_e32 v131, 31, v130
	s_add_u32 s2, s78, s0
	v_ashrrev_i32_e32 v135, 31, v134
	v_lshlrev_b64 v[136:137], 10, v[130:131]
	v_pk_mul_f32 v[146:147], v[128:129], s[52:53] op_sel_hi:[1,0]
	v_pk_mul_f32 v[144:145], v[126:127], s[52:53] op_sel_hi:[1,0]
	v_pk_mul_f32 v[148:149], v[124:125], s[52:53] op_sel_hi:[1,0]
	s_addc_u32 s3, s79, s1
	v_pk_mul_f32 v[150:151], v[122:123], s[52:53] op_sel_hi:[1,0]
	v_cvt_pk_bf16_f32 v144, v144, v145
	v_cvt_pk_bf16_f32 v145, v146, v147
	v_cvt_pk_bf16_f32 v147, v148, v149
	v_lshl_add_u64 v[148:149], s[2:3], 0, v[136:137]
	v_lshlrev_b64 v[136:137], 1, v[134:135]
	v_cvt_pk_bf16_f32 v146, v150, v151
	v_lshl_add_u64 v[148:149], v[148:149], 0, v[136:137]
	global_store_dwordx4 v[148:149], v[144:147], off sc1
	v_pk_mul_f32 v[150:151], v[108:109], s[52:53] op_sel_hi:[1,0]
	v_pk_mul_f32 v[152:153], v[106:107], s[52:53] op_sel_hi:[1,0]
	v_pk_mul_f32 v[146:147], v[116:117], s[52:53] op_sel_hi:[1,0]
	v_pk_mul_f32 v[144:145], v[114:115], s[52:53] op_sel_hi:[1,0]
	v_lshlrev_b32_e32 v0, 6, v143
	v_cvt_pk_bf16_f32 v144, v144, v145
	v_cvt_pk_bf16_f32 v145, v146, v147
	v_cvt_pk_bf16_f32 v146, v152, v153
	v_cvt_pk_bf16_f32 v147, v150, v151
	global_store_dwordx4 v[148:149], v[144:147], off offset:256 sc1
	v_pk_mul_f32 v[150:151], v[112:113], s[52:53] op_sel_hi:[1,0]
	v_pk_mul_f32 v[152:153], v[110:111], s[52:53] op_sel_hi:[1,0]
	v_or_b32_e32 v144, 16, v130
	v_ashrrev_i32_e32 v145, 31, v144
	v_lshlrev_b64 v[148:149], 10, v[144:145]
	v_pk_mul_f32 v[146:147], v[120:121], s[52:53] op_sel_hi:[1,0]
	v_pk_mul_f32 v[144:145], v[118:119], s[52:53] op_sel_hi:[1,0]
	v_lshl_add_u64 v[148:149], s[2:3], 0, v[148:149]
	v_cvt_pk_bf16_f32 v144, v144, v145
	v_cvt_pk_bf16_f32 v145, v146, v147
	v_cvt_pk_bf16_f32 v146, v152, v153
	v_cvt_pk_bf16_f32 v147, v150, v151
	v_lshl_add_u64 v[148:149], v[148:149], 0, v[136:137]
	global_store_dwordx4 v[148:149], v[144:147], off sc1
	v_pk_mul_f32 v[150:151], v[92:93], s[52:53] op_sel_hi:[1,0]
	v_pk_mul_f32 v[152:153], v[90:91], s[52:53] op_sel_hi:[1,0]
	v_pk_mul_f32 v[146:147], v[100:101], s[52:53] op_sel_hi:[1,0]
	v_pk_mul_f32 v[144:145], v[98:99], s[52:53] op_sel_hi:[1,0]
	v_cmp_eq_u32_e32 vcc, 0, v142
	v_cvt_pk_bf16_f32 v144, v144, v145
	v_cvt_pk_bf16_f32 v145, v146, v147
	v_cvt_pk_bf16_f32 v146, v152, v153
	v_cvt_pk_bf16_f32 v147, v150, v151
	global_store_dwordx4 v[148:149], v[144:147], off offset:256 sc1
	v_pk_mul_f32 v[150:151], v[96:97], s[52:53] op_sel_hi:[1,0]
	v_pk_mul_f32 v[152:153], v[94:95], s[52:53] op_sel_hi:[1,0]
	v_or_b32_e32 v144, 32, v130
	v_ashrrev_i32_e32 v145, 31, v144
	v_lshlrev_b64 v[148:149], 10, v[144:145]
	v_pk_mul_f32 v[146:147], v[104:105], s[52:53] op_sel_hi:[1,0]
	v_pk_mul_f32 v[144:145], v[102:103], s[52:53] op_sel_hi:[1,0]
	v_lshl_add_u64 v[148:149], s[2:3], 0, v[148:149]
	v_cvt_pk_bf16_f32 v144, v144, v145
	v_cvt_pk_bf16_f32 v145, v146, v147
	v_cvt_pk_bf16_f32 v146, v152, v153
	v_cvt_pk_bf16_f32 v147, v150, v151
	v_lshl_add_u64 v[148:149], v[148:149], 0, v[136:137]
	global_store_dwordx4 v[148:149], v[144:147], off sc1
	v_pk_mul_f32 v[150:151], v[76:77], s[52:53] op_sel_hi:[1,0]
	v_pk_mul_f32 v[152:153], v[74:75], s[52:53] op_sel_hi:[1,0]
	v_pk_mul_f32 v[146:147], v[84:85], s[52:53] op_sel_hi:[1,0]
	v_pk_mul_f32 v[144:145], v[82:83], s[52:53] op_sel_hi:[1,0]
	s_nop 0
	v_cvt_pk_bf16_f32 v144, v144, v145
	v_cvt_pk_bf16_f32 v145, v146, v147
	v_cvt_pk_bf16_f32 v146, v152, v153
	v_cvt_pk_bf16_f32 v147, v150, v151
	global_store_dwordx4 v[148:149], v[144:147], off offset:256 sc1
	v_pk_mul_f32 v[150:151], v[80:81], s[52:53] op_sel_hi:[1,0]
	v_pk_mul_f32 v[152:153], v[78:79], s[52:53] op_sel_hi:[1,0]
	v_or_b32_e32 v144, 48, v130
	v_ashrrev_i32_e32 v145, 31, v144
	v_lshlrev_b64 v[148:149], 10, v[144:145]
	v_pk_mul_f32 v[146:147], v[88:89], s[52:53] op_sel_hi:[1,0]
	v_pk_mul_f32 v[144:145], v[86:87], s[52:53] op_sel_hi:[1,0]
	v_lshl_add_u64 v[148:149], s[2:3], 0, v[148:149]
	v_cvt_pk_bf16_f32 v144, v144, v145
	v_cvt_pk_bf16_f32 v145, v146, v147
	v_cvt_pk_bf16_f32 v146, v152, v153
	v_cvt_pk_bf16_f32 v147, v150, v151
	v_lshl_add_u64 v[148:149], v[148:149], 0, v[136:137]
	global_store_dwordx4 v[148:149], v[144:147], off sc1
	v_pk_mul_f32 v[150:151], v[68:69], s[52:53] op_sel_hi:[1,0]
	v_pk_mul_f32 v[152:153], v[66:67], s[52:53] op_sel_hi:[1,0]
	v_pk_mul_f32 v[146:147], v[72:73], s[52:53] op_sel_hi:[1,0]
	v_pk_mul_f32 v[144:145], v[70:71], s[52:53] op_sel_hi:[1,0]
	s_nop 0
	v_cvt_pk_bf16_f32 v144, v144, v145
	v_cvt_pk_bf16_f32 v145, v146, v147
	v_cvt_pk_bf16_f32 v146, v152, v153
	v_cvt_pk_bf16_f32 v147, v150, v151
	global_store_dwordx4 v[148:149], v[144:147], off offset:256 sc1
	v_pk_mul_f32 v[150:151], v[60:61], s[52:53] op_sel_hi:[1,0]
	v_pk_mul_f32 v[152:153], v[58:59], s[52:53] op_sel_hi:[1,0]
	v_add_u32_e32 v144, 0x80, v130
	v_ashrrev_i32_e32 v145, 31, v144
	v_lshlrev_b64 v[148:149], 10, v[144:145]
	v_pk_mul_f32 v[146:147], v[64:65], s[52:53] op_sel_hi:[1,0]
	v_pk_mul_f32 v[144:145], v[62:63], s[52:53] op_sel_hi:[1,0]
	v_lshl_add_u64 v[148:149], s[2:3], 0, v[148:149]
	v_cvt_pk_bf16_f32 v144, v144, v145
	v_cvt_pk_bf16_f32 v145, v146, v147
	v_cvt_pk_bf16_f32 v146, v152, v153
	v_cvt_pk_bf16_f32 v147, v150, v151
	v_lshl_add_u64 v[148:149], v[148:149], 0, v[136:137]
	global_store_dwordx4 v[148:149], v[144:147], off sc1
; DI float shx(float v, int m, int lane) { return __int_as_float(__builtin_amdgcn_ds_bpermute((lane ^ m) << 2, __float_as_int(v))); }
; DI u32x4 pack8(const f32x4& a, const f32x4& b) { u32x4 w; w.x = pk2(a[0], a[1]); w.y = pk2(a[2], a[3]); w.z = pk2(b[0], b[1]); w.w = pk2(b[2], b[3]); return w; }
;     DI void operator()(const f32x4 (&acc)[2][2][4][2], const Unit& u, int wr, int wc, int fr, int fq) const {
;         const int c0 = u.pn * 256 + 32 * wc + 8 * fq; const int ln = fq * 16 + fr;
;         EPI_ROWS_BEGIN
;             const size_t row = (size_t)u.pm * 256 + rt;
; #pragma unroll
;             for (int bj = 0; bj < 2; ++bj) *(u32x4*)(k + row * AW + c0 + bj * 128) = pack8(acc[ai][bj][m][0] * sc, acc[ai][bj][m][1] * sc);
;         EPI_ROWS_END
; #pragma unroll
;         for (int bj = 0; bj < 2; ++bj)
; #pragma unroll
;             for (int n = 0; n < 2; ++n) { f32x4 s = (f32x4){0.f, 0.f, 0.f, 0.f};
; #pragma unroll
;                 for (int ai = 0; ai < 2; ++ai)
; #pragma unroll
;                     for (int m = 0; m < 4; ++m) s += acc[ai][bj][m][n];
; #pragma unroll
;                 for (int j = 0; j < 4; ++j) { float x = s[j]; x += shx(x, 1, ln); x += shx(x, 2, ln); x += shx(x, 4, ln); x += shx(x, 8, ln); s[j] = x; }
;                 if (fr == 0) { float* dst = kmean + (size_t)u.pm * AW + c0 + bj * 128 + 4 * n;
; #pragma unroll
;                     for (int j = 0; j < 4; ++j) unsafeAtomicAdd(dst + j, s[j] * sc); }
;                 asm volatile("" ::: "memory"); }
;     }
	v_pk_mul_f32 v[150:151], v[44:45], s[52:53] op_sel_hi:[1,0]
	v_pk_mul_f32 v[152:153], v[42:43], s[52:53] op_sel_hi:[1,0]
	v_pk_mul_f32 v[146:147], v[52:53], s[52:53] op_sel_hi:[1,0]
	v_pk_mul_f32 v[144:145], v[50:51], s[52:53] op_sel_hi:[1,0]
	s_nop 0
	v_cvt_pk_bf16_f32 v144, v144, v145
	v_cvt_pk_bf16_f32 v145, v146, v147
	v_cvt_pk_bf16_f32 v146, v152, v153
	v_cvt_pk_bf16_f32 v147, v150, v151
	global_store_dwordx4 v[148:149], v[144:147], off offset:256 sc1
	v_pk_mul_f32 v[150:151], v[48:49], s[52:53] op_sel_hi:[1,0]
	v_pk_mul_f32 v[152:153], v[46:47], s[52:53] op_sel_hi:[1,0]
	v_add_u32_e32 v144, 0x90, v130
	v_ashrrev_i32_e32 v145, 31, v144
	v_lshlrev_b64 v[148:149], 10, v[144:145]
	v_pk_mul_f32 v[146:147], v[56:57], s[52:53] op_sel_hi:[1,0]
	v_pk_mul_f32 v[144:145], v[54:55], s[52:53] op_sel_hi:[1,0]
	v_lshl_add_u64 v[148:149], s[2:3], 0, v[148:149]
	v_cvt_pk_bf16_f32 v144, v144, v145
	v_cvt_pk_bf16_f32 v145, v146, v147
	v_cvt_pk_bf16_f32 v146, v152, v153
	v_cvt_pk_bf16_f32 v147, v150, v151
	v_lshl_add_u64 v[148:149], v[148:149], 0, v[136:137]
	global_store_dwordx4 v[148:149], v[144:147], off sc1
	v_pk_mul_f32 v[150:151], v[28:29], s[52:53] op_sel_hi:[1,0]
	v_pk_mul_f32 v[152:153], v[26:27], s[52:53] op_sel_hi:[1,0]
	v_pk_mul_f32 v[146:147], v[36:37], s[52:53] op_sel_hi:[1,0]
	v_pk_mul_f32 v[144:145], v[34:35], s[52:53] op_sel_hi:[1,0]
	s_nop 0
	v_cvt_pk_bf16_f32 v144, v144, v145
	v_cvt_pk_bf16_f32 v145, v146, v147
	v_cvt_pk_bf16_f32 v146, v152, v153
	v_cvt_pk_bf16_f32 v147, v150, v151
	global_store_dwordx4 v[148:149], v[144:147], off offset:256 sc1
	v_pk_mul_f32 v[150:151], v[32:33], s[52:53] op_sel_hi:[1,0]
	v_pk_mul_f32 v[152:153], v[30:31], s[52:53] op_sel_hi:[1,0]
	v_add_u32_e32 v144, 0xa0, v130
	v_ashrrev_i32_e32 v145, 31, v144
	v_lshlrev_b64 v[148:149], 10, v[144:145]
	v_pk_mul_f32 v[146:147], v[40:41], s[52:53] op_sel_hi:[1,0]
	v_pk_mul_f32 v[144:145], v[38:39], s[52:53] op_sel_hi:[1,0]
	v_lshl_add_u64 v[148:149], s[2:3], 0, v[148:149]
	v_cvt_pk_bf16_f32 v144, v144, v145
	v_cvt_pk_bf16_f32 v145, v146, v147
	v_cvt_pk_bf16_f32 v146, v152, v153
	v_cvt_pk_bf16_f32 v147, v150, v151
	v_lshl_add_u64 v[148:149], v[148:149], 0, v[136:137]
	global_store_dwordx4 v[148:149], v[144:147], off sc1
	v_pk_mul_f32 v[150:151], v[12:13], s[52:53] op_sel_hi:[1,0]
	v_pk_mul_f32 v[152:153], v[10:11], s[52:53] op_sel_hi:[1,0]
	v_pk_mul_f32 v[146:147], v[20:21], s[52:53] op_sel_hi:[1,0]
	v_pk_mul_f32 v[144:145], v[18:19], s[52:53] op_sel_hi:[1,0]
	s_nop 0
	v_cvt_pk_bf16_f32 v144, v144, v145
	v_cvt_pk_bf16_f32 v145, v146, v147
	v_cvt_pk_bf16_f32 v146, v152, v153
	v_cvt_pk_bf16_f32 v147, v150, v151
	global_store_dwordx4 v[148:149], v[144:147], off offset:256 sc1
	v_pk_mul_f32 v[150:151], v[16:17], s[52:53] op_sel_hi:[1,0]
	v_pk_mul_f32 v[152:153], v[14:15], s[52:53] op_sel_hi:[1,0]
	v_add_u32_e32 v144, 0xb0, v130
	v_ashrrev_i32_e32 v145, 31, v144
	v_lshlrev_b64 v[148:149], 10, v[144:145]
	v_pk_mul_f32 v[146:147], v[24:25], s[52:53] op_sel_hi:[1,0]
	v_pk_mul_f32 v[144:145], v[22:23], s[52:53] op_sel_hi:[1,0]
	v_lshl_add_u64 v[148:149], s[2:3], 0, v[148:149]
	v_cvt_pk_bf16_f32 v144, v144, v145
	v_cvt_pk_bf16_f32 v145, v146, v147
	v_cvt_pk_bf16_f32 v146, v152, v153
	v_cvt_pk_bf16_f32 v147, v150, v151
	v_lshl_add_u64 v[136:137], v[148:149], 0, v[136:137]
	global_store_dwordx4 v[136:137], v[144:147], off sc1
	v_pk_mul_f32 v[148:149], v[4:5], s[52:53] op_sel_hi:[1,0]
	v_pk_mul_f32 v[150:151], v[2:3], s[52:53] op_sel_hi:[1,0]
	v_pk_mul_f32 v[146:147], v[8:9], s[52:53] op_sel_hi:[1,0]
	v_pk_mul_f32 v[144:145], v[6:7], s[52:53] op_sel_hi:[1,0]
	s_lshl_b64 s[2:3], s[18:19], 11
	v_cvt_pk_bf16_f32 v144, v144, v145
	v_cvt_pk_bf16_f32 v145, v146, v147
	v_cvt_pk_bf16_f32 v146, v150, v151
	v_cvt_pk_bf16_f32 v147, v148, v149
	global_store_dwordx4 v[136:137], v[144:147], off offset:256 sc1
	v_lshlrev_b32_e32 v137, 2, v142
	v_pk_add_f32 v[142:143], v[128:129], 0 op_sel_hi:[1,0]
	v_pk_add_f32 v[144:145], v[126:127], 0 op_sel_hi:[1,0]
	v_pk_add_f32 v[142:143], v[142:143], v[120:121]
	v_pk_add_f32 v[144:145], v[144:145], v[118:119]
	v_pk_add_f32 v[142:143], v[142:143], v[104:105]
	v_pk_add_f32 v[144:145], v[144:145], v[102:103]
	v_pk_add_f32 v[142:143], v[142:143], v[88:89]
	v_pk_add_f32 v[144:145], v[144:145], v[86:87]
	v_pk_add_f32 v[142:143], v[142:143], v[64:65]
	v_pk_add_f32 v[144:145], v[144:145], v[62:63]
	v_pk_add_f32 v[142:143], v[142:143], v[56:57]
	v_pk_add_f32 v[144:145], v[144:145], v[54:55]
	v_pk_add_f32 v[142:143], v[142:143], v[40:41]
	v_pk_add_f32 v[144:145], v[144:145], v[38:39]
	v_bitop3_b32 v136, v0, 4, v137 bitop3:0x36
	v_pk_add_f32 v[146:147], v[142:143], v[24:25]
	v_pk_add_f32 v[142:143], v[144:145], v[22:23]
	v_bitop3_b32 v133, v0, 8, v137 bitop3:0x36
	v_bitop3_b32 v131, v0, 16, v137 bitop3:0x36
	v_bitop3_b32 v0, v0, 32, v137 bitop3:0x36
	ds_bpermute_b32 v137, v136, v142
	ds_bpermute_b32 v144, v136, v143
	ds_bpermute_b32 v145, v136, v146
	ds_bpermute_b32 v148, v136, v147
	s_waitcnt lgkmcnt(0)
	v_add_f32_e32 v137, v142, v137
	v_add_f32_e32 v143, v143, v144
	v_add_f32_e32 v145, v146, v145
	v_add_f32_e32 v147, v147, v148
	ds_bpermute_b32 v142, v133, v137
	ds_bpermute_b32 v144, v133, v143
	ds_bpermute_b32 v146, v133, v145
	ds_bpermute_b32 v148, v133, v147
	s_waitcnt lgkmcnt(0)
	v_add_f32_e32 v137, v137, v142
	v_add_f32_e32 v143, v143, v144
	v_add_f32_e32 v145, v145, v146
	v_add_f32_e32 v147, v147, v148
	ds_bpermute_b32 v142, v131, v137
	ds_bpermute_b32 v144, v131, v143
	ds_bpermute_b32 v146, v131, v145
	ds_bpermute_b32 v148, v131, v147
	s_waitcnt lgkmcnt(0)
	v_add_f32_e32 v137, v137, v142
	v_add_f32_e32 v143, v143, v144
	v_add_f32_e32 v145, v145, v146
	v_add_f32_e32 v147, v147, v148
	ds_bpermute_b32 v142, v0, v137
	ds_bpermute_b32 v144, v0, v143
	ds_bpermute_b32 v146, v0, v145
	ds_bpermute_b32 v148, v0, v147
	s_and_saveexec_b64 s[28:29], vcc
	s_cbranch_execz .LBB0_261
	s_add_u32 s0, s95, s2
	s_waitcnt lgkmcnt(0)
	v_add_f32_e32 v137, v137, v142
	s_addc_u32 s1, s42, s3
	v_add_f32_e32 v144, v143, v144
	v_lshl_add_u64 v[142:143], v[134:135], 2, s[0:1]
	v_mul_f32_e32 v137, 0x3a800000, v137
	v_add_f32_e32 v145, v145, v146
	global_atomic_add_f32 v[142:143], v137, off
	v_mul_f32_e32 v137, 0x3a800000, v144
	v_add_f32_e32 v147, v147, v148
	global_atomic_add_f32 v[142:143], v137, off offset:4
	v_mul_f32_e32 v137, 0x3a800000, v145
	global_atomic_add_f32 v[142:143], v137, off offset:8
	v_mul_f32_e32 v137, 0x3a800000, v147
	global_atomic_add_f32 v[142:143], v137, off offset:12

; DI u32x4 pack8(const f32x4& a, const f32x4& b) { u32x4 w; w.x = pk2(a[0], a[1]); w.y = pk2(a[2], a[3]); w.z = pk2(b[0], b[1]); w.w = pk2(b[2], b[3]); return w; }
;     DI void operator()(const f32x4 (&acc)[2][2][4][2], const Unit& u, int wr, int wc, int fr, int fq) const {
;         EPI_ROWS_BEGIN
;             const size_t row = (size_t)u.pm * 256 + rt;
; #pragma unroll
;             for (int bj = 0; bj < 2; ++bj) *(u32x4*)(o + row * ldc + u.pn * 256 + bj * 128 + 32 * wc + 8 * fq) = pack8(acc[ai][bj][m][0] * sc, acc[ai][bj][m][1] * sc);
;         EPI_ROWS_END
;     }
;     DI void operator()(const f32x4 (&acc)[2][2][4][2], const Unit& u, int wr, int wc, int fr, int fq) const {
;         Unit u2 = u; u2.pn = u.pn & 1;
;         if (u.pn < 2) { EpiScaled E{q, AW, sc * (0.125f * LOG2E_C)}; E(acc, u2, wr, wc, fr, fq); }
;         else { EpiK E{k, kmean, sc}; E(acc, u2, wr, wc, fr, fq); }
.LBB0_268:
	s_and_b64 vcc, exec, s[2:3]
	s_cbranch_vccz .LBB0_270
	s_ashr_i32 s19, s18, 31
	s_lshl_b64 s[2:3], s[18:19], 8
	v_ashrrev_i32_e32 v131, 31, v130
	s_mov_b32 s0, 0x3938aa3b
	v_lshl_add_u64 v[134:135], s[2:3], 0, v[130:131]
	v_pk_mul_f32 v[126:127], v[126:127], s[0:1] op_sel_hi:[1,0]
	v_pk_mul_f32 v[122:123], v[122:123], s[0:1] op_sel_hi:[1,0]
	v_pk_mul_f32 v[136:137], v[124:125], s[0:1] op_sel_hi:[1,0]
	v_cvt_pk_bf16_f32 v124, v126, v127
	v_cvt_pk_bf16_f32 v126, v122, v123
	v_lshlrev_b64 v[122:123], 10, v[134:135]
	v_lshl_add_u64 v[122:123], s[10:11], 0, v[122:123]
	s_lshl_b32 s58, s30, 9
	s_waitcnt lgkmcnt(0)
	v_ashrrev_i32_e32 v133, 31, v132
	v_pk_mul_f32 v[128:129], v[128:129], s[0:1] op_sel_hi:[1,0]
	v_lshl_add_u64 v[122:123], v[122:123], 0, s[58:59]
	s_lshl_b32 s18, s21, 6
	s_mov_b32 s19, s59
	v_cvt_pk_bf16_f32 v125, v128, v129
	v_lshl_add_u64 v[128:129], v[122:123], 0, s[18:19]
	v_lshlrev_b64 v[122:123], 1, v[132:133]
	v_cvt_pk_bf16_f32 v127, v136, v137
	v_lshl_add_u64 v[128:129], v[128:129], 0, v[122:123]
	global_store_dwordx4 v[128:129], v[124:127], off sc1
	v_pk_mul_f32 v[116:117], v[116:117], s[0:1] op_sel_hi:[1,0]
	v_pk_mul_f32 v[114:115], v[114:115], s[0:1] op_sel_hi:[1,0]
	v_pk_mul_f32 v[124:125], v[108:109], s[0:1] op_sel_hi:[1,0]
	v_pk_mul_f32 v[108:109], v[106:107], s[0:1] op_sel_hi:[1,0]
	v_cvt_pk_bf16_f32 v106, v114, v115
	v_cvt_pk_bf16_f32 v107, v116, v117
	v_cvt_pk_bf16_f32 v108, v108, v109
	v_cvt_pk_bf16_f32 v109, v124, v125
	global_store_dwordx4 v[128:129], v[106:109], off offset:256 sc1
	v_pk_mul_f32 v[110:111], v[110:111], s[0:1] op_sel_hi:[1,0]
	v_pk_mul_f32 v[112:113], v[112:113], s[0:1] op_sel_hi:[1,0]
	v_or_b32_e32 v106, 16, v130
	v_ashrrev_i32_e32 v107, 31, v106
	v_lshl_add_u64 v[114:115], s[2:3], 0, v[106:107]
	v_pk_mul_f32 v[108:109], v[120:121], s[0:1] op_sel_hi:[1,0]
	v_pk_mul_f32 v[106:107], v[118:119], s[0:1] op_sel_hi:[1,0]
	v_pk_mul_f32 v[100:101], v[100:101], s[0:1] op_sel_hi:[1,0]
	v_cvt_pk_bf16_f32 v106, v106, v107
	v_cvt_pk_bf16_f32 v107, v108, v109
	v_cvt_pk_bf16_f32 v108, v110, v111
	v_lshlrev_b64 v[110:111], 10, v[114:115]
	v_lshl_add_u64 v[110:111], s[10:11], 0, v[110:111]
	v_lshl_add_u64 v[110:111], v[110:111], 0, s[58:59]
	v_lshl_add_u64 v[110:111], v[110:111], 0, s[18:19]
	v_cvt_pk_bf16_f32 v109, v112, v113
	v_lshl_add_u64 v[110:111], v[110:111], 0, v[122:123]
	global_store_dwordx4 v[110:111], v[106:109], off sc1
	v_pk_mul_f32 v[98:99], v[98:99], s[0:1] op_sel_hi:[1,0]
	v_pk_mul_f32 v[94:95], v[94:95], s[0:1] op_sel_hi:[1,0]
	v_pk_mul_f32 v[106:107], v[92:93], s[0:1] op_sel_hi:[1,0]
	v_pk_mul_f32 v[92:93], v[90:91], s[0:1] op_sel_hi:[1,0]
	v_cvt_pk_bf16_f32 v90, v98, v99
	v_cvt_pk_bf16_f32 v91, v100, v101
	v_cvt_pk_bf16_f32 v92, v92, v93
	v_cvt_pk_bf16_f32 v93, v106, v107
	global_store_dwordx4 v[110:111], v[90:93], off offset:256 sc1
	v_pk_mul_f32 v[96:97], v[96:97], s[0:1] op_sel_hi:[1,0]
	v_pk_mul_f32 v[84:85], v[84:85], s[0:1] op_sel_hi:[1,0]
	v_or_b32_e32 v90, 32, v130
	v_ashrrev_i32_e32 v91, 31, v90
	v_lshl_add_u64 v[98:99], s[2:3], 0, v[90:91]
	v_pk_mul_f32 v[92:93], v[104:105], s[0:1] op_sel_hi:[1,0]
	v_pk_mul_f32 v[90:91], v[102:103], s[0:1] op_sel_hi:[1,0]
	v_pk_mul_f32 v[82:83], v[82:83], s[0:1] op_sel_hi:[1,0]
	v_cvt_pk_bf16_f32 v90, v90, v91
	v_cvt_pk_bf16_f32 v91, v92, v93
	v_cvt_pk_bf16_f32 v92, v94, v95
	v_lshlrev_b64 v[94:95], 10, v[98:99]
	v_lshl_add_u64 v[94:95], s[10:11], 0, v[94:95]
	v_lshl_add_u64 v[94:95], v[94:95], 0, s[58:59]
	v_lshl_add_u64 v[94:95], v[94:95], 0, s[18:19]
	v_cvt_pk_bf16_f32 v93, v96, v97
	v_lshl_add_u64 v[94:95], v[94:95], 0, v[122:123]
	global_store_dwordx4 v[94:95], v[90:93], off sc1
	v_pk_mul_f32 v[78:79], v[78:79], s[0:1] op_sel_hi:[1,0]
	v_pk_mul_f32 v[80:81], v[80:81], s[0:1] op_sel_hi:[1,0]
	v_pk_mul_f32 v[90:91], v[76:77], s[0:1] op_sel_hi:[1,0]
	v_pk_mul_f32 v[76:77], v[74:75], s[0:1] op_sel_hi:[1,0]
	v_cvt_pk_bf16_f32 v74, v82, v83
	v_cvt_pk_bf16_f32 v75, v84, v85
	v_cvt_pk_bf16_f32 v76, v76, v77
	v_cvt_pk_bf16_f32 v77, v90, v91
	global_store_dwordx4 v[94:95], v[74:77], off offset:256 sc1
	v_pk_mul_f32 v[72:73], v[72:73], s[0:1] op_sel_hi:[1,0]
	v_pk_mul_f32 v[70:71], v[70:71], s[0:1] op_sel_hi:[1,0]
	v_or_b32_e32 v74, 48, v130
	v_ashrrev_i32_e32 v75, 31, v74
	v_lshl_add_u64 v[82:83], s[2:3], 0, v[74:75]
	v_pk_mul_f32 v[76:77], v[88:89], s[0:1] op_sel_hi:[1,0]
	v_pk_mul_f32 v[74:75], v[86:87], s[0:1] op_sel_hi:[1,0]
	v_pk_mul_f32 v[62:63], v[62:63], s[0:1] op_sel_hi:[1,0]
	v_cvt_pk_bf16_f32 v74, v74, v75
	v_cvt_pk_bf16_f32 v75, v76, v77
	v_cvt_pk_bf16_f32 v76, v78, v79
	v_lshlrev_b64 v[78:79], 10, v[82:83]
	v_lshl_add_u64 v[78:79], s[10:11], 0, v[78:79]
	v_lshl_add_u64 v[78:79], v[78:79], 0, s[58:59]
	v_lshl_add_u64 v[78:79], v[78:79], 0, s[18:19]
	v_cvt_pk_bf16_f32 v77, v80, v81
	v_lshl_add_u64 v[78:79], v[78:79], 0, v[122:123]
	global_store_dwordx4 v[78:79], v[74:77], off sc1
	v_pk_mul_f32 v[64:65], v[64:65], s[0:1] op_sel_hi:[1,0]
; DI u32x4 pack8(const f32x4& a, const f32x4& b) { u32x4 w; w.x = pk2(a[0], a[1]); w.y = pk2(a[2], a[3]); w.z = pk2(b[0], b[1]); w.w = pk2(b[2], b[3]); return w; }
;     DI void operator()(const f32x4 (&acc)[2][2][4][2], const Unit& u, int wr, int wc, int fr, int fq) const {
;         EPI_ROWS_BEGIN
;             const size_t row = (size_t)u.pm * 256 + rt;
; #pragma unroll
;             for (int bj = 0; bj < 2; ++bj) *(u32x4*)(o + row * ldc + u.pn * 256 + bj * 128 + 32 * wc + 8 * fq) = pack8(acc[ai][bj][m][0] * sc, acc[ai][bj][m][1] * sc);
;         EPI_ROWS_END
;     }
	v_pk_mul_f32 v[52:53], v[52:53], s[0:1] op_sel_hi:[1,0]
	v_pk_mul_f32 v[74:75], v[68:69], s[0:1] op_sel_hi:[1,0]
	v_pk_mul_f32 v[68:69], v[66:67], s[0:1] op_sel_hi:[1,0]
	v_cvt_pk_bf16_f32 v66, v70, v71
	v_cvt_pk_bf16_f32 v67, v72, v73
	v_cvt_pk_bf16_f32 v68, v68, v69
	v_cvt_pk_bf16_f32 v69, v74, v75
	global_store_dwordx4 v[78:79], v[66:69], off offset:256 sc1
	v_pk_mul_f32 v[50:51], v[50:51], s[0:1] op_sel_hi:[1,0]
	v_pk_mul_f32 v[46:47], v[46:47], s[0:1] op_sel_hi:[1,0]
	v_add_u32_e32 v66, 0x80, v130
	v_ashrrev_i32_e32 v67, 31, v66
	v_lshl_add_u64 v[66:67], s[2:3], 0, v[66:67]
	v_pk_mul_f32 v[68:69], v[60:61], s[0:1] op_sel_hi:[1,0]
	v_pk_mul_f32 v[60:61], v[58:59], s[0:1] op_sel_hi:[1,0]
	v_cvt_pk_bf16_f32 v58, v62, v63
	v_lshlrev_b64 v[62:63], 10, v[66:67]
	v_lshl_add_u64 v[62:63], s[10:11], 0, v[62:63]
	v_lshl_add_u64 v[62:63], v[62:63], 0, s[58:59]
	v_lshl_add_u64 v[62:63], v[62:63], 0, s[18:19]
	v_cvt_pk_bf16_f32 v59, v64, v65
	v_cvt_pk_bf16_f32 v60, v60, v61
	v_cvt_pk_bf16_f32 v61, v68, v69
	v_lshl_add_u64 v[62:63], v[62:63], 0, v[122:123]
	global_store_dwordx4 v[62:63], v[58:61], off sc1
	v_pk_mul_f32 v[48:49], v[48:49], s[0:1] op_sel_hi:[1,0]
	v_pk_mul_f32 v[36:37], v[36:37], s[0:1] op_sel_hi:[1,0]
	v_pk_mul_f32 v[58:59], v[44:45], s[0:1] op_sel_hi:[1,0]
	v_pk_mul_f32 v[44:45], v[42:43], s[0:1] op_sel_hi:[1,0]
	v_cvt_pk_bf16_f32 v42, v50, v51
	v_cvt_pk_bf16_f32 v43, v52, v53
	v_cvt_pk_bf16_f32 v44, v44, v45
	v_cvt_pk_bf16_f32 v45, v58, v59
	global_store_dwordx4 v[62:63], v[42:45], off offset:256 sc1
	v_pk_mul_f32 v[34:35], v[34:35], s[0:1] op_sel_hi:[1,0]
	v_pk_mul_f32 v[30:31], v[30:31], s[0:1] op_sel_hi:[1,0]
	v_add_u32_e32 v42, 0x90, v130
	v_ashrrev_i32_e32 v43, 31, v42
	v_lshl_add_u64 v[50:51], s[2:3], 0, v[42:43]
	v_pk_mul_f32 v[44:45], v[56:57], s[0:1] op_sel_hi:[1,0]
	v_pk_mul_f32 v[42:43], v[54:55], s[0:1] op_sel_hi:[1,0]
	v_pk_mul_f32 v[32:33], v[32:33], s[0:1] op_sel_hi:[1,0]
	v_cvt_pk_bf16_f32 v42, v42, v43
	v_cvt_pk_bf16_f32 v43, v44, v45
	v_cvt_pk_bf16_f32 v44, v46, v47
	v_lshlrev_b64 v[46:47], 10, v[50:51]
	v_lshl_add_u64 v[46:47], s[10:11], 0, v[46:47]
	v_lshl_add_u64 v[46:47], v[46:47], 0, s[58:59]
	v_lshl_add_u64 v[46:47], v[46:47], 0, s[18:19]
	v_cvt_pk_bf16_f32 v45, v48, v49
	v_lshl_add_u64 v[46:47], v[46:47], 0, v[122:123]
	global_store_dwordx4 v[46:47], v[42:45], off sc1
	v_pk_mul_f32 v[20:21], v[20:21], s[0:1] op_sel_hi:[1,0]
	v_pk_mul_f32 v[18:19], v[18:19], s[0:1] op_sel_hi:[1,0]
	v_pk_mul_f32 v[42:43], v[28:29], s[0:1] op_sel_hi:[1,0]
	v_pk_mul_f32 v[28:29], v[26:27], s[0:1] op_sel_hi:[1,0]
	v_cvt_pk_bf16_f32 v26, v34, v35
	v_cvt_pk_bf16_f32 v27, v36, v37
	v_cvt_pk_bf16_f32 v28, v28, v29
	v_cvt_pk_bf16_f32 v29, v42, v43
	global_store_dwordx4 v[46:47], v[26:29], off offset:256 sc1
	v_pk_mul_f32 v[14:15], v[14:15], s[0:1] op_sel_hi:[1,0]
	v_pk_mul_f32 v[16:17], v[16:17], s[0:1] op_sel_hi:[1,0]
	v_add_u32_e32 v26, 0xa0, v130
	v_ashrrev_i32_e32 v27, 31, v26
	v_lshl_add_u64 v[34:35], s[2:3], 0, v[26:27]
	v_pk_mul_f32 v[28:29], v[40:41], s[0:1] op_sel_hi:[1,0]
	v_pk_mul_f32 v[26:27], v[38:39], s[0:1] op_sel_hi:[1,0]
	v_pk_mul_f32 v[8:9], v[8:9], s[0:1] op_sel_hi:[1,0]
	v_cvt_pk_bf16_f32 v26, v26, v27
	v_cvt_pk_bf16_f32 v27, v28, v29
	v_cvt_pk_bf16_f32 v28, v30, v31
	v_lshlrev_b64 v[30:31], 10, v[34:35]
	v_lshl_add_u64 v[30:31], s[10:11], 0, v[30:31]
	v_lshl_add_u64 v[30:31], v[30:31], 0, s[58:59]
	v_lshl_add_u64 v[30:31], v[30:31], 0, s[18:19]
	v_cvt_pk_bf16_f32 v29, v32, v33
	v_lshl_add_u64 v[30:31], v[30:31], 0, v[122:123]
	global_store_dwordx4 v[30:31], v[26:29], off sc1
	v_pk_mul_f32 v[6:7], v[6:7], s[0:1] op_sel_hi:[1,0]
	s_nop 0
	v_pk_mul_f32 v[26:27], v[12:13], s[0:1] op_sel_hi:[1,0]
	v_pk_mul_f32 v[12:13], v[10:11], s[0:1] op_sel_hi:[1,0]
	v_cvt_pk_bf16_f32 v10, v18, v19
	v_cvt_pk_bf16_f32 v11, v20, v21
	v_cvt_pk_bf16_f32 v12, v12, v13
	v_cvt_pk_bf16_f32 v13, v26, v27
	global_store_dwordx4 v[30:31], v[10:13], off offset:256 sc1
	s_nop 1
	v_add_u32_e32 v10, 0xb0, v130
	v_ashrrev_i32_e32 v11, 31, v10
	v_lshl_add_u64 v[18:19], s[2:3], 0, v[10:11]
	v_pk_mul_f32 v[12:13], v[24:25], s[0:1] op_sel_hi:[1,0]
	v_pk_mul_f32 v[10:11], v[22:23], s[0:1] op_sel_hi:[1,0]
	s_nop 0
	v_cvt_pk_bf16_f32 v10, v10, v11
	v_cvt_pk_bf16_f32 v11, v12, v13
	v_cvt_pk_bf16_f32 v12, v14, v15
	v_lshlrev_b64 v[14:15], 10, v[18:19]
	v_lshl_add_u64 v[14:15], s[10:11], 0, v[14:15]
	v_lshl_add_u64 v[14:15], v[14:15], 0, s[58:59]
	v_lshl_add_u64 v[14:15], v[14:15], 0, s[18:19]
	v_cvt_pk_bf16_f32 v13, v16, v17
	v_lshl_add_u64 v[14:15], v[14:15], 0, v[122:123]
	global_store_dwordx4 v[14:15], v[10:13], off sc1
	s_nop 1
	v_pk_mul_f32 v[10:11], v[4:5], s[0:1] op_sel_hi:[1,0]
	v_pk_mul_f32 v[4:5], v[2:3], s[0:1] op_sel_hi:[1,0]
	v_cvt_pk_bf16_f32 v2, v6, v7
	v_cvt_pk_bf16_f32 v3, v8, v9
	v_cvt_pk_bf16_f32 v4, v4, v5
	v_cvt_pk_bf16_f32 v5, v10, v11
	global_store_dwordx4 v[14:15], v[2:5], off offset:256 sc1

;     DI void operator()(const f32x4 (&acc)[2][2][4][2], const Unit& u, int wr, int wc, int fr, int fq) const {
;         EPI_ROWS_BEGIN
;             if (u.half == 2 - ai) continue;
;             float* rowp = e + ((size_t)u.e * CROWS + u.pm * 256 + rt) * 128 + 32 * wc + 4 * fq;
; #pragma unroll
;             for (int n = 0; n < 2; ++n) *(f32x4*)(rowp + 16 * n) = acc[ai][0][m][n];
;         EPI_ROWS_END
;     }
.LBB0_339:
	s_mov_b32 s6, -1
	s_mov_b32 s7, s34
	s_ashr_i32 s11, s10, 31
	v_mbcnt_lo_u32_b32 v0, s6, 0
	v_mbcnt_hi_u32_b32 v0, s6, v0
	s_lshl_b32 s6, s7, 4
	s_andn2_b32 s6, s6, 63
	v_and_or_b32 v2, v0, 15, s6
	v_ashrrev_i32_e32 v0, 2, v0
	s_lshl_b32 s6, s7, 5
	v_and_b32_e32 v68, -4, v0
	s_lshl_b32 s1, s1, 8
	s_and_b32 s15, s6, 0x60
	v_ashrrev_i32_e32 v69, 31, v68
	s_lshl_b64 s[10:11], s[10:11], 10
	s_ashr_i32 s26, s1, 31
	s_and_b64 vcc, exec, s[24:25]
	s_cbranch_vccz .LBB0_341
	s_add_u32 s6, s10, s1
	v_ashrrev_i32_e32 v3, 31, v2
	s_addc_u32 s7, s11, s26
	v_lshl_add_u64 v[70:71], s[6:7], 0, v[2:3]
	v_lshlrev_b64 v[70:71], 9, v[70:71]
	v_lshl_add_u64 v[70:71], s[8:9], 0, v[70:71]
	s_lshl_b32 s58, s15, 2
	v_lshl_add_u64 v[70:71], v[70:71], 0, s[58:59]
	v_lshlrev_b64 v[72:73], 2, v[68:69]
	v_lshl_add_u64 v[70:71], v[70:71], 0, v[72:73]
	global_store_dwordx4 v[70:71], v[64:67], off sc1
	global_store_dwordx4 v[70:71], v[60:63], off offset:64 sc1
	s_nop 1
	v_or_b32_e32 v60, 16, v2
	v_ashrrev_i32_e32 v61, 31, v60
	v_lshl_add_u64 v[60:61], s[6:7], 0, v[60:61]
	v_lshlrev_b64 v[60:61], 9, v[60:61]
	v_lshl_add_u64 v[60:61], s[8:9], 0, v[60:61]
	v_lshl_add_u64 v[60:61], v[60:61], 0, s[58:59]
	v_lshl_add_u64 v[60:61], v[60:61], 0, v[72:73]
	global_store_dwordx4 v[60:61], v[56:59], off sc1
	global_store_dwordx4 v[60:61], v[52:55], off offset:64 sc1
	s_nop 1
	v_or_b32_e32 v52, 32, v2
	v_ashrrev_i32_e32 v53, 31, v52
	v_lshl_add_u64 v[52:53], s[6:7], 0, v[52:53]
	v_lshlrev_b64 v[52:53], 9, v[52:53]
	v_lshl_add_u64 v[52:53], s[8:9], 0, v[52:53]
	v_lshl_add_u64 v[52:53], v[52:53], 0, s[58:59]
	v_lshl_add_u64 v[52:53], v[52:53], 0, v[72:73]
	global_store_dwordx4 v[52:53], v[48:51], off sc1
	global_store_dwordx4 v[52:53], v[44:47], off offset:64 sc1
	s_nop 1
	v_or_b32_e32 v44, 48, v2
	v_ashrrev_i32_e32 v45, 31, v44
	v_lshl_add_u64 v[44:45], s[6:7], 0, v[44:45]
	v_lshlrev_b64 v[44:45], 9, v[44:45]
	v_lshl_add_u64 v[44:45], s[8:9], 0, v[44:45]
	v_lshl_add_u64 v[44:45], v[44:45], 0, s[58:59]
	v_lshl_add_u64 v[44:45], v[44:45], 0, v[72:73]
	global_store_dwordx4 v[44:45], v[40:43], off sc1
	global_store_dwordx4 v[44:45], v[36:39], off offset:64 sc1
	s_cbranch_execz .LBB0_342
	s_branch .LBB0_343

;     DI void operator()(const f32x4 (&acc)[2][2][4][2], const Unit& u, int wr, int wc, int fr, int fq) const {
;         EPI_ROWS_BEGIN
;             if (u.half == 2 - ai) continue;
;             float* rowp = e + ((size_t)u.e * CROWS + u.pm * 256 + rt) * 128 + 32 * wc + 4 * fq;
; #pragma unroll
;             for (int n = 0; n < 2; ++n) *(f32x4*)(rowp + 16 * n) = acc[ai][0][m][n];
;         EPI_ROWS_END
;     }
.LBB0_343:
	s_andn2_b64 vcc, exec, s[22:23]
	s_cbranch_vccnz .LBB0_346
	v_add_u32_e32 v36, 0x80, v2
	v_ashrrev_i32_e32 v37, 31, v36
	v_lshl_add_u64 v[36:37], s[6:7], 0, v[36:37]
	v_lshlrev_b64 v[36:37], 9, v[36:37]
	v_lshl_add_u64 v[36:37], s[8:9], 0, v[36:37]
	s_lshl_b32 s58, s15, 2
	v_lshl_add_u64 v[36:37], v[36:37], 0, s[58:59]
	v_lshl_add_u64 v[36:37], v[68:69], 2, v[36:37]
	s_and_b64 vcc, exec, s[4:5]
	global_store_dwordx4 v[36:37], v[32:35], off sc1
	global_store_dwordx4 v[36:37], v[28:31], off offset:64 sc1
	s_cbranch_vccnz .LBB0_346
	s_nop 0
	v_add_u32_e32 v28, 0x90, v2
	v_ashrrev_i32_e32 v29, 31, v28
	v_lshl_add_u64 v[28:29], s[6:7], 0, v[28:29]
	v_lshlrev_b64 v[28:29], 9, v[28:29]
	v_lshl_add_u64 v[28:29], s[8:9], 0, v[28:29]
	v_lshl_add_u64 v[28:29], v[28:29], 0, s[58:59]
	v_lshlrev_b64 v[30:31], 2, v[68:69]
	v_lshl_add_u64 v[28:29], v[28:29], 0, v[30:31]
	global_store_dwordx4 v[28:29], v[24:27], off sc1
	global_store_dwordx4 v[28:29], v[20:23], off offset:64 sc1
	s_nop 1
	v_add_u32_e32 v20, 0xa0, v2
	v_add_u32_e32 v2, 0xb0, v2
	v_ashrrev_i32_e32 v21, 31, v20
	v_ashrrev_i32_e32 v3, 31, v2
	v_lshl_add_u64 v[20:21], s[6:7], 0, v[20:21]
	v_lshl_add_u64 v[2:3], s[6:7], 0, v[2:3]
	v_lshlrev_b64 v[20:21], 9, v[20:21]
	v_lshlrev_b64 v[2:3], 9, v[2:3]
	v_lshl_add_u64 v[20:21], s[8:9], 0, v[20:21]
	v_lshl_add_u64 v[2:3], s[8:9], 0, v[2:3]
	v_lshl_add_u64 v[20:21], v[20:21], 0, s[58:59]
	v_lshl_add_u64 v[2:3], v[2:3], 0, s[58:59]
	v_lshl_add_u64 v[20:21], v[20:21], 0, v[30:31]
	v_lshl_add_u64 v[2:3], v[2:3], 0, v[30:31]
	global_store_dwordx4 v[20:21], v[16:19], off sc1
	global_store_dwordx4 v[20:21], v[12:15], off offset:64 sc1
	global_store_dwordx4 v[2:3], v[8:11], off sc1
	global_store_dwordx4 v[2:3], v[4:7], off offset:64 sc1

; DI float gelu_tanh(float x) { const float u = 0.7978845608028654f * (x + 0.044715f * x * x * x); return x * __builtin_amdgcn_rcpf(1.0f + __builtin_amdgcn_exp2f(-2.8853900817779268f * u)); }
; DI u32x4 pack8(const f32x4& a, const f32x4& b) { u32x4 w; w.x = pk2(a[0], a[1]); w.y = pk2(a[2], a[3]); w.z = pk2(b[0], b[1]); w.w = pk2(b[2], b[3]); return w; }
;     DI void operator()(const f32x4 (&acc)[2][2][4][2], const Unit& u, int wr, int wc, int fr, int fq) const {
;         EPI_ROWS_BEGIN
;             const int R = u.pm * 256 + rt;
; #pragma unroll
;             for (int bj = 0; bj < 2; ++bj) { const int col = u.pn * 256 + bj * 128 + 32 * wc + 8 * fq; const int j = col >> 4, c0 = col & 15;
;                 f32x4 a = acc[ai][bj][m][0], b = acc[ai][bj][m][1];
; #pragma unroll
;                 for (int q = 0; q < 4; ++q) { a[q] = gelu_tanh(a[q]); b[q] = gelu_tanh(b[q]); }
;                 *(u32x4*)(y + ((size_t)R * 32 + j) * SW + u.e * 16 + c0) = pack8(a, b); }
;         EPI_ROWS_END
;     }
.LBB0_772:
	v_mul_f32_e32 v139, 0x3d372713, v122
	v_mul_f32_e32 v139, v122, v139
	v_fma_f32 v139, v122, v139, v122
	s_mov_b32 s0, s20
	s_mov_b32 s1, -1
	v_mul_f32_e32 v139, 0x3f4c422a, v139
	v_mul_f32_e32 v139, 0xc038aa3b, v139
	v_mbcnt_lo_u32_b32 v0, s1, 0
	v_mbcnt_hi_u32_b32 v0, s1, v0
	s_lshl_b32 s1, s0, 4
	v_exp_f32_e32 v139, v139
	s_andn2_b32 s1, s1, 63
	s_lshl_b32 s0, s0, 5
	v_and_or_b32 v130, v0, 15, s1
	s_and_b32 s0, s0, 0x60
	v_ashrrev_i32_e32 v131, 1, v0
	v_lshl_add_u32 v130, s41, 8, v130
	s_lshl_b32 s1, s38, 8
	v_and_b32_e32 v138, -8, v131
	v_ashrrev_i32_e32 v131, 31, v130
	s_or_b32 s0, s0, s1
	v_add_f32_e32 v139, 1.0, v139
	v_lshlrev_b64 v[136:137], 15, v[130:131]
	v_add_u32_e32 v131, s0, v138
	v_mul_f32_e32 v138, 0x3d372713, v126
	v_rcp_f32_e32 v140, v139
	v_mul_f32_e32 v139, 0x3d372713, v127
	v_mul_f32_e32 v138, v126, v138
	v_mul_f32_e32 v139, v127, v139
	v_fma_f32 v138, v126, v138, v126
	v_fma_f32 v139, v127, v139, v127
	v_mul_f32_e32 v138, 0x3f4c422a, v138
	v_mul_f32_e32 v139, 0x3f4c422a, v139
	v_mul_f32_e32 v138, 0xc038aa3b, v138
	v_mul_f32_e32 v139, 0xc038aa3b, v139
	v_exp_f32_e32 v138, v138
	v_exp_f32_e32 v139, v139
	s_lshl_b32 s0, s33, 4
	s_ashr_i32 s1, s0, 31
	v_add_f32_e32 v138, 1.0, v138
	v_add_f32_e32 v139, 1.0, v139
	v_rcp_f32_e32 v138, v138
	v_rcp_f32_e32 v139, v139
	s_lshl_b64 s[16:17], s[0:1], 1
	v_and_b32_e32 v0, 16, v0
	s_mov_b64 s[2:3], -1
	v_pk_mul_f32 v[126:127], v[126:127], v[138:139]
	v_mul_f32_e32 v138, 0x3d372713, v123
	v_mul_f32_e32 v138, v123, v138
	v_fma_f32 v138, v123, v138, v123
	v_mul_f32_e32 v138, 0x3f4c422a, v138
	v_mul_f32_e32 v138, 0xc038aa3b, v138
	v_mul_f32_e32 v139, 0x3d372713, v124
	v_exp_f32_e32 v138, v138
	v_mul_f32_e32 v139, v124, v139
	v_fma_f32 v139, v124, v139, v124
	v_mul_f32_e32 v139, 0x3f4c422a, v139
	v_mul_f32_e32 v139, 0xc038aa3b, v139
	v_add_f32_e32 v138, 1.0, v138
	v_exp_f32_e32 v139, v139
	v_rcp_f32_e32 v141, v138
	v_mul_f32_e32 v138, 0x3d372713, v128
	v_mul_f32_e32 v138, v128, v138
	v_add_f32_e32 v139, 1.0, v139
	v_pk_mul_f32 v[122:123], v[122:123], v[140:141]
	v_rcp_f32_e32 v140, v139
	v_mul_f32_e32 v139, 0x3d372713, v129
	v_mul_f32_e32 v139, v129, v139
	v_fma_f32 v138, v128, v138, v128
	v_fma_f32 v139, v129, v139, v129
	v_mul_f32_e32 v138, 0x3f4c422a, v138
	v_mul_f32_e32 v139, 0x3f4c422a, v139
	v_mul_f32_e32 v138, 0xc038aa3b, v138
	v_mul_f32_e32 v139, 0xc038aa3b, v139
	v_exp_f32_e32 v138, v138
	v_exp_f32_e32 v139, v139
	s_andn2_b64 vcc, exec, s[14:15]
	v_add_f32_e32 v138, 1.0, v138
	v_add_f32_e32 v139, 1.0, v139
	v_rcp_f32_e32 v138, v138
	v_rcp_f32_e32 v139, v139
	s_nop 0
	v_pk_mul_f32 v[128:129], v[128:129], v[138:139]
	v_mul_f32_e32 v138, 0x3d372713, v125
	v_mul_f32_e32 v138, v125, v138
	v_fma_f32 v138, v125, v138, v125
	v_mul_f32_e32 v138, 0x3f4c422a, v138
	v_mul_f32_e32 v138, 0xc038aa3b, v138
	v_exp_f32_e32 v138, v138
	s_nop 0
	v_add_f32_e32 v138, 1.0, v138
	v_rcp_f32_e32 v141, v138
	s_nop 0
	v_pk_mul_f32 v[138:139], v[124:125], v[140:141]
	v_ashrrev_i32_e32 v140, 4, v131
	v_ashrrev_i32_e32 v141, 31, v140
	v_cvt_pk_bf16_f32 v124, v126, v127
	v_cvt_pk_bf16_f32 v125, v128, v129
	v_cvt_pk_bf16_f32 v126, v122, v123
	v_lshl_add_u64 v[128:129], s[6:7], 0, v[136:137]
	v_lshlrev_b64 v[122:123], 10, v[140:141]
	v_lshl_add_u64 v[136:137], v[128:129], 0, v[122:123]
	v_lshl_add_u64 v[136:137], v[136:137], 0, s[16:17]
	v_cvt_pk_bf16_f32 v127, v138, v139
	v_lshl_add_u64 v[136:137], v[136:137], 0, v[0:1]
	global_store_dwordx4 v[136:137], v[124:127], off sc1
	v_add_u32_e32 v131, 0x80, v131
	s_nop 0
	v_mul_f32_e32 v125, 0x3d372713, v114
	v_mul_f32_e32 v125, v114, v125
	v_fma_f32 v125, v114, v125, v114
	v_mul_f32_e32 v125, 0x3f4c422a, v125
	v_mul_f32_e32 v125, 0xc038aa3b, v125
	v_exp_f32_e32 v125, v125
	v_mul_f32_e32 v124, 0x3d372713, v118
	v_mul_f32_e32 v124, v118, v124
	v_fma_f32 v124, v118, v124, v118
	v_add_f32_e32 v125, 1.0, v125
	v_rcp_f32_e32 v126, v125
	v_mul_f32_e32 v125, 0x3d372713, v119
	v_mul_f32_e32 v125, v119, v125
	v_fma_f32 v125, v119, v125, v119
	v_mul_f32_e32 v124, 0x3f4c422a, v124
	v_mul_f32_e32 v125, 0x3f4c422a, v125
	v_mul_f32_e32 v124, 0xc038aa3b, v124
	v_mul_f32_e32 v125, 0xc038aa3b, v125
	v_exp_f32_e32 v124, v124
	v_exp_f32_e32 v125, v125
	v_add_f32_e32 v124, 1.0, v124
	v_add_f32_e32 v125, 1.0, v125
	v_rcp_f32_e32 v124, v124
	v_rcp_f32_e32 v125, v125
	s_nop 0
	v_pk_mul_f32 v[118:119], v[118:119], v[124:125]
	v_mul_f32_e32 v124, 0x3d372713, v115
	v_mul_f32_e32 v124, v115, v124
	v_fma_f32 v124, v115, v124, v115
	v_mul_f32_e32 v124, 0x3f4c422a, v124
	v_mul_f32_e32 v124, 0xc038aa3b, v124
	v_mul_f32_e32 v125, 0x3d372713, v116
	v_exp_f32_e32 v124, v124
	v_mul_f32_e32 v125, v116, v125
	v_fma_f32 v125, v116, v125, v116
	v_mul_f32_e32 v125, 0x3f4c422a, v125
	v_mul_f32_e32 v125, 0xc038aa3b, v125
	v_add_f32_e32 v124, 1.0, v124
	v_exp_f32_e32 v125, v125
	v_rcp_f32_e32 v127, v124
	v_mul_f32_e32 v124, 0x3d372713, v120
	v_mul_f32_e32 v124, v120, v124
	v_add_f32_e32 v125, 1.0, v125
	v_pk_mul_f32 v[114:115], v[114:115], v[126:127]
	v_rcp_f32_e32 v126, v125
	v_mul_f32_e32 v125, 0x3d372713, v121
	v_mul_f32_e32 v125, v121, v125
	v_fma_f32 v124, v120, v124, v120
	v_fma_f32 v125, v121, v125, v121
	v_mul_f32_e32 v124, 0x3f4c422a, v124
	v_mul_f32_e32 v125, 0x3f4c422a, v125
	v_mul_f32_e32 v124, 0xc038aa3b, v124
	v_mul_f32_e32 v125, 0xc038aa3b, v125
	v_exp_f32_e32 v124, v124
	v_exp_f32_e32 v125, v125
	v_add_f32_e32 v124, 1.0, v124
	v_add_f32_e32 v125, 1.0, v125
	v_rcp_f32_e32 v124, v124
	v_rcp_f32_e32 v125, v125
	s_nop 0
	v_pk_mul_f32 v[120:121], v[120:121], v[124:125]
	v_mul_f32_e32 v124, 0x3d372713, v117
	v_mul_f32_e32 v124, v117, v124
	v_fma_f32 v124, v117, v124, v117
; DI float gelu_tanh(float x) { const float u = 0.7978845608028654f * (x + 0.044715f * x * x * x); return x * __builtin_amdgcn_rcpf(1.0f + __builtin_amdgcn_exp2f(-2.8853900817779268f * u)); }
; DI u32x4 pack8(const f32x4& a, const f32x4& b) { u32x4 w; w.x = pk2(a[0], a[1]); w.y = pk2(a[2], a[3]); w.z = pk2(b[0], b[1]); w.w = pk2(b[2], b[3]); return w; }
;     DI void operator()(const f32x4 (&acc)[2][2][4][2], const Unit& u, int wr, int wc, int fr, int fq) const {
;         EPI_ROWS_BEGIN
;             const int R = u.pm * 256 + rt;
; #pragma unroll
;             for (int bj = 0; bj < 2; ++bj) { const int col = u.pn * 256 + bj * 128 + 32 * wc + 8 * fq; const int j = col >> 4, c0 = col & 15;
;                 f32x4 a = acc[ai][bj][m][0], b = acc[ai][bj][m][1];
; #pragma unroll
;                 for (int q = 0; q < 4; ++q) { a[q] = gelu_tanh(a[q]); b[q] = gelu_tanh(b[q]); }
;                 *(u32x4*)(y + ((size_t)R * 32 + j) * SW + u.e * 16 + c0) = pack8(a, b); }
;         EPI_ROWS_END
;     }
	v_mul_f32_e32 v124, 0x3f4c422a, v124
	v_mul_f32_e32 v124, 0xc038aa3b, v124
	v_exp_f32_e32 v124, v124
	s_nop 0
	v_add_f32_e32 v124, 1.0, v124
	v_rcp_f32_e32 v127, v124
	s_nop 0
	v_pk_mul_f32 v[124:125], v[116:117], v[126:127]
	v_ashrrev_i32_e32 v126, 4, v131
	v_ashrrev_i32_e32 v127, 31, v126
	v_cvt_pk_bf16_f32 v116, v118, v119
	v_cvt_pk_bf16_f32 v118, v114, v115
	v_lshlrev_b64 v[114:115], 10, v[126:127]
	v_cvt_pk_bf16_f32 v117, v120, v121
	v_lshl_add_u64 v[120:121], v[128:129], 0, v[114:115]
	v_lshl_add_u64 v[120:121], v[120:121], 0, s[16:17]
	v_cvt_pk_bf16_f32 v119, v124, v125
	v_lshl_add_u64 v[120:121], v[120:121], 0, v[0:1]
	global_store_dwordx4 v[120:121], v[116:119], off sc1
	s_nop 1
	v_mul_f32_e32 v119, 0x3d372713, v106
	v_mul_f32_e32 v119, v106, v119
	v_fma_f32 v119, v106, v119, v106
	v_mul_f32_e32 v119, 0x3f4c422a, v119
	v_mul_f32_e32 v119, 0xc038aa3b, v119
	v_exp_f32_e32 v119, v119
	v_mul_f32_e32 v118, 0x3d372713, v110
	v_mul_f32_e32 v118, v110, v118
	v_fma_f32 v118, v110, v118, v110
	v_add_f32_e32 v119, 1.0, v119
	v_rcp_f32_e32 v120, v119
	v_mul_f32_e32 v119, 0x3d372713, v111
	v_mul_f32_e32 v119, v111, v119
	v_fma_f32 v119, v111, v119, v111
	v_mul_f32_e32 v118, 0x3f4c422a, v118
	v_mul_f32_e32 v119, 0x3f4c422a, v119
	v_mul_f32_e32 v118, 0xc038aa3b, v118
	v_mul_f32_e32 v119, 0xc038aa3b, v119
	v_exp_f32_e32 v118, v118
	v_exp_f32_e32 v119, v119
	v_or_b32_e32 v116, 16, v130
	v_ashrrev_i32_e32 v117, 31, v116
	v_add_f32_e32 v118, 1.0, v118
	v_add_f32_e32 v119, 1.0, v119
	v_rcp_f32_e32 v118, v118
	v_rcp_f32_e32 v119, v119
	v_lshlrev_b64 v[116:117], 15, v[116:117]
	v_pk_mul_f32 v[110:111], v[110:111], v[118:119]
	v_mul_f32_e32 v118, 0x3d372713, v107
	v_mul_f32_e32 v118, v107, v118
	v_fma_f32 v118, v107, v118, v107
	v_mul_f32_e32 v118, 0x3f4c422a, v118
	v_mul_f32_e32 v118, 0xc038aa3b, v118
	v_exp_f32_e32 v118, v118
	s_nop 0
	v_add_f32_e32 v118, 1.0, v118
	v_rcp_f32_e32 v121, v118
	s_nop 0
	v_pk_mul_f32 v[118:119], v[106:107], v[120:121]
	v_mul_f32_e32 v107, 0x3d372713, v108
	v_mul_f32_e32 v107, v108, v107
	v_fma_f32 v107, v108, v107, v108
	v_mul_f32_e32 v107, 0x3f4c422a, v107
	v_mul_f32_e32 v107, 0xc038aa3b, v107
	v_exp_f32_e32 v107, v107
	v_mul_f32_e32 v106, 0x3d372713, v112
	v_mul_f32_e32 v106, v112, v106
	v_fma_f32 v106, v112, v106, v112
	v_add_f32_e32 v107, 1.0, v107
	v_rcp_f32_e32 v120, v107
	v_mul_f32_e32 v107, 0x3d372713, v113
	v_mul_f32_e32 v107, v113, v107
	v_fma_f32 v107, v113, v107, v113
	v_mul_f32_e32 v106, 0x3f4c422a, v106
	v_mul_f32_e32 v107, 0x3f4c422a, v107
	v_mul_f32_e32 v106, 0xc038aa3b, v106
	v_mul_f32_e32 v107, 0xc038aa3b, v107
	v_exp_f32_e32 v106, v106
	v_exp_f32_e32 v107, v107
	v_add_f32_e32 v106, 1.0, v106
	v_add_f32_e32 v107, 1.0, v107
	v_rcp_f32_e32 v106, v106
	v_rcp_f32_e32 v107, v107
	s_nop 0
	v_pk_mul_f32 v[112:113], v[112:113], v[106:107]
	v_mul_f32_e32 v106, 0x3d372713, v109
	v_mul_f32_e32 v106, v109, v106
	v_fma_f32 v106, v109, v106, v109
	v_mul_f32_e32 v106, 0x3f4c422a, v106
	v_mul_f32_e32 v106, 0xc038aa3b, v106
	v_exp_f32_e32 v106, v106
	v_cvt_pk_bf16_f32 v107, v112, v113
	v_add_f32_e32 v106, 1.0, v106
	v_rcp_f32_e32 v121, v106
	v_cvt_pk_bf16_f32 v106, v110, v111
	v_lshl_add_u64 v[110:111], s[6:7], 0, v[116:117]
	v_lshl_add_u64 v[112:113], v[110:111], 0, v[122:123]
	v_pk_mul_f32 v[120:121], v[108:109], v[120:121]
	v_lshl_add_u64 v[112:113], v[112:113], 0, s[16:17]
	v_cvt_pk_bf16_f32 v108, v118, v119
	v_cvt_pk_bf16_f32 v109, v120, v121
	v_lshl_add_u64 v[112:113], v[112:113], 0, v[0:1]
	global_store_dwordx4 v[112:113], v[106:109], off sc1
	s_nop 1
	v_mul_f32_e32 v107, 0x3d372713, v98
	v_mul_f32_e32 v107, v98, v107
	v_fma_f32 v107, v98, v107, v98
	v_mul_f32_e32 v107, 0x3f4c422a, v107
	v_mul_f32_e32 v107, 0xc038aa3b, v107
	v_exp_f32_e32 v107, v107
	v_mul_f32_e32 v106, 0x3d372713, v102
	v_mul_f32_e32 v106, v102, v106
	v_fma_f32 v106, v102, v106, v102
	v_add_f32_e32 v107, 1.0, v107
	v_rcp_f32_e32 v108, v107
	v_mul_f32_e32 v107, 0x3d372713, v103
	v_mul_f32_e32 v107, v103, v107
	v_fma_f32 v107, v103, v107, v103
	v_mul_f32_e32 v106, 0x3f4c422a, v106
	v_mul_f32_e32 v107, 0x3f4c422a, v107
	v_mul_f32_e32 v106, 0xc038aa3b, v106
	v_mul_f32_e32 v107, 0xc038aa3b, v107
	v_exp_f32_e32 v106, v106
	v_exp_f32_e32 v107, v107
	v_add_f32_e32 v106, 1.0, v106
	v_add_f32_e32 v107, 1.0, v107
	v_rcp_f32_e32 v106, v106
	v_rcp_f32_e32 v107, v107
	s_nop 0
	v_pk_mul_f32 v[102:103], v[102:103], v[106:107]
	v_mul_f32_e32 v106, 0x3d372713, v99
	v_mul_f32_e32 v106, v99, v106
	v_fma_f32 v106, v99, v106, v99
	v_mul_f32_e32 v106, 0x3f4c422a, v106
	v_mul_f32_e32 v106, 0xc038aa3b, v106
	v_exp_f32_e32 v106, v106
	s_nop 0
	v_add_f32_e32 v106, 1.0, v106
	v_rcp_f32_e32 v109, v106
	s_nop 0
	v_pk_mul_f32 v[106:107], v[98:99], v[108:109]
	v_mul_f32_e32 v99, 0x3d372713, v100
	v_mul_f32_e32 v99, v100, v99
	v_fma_f32 v99, v100, v99, v100
	v_mul_f32_e32 v99, 0x3f4c422a, v99
	v_mul_f32_e32 v99, 0xc038aa3b, v99
	v_exp_f32_e32 v99, v99
	v_mul_f32_e32 v98, 0x3d372713, v104
	v_mul_f32_e32 v98, v104, v98
	v_fma_f32 v98, v104, v98, v104
	v_add_f32_e32 v99, 1.0, v99
	v_rcp_f32_e32 v108, v99
	v_mul_f32_e32 v99, 0x3d372713, v105
	v_mul_f32_e32 v99, v105, v99
	v_fma_f32 v99, v105, v99, v105
	v_mul_f32_e32 v98, 0x3f4c422a, v98
	v_mul_f32_e32 v99, 0x3f4c422a, v99
	v_mul_f32_e32 v98, 0xc038aa3b, v98
	v_mul_f32_e32 v99, 0xc038aa3b, v99
	v_exp_f32_e32 v98, v98
	v_exp_f32_e32 v99, v99
	v_add_f32_e32 v98, 1.0, v98
	v_add_f32_e32 v99, 1.0, v99
	v_rcp_f32_e32 v98, v98
	v_rcp_f32_e32 v99, v99
	s_nop 0
	v_pk_mul_f32 v[104:105], v[104:105], v[98:99]
	v_mul_f32_e32 v98, 0x3d372713, v101
	v_mul_f32_e32 v98, v101, v98
	v_fma_f32 v98, v101, v98, v101
	v_mul_f32_e32 v98, 0x3f4c422a, v98
; DI float gelu_tanh(float x) { const float u = 0.7978845608028654f * (x + 0.044715f * x * x * x); return x * __builtin_amdgcn_rcpf(1.0f + __builtin_amdgcn_exp2f(-2.8853900817779268f * u)); }
; DI u32x4 pack8(const f32x4& a, const f32x4& b) { u32x4 w; w.x = pk2(a[0], a[1]); w.y = pk2(a[2], a[3]); w.z = pk2(b[0], b[1]); w.w = pk2(b[2], b[3]); return w; }
;     DI void operator()(const f32x4 (&acc)[2][2][4][2], const Unit& u, int wr, int wc, int fr, int fq) const {
;         EPI_ROWS_BEGIN
;             const int R = u.pm * 256 + rt;
; #pragma unroll
;             for (int bj = 0; bj < 2; ++bj) { const int col = u.pn * 256 + bj * 128 + 32 * wc + 8 * fq; const int j = col >> 4, c0 = col & 15;
;                 f32x4 a = acc[ai][bj][m][0], b = acc[ai][bj][m][1];
; #pragma unroll
;                 for (int q = 0; q < 4; ++q) { a[q] = gelu_tanh(a[q]); b[q] = gelu_tanh(b[q]); }
;                 *(u32x4*)(y + ((size_t)R * 32 + j) * SW + u.e * 16 + c0) = pack8(a, b); }
;         EPI_ROWS_END
;     }
	v_mul_f32_e32 v98, 0xc038aa3b, v98
	v_exp_f32_e32 v98, v98
	v_cvt_pk_bf16_f32 v99, v104, v105
	v_add_f32_e32 v98, 1.0, v98
	v_rcp_f32_e32 v109, v98
	v_cvt_pk_bf16_f32 v98, v102, v103
	v_lshl_add_u64 v[102:103], v[110:111], 0, v[114:115]
	v_lshl_add_u64 v[102:103], v[102:103], 0, s[16:17]
	v_pk_mul_f32 v[108:109], v[100:101], v[108:109]
	v_cvt_pk_bf16_f32 v100, v106, v107
	v_cvt_pk_bf16_f32 v101, v108, v109
	v_lshl_add_u64 v[102:103], v[102:103], 0, v[0:1]
	global_store_dwordx4 v[102:103], v[98:101], off sc1
	s_nop 1
	v_mul_f32_e32 v101, 0x3d372713, v90
	v_mul_f32_e32 v101, v90, v101
	v_fma_f32 v101, v90, v101, v90
	v_mul_f32_e32 v101, 0x3f4c422a, v101
	v_mul_f32_e32 v101, 0xc038aa3b, v101
	v_exp_f32_e32 v101, v101
	v_mul_f32_e32 v100, 0x3d372713, v94
	v_mul_f32_e32 v100, v94, v100
	v_fma_f32 v100, v94, v100, v94
	v_add_f32_e32 v101, 1.0, v101
	v_rcp_f32_e32 v102, v101
	v_mul_f32_e32 v101, 0x3d372713, v95
	v_mul_f32_e32 v101, v95, v101
	v_fma_f32 v101, v95, v101, v95
	v_mul_f32_e32 v100, 0x3f4c422a, v100
	v_mul_f32_e32 v101, 0x3f4c422a, v101
	v_mul_f32_e32 v100, 0xc038aa3b, v100
	v_mul_f32_e32 v101, 0xc038aa3b, v101
	v_exp_f32_e32 v100, v100
	v_exp_f32_e32 v101, v101
	v_or_b32_e32 v98, 32, v130
	v_ashrrev_i32_e32 v99, 31, v98
	v_add_f32_e32 v100, 1.0, v100
	v_add_f32_e32 v101, 1.0, v101
	v_rcp_f32_e32 v100, v100
	v_rcp_f32_e32 v101, v101
	v_lshlrev_b64 v[98:99], 15, v[98:99]
	v_pk_mul_f32 v[94:95], v[94:95], v[100:101]
	v_mul_f32_e32 v100, 0x3d372713, v91
	v_mul_f32_e32 v100, v91, v100
	v_fma_f32 v100, v91, v100, v91
	v_mul_f32_e32 v100, 0x3f4c422a, v100
	v_mul_f32_e32 v100, 0xc038aa3b, v100
	v_exp_f32_e32 v100, v100
	s_nop 0
	v_add_f32_e32 v100, 1.0, v100
	v_rcp_f32_e32 v103, v100
	s_nop 0
	v_pk_mul_f32 v[100:101], v[90:91], v[102:103]
	v_mul_f32_e32 v91, 0x3d372713, v92
	v_mul_f32_e32 v91, v92, v91
	v_fma_f32 v91, v92, v91, v92
	v_mul_f32_e32 v91, 0x3f4c422a, v91
	v_mul_f32_e32 v91, 0xc038aa3b, v91
	v_exp_f32_e32 v91, v91
	v_mul_f32_e32 v90, 0x3d372713, v96
	v_mul_f32_e32 v90, v96, v90
	v_fma_f32 v90, v96, v90, v96
	v_add_f32_e32 v91, 1.0, v91
	v_rcp_f32_e32 v102, v91
	v_mul_f32_e32 v91, 0x3d372713, v97
	v_mul_f32_e32 v91, v97, v91
	v_fma_f32 v91, v97, v91, v97
	v_mul_f32_e32 v90, 0x3f4c422a, v90
	v_mul_f32_e32 v91, 0x3f4c422a, v91
	v_mul_f32_e32 v90, 0xc038aa3b, v90
	v_mul_f32_e32 v91, 0xc038aa3b, v91
	v_exp_f32_e32 v90, v90
	v_exp_f32_e32 v91, v91
	v_add_f32_e32 v90, 1.0, v90
	v_add_f32_e32 v91, 1.0, v91
	v_rcp_f32_e32 v90, v90
	v_rcp_f32_e32 v91, v91
	s_nop 0
	v_pk_mul_f32 v[96:97], v[96:97], v[90:91]
	v_mul_f32_e32 v90, 0x3d372713, v93
	v_mul_f32_e32 v90, v93, v90
	v_fma_f32 v90, v93, v90, v93
	v_mul_f32_e32 v90, 0x3f4c422a, v90
	v_mul_f32_e32 v90, 0xc038aa3b, v90
	v_exp_f32_e32 v90, v90
	v_cvt_pk_bf16_f32 v91, v96, v97
	v_add_f32_e32 v90, 1.0, v90
	v_rcp_f32_e32 v103, v90
	v_cvt_pk_bf16_f32 v90, v94, v95
	v_lshl_add_u64 v[94:95], s[6:7], 0, v[98:99]
	v_lshl_add_u64 v[96:97], v[94:95], 0, v[122:123]
	v_pk_mul_f32 v[102:103], v[92:93], v[102:103]
	v_lshl_add_u64 v[96:97], v[96:97], 0, s[16:17]
	v_cvt_pk_bf16_f32 v92, v100, v101
	v_cvt_pk_bf16_f32 v93, v102, v103
	v_lshl_add_u64 v[96:97], v[96:97], 0, v[0:1]
	global_store_dwordx4 v[96:97], v[90:93], off sc1
	s_nop 1
	v_mul_f32_e32 v91, 0x3d372713, v82
	v_mul_f32_e32 v91, v82, v91
	v_fma_f32 v91, v82, v91, v82
	v_mul_f32_e32 v91, 0x3f4c422a, v91
	v_mul_f32_e32 v91, 0xc038aa3b, v91
	v_exp_f32_e32 v91, v91
	v_mul_f32_e32 v90, 0x3d372713, v86
	v_mul_f32_e32 v90, v86, v90
	v_fma_f32 v90, v86, v90, v86
	v_add_f32_e32 v91, 1.0, v91
	v_rcp_f32_e32 v92, v91
	v_mul_f32_e32 v91, 0x3d372713, v87
	v_mul_f32_e32 v91, v87, v91
	v_fma_f32 v91, v87, v91, v87
	v_mul_f32_e32 v90, 0x3f4c422a, v90
	v_mul_f32_e32 v91, 0x3f4c422a, v91
	v_mul_f32_e32 v90, 0xc038aa3b, v90
	v_mul_f32_e32 v91, 0xc038aa3b, v91
	v_exp_f32_e32 v90, v90
	v_exp_f32_e32 v91, v91
	v_add_f32_e32 v90, 1.0, v90
	v_add_f32_e32 v91, 1.0, v91
	v_rcp_f32_e32 v90, v90
	v_rcp_f32_e32 v91, v91
	s_nop 0
	v_pk_mul_f32 v[86:87], v[86:87], v[90:91]
	v_mul_f32_e32 v90, 0x3d372713, v83
	v_mul_f32_e32 v90, v83, v90
	v_fma_f32 v90, v83, v90, v83
	v_mul_f32_e32 v90, 0x3f4c422a, v90
	v_mul_f32_e32 v90, 0xc038aa3b, v90
	v_exp_f32_e32 v90, v90
	s_nop 0
	v_add_f32_e32 v90, 1.0, v90
	v_rcp_f32_e32 v93, v90
	s_nop 0
	v_pk_mul_f32 v[90:91], v[82:83], v[92:93]
	v_mul_f32_e32 v83, 0x3d372713, v84
	v_mul_f32_e32 v83, v84, v83
	v_fma_f32 v83, v84, v83, v84
	v_mul_f32_e32 v83, 0x3f4c422a, v83
	v_mul_f32_e32 v83, 0xc038aa3b, v83
	v_exp_f32_e32 v83, v83
	v_mul_f32_e32 v82, 0x3d372713, v88
	v_mul_f32_e32 v82, v88, v82
	v_fma_f32 v82, v88, v82, v88
	v_add_f32_e32 v83, 1.0, v83
	v_rcp_f32_e32 v92, v83
	v_mul_f32_e32 v83, 0x3d372713, v89
	v_mul_f32_e32 v83, v89, v83
	v_fma_f32 v83, v89, v83, v89
	v_mul_f32_e32 v82, 0x3f4c422a, v82
	v_mul_f32_e32 v83, 0x3f4c422a, v83
	v_mul_f32_e32 v82, 0xc038aa3b, v82
	v_mul_f32_e32 v83, 0xc038aa3b, v83
	v_exp_f32_e32 v82, v82
	v_exp_f32_e32 v83, v83
	v_add_f32_e32 v82, 1.0, v82
	v_add_f32_e32 v83, 1.0, v83
	v_rcp_f32_e32 v82, v82
	v_rcp_f32_e32 v83, v83
	s_nop 0
	v_pk_mul_f32 v[88:89], v[88:89], v[82:83]
	v_mul_f32_e32 v82, 0x3d372713, v85
	v_mul_f32_e32 v82, v85, v82
	v_fma_f32 v82, v85, v82, v85
	v_mul_f32_e32 v82, 0x3f4c422a, v82
	v_mul_f32_e32 v82, 0xc038aa3b, v82
	v_exp_f32_e32 v82, v82
	v_cvt_pk_bf16_f32 v83, v88, v89
	v_add_f32_e32 v82, 1.0, v82
	v_rcp_f32_e32 v93, v82
	v_cvt_pk_bf16_f32 v82, v86, v87
	v_lshl_add_u64 v[86:87], v[94:95], 0, v[114:115]
	v_lshl_add_u64 v[86:87], v[86:87], 0, s[16:17]
	v_pk_mul_f32 v[92:93], v[84:85], v[92:93]
	v_cvt_pk_bf16_f32 v84, v90, v91
	v_cvt_pk_bf16_f32 v85, v92, v93
; DI float gelu_tanh(float x) { const float u = 0.7978845608028654f * (x + 0.044715f * x * x * x); return x * __builtin_amdgcn_rcpf(1.0f + __builtin_amdgcn_exp2f(-2.8853900817779268f * u)); }
; DI u32x4 pack8(const f32x4& a, const f32x4& b) { u32x4 w; w.x = pk2(a[0], a[1]); w.y = pk2(a[2], a[3]); w.z = pk2(b[0], b[1]); w.w = pk2(b[2], b[3]); return w; }
;     DI void operator()(const f32x4 (&acc)[2][2][4][2], const Unit& u, int wr, int wc, int fr, int fq) const {
;         EPI_ROWS_BEGIN
;             const int R = u.pm * 256 + rt;
; #pragma unroll
;             for (int bj = 0; bj < 2; ++bj) { const int col = u.pn * 256 + bj * 128 + 32 * wc + 8 * fq; const int j = col >> 4, c0 = col & 15;
;                 f32x4 a = acc[ai][bj][m][0], b = acc[ai][bj][m][1];
; #pragma unroll
;                 for (int q = 0; q < 4; ++q) { a[q] = gelu_tanh(a[q]); b[q] = gelu_tanh(b[q]); }
;                 *(u32x4*)(y + ((size_t)R * 32 + j) * SW + u.e * 16 + c0) = pack8(a, b); }
;         EPI_ROWS_END
;     }
	v_lshl_add_u64 v[86:87], v[86:87], 0, v[0:1]
	global_store_dwordx4 v[86:87], v[82:85], off sc1
	s_nop 1
	v_mul_f32_e32 v85, 0x3d372713, v74
	v_mul_f32_e32 v85, v74, v85
	v_fma_f32 v85, v74, v85, v74
	v_mul_f32_e32 v85, 0x3f4c422a, v85
	v_mul_f32_e32 v85, 0xc038aa3b, v85
	v_exp_f32_e32 v85, v85
	v_mul_f32_e32 v84, 0x3d372713, v78
	v_mul_f32_e32 v84, v78, v84
	v_fma_f32 v84, v78, v84, v78
	v_add_f32_e32 v85, 1.0, v85
	v_rcp_f32_e32 v86, v85
	v_mul_f32_e32 v85, 0x3d372713, v79
	v_mul_f32_e32 v85, v79, v85
	v_fma_f32 v85, v79, v85, v79
	v_mul_f32_e32 v84, 0x3f4c422a, v84
	v_mul_f32_e32 v85, 0x3f4c422a, v85
	v_mul_f32_e32 v84, 0xc038aa3b, v84
	v_mul_f32_e32 v85, 0xc038aa3b, v85
	v_exp_f32_e32 v84, v84
	v_exp_f32_e32 v85, v85
	v_or_b32_e32 v82, 48, v130
	v_ashrrev_i32_e32 v83, 31, v82
	v_add_f32_e32 v84, 1.0, v84
	v_add_f32_e32 v85, 1.0, v85
	v_rcp_f32_e32 v84, v84
	v_rcp_f32_e32 v85, v85
	v_lshlrev_b64 v[82:83], 15, v[82:83]
	v_pk_mul_f32 v[78:79], v[78:79], v[84:85]
	v_mul_f32_e32 v84, 0x3d372713, v75
	v_mul_f32_e32 v84, v75, v84
	v_fma_f32 v84, v75, v84, v75
	v_mul_f32_e32 v84, 0x3f4c422a, v84
	v_mul_f32_e32 v84, 0xc038aa3b, v84
	v_exp_f32_e32 v84, v84
	s_nop 0
	v_add_f32_e32 v84, 1.0, v84
	v_rcp_f32_e32 v87, v84
	s_nop 0
	v_pk_mul_f32 v[84:85], v[74:75], v[86:87]
	v_mul_f32_e32 v75, 0x3d372713, v76
	v_mul_f32_e32 v75, v76, v75
	v_fma_f32 v75, v76, v75, v76
	v_mul_f32_e32 v75, 0x3f4c422a, v75
	v_mul_f32_e32 v75, 0xc038aa3b, v75
	v_exp_f32_e32 v75, v75
	v_mul_f32_e32 v74, 0x3d372713, v80
	v_mul_f32_e32 v74, v80, v74
	v_fma_f32 v74, v80, v74, v80
	v_add_f32_e32 v75, 1.0, v75
	v_rcp_f32_e32 v86, v75
	v_mul_f32_e32 v75, 0x3d372713, v81
	v_mul_f32_e32 v75, v81, v75
	v_fma_f32 v75, v81, v75, v81
	v_mul_f32_e32 v74, 0x3f4c422a, v74
	v_mul_f32_e32 v75, 0x3f4c422a, v75
	v_mul_f32_e32 v74, 0xc038aa3b, v74
	v_mul_f32_e32 v75, 0xc038aa3b, v75
	v_exp_f32_e32 v74, v74
	v_exp_f32_e32 v75, v75
	v_add_f32_e32 v74, 1.0, v74
	v_add_f32_e32 v75, 1.0, v75
	v_rcp_f32_e32 v74, v74
	v_rcp_f32_e32 v75, v75
	s_nop 0
	v_pk_mul_f32 v[80:81], v[80:81], v[74:75]
	v_mul_f32_e32 v74, 0x3d372713, v77
	v_mul_f32_e32 v74, v77, v74
	v_fma_f32 v74, v77, v74, v77
	v_mul_f32_e32 v74, 0x3f4c422a, v74
	v_mul_f32_e32 v74, 0xc038aa3b, v74
	v_exp_f32_e32 v74, v74
	v_cvt_pk_bf16_f32 v75, v80, v81
	v_add_f32_e32 v74, 1.0, v74
	v_rcp_f32_e32 v87, v74
	v_cvt_pk_bf16_f32 v74, v78, v79
	v_lshl_add_u64 v[78:79], s[6:7], 0, v[82:83]
	v_lshl_add_u64 v[80:81], v[78:79], 0, v[122:123]
	v_pk_mul_f32 v[86:87], v[76:77], v[86:87]
	v_lshl_add_u64 v[80:81], v[80:81], 0, s[16:17]
	v_cvt_pk_bf16_f32 v76, v84, v85
	v_cvt_pk_bf16_f32 v77, v86, v87
	v_lshl_add_u64 v[80:81], v[80:81], 0, v[0:1]
	global_store_dwordx4 v[80:81], v[74:77], off sc1
	s_nop 1
	v_mul_f32_e32 v75, 0x3d372713, v66
	v_mul_f32_e32 v75, v66, v75
	v_fma_f32 v75, v66, v75, v66
	v_mul_f32_e32 v75, 0x3f4c422a, v75
	v_mul_f32_e32 v75, 0xc038aa3b, v75
	v_exp_f32_e32 v75, v75
	v_mul_f32_e32 v74, 0x3d372713, v70
	v_mul_f32_e32 v74, v70, v74
	v_fma_f32 v74, v70, v74, v70
	v_add_f32_e32 v75, 1.0, v75
	v_rcp_f32_e32 v76, v75
	v_mul_f32_e32 v75, 0x3d372713, v71
	v_mul_f32_e32 v75, v71, v75
	v_fma_f32 v75, v71, v75, v71
	v_mul_f32_e32 v74, 0x3f4c422a, v74
	v_mul_f32_e32 v75, 0x3f4c422a, v75
	v_mul_f32_e32 v74, 0xc038aa3b, v74
	v_mul_f32_e32 v75, 0xc038aa3b, v75
	v_exp_f32_e32 v74, v74
	v_exp_f32_e32 v75, v75
	v_add_f32_e32 v74, 1.0, v74
	v_add_f32_e32 v75, 1.0, v75
	v_rcp_f32_e32 v74, v74
	v_rcp_f32_e32 v75, v75
	s_nop 0
	v_pk_mul_f32 v[70:71], v[70:71], v[74:75]
	v_mul_f32_e32 v74, 0x3d372713, v67
	v_mul_f32_e32 v74, v67, v74
	v_fma_f32 v74, v67, v74, v67
	v_mul_f32_e32 v74, 0x3f4c422a, v74
	v_mul_f32_e32 v74, 0xc038aa3b, v74
	v_exp_f32_e32 v74, v74
	s_nop 0
	v_add_f32_e32 v74, 1.0, v74
	v_rcp_f32_e32 v77, v74
	s_nop 0
	v_pk_mul_f32 v[74:75], v[66:67], v[76:77]
	v_mul_f32_e32 v67, 0x3d372713, v68
	v_mul_f32_e32 v67, v68, v67
	v_fma_f32 v67, v68, v67, v68
	v_mul_f32_e32 v67, 0x3f4c422a, v67
	v_mul_f32_e32 v67, 0xc038aa3b, v67
	v_exp_f32_e32 v67, v67
	v_mul_f32_e32 v66, 0x3d372713, v72
	v_mul_f32_e32 v66, v72, v66
	v_fma_f32 v66, v72, v66, v72
	v_add_f32_e32 v67, 1.0, v67
	v_rcp_f32_e32 v76, v67
	v_mul_f32_e32 v67, 0x3d372713, v73
	v_mul_f32_e32 v67, v73, v67
	v_fma_f32 v67, v73, v67, v73
	v_mul_f32_e32 v66, 0x3f4c422a, v66
	v_mul_f32_e32 v67, 0x3f4c422a, v67
	v_mul_f32_e32 v66, 0xc038aa3b, v66
	v_mul_f32_e32 v67, 0xc038aa3b, v67
	v_exp_f32_e32 v66, v66
	v_exp_f32_e32 v67, v67
	v_add_f32_e32 v66, 1.0, v66
	v_add_f32_e32 v67, 1.0, v67
	v_rcp_f32_e32 v66, v66
	v_rcp_f32_e32 v67, v67
	s_nop 0
	v_pk_mul_f32 v[72:73], v[72:73], v[66:67]
	v_mul_f32_e32 v66, 0x3d372713, v69
	v_mul_f32_e32 v66, v69, v66
	v_fma_f32 v66, v69, v66, v69
	v_mul_f32_e32 v66, 0x3f4c422a, v66
	v_mul_f32_e32 v66, 0xc038aa3b, v66
	v_exp_f32_e32 v66, v66
	v_cvt_pk_bf16_f32 v67, v72, v73
	v_add_f32_e32 v66, 1.0, v66
	v_rcp_f32_e32 v77, v66
	v_cvt_pk_bf16_f32 v66, v70, v71
	v_lshl_add_u64 v[70:71], v[78:79], 0, v[114:115]
	v_lshl_add_u64 v[70:71], v[70:71], 0, s[16:17]
	v_pk_mul_f32 v[76:77], v[68:69], v[76:77]
	v_cvt_pk_bf16_f32 v68, v74, v75
	v_cvt_pk_bf16_f32 v69, v76, v77
	v_lshl_add_u64 v[70:71], v[70:71], 0, v[0:1]
	global_store_dwordx4 v[70:71], v[66:69], off sc1
	s_nop 1
	v_mul_f32_e32 v69, 0x3d372713, v58
	v_mul_f32_e32 v69, v58, v69
	v_fma_f32 v69, v58, v69, v58
	v_mul_f32_e32 v69, 0x3f4c422a, v69
	v_mul_f32_e32 v69, 0xc038aa3b, v69
	v_exp_f32_e32 v69, v69
	v_mul_f32_e32 v68, 0x3d372713, v62
	v_mul_f32_e32 v68, v62, v68
	v_fma_f32 v68, v62, v68, v62
	v_add_f32_e32 v69, 1.0, v69
	v_rcp_f32_e32 v70, v69
	v_mul_f32_e32 v69, 0x3d372713, v63
	v_mul_f32_e32 v69, v63, v69
; DI float gelu_tanh(float x) { const float u = 0.7978845608028654f * (x + 0.044715f * x * x * x); return x * __builtin_amdgcn_rcpf(1.0f + __builtin_amdgcn_exp2f(-2.8853900817779268f * u)); }
; DI u32x4 pack8(const f32x4& a, const f32x4& b) { u32x4 w; w.x = pk2(a[0], a[1]); w.y = pk2(a[2], a[3]); w.z = pk2(b[0], b[1]); w.w = pk2(b[2], b[3]); return w; }
;     DI void operator()(const f32x4 (&acc)[2][2][4][2], const Unit& u, int wr, int wc, int fr, int fq) const {
;         EPI_ROWS_BEGIN
;             const int R = u.pm * 256 + rt;
; #pragma unroll
;             for (int bj = 0; bj < 2; ++bj) { const int col = u.pn * 256 + bj * 128 + 32 * wc + 8 * fq; const int j = col >> 4, c0 = col & 15;
;                 f32x4 a = acc[ai][bj][m][0], b = acc[ai][bj][m][1];
; #pragma unroll
;                 for (int q = 0; q < 4; ++q) { a[q] = gelu_tanh(a[q]); b[q] = gelu_tanh(b[q]); }
;                 *(u32x4*)(y + ((size_t)R * 32 + j) * SW + u.e * 16 + c0) = pack8(a, b); }
;         EPI_ROWS_END
;     }
	v_fma_f32 v69, v63, v69, v63
	v_mul_f32_e32 v68, 0x3f4c422a, v68
	v_mul_f32_e32 v69, 0x3f4c422a, v69
	v_mul_f32_e32 v68, 0xc038aa3b, v68
	v_mul_f32_e32 v69, 0xc038aa3b, v69
	v_exp_f32_e32 v68, v68
	v_exp_f32_e32 v69, v69
	v_add_u32_e32 v66, 0x80, v130
	v_ashrrev_i32_e32 v67, 31, v66
	v_add_f32_e32 v68, 1.0, v68
	v_add_f32_e32 v69, 1.0, v69
	v_rcp_f32_e32 v68, v68
	v_rcp_f32_e32 v69, v69
	v_lshlrev_b64 v[66:67], 15, v[66:67]
	v_pk_mul_f32 v[62:63], v[62:63], v[68:69]
	v_mul_f32_e32 v68, 0x3d372713, v59
	v_mul_f32_e32 v68, v59, v68
	v_fma_f32 v68, v59, v68, v59
	v_mul_f32_e32 v68, 0x3f4c422a, v68
	v_mul_f32_e32 v68, 0xc038aa3b, v68
	v_exp_f32_e32 v68, v68
	s_nop 0
	v_add_f32_e32 v68, 1.0, v68
	v_rcp_f32_e32 v71, v68
	s_nop 0
	v_pk_mul_f32 v[68:69], v[58:59], v[70:71]
	v_mul_f32_e32 v59, 0x3d372713, v60
	v_mul_f32_e32 v59, v60, v59
	v_fma_f32 v59, v60, v59, v60
	v_mul_f32_e32 v59, 0x3f4c422a, v59
	v_mul_f32_e32 v59, 0xc038aa3b, v59
	v_exp_f32_e32 v59, v59
	v_mul_f32_e32 v58, 0x3d372713, v64
	v_mul_f32_e32 v58, v64, v58
	v_fma_f32 v58, v64, v58, v64
	v_add_f32_e32 v59, 1.0, v59
	v_rcp_f32_e32 v70, v59
	v_mul_f32_e32 v59, 0x3d372713, v65
	v_mul_f32_e32 v59, v65, v59
	v_fma_f32 v59, v65, v59, v65
	v_mul_f32_e32 v58, 0x3f4c422a, v58
	v_mul_f32_e32 v59, 0x3f4c422a, v59
	v_mul_f32_e32 v58, 0xc038aa3b, v58
	v_mul_f32_e32 v59, 0xc038aa3b, v59
	v_exp_f32_e32 v58, v58
	v_exp_f32_e32 v59, v59
	v_add_f32_e32 v58, 1.0, v58
	v_add_f32_e32 v59, 1.0, v59
	v_rcp_f32_e32 v58, v58
	v_rcp_f32_e32 v59, v59
	s_nop 0
	v_pk_mul_f32 v[64:65], v[64:65], v[58:59]
	v_mul_f32_e32 v58, 0x3d372713, v61
	v_mul_f32_e32 v58, v61, v58
	v_fma_f32 v58, v61, v58, v61
	v_mul_f32_e32 v58, 0x3f4c422a, v58
	v_mul_f32_e32 v58, 0xc038aa3b, v58
	v_exp_f32_e32 v58, v58
	v_cvt_pk_bf16_f32 v59, v64, v65
	v_add_f32_e32 v58, 1.0, v58
	v_rcp_f32_e32 v71, v58
	v_cvt_pk_bf16_f32 v58, v62, v63
	v_lshl_add_u64 v[62:63], s[6:7], 0, v[66:67]
	v_lshl_add_u64 v[64:65], v[62:63], 0, v[122:123]
	v_pk_mul_f32 v[70:71], v[60:61], v[70:71]
	v_lshl_add_u64 v[64:65], v[64:65], 0, s[16:17]
	v_cvt_pk_bf16_f32 v60, v68, v69
	v_cvt_pk_bf16_f32 v61, v70, v71
	v_lshl_add_u64 v[64:65], v[64:65], 0, v[0:1]
	global_store_dwordx4 v[64:65], v[58:61], off sc1
	s_nop 1
	v_mul_f32_e32 v59, 0x3d372713, v50
	v_mul_f32_e32 v59, v50, v59
	v_fma_f32 v59, v50, v59, v50
	v_mul_f32_e32 v59, 0x3f4c422a, v59
	v_mul_f32_e32 v59, 0xc038aa3b, v59
	v_exp_f32_e32 v59, v59
	v_mul_f32_e32 v58, 0x3d372713, v54
	v_mul_f32_e32 v58, v54, v58
	v_fma_f32 v58, v54, v58, v54
	v_add_f32_e32 v59, 1.0, v59
	v_rcp_f32_e32 v60, v59
	v_mul_f32_e32 v59, 0x3d372713, v55
	v_mul_f32_e32 v59, v55, v59
	v_fma_f32 v59, v55, v59, v55
	v_mul_f32_e32 v58, 0x3f4c422a, v58
	v_mul_f32_e32 v59, 0x3f4c422a, v59
	v_mul_f32_e32 v58, 0xc038aa3b, v58
	v_mul_f32_e32 v59, 0xc038aa3b, v59
	v_exp_f32_e32 v58, v58
	v_exp_f32_e32 v59, v59
	v_add_f32_e32 v58, 1.0, v58
	v_add_f32_e32 v59, 1.0, v59
	v_rcp_f32_e32 v58, v58
	v_rcp_f32_e32 v59, v59
	s_nop 0
	v_pk_mul_f32 v[54:55], v[54:55], v[58:59]
	v_mul_f32_e32 v58, 0x3d372713, v51
	v_mul_f32_e32 v58, v51, v58
	v_fma_f32 v58, v51, v58, v51
	v_mul_f32_e32 v58, 0x3f4c422a, v58
	v_mul_f32_e32 v58, 0xc038aa3b, v58
	v_exp_f32_e32 v58, v58
	s_nop 0
	v_add_f32_e32 v58, 1.0, v58
	v_rcp_f32_e32 v61, v58
	s_nop 0
	v_pk_mul_f32 v[58:59], v[50:51], v[60:61]
	v_mul_f32_e32 v51, 0x3d372713, v52
	v_mul_f32_e32 v51, v52, v51
	v_fma_f32 v51, v52, v51, v52
	v_mul_f32_e32 v51, 0x3f4c422a, v51
	v_mul_f32_e32 v51, 0xc038aa3b, v51
	v_exp_f32_e32 v51, v51
	v_mul_f32_e32 v50, 0x3d372713, v56
	v_mul_f32_e32 v50, v56, v50
	v_fma_f32 v50, v56, v50, v56
	v_add_f32_e32 v51, 1.0, v51
	v_rcp_f32_e32 v60, v51
	v_mul_f32_e32 v51, 0x3d372713, v57
	v_mul_f32_e32 v51, v57, v51
	v_fma_f32 v51, v57, v51, v57
	v_mul_f32_e32 v50, 0x3f4c422a, v50
	v_mul_f32_e32 v51, 0x3f4c422a, v51
	v_mul_f32_e32 v50, 0xc038aa3b, v50
	v_mul_f32_e32 v51, 0xc038aa3b, v51
	v_exp_f32_e32 v50, v50
	v_exp_f32_e32 v51, v51
	v_add_f32_e32 v50, 1.0, v50
	v_add_f32_e32 v51, 1.0, v51
	v_rcp_f32_e32 v50, v50
	v_rcp_f32_e32 v51, v51
	s_nop 0
	v_pk_mul_f32 v[56:57], v[56:57], v[50:51]
	v_mul_f32_e32 v50, 0x3d372713, v53
	v_mul_f32_e32 v50, v53, v50
	v_fma_f32 v50, v53, v50, v53
	v_mul_f32_e32 v50, 0x3f4c422a, v50
	v_mul_f32_e32 v50, 0xc038aa3b, v50
	v_exp_f32_e32 v50, v50
	v_cvt_pk_bf16_f32 v51, v56, v57
	v_add_f32_e32 v50, 1.0, v50
	v_rcp_f32_e32 v61, v50
	v_cvt_pk_bf16_f32 v50, v54, v55
	v_lshl_add_u64 v[54:55], v[62:63], 0, v[114:115]
	v_lshl_add_u64 v[54:55], v[54:55], 0, s[16:17]
	v_pk_mul_f32 v[60:61], v[52:53], v[60:61]
	v_cvt_pk_bf16_f32 v52, v58, v59
	v_cvt_pk_bf16_f32 v53, v60, v61
	v_lshl_add_u64 v[54:55], v[54:55], 0, v[0:1]
	global_store_dwordx4 v[54:55], v[50:53], off sc1
	s_nop 1
	v_mul_f32_e32 v53, 0x3d372713, v42
	v_mul_f32_e32 v53, v42, v53
	v_fma_f32 v53, v42, v53, v42
	v_mul_f32_e32 v53, 0x3f4c422a, v53
	v_mul_f32_e32 v53, 0xc038aa3b, v53
	v_exp_f32_e32 v53, v53
	v_mul_f32_e32 v52, 0x3d372713, v46
	v_mul_f32_e32 v52, v46, v52
	v_fma_f32 v52, v46, v52, v46
	v_add_f32_e32 v53, 1.0, v53
	v_rcp_f32_e32 v54, v53
	v_mul_f32_e32 v53, 0x3d372713, v47
	v_mul_f32_e32 v53, v47, v53
	v_fma_f32 v53, v47, v53, v47
	v_mul_f32_e32 v52, 0x3f4c422a, v52
	v_mul_f32_e32 v53, 0x3f4c422a, v53
	v_mul_f32_e32 v52, 0xc038aa3b, v52
	v_mul_f32_e32 v53, 0xc038aa3b, v53
	v_exp_f32_e32 v52, v52
	v_exp_f32_e32 v53, v53
	v_add_u32_e32 v50, 0x90, v130
	v_ashrrev_i32_e32 v51, 31, v50
	v_add_f32_e32 v52, 1.0, v52
	v_add_f32_e32 v53, 1.0, v53
	v_rcp_f32_e32 v52, v52
	v_rcp_f32_e32 v53, v53
	v_lshlrev_b64 v[50:51], 15, v[50:51]
	v_pk_mul_f32 v[46:47], v[46:47], v[52:53]
	v_mul_f32_e32 v52, 0x3d372713, v43
; DI float gelu_tanh(float x) { const float u = 0.7978845608028654f * (x + 0.044715f * x * x * x); return x * __builtin_amdgcn_rcpf(1.0f + __builtin_amdgcn_exp2f(-2.8853900817779268f * u)); }
; DI u32x4 pack8(const f32x4& a, const f32x4& b) { u32x4 w; w.x = pk2(a[0], a[1]); w.y = pk2(a[2], a[3]); w.z = pk2(b[0], b[1]); w.w = pk2(b[2], b[3]); return w; }
;     DI void operator()(const f32x4 (&acc)[2][2][4][2], const Unit& u, int wr, int wc, int fr, int fq) const {
;         EPI_ROWS_BEGIN
;             const int R = u.pm * 256 + rt;
; #pragma unroll
;             for (int bj = 0; bj < 2; ++bj) { const int col = u.pn * 256 + bj * 128 + 32 * wc + 8 * fq; const int j = col >> 4, c0 = col & 15;
;                 f32x4 a = acc[ai][bj][m][0], b = acc[ai][bj][m][1];
; #pragma unroll
;                 for (int q = 0; q < 4; ++q) { a[q] = gelu_tanh(a[q]); b[q] = gelu_tanh(b[q]); }
;                 *(u32x4*)(y + ((size_t)R * 32 + j) * SW + u.e * 16 + c0) = pack8(a, b); }
;         EPI_ROWS_END
;     }
	v_mul_f32_e32 v52, v43, v52
	v_fma_f32 v52, v43, v52, v43
	v_mul_f32_e32 v52, 0x3f4c422a, v52
	v_mul_f32_e32 v52, 0xc038aa3b, v52
	v_exp_f32_e32 v52, v52
	s_nop 0
	v_add_f32_e32 v52, 1.0, v52
	v_rcp_f32_e32 v55, v52
	s_nop 0
	v_pk_mul_f32 v[52:53], v[42:43], v[54:55]
	v_mul_f32_e32 v43, 0x3d372713, v44
	v_mul_f32_e32 v43, v44, v43
	v_fma_f32 v43, v44, v43, v44
	v_mul_f32_e32 v43, 0x3f4c422a, v43
	v_mul_f32_e32 v43, 0xc038aa3b, v43
	v_exp_f32_e32 v43, v43
	v_mul_f32_e32 v42, 0x3d372713, v48
	v_mul_f32_e32 v42, v48, v42
	v_fma_f32 v42, v48, v42, v48
	v_add_f32_e32 v43, 1.0, v43
	v_rcp_f32_e32 v54, v43
	v_mul_f32_e32 v43, 0x3d372713, v49
	v_mul_f32_e32 v43, v49, v43
	v_fma_f32 v43, v49, v43, v49
	v_mul_f32_e32 v42, 0x3f4c422a, v42
	v_mul_f32_e32 v43, 0x3f4c422a, v43
	v_mul_f32_e32 v42, 0xc038aa3b, v42
	v_mul_f32_e32 v43, 0xc038aa3b, v43
	v_exp_f32_e32 v42, v42
	v_exp_f32_e32 v43, v43
	v_add_f32_e32 v42, 1.0, v42
	v_add_f32_e32 v43, 1.0, v43
	v_rcp_f32_e32 v42, v42
	v_rcp_f32_e32 v43, v43
	s_nop 0
	v_pk_mul_f32 v[48:49], v[48:49], v[42:43]
	v_mul_f32_e32 v42, 0x3d372713, v45
	v_mul_f32_e32 v42, v45, v42
	v_fma_f32 v42, v45, v42, v45
	v_mul_f32_e32 v42, 0x3f4c422a, v42
	v_mul_f32_e32 v42, 0xc038aa3b, v42
	v_exp_f32_e32 v42, v42
	v_cvt_pk_bf16_f32 v43, v48, v49
	v_add_f32_e32 v42, 1.0, v42
	v_rcp_f32_e32 v55, v42
	v_cvt_pk_bf16_f32 v42, v46, v47
	v_lshl_add_u64 v[46:47], s[6:7], 0, v[50:51]
	v_lshl_add_u64 v[48:49], v[46:47], 0, v[122:123]
	v_pk_mul_f32 v[54:55], v[44:45], v[54:55]
	v_lshl_add_u64 v[48:49], v[48:49], 0, s[16:17]
	v_cvt_pk_bf16_f32 v44, v52, v53
	v_cvt_pk_bf16_f32 v45, v54, v55
	v_lshl_add_u64 v[48:49], v[48:49], 0, v[0:1]
	global_store_dwordx4 v[48:49], v[42:45], off sc1
	s_nop 1
	v_mul_f32_e32 v43, 0x3d372713, v34
	v_mul_f32_e32 v43, v34, v43
	v_fma_f32 v43, v34, v43, v34
	v_mul_f32_e32 v43, 0x3f4c422a, v43
	v_mul_f32_e32 v43, 0xc038aa3b, v43
	v_exp_f32_e32 v43, v43
	v_mul_f32_e32 v42, 0x3d372713, v38
	v_mul_f32_e32 v42, v38, v42
	v_fma_f32 v42, v38, v42, v38
	v_add_f32_e32 v43, 1.0, v43
	v_rcp_f32_e32 v44, v43
	v_mul_f32_e32 v43, 0x3d372713, v39
	v_mul_f32_e32 v43, v39, v43
	v_fma_f32 v43, v39, v43, v39
	v_mul_f32_e32 v42, 0x3f4c422a, v42
	v_mul_f32_e32 v43, 0x3f4c422a, v43
	v_mul_f32_e32 v42, 0xc038aa3b, v42
	v_mul_f32_e32 v43, 0xc038aa3b, v43
	v_exp_f32_e32 v42, v42
	v_exp_f32_e32 v43, v43
	v_add_f32_e32 v42, 1.0, v42
	v_add_f32_e32 v43, 1.0, v43
	v_rcp_f32_e32 v42, v42
	v_rcp_f32_e32 v43, v43
	s_nop 0
	v_pk_mul_f32 v[38:39], v[38:39], v[42:43]
	v_mul_f32_e32 v42, 0x3d372713, v35
	v_mul_f32_e32 v42, v35, v42
	v_fma_f32 v42, v35, v42, v35
	v_mul_f32_e32 v42, 0x3f4c422a, v42
	v_mul_f32_e32 v42, 0xc038aa3b, v42
	v_exp_f32_e32 v42, v42
	s_nop 0
	v_add_f32_e32 v42, 1.0, v42
	v_rcp_f32_e32 v45, v42
	s_nop 0
	v_pk_mul_f32 v[42:43], v[34:35], v[44:45]
	v_mul_f32_e32 v35, 0x3d372713, v36
	v_mul_f32_e32 v35, v36, v35
	v_fma_f32 v35, v36, v35, v36
	v_mul_f32_e32 v35, 0x3f4c422a, v35
	v_mul_f32_e32 v35, 0xc038aa3b, v35
	v_exp_f32_e32 v35, v35
	v_mul_f32_e32 v34, 0x3d372713, v40
	v_mul_f32_e32 v34, v40, v34
	v_fma_f32 v34, v40, v34, v40
	v_add_f32_e32 v35, 1.0, v35
	v_rcp_f32_e32 v44, v35
	v_mul_f32_e32 v35, 0x3d372713, v41
	v_mul_f32_e32 v35, v41, v35
	v_fma_f32 v35, v41, v35, v41
	v_mul_f32_e32 v34, 0x3f4c422a, v34
	v_mul_f32_e32 v35, 0x3f4c422a, v35
	v_mul_f32_e32 v34, 0xc038aa3b, v34
	v_mul_f32_e32 v35, 0xc038aa3b, v35
	v_exp_f32_e32 v34, v34
	v_exp_f32_e32 v35, v35
	v_add_f32_e32 v34, 1.0, v34
	v_add_f32_e32 v35, 1.0, v35
	v_rcp_f32_e32 v34, v34
	v_rcp_f32_e32 v35, v35
	s_nop 0
	v_pk_mul_f32 v[40:41], v[40:41], v[34:35]
	v_mul_f32_e32 v34, 0x3d372713, v37
	v_mul_f32_e32 v34, v37, v34
	v_fma_f32 v34, v37, v34, v37
	v_mul_f32_e32 v34, 0x3f4c422a, v34
	v_mul_f32_e32 v34, 0xc038aa3b, v34
	v_exp_f32_e32 v34, v34
	v_cvt_pk_bf16_f32 v35, v40, v41
	v_add_f32_e32 v34, 1.0, v34
	v_rcp_f32_e32 v45, v34
	v_cvt_pk_bf16_f32 v34, v38, v39
	v_lshl_add_u64 v[38:39], v[46:47], 0, v[114:115]
	v_lshl_add_u64 v[38:39], v[38:39], 0, s[16:17]
	v_pk_mul_f32 v[44:45], v[36:37], v[44:45]
	v_cvt_pk_bf16_f32 v36, v42, v43
	v_cvt_pk_bf16_f32 v37, v44, v45
	v_lshl_add_u64 v[38:39], v[38:39], 0, v[0:1]
	global_store_dwordx4 v[38:39], v[34:37], off sc1
	s_nop 1
	v_mul_f32_e32 v37, 0x3d372713, v26
	v_mul_f32_e32 v37, v26, v37
	v_fma_f32 v37, v26, v37, v26
	v_mul_f32_e32 v37, 0x3f4c422a, v37
	v_mul_f32_e32 v37, 0xc038aa3b, v37
	v_exp_f32_e32 v37, v37
	v_mul_f32_e32 v36, 0x3d372713, v30
	v_mul_f32_e32 v36, v30, v36
	v_fma_f32 v36, v30, v36, v30
	v_add_f32_e32 v37, 1.0, v37
	v_rcp_f32_e32 v38, v37
	v_mul_f32_e32 v37, 0x3d372713, v31
	v_mul_f32_e32 v37, v31, v37
	v_fma_f32 v37, v31, v37, v31
	v_mul_f32_e32 v36, 0x3f4c422a, v36
	v_mul_f32_e32 v37, 0x3f4c422a, v37
	v_mul_f32_e32 v36, 0xc038aa3b, v36
	v_mul_f32_e32 v37, 0xc038aa3b, v37
	v_exp_f32_e32 v36, v36
	v_exp_f32_e32 v37, v37
	v_add_u32_e32 v34, 0xa0, v130
	v_ashrrev_i32_e32 v35, 31, v34
	v_add_f32_e32 v36, 1.0, v36
	v_add_f32_e32 v37, 1.0, v37
	v_rcp_f32_e32 v36, v36
	v_rcp_f32_e32 v37, v37
	v_lshlrev_b64 v[34:35], 15, v[34:35]
	v_pk_mul_f32 v[30:31], v[30:31], v[36:37]
	v_mul_f32_e32 v36, 0x3d372713, v27
	v_mul_f32_e32 v36, v27, v36
	v_fma_f32 v36, v27, v36, v27
	v_mul_f32_e32 v36, 0x3f4c422a, v36
	v_mul_f32_e32 v36, 0xc038aa3b, v36
	v_exp_f32_e32 v36, v36
	s_nop 0
	v_add_f32_e32 v36, 1.0, v36
	v_rcp_f32_e32 v39, v36
	s_nop 0
	v_pk_mul_f32 v[36:37], v[26:27], v[38:39]
	v_mul_f32_e32 v27, 0x3d372713, v28
	v_mul_f32_e32 v27, v28, v27
	v_fma_f32 v27, v28, v27, v28
	v_mul_f32_e32 v27, 0x3f4c422a, v27
	v_mul_f32_e32 v27, 0xc038aa3b, v27
	v_exp_f32_e32 v27, v27
	v_mul_f32_e32 v26, 0x3d372713, v32
	v_mul_f32_e32 v26, v32, v26
; DI float gelu_tanh(float x) { const float u = 0.7978845608028654f * (x + 0.044715f * x * x * x); return x * __builtin_amdgcn_rcpf(1.0f + __builtin_amdgcn_exp2f(-2.8853900817779268f * u)); }
; DI u32x4 pack8(const f32x4& a, const f32x4& b) { u32x4 w; w.x = pk2(a[0], a[1]); w.y = pk2(a[2], a[3]); w.z = pk2(b[0], b[1]); w.w = pk2(b[2], b[3]); return w; }
;     DI void operator()(const f32x4 (&acc)[2][2][4][2], const Unit& u, int wr, int wc, int fr, int fq) const {
;         EPI_ROWS_BEGIN
;             const int R = u.pm * 256 + rt;
; #pragma unroll
;             for (int bj = 0; bj < 2; ++bj) { const int col = u.pn * 256 + bj * 128 + 32 * wc + 8 * fq; const int j = col >> 4, c0 = col & 15;
;                 f32x4 a = acc[ai][bj][m][0], b = acc[ai][bj][m][1];
; #pragma unroll
;                 for (int q = 0; q < 4; ++q) { a[q] = gelu_tanh(a[q]); b[q] = gelu_tanh(b[q]); }
;                 *(u32x4*)(y + ((size_t)R * 32 + j) * SW + u.e * 16 + c0) = pack8(a, b); }
;         EPI_ROWS_END
;     }
	v_fma_f32 v26, v32, v26, v32
	v_add_f32_e32 v27, 1.0, v27
	v_rcp_f32_e32 v38, v27
	v_mul_f32_e32 v27, 0x3d372713, v33
	v_mul_f32_e32 v27, v33, v27
	v_fma_f32 v27, v33, v27, v33
	v_mul_f32_e32 v26, 0x3f4c422a, v26
	v_mul_f32_e32 v27, 0x3f4c422a, v27
	v_mul_f32_e32 v26, 0xc038aa3b, v26
	v_mul_f32_e32 v27, 0xc038aa3b, v27
	v_exp_f32_e32 v26, v26
	v_exp_f32_e32 v27, v27
	v_add_f32_e32 v26, 1.0, v26
	v_add_f32_e32 v27, 1.0, v27
	v_rcp_f32_e32 v26, v26
	v_rcp_f32_e32 v27, v27
	s_nop 0
	v_pk_mul_f32 v[32:33], v[32:33], v[26:27]
	v_mul_f32_e32 v26, 0x3d372713, v29
	v_mul_f32_e32 v26, v29, v26
	v_fma_f32 v26, v29, v26, v29
	v_mul_f32_e32 v26, 0x3f4c422a, v26
	v_mul_f32_e32 v26, 0xc038aa3b, v26
	v_exp_f32_e32 v26, v26
	v_cvt_pk_bf16_f32 v27, v32, v33
	v_add_f32_e32 v26, 1.0, v26
	v_rcp_f32_e32 v39, v26
	v_cvt_pk_bf16_f32 v26, v30, v31
	v_lshl_add_u64 v[30:31], s[6:7], 0, v[34:35]
	v_lshl_add_u64 v[32:33], v[30:31], 0, v[122:123]
	v_pk_mul_f32 v[38:39], v[28:29], v[38:39]
	v_lshl_add_u64 v[32:33], v[32:33], 0, s[16:17]
	v_cvt_pk_bf16_f32 v28, v36, v37
	v_cvt_pk_bf16_f32 v29, v38, v39
	v_lshl_add_u64 v[32:33], v[32:33], 0, v[0:1]
	global_store_dwordx4 v[32:33], v[26:29], off sc1
	s_nop 1
	v_mul_f32_e32 v27, 0x3d372713, v18
	v_mul_f32_e32 v27, v18, v27
	v_fma_f32 v27, v18, v27, v18
	v_mul_f32_e32 v27, 0x3f4c422a, v27
	v_mul_f32_e32 v27, 0xc038aa3b, v27
	v_exp_f32_e32 v27, v27
	v_mul_f32_e32 v26, 0x3d372713, v22
	v_mul_f32_e32 v26, v22, v26
	v_fma_f32 v26, v22, v26, v22
	v_add_f32_e32 v27, 1.0, v27
	v_rcp_f32_e32 v28, v27
	v_mul_f32_e32 v27, 0x3d372713, v23
	v_mul_f32_e32 v27, v23, v27
	v_fma_f32 v27, v23, v27, v23
	v_mul_f32_e32 v26, 0x3f4c422a, v26
	v_mul_f32_e32 v27, 0x3f4c422a, v27
	v_mul_f32_e32 v26, 0xc038aa3b, v26
	v_mul_f32_e32 v27, 0xc038aa3b, v27
	v_exp_f32_e32 v26, v26
	v_exp_f32_e32 v27, v27
	v_add_f32_e32 v26, 1.0, v26
	v_add_f32_e32 v27, 1.0, v27
	v_rcp_f32_e32 v26, v26
	v_rcp_f32_e32 v27, v27
	s_nop 0
	v_pk_mul_f32 v[22:23], v[22:23], v[26:27]
	v_mul_f32_e32 v26, 0x3d372713, v19
	v_mul_f32_e32 v26, v19, v26
	v_fma_f32 v26, v19, v26, v19
	v_mul_f32_e32 v26, 0x3f4c422a, v26
	v_mul_f32_e32 v26, 0xc038aa3b, v26
	v_exp_f32_e32 v26, v26
	s_nop 0
	v_add_f32_e32 v26, 1.0, v26
	v_rcp_f32_e32 v29, v26
	s_nop 0
	v_pk_mul_f32 v[26:27], v[18:19], v[28:29]
	v_mul_f32_e32 v19, 0x3d372713, v20
	v_mul_f32_e32 v19, v20, v19
	v_fma_f32 v19, v20, v19, v20
	v_mul_f32_e32 v19, 0x3f4c422a, v19
	v_mul_f32_e32 v19, 0xc038aa3b, v19
	v_exp_f32_e32 v19, v19
	v_mul_f32_e32 v18, 0x3d372713, v24
	v_mul_f32_e32 v18, v24, v18
	v_fma_f32 v18, v24, v18, v24
	v_add_f32_e32 v19, 1.0, v19
	v_rcp_f32_e32 v28, v19
	v_mul_f32_e32 v19, 0x3d372713, v25
	v_mul_f32_e32 v19, v25, v19
	v_fma_f32 v19, v25, v19, v25
	v_mul_f32_e32 v18, 0x3f4c422a, v18
	v_mul_f32_e32 v19, 0x3f4c422a, v19
	v_mul_f32_e32 v18, 0xc038aa3b, v18
	v_mul_f32_e32 v19, 0xc038aa3b, v19
	v_exp_f32_e32 v18, v18
	v_exp_f32_e32 v19, v19
	v_add_f32_e32 v18, 1.0, v18
	v_add_f32_e32 v19, 1.0, v19
	v_rcp_f32_e32 v18, v18
	v_rcp_f32_e32 v19, v19
	s_nop 0
	v_pk_mul_f32 v[24:25], v[24:25], v[18:19]
	v_mul_f32_e32 v18, 0x3d372713, v21
	v_mul_f32_e32 v18, v21, v18
	v_fma_f32 v18, v21, v18, v21
	v_mul_f32_e32 v18, 0x3f4c422a, v18
	v_mul_f32_e32 v18, 0xc038aa3b, v18
	v_exp_f32_e32 v18, v18
	v_cvt_pk_bf16_f32 v19, v24, v25
	v_add_f32_e32 v18, 1.0, v18
	v_rcp_f32_e32 v29, v18
	v_cvt_pk_bf16_f32 v18, v22, v23
	v_lshl_add_u64 v[22:23], v[30:31], 0, v[114:115]
	v_lshl_add_u64 v[22:23], v[22:23], 0, s[16:17]
	v_pk_mul_f32 v[28:29], v[20:21], v[28:29]
	v_cvt_pk_bf16_f32 v20, v26, v27
	v_cvt_pk_bf16_f32 v21, v28, v29
	v_lshl_add_u64 v[22:23], v[22:23], 0, v[0:1]
	global_store_dwordx4 v[22:23], v[18:21], off sc1
	s_nop 1
	v_mul_f32_e32 v21, 0x3d372713, v10
	v_mul_f32_e32 v21, v10, v21
	v_fma_f32 v21, v10, v21, v10
	v_mul_f32_e32 v21, 0x3f4c422a, v21
	v_mul_f32_e32 v21, 0xc038aa3b, v21
	v_exp_f32_e32 v21, v21
	v_mul_f32_e32 v20, 0x3d372713, v14
	v_mul_f32_e32 v20, v14, v20
	v_fma_f32 v20, v14, v20, v14
	v_add_f32_e32 v21, 1.0, v21
	v_rcp_f32_e32 v22, v21
	v_mul_f32_e32 v21, 0x3d372713, v15
	v_mul_f32_e32 v21, v15, v21
	v_fma_f32 v21, v15, v21, v15
	v_mul_f32_e32 v20, 0x3f4c422a, v20
	v_mul_f32_e32 v21, 0x3f4c422a, v21
	v_mul_f32_e32 v20, 0xc038aa3b, v20
	v_mul_f32_e32 v21, 0xc038aa3b, v21
	v_exp_f32_e32 v20, v20
	v_exp_f32_e32 v21, v21
	v_add_u32_e32 v18, 0xb0, v130
	v_ashrrev_i32_e32 v19, 31, v18
	v_add_f32_e32 v20, 1.0, v20
; DI float gelu_tanh(float x) { const float u = 0.7978845608028654f * (x + 0.044715f * x * x * x); return x * __builtin_amdgcn_rcpf(1.0f + __builtin_amdgcn_exp2f(-2.8853900817779268f * u)); }
; #define PG8_BAR __builtin_amdgcn_s_barrier()
; DI u32x4 pack8(const f32x4& a, const f32x4& b) { u32x4 w; w.x = pk2(a[0], a[1]); w.y = pk2(a[2], a[3]); w.z = pk2(b[0], b[1]); w.w = pk2(b[2], b[3]); return w; }
;     ...
;         if (wr == 1) PG8_BAR;
;     DI void operator()(const f32x4 (&acc)[2][2][4][2], const Unit& u, int wr, int wc, int fr, int fq) const {
;         EPI_ROWS_BEGIN
;             const int R = u.pm * 256 + rt;
; #pragma unroll
;             for (int bj = 0; bj < 2; ++bj) { const int col = u.pn * 256 + bj * 128 + 32 * wc + 8 * fq; const int j = col >> 4, c0 = col & 15;
;                 f32x4 a = acc[ai][bj][m][0], b = acc[ai][bj][m][1];
; #pragma unroll
;                 for (int q = 0; q < 4; ++q) { a[q] = gelu_tanh(a[q]); b[q] = gelu_tanh(b[q]); }
;                 *(u32x4*)(y + ((size_t)R * 32 + j) * SW + u.e * 16 + c0) = pack8(a, b); }
;         EPI_ROWS_END
;     }
	v_add_f32_e32 v21, 1.0, v21
	v_rcp_f32_e32 v20, v20
	v_rcp_f32_e32 v21, v21
	v_lshlrev_b64 v[18:19], 15, v[18:19]
	v_pk_mul_f32 v[14:15], v[14:15], v[20:21]
	v_mul_f32_e32 v20, 0x3d372713, v11
	v_mul_f32_e32 v20, v11, v20
	v_fma_f32 v20, v11, v20, v11
	v_mul_f32_e32 v20, 0x3f4c422a, v20
	v_mul_f32_e32 v20, 0xc038aa3b, v20
	v_exp_f32_e32 v20, v20
	s_nop 0
	v_add_f32_e32 v20, 1.0, v20
	v_rcp_f32_e32 v23, v20
	s_nop 0
	v_pk_mul_f32 v[20:21], v[10:11], v[22:23]
	v_mul_f32_e32 v11, 0x3d372713, v12
	v_mul_f32_e32 v11, v12, v11
	v_fma_f32 v11, v12, v11, v12
	v_mul_f32_e32 v11, 0x3f4c422a, v11
	v_mul_f32_e32 v11, 0xc038aa3b, v11
	v_exp_f32_e32 v11, v11
	v_mul_f32_e32 v10, 0x3d372713, v16
	v_mul_f32_e32 v10, v16, v10
	v_fma_f32 v10, v16, v10, v16
	v_add_f32_e32 v11, 1.0, v11
	v_rcp_f32_e32 v22, v11
	v_mul_f32_e32 v11, 0x3d372713, v17
	v_mul_f32_e32 v11, v17, v11
	v_fma_f32 v11, v17, v11, v17
	v_mul_f32_e32 v10, 0x3f4c422a, v10
	v_mul_f32_e32 v11, 0x3f4c422a, v11
	v_mul_f32_e32 v10, 0xc038aa3b, v10
	v_mul_f32_e32 v11, 0xc038aa3b, v11
	v_exp_f32_e32 v10, v10
	v_exp_f32_e32 v11, v11
	v_add_f32_e32 v10, 1.0, v10
	v_add_f32_e32 v11, 1.0, v11
	v_rcp_f32_e32 v10, v10
	v_rcp_f32_e32 v11, v11
	s_nop 0
	v_pk_mul_f32 v[16:17], v[16:17], v[10:11]
	v_mul_f32_e32 v10, 0x3d372713, v13
	v_mul_f32_e32 v10, v13, v10
	v_fma_f32 v10, v13, v10, v13
	v_mul_f32_e32 v10, 0x3f4c422a, v10
	v_mul_f32_e32 v10, 0xc038aa3b, v10
	v_exp_f32_e32 v10, v10
	v_cvt_pk_bf16_f32 v11, v16, v17
	v_add_f32_e32 v10, 1.0, v10
	v_rcp_f32_e32 v23, v10
	v_cvt_pk_bf16_f32 v10, v14, v15
	v_lshl_add_u64 v[14:15], s[6:7], 0, v[18:19]
	v_lshl_add_u64 v[16:17], v[14:15], 0, v[122:123]
	v_pk_mul_f32 v[22:23], v[12:13], v[22:23]
	v_lshl_add_u64 v[16:17], v[16:17], 0, s[16:17]
	v_cvt_pk_bf16_f32 v12, v20, v21
	v_cvt_pk_bf16_f32 v13, v22, v23
	v_lshl_add_u64 v[16:17], v[16:17], 0, v[0:1]
	global_store_dwordx4 v[16:17], v[10:13], off sc1
	s_nop 1
	v_mul_f32_e32 v11, 0x3d372713, v2
	v_mul_f32_e32 v11, v2, v11
	v_fma_f32 v11, v2, v11, v2
	v_mul_f32_e32 v11, 0x3f4c422a, v11
	v_mul_f32_e32 v11, 0xc038aa3b, v11
	v_exp_f32_e32 v11, v11
	v_mul_f32_e32 v10, 0x3d372713, v6
	v_mul_f32_e32 v10, v6, v10
	v_fma_f32 v10, v6, v10, v6
	v_add_f32_e32 v11, 1.0, v11
	v_rcp_f32_e32 v12, v11
	v_mul_f32_e32 v11, 0x3d372713, v7
	v_mul_f32_e32 v11, v7, v11
	v_fma_f32 v11, v7, v11, v7
	v_mul_f32_e32 v10, 0x3f4c422a, v10
	v_mul_f32_e32 v11, 0x3f4c422a, v11
	v_mul_f32_e32 v10, 0xc038aa3b, v10
	v_mul_f32_e32 v11, 0xc038aa3b, v11
	v_exp_f32_e32 v10, v10
	v_exp_f32_e32 v11, v11
	v_add_f32_e32 v10, 1.0, v10
	v_add_f32_e32 v11, 1.0, v11
	v_rcp_f32_e32 v10, v10
	v_rcp_f32_e32 v11, v11
	s_nop 0
	v_pk_mul_f32 v[6:7], v[6:7], v[10:11]
	v_mul_f32_e32 v10, 0x3d372713, v3
	v_mul_f32_e32 v10, v3, v10
	v_fma_f32 v10, v3, v10, v3
	v_mul_f32_e32 v10, 0x3f4c422a, v10
	v_mul_f32_e32 v10, 0xc038aa3b, v10
	v_exp_f32_e32 v10, v10
	s_nop 0
	v_add_f32_e32 v10, 1.0, v10
	v_rcp_f32_e32 v13, v10
	s_nop 0
	v_pk_mul_f32 v[10:11], v[2:3], v[12:13]
	v_mul_f32_e32 v3, 0x3d372713, v4
	v_mul_f32_e32 v3, v4, v3
	v_fma_f32 v3, v4, v3, v4
	v_mul_f32_e32 v3, 0x3f4c422a, v3
	v_mul_f32_e32 v3, 0xc038aa3b, v3
	v_exp_f32_e32 v3, v3
	v_mul_f32_e32 v2, 0x3d372713, v8
	v_mul_f32_e32 v2, v8, v2
	v_fma_f32 v2, v8, v2, v8
	v_add_f32_e32 v3, 1.0, v3
	v_rcp_f32_e32 v12, v3
	v_mul_f32_e32 v3, 0x3d372713, v9
	v_mul_f32_e32 v3, v9, v3
	v_fma_f32 v3, v9, v3, v9
	v_mul_f32_e32 v2, 0x3f4c422a, v2
	v_mul_f32_e32 v3, 0x3f4c422a, v3
	v_mul_f32_e32 v2, 0xc038aa3b, v2
	v_mul_f32_e32 v3, 0xc038aa3b, v3
	v_exp_f32_e32 v2, v2
	v_exp_f32_e32 v3, v3
	v_add_f32_e32 v2, 1.0, v2
	v_add_f32_e32 v3, 1.0, v3
	v_rcp_f32_e32 v2, v2
	v_rcp_f32_e32 v3, v3
	s_nop 0
	v_pk_mul_f32 v[8:9], v[8:9], v[2:3]
	v_mul_f32_e32 v2, 0x3d372713, v5
	v_mul_f32_e32 v2, v5, v2
	v_fma_f32 v2, v5, v2, v5
	v_mul_f32_e32 v2, 0x3f4c422a, v2
	v_mul_f32_e32 v2, 0xc038aa3b, v2
	v_exp_f32_e32 v2, v2
	v_cvt_pk_bf16_f32 v3, v8, v9
	v_add_f32_e32 v2, 1.0, v2
	v_rcp_f32_e32 v13, v2
	v_cvt_pk_bf16_f32 v2, v6, v7
	v_lshl_add_u64 v[6:7], v[14:15], 0, v[114:115]
	v_lshl_add_u64 v[6:7], v[6:7], 0, s[16:17]
	v_pk_mul_f32 v[12:13], v[4:5], v[12:13]
	v_cvt_pk_bf16_f32 v4, v10, v11
	v_cvt_pk_bf16_f32 v5, v12, v13
	v_lshl_add_u64 v[6:7], v[6:7], 0, v[0:1]
	global_store_dwordx4 v[6:7], v[2:5], off sc1
	s_cbranch_vccnz .LBB0_765
	s_andn2_b64 vcc, exec, s[4:5]
	s_cbranch_vccnz .LBB0_764
	s_barrier
	s_branch .LBB0_764

; DI unsigned pk4_fp8(float a, float b, float c, float d) { int r = 0; r = __builtin_amdgcn_cvt_pk_fp8_f32(sat8(a), sat8(b), r, false); r = __builtin_amdgcn_cvt_pk_fp8_f32(sat8(c), sat8(d), r, true); return (unsigned)r; }
; DI float sigmoidf_(float x) { return __builtin_amdgcn_rcpf(1.0f + __builtin_amdgcn_exp2f(-1.4426950408889634f * x)); }
;     DI void operator()(const f32x4 (&acc)[2][2][4][2], const Unit& u, int wr, int wc, int fr, int fq) const {
;     ...
;             for (int p2 = 0; p2 < 2; ++p2) { const size_t row0 = (size_t)u.pm * 256 + 128 * ai + 64 * wr + 32 * p2 + fr; u32x2 w[2];
; #pragma unroll
;                 for (int r2 = 0; r2 < 2; ++r2) { const int m = 2 * p2 + r2; f32x4 a = acc[ai][0][m][0], b = acc[ai][0][m][1]; const f32x4 ga = acc[ai][1][m][0], gb = acc[ai][1][m][1];
; #pragma unroll
;                     for (int q = 0; q < 4; ++q) { a[q] *= AZ8_SCALE * sigmoidf_(ga[q]); b[q] *= AZ8_SCALE * sigmoidf_(gb[q]); }
;                     w[r2].x = pk4_fp8(a[0], a[1], a[2], a[3]); w[r2].y = pk4_fp8(b[0], b[1], b[2], b[3]); }
.LBB0_837:
	s_mov_b32 s2, s26
	s_mov_b32 s0, -1
	s_lshl_b32 s3, s2, 4
	v_mbcnt_lo_u32_b32 v0, s0, 0
	s_ashr_i32 s21, s20, 31
	s_andn2_b32 s3, s3, 63
	v_mbcnt_hi_u32_b32 v0, s0, v0
	s_lshl_b64 s[0:1], s[20:21], 8
	s_ashr_i32 s13, s3, 31
	s_add_u32 s0, s0, s3
	v_mul_f32_e32 v114, 0xbfb8aa3b, v114
	s_addc_u32 s1, s1, s13
	v_mul_f32_e32 v118, 0xbfb8aa3b, v118
	v_exp_f32_e32 v114, v114
	v_mov_b32_e32 v135, s1
	s_lshl_b32 s1, s2, 5
	v_exp_f32_e32 v118, v118
	s_and_b32 s1, s1, 0x60
	v_and_or_b32 v134, v0, 15, s0
	s_lshl_b32 s0, s43, 7
	v_and_b32_e32 v138, 16, v0
	s_or_b32 s0, s0, s1
	v_ashrrev_i32_e32 v0, 1, v0
	s_addk_i32 s0, 0x200
	v_and_b32_e32 v0, -8, v0
	v_add_f32_e32 v114, 1.0, v114
	v_add_u32_e32 v136, s0, v0
	v_add_f32_e32 v0, 1.0, v118
	v_rcp_f32_e32 v114, v114
	v_mul_f32_e32 v118, 0xbfb8aa3b, v119
	v_exp_f32_e32 v118, v118
	v_mul_f32_e32 v115, 0xbfb8aa3b, v115
	v_mul_f32_e32 v114, 0x41000000, v114
	v_mul_f32_e32 v119, v122, v114
	v_add_f32_e32 v114, 1.0, v118
	v_mul_f32_e32 v118, 0xbfb8aa3b, v120
	v_mul_f32_e32 v120, 0xbfb8aa3b, v121
	v_exp_f32_e32 v118, v118
	v_exp_f32_e32 v120, v120
	v_mul_f32_e32 v117, 0xbfb8aa3b, v117
	v_rcp_f32_e32 v0, v0
	v_exp_f32_e32 v115, v115
	v_rcp_f32_e32 v114, v114
	v_exp_f32_e32 v117, v117
	v_add_f32_e32 v118, 1.0, v118
	v_mul_f32_e32 v116, 0xbfb8aa3b, v116
	v_add_f32_e32 v120, 1.0, v120
	v_mul_f32_e32 v0, 0x41000000, v0
	v_add_f32_e32 v115, 1.0, v115
	v_mul_f32_e32 v114, 0x41000000, v114
	v_rcp_f32_e32 v118, v118
	v_exp_f32_e32 v116, v116
	v_rcp_f32_e32 v120, v120
	v_add_f32_e32 v117, 1.0, v117
	v_mul_f32_e32 v0, v126, v0
	v_rcp_f32_e32 v115, v115
	v_mul_f32_e32 v114, v127, v114
	v_rcp_f32_e32 v117, v117
	v_med3_f32 v0, v0, s53, v204
	v_med3_f32 v121, v114, s53, v204
	v_mov_b32_e32 v114, v1
	v_mul_f32_e32 v102, 0xbfb8aa3b, v102
	v_cvt_pk_fp8_f32 v114, v0, v121
	v_exp_f32_e32 v102, v102
	v_mul_f32_e32 v118, 0x41000000, v118
	v_add_f32_e32 v116, 1.0, v116
	v_mul_f32_e32 v120, 0x41000000, v120
	v_mul_f32_e32 v115, 0x41000000, v115
	v_mul_f32_e32 v118, v128, v118
	v_rcp_f32_e32 v116, v116
	v_mul_f32_e32 v120, v129, v120
	v_mul_f32_e32 v117, 0x41000000, v117
	v_mul_f32_e32 v115, v123, v115
	v_mul_f32_e32 v0, v125, v117
	v_med3_f32 v117, v118, s53, v204
	v_med3_f32 v118, v120, s53, v204
	v_cvt_pk_fp8_f32 v114, v117, v118 op_sel:[0,0,1]
	v_med3_f32 v117, v119, s53, v204
	v_med3_f32 v118, v115, s53, v204
	v_mov_b32_e32 v115, v1
	v_add_f32_e32 v102, 1.0, v102
	v_cvt_pk_fp8_f32 v115, v117, v118
	v_rcp_f32_e32 v102, v102
	v_mul_f32_e32 v116, 0x41000000, v116
	v_mul_f32_e32 v116, v124, v116
	v_med3_f32 v116, v116, s53, v204
	v_med3_f32 v0, v0, s53, v204
	v_cvt_pk_fp8_f32 v115, v116, v0 op_sel:[0,0,1]
	v_mul_f32_e32 v0, 0x41000000, v102
	v_mul_f32_e32 v102, 0xbfb8aa3b, v103
	v_mul_f32_e32 v98, 0xbfb8aa3b, v98
	v_exp_f32_e32 v102, v102
	v_mul_f32_e32 v99, 0xbfb8aa3b, v99
	v_exp_f32_e32 v98, v98
	v_exp_f32_e32 v99, v99
	v_mul_f32_e32 v103, 0xbfb8aa3b, v104
	v_mul_f32_e32 v104, 0xbfb8aa3b, v105
	v_add_f32_e32 v102, 1.0, v102
	v_exp_f32_e32 v103, v103
	v_mul_f32_e32 v100, 0xbfb8aa3b, v100
	v_exp_f32_e32 v104, v104
	v_mul_f32_e32 v101, 0xbfb8aa3b, v101
	v_add_f32_e32 v98, 1.0, v98
	v_rcp_f32_e32 v102, v102
	v_add_f32_e32 v99, 1.0, v99
	v_exp_f32_e32 v100, v100
	v_exp_f32_e32 v101, v101
	v_rcp_f32_e32 v98, v98
	v_rcp_f32_e32 v99, v99
	v_add_f32_e32 v103, 1.0, v103
	v_add_f32_e32 v104, 1.0, v104
	v_mul_f32_e32 v102, 0x41000000, v102
	v_rcp_f32_e32 v103, v103
	v_add_f32_e32 v100, 1.0, v100
	v_rcp_f32_e32 v104, v104
	v_add_f32_e32 v101, 1.0, v101
	v_mul_f32_e32 v0, v110, v0
	v_mul_f32_e32 v98, 0x41000000, v98
	v_mul_f32_e32 v102, v111, v102
	v_mul_f32_e32 v99, 0x41000000, v99
	v_rcp_f32_e32 v100, v100
	v_rcp_f32_e32 v101, v101
	v_mul_f32_e32 v98, v106, v98
	v_mul_f32_e32 v99, v107, v99
	v_med3_f32 v0, v0, s53, v204
	v_med3_f32 v102, v102, s53, v204
	v_mov_b32_e32 v116, v1
	v_mul_f32_e32 v82, 0xbfb8aa3b, v82
	v_cvt_pk_fp8_f32 v116, v0, v102
	v_med3_f32 v98, v98, s53, v204
	v_med3_f32 v99, v99, s53, v204
	v_mov_b32_e32 v117, v1
	v_exp_f32_e32 v82, v82
	v_mul_f32_e32 v103, 0x41000000, v103
	v_mul_f32_e32 v104, 0x41000000, v104
	v_cvt_pk_fp8_f32 v117, v98, v99
	v_mul_f32_e32 v103, v112, v103
	v_mul_f32_e32 v100, 0x41000000, v100
	v_mul_f32_e32 v104, v113, v104
	v_mul_f32_e32 v101, 0x41000000, v101
	v_mul_f32_e32 v100, v108, v100
	v_mul_f32_e32 v101, v109, v101
	v_med3_f32 v0, v103, s53, v204
	v_med3_f32 v102, v104, s53, v204
	v_cvt_pk_fp8_f32 v116, v0, v102 op_sel:[0,0,1]
	v_med3_f32 v0, v100, s53, v204
	v_med3_f32 v98, v101, s53, v204
	v_add_f32_e32 v82, 1.0, v82
	v_cvt_pk_fp8_f32 v117, v0, v98 op_sel:[0,0,1]
	v_mul_f32_e32 v0, 0xbfb8aa3b, v86
	v_rcp_f32_e32 v82, v82
	v_mul_f32_e32 v86, 0xbfb8aa3b, v87
	v_exp_f32_e32 v86, v86
	v_exp_f32_e32 v0, v0
	v_mul_f32_e32 v82, 0x41000000, v82
	v_mul_f32_e32 v87, v90, v82
	v_add_f32_e32 v82, 1.0, v86
	v_mul_f32_e32 v86, 0xbfb8aa3b, v88
	v_mul_f32_e32 v88, 0xbfb8aa3b, v89
	v_add_f32_e32 v0, 1.0, v0
	v_mul_f32_e32 v83, 0xbfb8aa3b, v83
	v_exp_f32_e32 v86, v86
	v_exp_f32_e32 v88, v88
	v_mul_f32_e32 v85, 0xbfb8aa3b, v85
	v_rcp_f32_e32 v0, v0
	v_exp_f32_e32 v83, v83
	v_rcp_f32_e32 v82, v82
	v_exp_f32_e32 v85, v85
	v_add_f32_e32 v86, 1.0, v86
	v_mul_f32_e32 v84, 0xbfb8aa3b, v84
	v_add_f32_e32 v88, 1.0, v88
	v_mul_f32_e32 v0, 0x41000000, v0
	v_add_f32_e32 v83, 1.0, v83
	v_mul_f32_e32 v82, 0x41000000, v82
	v_rcp_f32_e32 v86, v86
	v_exp_f32_e32 v84, v84
	v_rcp_f32_e32 v88, v88
	v_add_f32_e32 v85, 1.0, v85
	v_mul_f32_e32 v0, v94, v0
	v_rcp_f32_e32 v83, v83
	v_mul_f32_e32 v82, v95, v82
	v_rcp_f32_e32 v85, v85
	v_med3_f32 v0, v0, s53, v204
	v_med3_f32 v89, v82, s53, v204
	v_mov_b32_e32 v82, v1
; DI unsigned pk4_fp8(float a, float b, float c, float d) { int r = 0; r = __builtin_amdgcn_cvt_pk_fp8_f32(sat8(a), sat8(b), r, false); r = __builtin_amdgcn_cvt_pk_fp8_f32(sat8(c), sat8(d), r, true); return (unsigned)r; }
; DI float sigmoidf_(float x) { return __builtin_amdgcn_rcpf(1.0f + __builtin_amdgcn_exp2f(-1.4426950408889634f * x)); }
;     DI void operator()(const f32x4 (&acc)[2][2][4][2], const Unit& u, int wr, int wc, int fr, int fq) const {
;     ...
;             for (int p2 = 0; p2 < 2; ++p2) { const size_t row0 = (size_t)u.pm * 256 + 128 * ai + 64 * wr + 32 * p2 + fr; u32x2 w[2];
; #pragma unroll
;                 for (int r2 = 0; r2 < 2; ++r2) { const int m = 2 * p2 + r2; f32x4 a = acc[ai][0][m][0], b = acc[ai][0][m][1]; const f32x4 ga = acc[ai][1][m][0], gb = acc[ai][1][m][1];
; #pragma unroll
;                     for (int q = 0; q < 4; ++q) { a[q] *= AZ8_SCALE * sigmoidf_(ga[q]); b[q] *= AZ8_SCALE * sigmoidf_(gb[q]); }
;                     w[r2].x = pk4_fp8(a[0], a[1], a[2], a[3]); w[r2].y = pk4_fp8(b[0], b[1], b[2], b[3]); }
	v_mul_f32_e32 v70, 0xbfb8aa3b, v70
	v_cvt_pk_fp8_f32 v82, v0, v89
	v_exp_f32_e32 v70, v70
	v_mul_f32_e32 v86, 0x41000000, v86
	v_add_f32_e32 v84, 1.0, v84
	v_mul_f32_e32 v88, 0x41000000, v88
	v_mul_f32_e32 v83, 0x41000000, v83
	v_mul_f32_e32 v86, v96, v86
	v_rcp_f32_e32 v84, v84
	v_mul_f32_e32 v88, v97, v88
	v_mul_f32_e32 v85, 0x41000000, v85
	v_mul_f32_e32 v83, v91, v83
	v_mul_f32_e32 v0, v93, v85
	v_med3_f32 v85, v86, s53, v204
	v_med3_f32 v86, v88, s53, v204
	v_cvt_pk_fp8_f32 v82, v85, v86 op_sel:[0,0,1]
	v_med3_f32 v85, v87, s53, v204
	v_med3_f32 v86, v83, s53, v204
	v_mov_b32_e32 v83, v1
	v_add_f32_e32 v70, 1.0, v70
	v_cvt_pk_fp8_f32 v83, v85, v86
	v_rcp_f32_e32 v70, v70
	v_mul_f32_e32 v84, 0x41000000, v84
	v_mul_f32_e32 v84, v92, v84
	v_med3_f32 v84, v84, s53, v204
	v_med3_f32 v0, v0, s53, v204
	v_cvt_pk_fp8_f32 v83, v84, v0 op_sel:[0,0,1]
	v_mul_f32_e32 v0, 0x41000000, v70
	v_mul_f32_e32 v70, 0xbfb8aa3b, v71
	v_mul_f32_e32 v66, 0xbfb8aa3b, v66
	v_exp_f32_e32 v70, v70
	v_mul_f32_e32 v67, 0xbfb8aa3b, v67
	v_exp_f32_e32 v66, v66
	v_exp_f32_e32 v67, v67
	v_mul_f32_e32 v71, 0xbfb8aa3b, v72
	v_mul_f32_e32 v72, 0xbfb8aa3b, v73
	v_add_f32_e32 v70, 1.0, v70
	v_exp_f32_e32 v71, v71
	v_mul_f32_e32 v68, 0xbfb8aa3b, v68
	v_exp_f32_e32 v72, v72
	v_mul_f32_e32 v69, 0xbfb8aa3b, v69
	v_add_f32_e32 v66, 1.0, v66
	v_rcp_f32_e32 v70, v70
	v_add_f32_e32 v67, 1.0, v67
	v_exp_f32_e32 v68, v68
	v_exp_f32_e32 v69, v69
	v_rcp_f32_e32 v66, v66
	v_rcp_f32_e32 v67, v67
	v_add_f32_e32 v71, 1.0, v71
	v_add_f32_e32 v72, 1.0, v72
	v_mul_f32_e32 v70, 0x41000000, v70
	v_rcp_f32_e32 v71, v71
	v_add_f32_e32 v68, 1.0, v68
	v_rcp_f32_e32 v72, v72
	v_add_f32_e32 v69, 1.0, v69
	v_mul_f32_e32 v0, v78, v0
	v_mul_f32_e32 v66, 0x41000000, v66
	v_mul_f32_e32 v70, v79, v70
	v_mul_f32_e32 v67, 0x41000000, v67
	v_rcp_f32_e32 v68, v68
	v_rcp_f32_e32 v69, v69
	v_mul_f32_e32 v66, v74, v66
	v_mul_f32_e32 v67, v75, v67
	v_med3_f32 v0, v0, s53, v204
	v_med3_f32 v70, v70, s53, v204
	v_mov_b32_e32 v84, v1
	v_mul_f32_e32 v50, 0xbfb8aa3b, v50
	v_cvt_pk_fp8_f32 v84, v0, v70
	v_med3_f32 v66, v66, s53, v204
	v_med3_f32 v67, v67, s53, v204
	v_mov_b32_e32 v85, v1
	v_exp_f32_e32 v50, v50
	v_mul_f32_e32 v71, 0x41000000, v71
	v_mul_f32_e32 v72, 0x41000000, v72
	v_cvt_pk_fp8_f32 v85, v66, v67
	v_mul_f32_e32 v71, v80, v71
	v_mul_f32_e32 v68, 0x41000000, v68
	v_mul_f32_e32 v72, v81, v72
	v_mul_f32_e32 v69, 0x41000000, v69
	v_mul_f32_e32 v68, v76, v68
	v_mul_f32_e32 v69, v77, v69
	v_med3_f32 v0, v71, s53, v204
	v_med3_f32 v70, v72, s53, v204
	v_cvt_pk_fp8_f32 v84, v0, v70 op_sel:[0,0,1]
	v_med3_f32 v0, v68, s53, v204
	v_med3_f32 v66, v69, s53, v204
	v_add_f32_e32 v50, 1.0, v50
	v_cvt_pk_fp8_f32 v85, v0, v66 op_sel:[0,0,1]
	v_mul_f32_e32 v0, 0xbfb8aa3b, v54
	v_rcp_f32_e32 v50, v50
	v_mul_f32_e32 v54, 0xbfb8aa3b, v55
	v_exp_f32_e32 v54, v54
	v_exp_f32_e32 v0, v0
	v_mul_f32_e32 v50, 0x41000000, v50
	v_mul_f32_e32 v55, v58, v50
	v_add_f32_e32 v50, 1.0, v54
	v_mul_f32_e32 v54, 0xbfb8aa3b, v56
	v_mul_f32_e32 v56, 0xbfb8aa3b, v57
	v_add_f32_e32 v0, 1.0, v0
	v_mul_f32_e32 v51, 0xbfb8aa3b, v51
	v_exp_f32_e32 v54, v54
	v_exp_f32_e32 v56, v56
	v_mul_f32_e32 v53, 0xbfb8aa3b, v53
	v_rcp_f32_e32 v0, v0
	v_exp_f32_e32 v51, v51
	v_rcp_f32_e32 v50, v50
	v_exp_f32_e32 v53, v53
	v_add_f32_e32 v54, 1.0, v54
	v_mul_f32_e32 v52, 0xbfb8aa3b, v52
	v_add_f32_e32 v56, 1.0, v56
	v_mul_f32_e32 v0, 0x41000000, v0
	v_add_f32_e32 v51, 1.0, v51
	v_mul_f32_e32 v50, 0x41000000, v50
	v_rcp_f32_e32 v54, v54
	v_exp_f32_e32 v52, v52
	v_rcp_f32_e32 v56, v56
	v_add_f32_e32 v53, 1.0, v53
	v_mul_f32_e32 v0, v62, v0
	v_rcp_f32_e32 v51, v51
	v_mul_f32_e32 v50, v63, v50
	v_rcp_f32_e32 v53, v53
	v_med3_f32 v0, v0, s53, v204
	v_med3_f32 v57, v50, s53, v204
	v_mov_b32_e32 v50, v1
	v_mul_f32_e32 v38, 0xbfb8aa3b, v38
	v_cvt_pk_fp8_f32 v50, v0, v57
	v_exp_f32_e32 v38, v38
	v_mul_f32_e32 v54, 0x41000000, v54
	v_add_f32_e32 v52, 1.0, v52
	v_mul_f32_e32 v56, 0x41000000, v56
	v_mul_f32_e32 v51, 0x41000000, v51
	v_mul_f32_e32 v54, v64, v54
	v_rcp_f32_e32 v52, v52
	v_mul_f32_e32 v56, v65, v56
	v_mul_f32_e32 v53, 0x41000000, v53
	v_mul_f32_e32 v51, v59, v51
	v_mul_f32_e32 v0, v61, v53
	v_med3_f32 v53, v54, s53, v204
	v_med3_f32 v54, v56, s53, v204
	v_cvt_pk_fp8_f32 v50, v53, v54 op_sel:[0,0,1]
	v_med3_f32 v53, v55, s53, v204
	v_med3_f32 v54, v51, s53, v204
	v_mov_b32_e32 v51, v1
	v_add_f32_e32 v38, 1.0, v38
	v_cvt_pk_fp8_f32 v51, v53, v54
	v_rcp_f32_e32 v38, v38
	v_mul_f32_e32 v52, 0x41000000, v52
	v_mul_f32_e32 v52, v60, v52
	v_med3_f32 v52, v52, s53, v204
	v_med3_f32 v0, v0, s53, v204
	v_cvt_pk_fp8_f32 v51, v52, v0 op_sel:[0,0,1]
	v_mul_f32_e32 v0, 0x41000000, v38
	v_mul_f32_e32 v38, 0xbfb8aa3b, v39
	v_mul_f32_e32 v34, 0xbfb8aa3b, v34
	v_exp_f32_e32 v38, v38
	v_mul_f32_e32 v35, 0xbfb8aa3b, v35
	v_exp_f32_e32 v34, v34
	v_exp_f32_e32 v35, v35
	v_mul_f32_e32 v39, 0xbfb8aa3b, v40
	v_mul_f32_e32 v40, 0xbfb8aa3b, v41
	v_add_f32_e32 v38, 1.0, v38
	v_exp_f32_e32 v39, v39
	v_mul_f32_e32 v36, 0xbfb8aa3b, v36
	v_exp_f32_e32 v40, v40
	v_mul_f32_e32 v37, 0xbfb8aa3b, v37
	v_add_f32_e32 v34, 1.0, v34
	v_rcp_f32_e32 v38, v38
	v_add_f32_e32 v35, 1.0, v35
	v_exp_f32_e32 v36, v36
	v_exp_f32_e32 v37, v37
	v_rcp_f32_e32 v34, v34
	v_rcp_f32_e32 v35, v35
	v_add_f32_e32 v39, 1.0, v39
	v_add_f32_e32 v40, 1.0, v40
	v_mul_f32_e32 v38, 0x41000000, v38
	v_rcp_f32_e32 v39, v39
	v_add_f32_e32 v36, 1.0, v36
	v_rcp_f32_e32 v40, v40
	v_add_f32_e32 v37, 1.0, v37
	v_mul_f32_e32 v0, v46, v0
	v_mul_f32_e32 v34, 0x41000000, v34
	v_mul_f32_e32 v38, v47, v38
	v_mul_f32_e32 v35, 0x41000000, v35
	v_rcp_f32_e32 v36, v36
	v_rcp_f32_e32 v37, v37
	v_mul_f32_e32 v34, v42, v34
	v_mul_f32_e32 v35, v43, v35
; DI unsigned pk4_fp8(float a, float b, float c, float d) { int r = 0; r = __builtin_amdgcn_cvt_pk_fp8_f32(sat8(a), sat8(b), r, false); r = __builtin_amdgcn_cvt_pk_fp8_f32(sat8(c), sat8(d), r, true); return (unsigned)r; }
; DI float sigmoidf_(float x) { return __builtin_amdgcn_rcpf(1.0f + __builtin_amdgcn_exp2f(-1.4426950408889634f * x)); }
;     DI void operator()(const f32x4 (&acc)[2][2][4][2], const Unit& u, int wr, int wc, int fr, int fq) const {
;     ...
;             for (int p2 = 0; p2 < 2; ++p2) { const size_t row0 = (size_t)u.pm * 256 + 128 * ai + 64 * wr + 32 * p2 + fr; u32x2 w[2];
; #pragma unroll
;                 for (int r2 = 0; r2 < 2; ++r2) { const int m = 2 * p2 + r2; f32x4 a = acc[ai][0][m][0], b = acc[ai][0][m][1]; const f32x4 ga = acc[ai][1][m][0], gb = acc[ai][1][m][1];
; #pragma unroll
;                     for (int q = 0; q < 4; ++q) { a[q] *= AZ8_SCALE * sigmoidf_(ga[q]); b[q] *= AZ8_SCALE * sigmoidf_(gb[q]); }
;                     w[r2].x = pk4_fp8(a[0], a[1], a[2], a[3]); w[r2].y = pk4_fp8(b[0], b[1], b[2], b[3]); }
;                 const size_t c = (size_t)(AW + u.pn * 128 + 32 * wc + 8 * fq);
;                 store_pair8(z, row0 * D + c, (row0 + 16) * D + c, w[0], w[1], oddq); }
	v_med3_f32 v0, v0, s53, v204
	v_med3_f32 v38, v38, s53, v204
	v_mov_b32_e32 v52, v1
	v_mul_f32_e32 v18, 0xbfb8aa3b, v18
	v_cvt_pk_fp8_f32 v52, v0, v38
	v_med3_f32 v34, v34, s53, v204
	v_med3_f32 v35, v35, s53, v204
	v_mov_b32_e32 v53, v1
	v_exp_f32_e32 v18, v18
	v_mul_f32_e32 v39, 0x41000000, v39
	v_mul_f32_e32 v40, 0x41000000, v40
	v_cvt_pk_fp8_f32 v53, v34, v35
	v_mul_f32_e32 v39, v48, v39
	v_mul_f32_e32 v36, 0x41000000, v36
	v_mul_f32_e32 v40, v49, v40
	v_mul_f32_e32 v37, 0x41000000, v37
	v_mul_f32_e32 v36, v44, v36
	v_mul_f32_e32 v37, v45, v37
	v_med3_f32 v0, v39, s53, v204
	v_med3_f32 v38, v40, s53, v204
	v_cvt_pk_fp8_f32 v52, v0, v38 op_sel:[0,0,1]
	v_med3_f32 v0, v36, s53, v204
	v_med3_f32 v34, v37, s53, v204
	v_add_f32_e32 v18, 1.0, v18
	v_cvt_pk_fp8_f32 v53, v0, v34 op_sel:[0,0,1]
	v_mul_f32_e32 v0, 0xbfb8aa3b, v22
	v_rcp_f32_e32 v18, v18
	v_mul_f32_e32 v22, 0xbfb8aa3b, v23
	v_exp_f32_e32 v22, v22
	v_exp_f32_e32 v0, v0
	v_mul_f32_e32 v18, 0x41000000, v18
	v_mul_f32_e32 v23, v26, v18
	v_add_f32_e32 v18, 1.0, v22
	v_mul_f32_e32 v22, 0xbfb8aa3b, v24
	v_mul_f32_e32 v24, 0xbfb8aa3b, v25
	v_add_f32_e32 v0, 1.0, v0
	v_mul_f32_e32 v19, 0xbfb8aa3b, v19
	v_exp_f32_e32 v22, v22
	v_exp_f32_e32 v24, v24
	v_mul_f32_e32 v21, 0xbfb8aa3b, v21
	v_rcp_f32_e32 v0, v0
	v_exp_f32_e32 v19, v19
	v_rcp_f32_e32 v18, v18
	v_exp_f32_e32 v21, v21
	v_add_f32_e32 v22, 1.0, v22
	v_mul_f32_e32 v20, 0xbfb8aa3b, v20
	v_add_f32_e32 v24, 1.0, v24
	v_mul_f32_e32 v0, 0x41000000, v0
	v_add_f32_e32 v19, 1.0, v19
	v_mul_f32_e32 v18, 0x41000000, v18
	v_rcp_f32_e32 v22, v22
	v_exp_f32_e32 v20, v20
	v_rcp_f32_e32 v24, v24
	v_add_f32_e32 v21, 1.0, v21
	v_mul_f32_e32 v0, v30, v0
	v_rcp_f32_e32 v19, v19
	v_mul_f32_e32 v18, v31, v18
	v_rcp_f32_e32 v21, v21
	v_med3_f32 v0, v0, s53, v204
	v_med3_f32 v25, v18, s53, v204
	v_mov_b32_e32 v18, v1
	v_mul_f32_e32 v6, 0xbfb8aa3b, v6
	v_cvt_pk_fp8_f32 v18, v0, v25
	v_exp_f32_e32 v6, v6
	v_mul_f32_e32 v22, 0x41000000, v22
	v_add_f32_e32 v20, 1.0, v20
	v_mul_f32_e32 v24, 0x41000000, v24
	v_mul_f32_e32 v19, 0x41000000, v19
	v_mul_f32_e32 v22, v32, v22
	v_rcp_f32_e32 v20, v20
	v_mul_f32_e32 v24, v33, v24
	v_mul_f32_e32 v21, 0x41000000, v21
	v_mul_f32_e32 v19, v27, v19
	v_mul_f32_e32 v0, v29, v21
	v_med3_f32 v21, v22, s53, v204
	v_med3_f32 v22, v24, s53, v204
	v_cvt_pk_fp8_f32 v18, v21, v22 op_sel:[0,0,1]
	v_med3_f32 v21, v23, s53, v204
	v_med3_f32 v22, v19, s53, v204
	v_mov_b32_e32 v19, v1
	v_add_f32_e32 v6, 1.0, v6
	v_cvt_pk_fp8_f32 v19, v21, v22
	v_rcp_f32_e32 v6, v6
	v_mul_f32_e32 v20, 0x41000000, v20
	v_mul_f32_e32 v20, v28, v20
	v_med3_f32 v20, v20, s53, v204
	v_med3_f32 v0, v0, s53, v204
	v_cvt_pk_fp8_f32 v19, v20, v0 op_sel:[0,0,1]
	v_mul_f32_e32 v0, 0x41000000, v6
	v_mul_f32_e32 v6, 0xbfb8aa3b, v7
	v_mul_f32_e32 v2, 0xbfb8aa3b, v2
	v_exp_f32_e32 v6, v6
	v_mul_f32_e32 v3, 0xbfb8aa3b, v3
	v_exp_f32_e32 v2, v2
	v_exp_f32_e32 v3, v3
	v_mul_f32_e32 v7, 0xbfb8aa3b, v8
	v_mul_f32_e32 v8, 0xbfb8aa3b, v9
	v_add_f32_e32 v6, 1.0, v6
	v_exp_f32_e32 v7, v7
	v_mul_f32_e32 v4, 0xbfb8aa3b, v4
	v_exp_f32_e32 v8, v8
	v_mul_f32_e32 v5, 0xbfb8aa3b, v5
	v_add_f32_e32 v2, 1.0, v2
	v_rcp_f32_e32 v6, v6
	v_add_f32_e32 v3, 1.0, v3
	v_exp_f32_e32 v4, v4
	v_exp_f32_e32 v5, v5
	v_rcp_f32_e32 v2, v2
	v_rcp_f32_e32 v3, v3
	v_add_f32_e32 v7, 1.0, v7
	v_add_f32_e32 v8, 1.0, v8
	v_mul_f32_e32 v6, 0x41000000, v6
	v_rcp_f32_e32 v7, v7
	v_add_f32_e32 v4, 1.0, v4
	v_rcp_f32_e32 v8, v8
	v_add_f32_e32 v5, 1.0, v5
	v_mul_f32_e32 v0, v14, v0
	v_mul_f32_e32 v2, 0x41000000, v2
	v_mul_f32_e32 v6, v15, v6
	v_mul_f32_e32 v3, 0x41000000, v3
	v_rcp_f32_e32 v4, v4
	v_rcp_f32_e32 v5, v5
	v_mul_f32_e32 v2, v10, v2
	v_mul_f32_e32 v3, v11, v3
	v_med3_f32 v0, v0, s53, v204
	v_med3_f32 v6, v6, s53, v204
	v_mov_b32_e32 v20, v1
	v_cvt_pk_fp8_f32 v20, v0, v6
	v_med3_f32 v2, v2, s53, v204
	v_med3_f32 v3, v3, s53, v204
	v_mov_b32_e32 v21, v1
	v_ashrrev_i32_e32 v137, 31, v136
	v_lshlrev_b64 v[98:99], 10, v[134:135]
	v_mul_f32_e32 v7, 0x41000000, v7
	v_mul_f32_e32 v8, 0x41000000, v8
	v_cvt_pk_fp8_f32 v21, v2, v3
	v_lshl_add_u64 v[98:99], v[98:99], 0, v[136:137]
	s_mov_b64 s[0:1], 0x3ff8
	v_mul_f32_e32 v7, v16, v7
	v_mul_f32_e32 v4, 0x41000000, v4
	v_mul_f32_e32 v8, v17, v8
	v_mul_f32_e32 v5, 0x41000000, v5
	v_lshl_add_u64 v[100:101], v[98:99], 0, s[0:1]
	s_mov_b64 s[0:1], 0x8000
	v_mul_f32_e32 v4, v12, v4
	v_mul_f32_e32 v5, v13, v5
	v_med3_f32 v0, v7, s53, v204
	v_med3_f32 v6, v8, s53, v204
	v_lshl_add_u64 v[66:67], v[98:99], 0, s[0:1]
	s_mov_b64 s[0:1], 0xbff8
	v_cvt_pk_fp8_f32 v20, v0, v6 op_sel:[0,0,1]
	v_med3_f32 v0, v4, s53, v204
	v_med3_f32 v2, v5, s53, v204
	v_lshl_add_u64 v[68:69], v[98:99], 0, s[0:1]
	s_mov_b64 s[0:1], 0x23ff8
	v_cvt_pk_fp8_f32 v21, v0, v2 op_sel:[0,0,1]
	v_lshl_add_u64 v[36:37], v[98:99], 0, s[0:1]
	s_mov_b64 s[0:1], 0x2bff8
	v_cmp_eq_u32_e32 vcc, 0, v138
	v_lshl_add_u64 v[34:35], v[98:99], 0, s[80:81]
	v_lshl_add_u64 v[2:3], v[98:99], 0, s[68:69]
	v_lshl_add_u64 v[4:5], v[98:99], 0, s[0:1]
	v_cndmask_b32_e32 v101, v101, v99, vcc
	v_cndmask_b32_e32 v100, v100, v98, vcc
	v_cndmask_b32_e32 v67, v69, v67, vcc
	v_cndmask_b32_e32 v66, v68, v66, vcc
	v_cndmask_b32_e32 v35, v37, v35, vcc
	v_cndmask_b32_e32 v34, v36, v34, vcc
	v_cndmask_b32_e32 v3, v5, v3, vcc
	v_cndmask_b32_e32 v2, v4, v2, vcc
	v_permlane16_swap_b32_e32 v114, v116
	v_permlane16_swap_b32_e32 v115, v117
	v_lshl_add_u64 v[100:101], s[8:9], 0, v[100:101]
	v_permlane16_swap_b32_e32 v82, v84
	v_permlane16_swap_b32_e32 v83, v85
	v_lshl_add_u64 v[66:67], s[8:9], 0, v[66:67]
	v_permlane16_swap_b32_e32 v50, v52
	v_permlane16_swap_b32_e32 v51, v53
	v_lshl_add_u64 v[34:35], s[8:9], 0, v[34:35]
	v_permlane16_swap_b32_e32 v18, v20
	v_permlane16_swap_b32_e32 v19, v21
	v_lshl_add_u64 v[2:3], s[8:9], 0, v[2:3]
	s_andn2_b64 vcc, exec, s[4:5]
	s_mov_b64 s[2:3], -1
	global_store_dwordx4 v[100:101], v[114:117], off sc1
	global_store_dwordx4 v[66:67], v[82:85], off sc1
	global_store_dwordx4 v[34:35], v[50:53], off sc1
	global_store_dwordx4 v[2:3], v[18:21], off sc1
	s_cbranch_vccnz .LBB0_826
	s_andn2_b64 vcc, exec, s[6:7]
	s_cbranch_vccnz .LBB0_825
	s_barrier
	s_branch .LBB0_825

; DI unsigned pk4_fp8(float a, float b, float c, float d) { int r = 0; r = __builtin_amdgcn_cvt_pk_fp8_f32(sat8(a), sat8(b), r, false); r = __builtin_amdgcn_cvt_pk_fp8_f32(sat8(c), sat8(d), r, true); return (unsigned)r; }
;     DI void operator()(const f32x4 (&acc)[2][2][4][2], const Unit& u, int wr, int wc, int fr, int fq) const {
;     ...
;             u32x2 gs[4][2];
; #pragma unroll
;             for (int m = 0; m < 4; ++m) { const size_t row = (size_t)u.pm * 256 + 128 * ai + 64 * wr + 16 * m + fr;
; #pragma unroll
;                 for (int bj = 0; bj < 2; ++bj) gs[m][bj] = *(const u32x2*)(gssm + row * D + u.pn * 256 + bj * 128 + 32 * wc + 8 * fq); }
;             asm volatile("" ::: "memory");
; #pragma unroll
;             for (int p2 = 0; p2 < 2; ++p2) { const size_t row0 = (size_t)u.pm * 256 + 128 * ai + 64 * wr + 32 * p2 + fr;
; #pragma unroll
;                 for (int bj = 0; bj < 2; ++bj) { u32x2 wq[2];
; #pragma unroll
;                     for (int r2 = 0; r2 < 2; ++r2) { const int m = 2 * p2 + r2; f32x4 sa, sb;
; #pragma unroll
;                         for (int q = 0; q < 4; ++q) { sa[q] = (MRG8_SCALE / (W8_SCALE * AZ8_SCALE)) * t1[(gs[m][bj].x >> (8 * q)) & 255u]; sb[q] = (MRG8_SCALE / (W8_SCALE * AZ8_SCALE)) * t1[(gs[m][bj].y >> (8 * q)) & 255u]; }
;                         const f32x4 va = acc[ai][bj][m][0] * sa, vb = acc[ai][bj][m][1] * sb;
;                         wq[r2].x = pk4_fp8(va[0], va[1], va[2], va[3]); wq[r2].y = pk4_fp8(vb[0], vb[1], vb[2], vb[3]); }
;                     const size_t c = (size_t)(u.pn * 256 + bj * 128 + 32 * wc + 8 * fq);
;                     store_pair8(mrg, row0 * D + c, (row0 + 16) * D + c, wq[0], wq[1], (fq & 1) != 0); } }
.LBB0_910:
	s_mov_b32 s0, -1
	s_mov_b32 s1, s37
	s_nop 0
	v_mbcnt_lo_u32_b32 v0, s0, 0
	v_mbcnt_hi_u32_b32 v0, s0, v0
	s_lshl_b32 s0, s1, 4
	s_andn2_b32 s0, s0, 63
	s_ashr_i32 s2, s0, 31
	s_add_u32 s0, s26, s0
	s_addc_u32 s2, s27, s2
	v_and_or_b32 v132, v0, 15, s0
	s_lshl_b32 s0, s1, 5
	s_and_b32 s0, s0, 0x60
	v_ashrrev_i32_e32 v2, 1, v0
	v_and_b32_e32 v134, -8, v2
	s_or_b32 s1, s0, s9
	v_add_u32_e32 v2, s1, v134
	s_add_u32 s1, s14, s9
	v_mov_b32_e32 v133, s2
	s_addc_u32 s2, s15, s19
	s_add_u32 s0, s1, s0
	v_ashrrev_i32_e32 v135, 31, v134
	s_addc_u32 s1, s2, 0
	v_lshl_add_u64 v[136:137], s[0:1], 0, v[134:135]
	v_lshlrev_b64 v[132:133], 10, v[132:133]
	v_lshl_add_u64 v[134:135], v[136:137], 0, v[132:133]
	global_load_dwordx2 v[154:155], v[134:135], off
	global_load_dwordx2 v[148:149], v[134:135], off offset:128
	s_movk_i32 s0, 0x4000
	v_add_co_u32_e64 v138, s[6:7], s0, v134
	v_or_b32_e32 v140, 0x8000, v132
	s_nop 0
	v_addc_co_u32_e64 v139, s[6:7], 0, v135, s[6:7]
	global_load_dwordx2 v[152:153], v[138:139], off
	global_load_dwordx2 v[146:147], v[138:139], off offset:128
	v_mov_b32_e32 v141, v133
	v_lshl_add_u64 v[136:137], v[136:137], 0, v[140:141]
	s_mov_b32 s0, 0xc000
	v_and_b32_e32 v0, 16, v0
	global_load_dwordx2 v[144:145], v[136:137], off
	global_load_dwordx2 v[138:139], v[136:137], off offset:128
	v_add_co_u32_e64 v136, s[6:7], s0, v134
	v_cmp_eq_u32_e32 vcc, 0, v0
	s_nop 0
	v_addc_co_u32_e64 v137, s[6:7], 0, v135, s[6:7]
	s_add_i32 s2, 0, 0x20400
	global_load_dwordx2 v[142:143], v[136:137], off
	s_nop 0
	global_load_dwordx2 v[136:137], v[136:137], off offset:128
	s_mov_b64 s[0:1], 0x3ff8
	v_lshl_add_u64 v[150:151], v[132:133], 0, s[0:1]
	s_mov_b64 s[0:1], 0xbff8
	s_waitcnt vmcnt(0)
	v_and_b32_e32 v0, 0xff, v154
	v_lshl_add_u32 v0, v0, 2, s2
	ds_read_b32 v156, v0
	v_and_b32_e32 v0, 0xff, v155
	v_lshl_add_u32 v0, v0, 2, s2
	ds_read_b32 v158, v0
	v_bfe_u32 v0, v154, 8, 8
	v_lshl_add_u32 v0, v0, 2, s2
	ds_read_b32 v157, v0
	v_bfe_u32 v0, v155, 8, 8
	v_lshl_add_u32 v0, v0, 2, s2
	ds_read_b32 v159, v0
	v_bfe_u32 v0, v154, 16, 8
	v_lshl_add_u32 v0, v0, 2, s2
	ds_read_b32 v160, v0
	v_bfe_u32 v0, v155, 16, 8
	v_lshl_add_u32 v0, v0, 2, s2
	ds_read_b32 v162, v0
	v_lshrrev_b32_e32 v0, 24, v154
	v_lshl_add_u32 v0, v0, 2, s2
	ds_read_b32 v161, v0
	s_waitcnt lgkmcnt(4)
	v_pk_mul_f32 v[156:157], v[156:157], s[92:93] op_sel_hi:[1,0]
	v_lshrrev_b32_e32 v0, 24, v155
	v_lshl_add_u32 v0, v0, 2, s2
	s_waitcnt lgkmcnt(3)
	v_pk_mul_f32 v[154:155], v[158:159], s[92:93] op_sel_hi:[1,0]
	v_pk_mul_f32 v[128:129], v[128:129], v[156:157]
	ds_read_b32 v163, v0
	v_pk_mul_f32 v[154:155], v[124:125], v[154:155]
	v_med3_f32 v0, v128, s53, v204
	v_med3_f32 v3, v129, s53, v204
	v_mov_b32_e32 v124, v1
	v_cvt_pk_fp8_f32 v124, v0, v3
	s_waitcnt lgkmcnt(1)
	v_pk_mul_f32 v[160:161], v[160:161], s[92:93] op_sel_hi:[1,0]
	v_mov_b32_e32 v125, v1
	v_pk_mul_f32 v[130:131], v[130:131], v[160:161]
	s_waitcnt lgkmcnt(0)
	v_pk_mul_f32 v[158:159], v[162:163], s[92:93] op_sel_hi:[1,0]
	v_med3_f32 v0, v130, s53, v204
	v_med3_f32 v3, v131, s53, v204
	v_cvt_pk_fp8_f32 v124, v0, v3 op_sel:[0,0,1]
	v_med3_f32 v0, v154, s53, v204
	v_med3_f32 v3, v155, s53, v204
	v_cvt_pk_fp8_f32 v125, v0, v3
	v_pk_mul_f32 v[126:127], v[126:127], v[158:159]
	s_nop 0
	v_med3_f32 v0, v126, s53, v204
	v_med3_f32 v3, v127, s53, v204
	v_cvt_pk_fp8_f32 v125, v0, v3 op_sel:[0,0,1]
	v_and_b32_e32 v0, 0xff, v152
	v_lshl_add_u32 v0, v0, 2, s2
	ds_read_b32 v126, v0
	v_and_b32_e32 v0, 0xff, v153
	v_lshl_add_u32 v0, v0, 2, s2
	ds_read_b32 v128, v0
	v_bfe_u32 v0, v152, 8, 8
	v_lshl_add_u32 v0, v0, 2, s2
	ds_read_b32 v127, v0
	v_bfe_u32 v0, v153, 8, 8
	v_lshl_add_u32 v0, v0, 2, s2
	ds_read_b32 v129, v0
	v_bfe_u32 v0, v152, 16, 8
	v_lshl_add_u32 v0, v0, 2, s2
	ds_read_b32 v130, v0
	v_bfe_u32 v0, v153, 16, 8
	v_lshl_add_u32 v0, v0, 2, s2
	ds_read_b32 v154, v0
	v_lshrrev_b32_e32 v0, 24, v152
	v_lshl_add_u32 v0, v0, 2, s2
	ds_read_b32 v131, v0
	s_waitcnt lgkmcnt(4)
	v_pk_mul_f32 v[126:127], v[126:127], s[92:93] op_sel_hi:[1,0]
	v_lshrrev_b32_e32 v0, 24, v153
	v_lshl_add_u32 v0, v0, 2, s2
	v_pk_mul_f32 v[120:121], v[120:121], v[126:127]
	ds_read_b32 v155, v0
	v_med3_f32 v0, v120, s53, v204
	v_med3_f32 v3, v121, s53, v204
	v_mov_b32_e32 v126, v1
	v_cvt_pk_fp8_f32 v126, v0, v3
	s_waitcnt lgkmcnt(1)
	v_pk_mul_f32 v[130:131], v[130:131], s[92:93] op_sel_hi:[1,0]
	v_pk_mul_f32 v[128:129], v[128:129], s[92:93] op_sel_hi:[1,0]
	v_pk_mul_f32 v[122:123], v[122:123], v[130:131]
	v_pk_mul_f32 v[116:117], v[116:117], v[128:129]
	v_med3_f32 v0, v122, s53, v204
	v_med3_f32 v3, v123, s53, v204
	v_cvt_pk_fp8_f32 v126, v0, v3 op_sel:[0,0,1]
	v_med3_f32 v0, v116, s53, v204
	v_med3_f32 v3, v117, s53, v204
	v_mov_b32_e32 v127, v1
	v_cvt_pk_fp8_f32 v127, v0, v3
	s_waitcnt lgkmcnt(0)
	v_pk_mul_f32 v[152:153], v[154:155], s[92:93] op_sel_hi:[1,0]
	v_cndmask_b32_e32 v117, v151, v133, vcc
	v_pk_mul_f32 v[118:119], v[118:119], v[152:153]
	v_cndmask_b32_e32 v116, v150, v132, vcc
	v_med3_f32 v0, v118, s53, v204
	v_med3_f32 v3, v119, s53, v204
	v_cvt_pk_fp8_f32 v127, v0, v3 op_sel:[0,0,1]
	v_ashrrev_i32_e32 v3, 31, v2
	v_lshl_add_u64 v[116:117], s[10:11], 0, v[116:117]
	v_and_b32_e32 v0, 0xff, v148
	v_permlane16_swap_b32_e32 v124, v126
	v_permlane16_swap_b32_e32 v125, v127
	v_lshl_add_u64 v[118:119], v[116:117], 0, v[2:3]
	v_lshl_add_u32 v0, v0, 2, s2
	global_store_dwordx4 v[118:119], v[124:127], off sc1
	ds_read_b32 v118, v0
	v_and_b32_e32 v0, 0xff, v149
	v_lshl_add_u32 v0, v0, 2, s2
	ds_read_b32 v120, v0
	v_bfe_u32 v0, v148, 8, 8
	v_lshl_add_u32 v0, v0, 2, s2
	ds_read_b32 v119, v0
	v_bfe_u32 v0, v149, 8, 8
	v_lshl_add_u32 v0, v0, 2, s2
	ds_read_b32 v121, v0
	v_bfe_u32 v0, v148, 16, 8
	v_lshl_add_u32 v0, v0, 2, s2
	ds_read_b32 v122, v0
	v_bfe_u32 v0, v149, 16, 8
	v_lshl_add_u32 v0, v0, 2, s2
	ds_read_b32 v124, v0
	v_lshrrev_b32_e32 v0, 24, v148
	v_lshl_add_u32 v0, v0, 2, s2
	ds_read_b32 v123, v0
	s_waitcnt lgkmcnt(4)
; DI unsigned pk4_fp8(float a, float b, float c, float d) { int r = 0; r = __builtin_amdgcn_cvt_pk_fp8_f32(sat8(a), sat8(b), r, false); r = __builtin_amdgcn_cvt_pk_fp8_f32(sat8(c), sat8(d), r, true); return (unsigned)r; }
;     DI void operator()(const f32x4 (&acc)[2][2][4][2], const Unit& u, int wr, int wc, int fr, int fq) const {
;     ...
;             for (int p2 = 0; p2 < 2; ++p2) { const size_t row0 = (size_t)u.pm * 256 + 128 * ai + 64 * wr + 32 * p2 + fr;
; #pragma unroll
;                 for (int bj = 0; bj < 2; ++bj) { u32x2 wq[2];
; #pragma unroll
;                     for (int r2 = 0; r2 < 2; ++r2) { const int m = 2 * p2 + r2; f32x4 sa, sb;
; #pragma unroll
;                         for (int q = 0; q < 4; ++q) { sa[q] = (MRG8_SCALE / (W8_SCALE * AZ8_SCALE)) * t1[(gs[m][bj].x >> (8 * q)) & 255u]; sb[q] = (MRG8_SCALE / (W8_SCALE * AZ8_SCALE)) * t1[(gs[m][bj].y >> (8 * q)) & 255u]; }
;                         const f32x4 va = acc[ai][bj][m][0] * sa, vb = acc[ai][bj][m][1] * sb;
;                         wq[r2].x = pk4_fp8(va[0], va[1], va[2], va[3]); wq[r2].y = pk4_fp8(vb[0], vb[1], vb[2], vb[3]); }
;                     const size_t c = (size_t)(u.pn * 256 + bj * 128 + 32 * wc + 8 * fq);
;                     store_pair8(mrg, row0 * D + c, (row0 + 16) * D + c, wq[0], wq[1], (fq & 1) != 0); } }
	v_pk_mul_f32 v[118:119], v[118:119], s[92:93] op_sel_hi:[1,0]
	v_lshrrev_b32_e32 v0, 24, v149
	v_lshl_add_u32 v0, v0, 2, s2
	s_waitcnt lgkmcnt(3)
	v_pk_mul_f32 v[120:121], v[120:121], s[92:93] op_sel_hi:[1,0]
	v_pk_mul_f32 v[112:113], v[112:113], v[118:119]
	ds_read_b32 v125, v0
	v_pk_mul_f32 v[118:119], v[108:109], v[120:121]
	v_med3_f32 v0, v112, s53, v204
	v_med3_f32 v109, v113, s53, v204
	v_mov_b32_e32 v108, v1
	v_cvt_pk_fp8_f32 v108, v0, v109
	s_waitcnt lgkmcnt(1)
	v_pk_mul_f32 v[122:123], v[122:123], s[92:93] op_sel_hi:[1,0]
	v_med3_f32 v112, v119, s53, v204
	v_pk_mul_f32 v[114:115], v[114:115], v[122:123]
	s_waitcnt lgkmcnt(0)
	v_pk_mul_f32 v[124:125], v[124:125], s[92:93] op_sel_hi:[1,0]
	v_med3_f32 v0, v114, s53, v204
	v_med3_f32 v109, v115, s53, v204
	v_cvt_pk_fp8_f32 v108, v0, v109 op_sel:[0,0,1]
	v_med3_f32 v0, v118, s53, v204
	v_mov_b32_e32 v109, v1
	v_cvt_pk_fp8_f32 v109, v0, v112
	v_pk_mul_f32 v[110:111], v[110:111], v[124:125]
	s_nop 0
	v_med3_f32 v0, v110, s53, v204
	v_med3_f32 v110, v111, s53, v204
	v_cvt_pk_fp8_f32 v109, v0, v110 op_sel:[0,0,1]
	v_and_b32_e32 v0, 0xff, v146
	v_lshl_add_u32 v0, v0, 2, s2
	ds_read_b32 v110, v0
	v_and_b32_e32 v0, 0xff, v147
	v_lshl_add_u32 v0, v0, 2, s2
	ds_read_b32 v112, v0
	v_bfe_u32 v0, v146, 8, 8
	v_lshl_add_u32 v0, v0, 2, s2
	ds_read_b32 v111, v0
	v_bfe_u32 v0, v147, 8, 8
	v_lshl_add_u32 v0, v0, 2, s2
	ds_read_b32 v113, v0
	v_bfe_u32 v0, v146, 16, 8
	v_lshl_add_u32 v0, v0, 2, s2
	ds_read_b32 v114, v0
	v_bfe_u32 v0, v147, 16, 8
	v_lshl_add_u32 v0, v0, 2, s2
	ds_read_b32 v118, v0
	v_lshrrev_b32_e32 v0, 24, v146
	v_lshl_add_u32 v0, v0, 2, s2
	ds_read_b32 v115, v0
	s_waitcnt lgkmcnt(4)
	v_pk_mul_f32 v[110:111], v[110:111], s[92:93] op_sel_hi:[1,0]
	v_lshrrev_b32_e32 v0, 24, v147
	v_lshl_add_u32 v0, v0, 2, s2
	v_pk_mul_f32 v[104:105], v[104:105], v[110:111]
	ds_read_b32 v119, v0
	v_med3_f32 v0, v104, s53, v204
	v_med3_f32 v104, v105, s53, v204
	v_mov_b32_e32 v110, v1
	v_cvt_pk_fp8_f32 v110, v0, v104
	s_waitcnt lgkmcnt(1)
	v_pk_mul_f32 v[114:115], v[114:115], s[92:93] op_sel_hi:[1,0]
	v_pk_mul_f32 v[112:113], v[112:113], s[92:93] op_sel_hi:[1,0]
	v_pk_mul_f32 v[106:107], v[106:107], v[114:115]
	v_pk_mul_f32 v[100:101], v[100:101], v[112:113]
	v_med3_f32 v0, v106, s53, v204
	v_med3_f32 v104, v107, s53, v204
	v_cvt_pk_fp8_f32 v110, v0, v104 op_sel:[0,0,1]
	v_med3_f32 v0, v100, s53, v204
	v_med3_f32 v100, v101, s53, v204
	v_mov_b32_e32 v111, v1
	v_cvt_pk_fp8_f32 v111, v0, v100
	s_waitcnt lgkmcnt(0)
	v_pk_mul_f32 v[118:119], v[118:119], s[92:93] op_sel_hi:[1,0]
	v_permlane16_swap_b32_e32 v108, v110
	v_pk_mul_f32 v[102:103], v[102:103], v[118:119]
	s_nop 0
	v_med3_f32 v0, v102, s53, v204
	v_med3_f32 v100, v103, s53, v204
	v_cvt_pk_fp8_f32 v111, v0, v100 op_sel:[0,0,1]
	v_and_b32_e32 v0, 0xff, v144
	v_lshl_add_u32 v0, v0, 2, s2
	ds_read_b32 v104, v0
	v_and_b32_e32 v0, 0xff, v145
	v_lshl_add_u32 v0, v0, 2, s2
	ds_read_b32 v106, v0
	v_bfe_u32 v0, v144, 8, 8
	v_lshl_add_u32 v0, v0, 2, s2
	ds_read_b32 v105, v0
	v_bfe_u32 v0, v145, 8, 8
	v_add_u32_e32 v100, 0x80, v2
	v_lshl_add_u32 v0, v0, 2, s2
	v_ashrrev_i32_e32 v101, 31, v100
	ds_read_b32 v107, v0
	v_bfe_u32 v0, v144, 16, 8
	v_permlane16_swap_b32_e32 v109, v111
	v_lshl_add_u64 v[102:103], v[116:117], 0, v[100:101]
	v_lshl_add_u32 v0, v0, 2, s2
	global_store_dwordx4 v[102:103], v[108:111], off sc1
	ds_read_b32 v108, v0
	v_bfe_u32 v0, v145, 16, 8
	v_lshl_add_u32 v0, v0, 2, s2
	ds_read_b32 v110, v0
	v_lshrrev_b32_e32 v0, 24, v144
	v_lshl_add_u32 v0, v0, 2, s2
	ds_read_b32 v109, v0
	s_waitcnt lgkmcnt(4)
	v_pk_mul_f32 v[104:105], v[104:105], s[92:93] op_sel_hi:[1,0]
	v_lshrrev_b32_e32 v0, 24, v145
	v_lshl_add_u32 v0, v0, 2, s2
	s_waitcnt lgkmcnt(3)
	v_pk_mul_f32 v[106:107], v[106:107], s[92:93] op_sel_hi:[1,0]
	v_pk_mul_f32 v[96:97], v[96:97], v[104:105]
	ds_read_b32 v111, v0
	v_pk_mul_f32 v[104:105], v[92:93], v[106:107]
	v_med3_f32 v0, v96, s53, v204
	v_med3_f32 v93, v97, s53, v204
	v_mov_b32_e32 v92, v1
	v_cvt_pk_fp8_f32 v92, v0, v93
	s_waitcnt lgkmcnt(1)
	v_pk_mul_f32 v[108:109], v[108:109], s[92:93] op_sel_hi:[1,0]
	v_med3_f32 v96, v105, s53, v204
	v_pk_mul_f32 v[98:99], v[98:99], v[108:109]
	s_waitcnt lgkmcnt(0)
	v_pk_mul_f32 v[110:111], v[110:111], s[92:93] op_sel_hi:[1,0]
	v_med3_f32 v0, v98, s53, v204
	v_med3_f32 v93, v99, s53, v204
	v_cvt_pk_fp8_f32 v92, v0, v93 op_sel:[0,0,1]
	v_med3_f32 v0, v104, s53, v204
	v_mov_b32_e32 v93, v1
	v_cvt_pk_fp8_f32 v93, v0, v96
	v_pk_mul_f32 v[94:95], v[94:95], v[110:111]
	v_lshl_add_u64 v[102:103], v[132:133], 0, s[0:1]
	v_med3_f32 v0, v94, s53, v204
	v_med3_f32 v94, v95, s53, v204
	v_cvt_pk_fp8_f32 v93, v0, v94 op_sel:[0,0,1]
	v_and_b32_e32 v0, 0xff, v142
	v_lshl_add_u32 v0, v0, 2, s2
	ds_read_b32 v94, v0
	v_and_b32_e32 v0, 0xff, v143
	v_lshl_add_u32 v0, v0, 2, s2
	ds_read_b32 v96, v0
	v_bfe_u32 v0, v142, 8, 8
	v_lshl_add_u32 v0, v0, 2, s2
	ds_read_b32 v95, v0
	v_bfe_u32 v0, v143, 8, 8
	v_lshl_add_u32 v0, v0, 2, s2
	ds_read_b32 v97, v0
	v_bfe_u32 v0, v142, 16, 8
	v_lshl_add_u32 v0, v0, 2, s2
	ds_read_b32 v98, v0
	v_bfe_u32 v0, v143, 16, 8
	v_lshl_add_u32 v0, v0, 2, s2
	ds_read_b32 v104, v0
	v_lshrrev_b32_e32 v0, 24, v142
	v_lshl_add_u32 v0, v0, 2, s2
	ds_read_b32 v99, v0
	s_waitcnt lgkmcnt(4)
	v_pk_mul_f32 v[94:95], v[94:95], s[92:93] op_sel_hi:[1,0]
	v_lshrrev_b32_e32 v0, 24, v143
	v_lshl_add_u32 v0, v0, 2, s2
	v_pk_mul_f32 v[88:89], v[88:89], v[94:95]
	ds_read_b32 v105, v0
	v_med3_f32 v0, v88, s53, v204
	v_med3_f32 v88, v89, s53, v204
	v_mov_b32_e32 v94, v1
	v_cvt_pk_fp8_f32 v94, v0, v88
	s_waitcnt lgkmcnt(1)
; DI unsigned pk4_fp8(float a, float b, float c, float d) { int r = 0; r = __builtin_amdgcn_cvt_pk_fp8_f32(sat8(a), sat8(b), r, false); r = __builtin_amdgcn_cvt_pk_fp8_f32(sat8(c), sat8(d), r, true); return (unsigned)r; }
;     DI void operator()(const f32x4 (&acc)[2][2][4][2], const Unit& u, int wr, int wc, int fr, int fq) const {
;     ...
;             u32x2 gs[4][2];
; #pragma unroll
;             for (int m = 0; m < 4; ++m) { const size_t row = (size_t)u.pm * 256 + 128 * ai + 64 * wr + 16 * m + fr;
; #pragma unroll
;                 for (int bj = 0; bj < 2; ++bj) gs[m][bj] = *(const u32x2*)(gssm + row * D + u.pn * 256 + bj * 128 + 32 * wc + 8 * fq); }
;             asm volatile("" ::: "memory");
; #pragma unroll
;             for (int p2 = 0; p2 < 2; ++p2) { const size_t row0 = (size_t)u.pm * 256 + 128 * ai + 64 * wr + 32 * p2 + fr;
; #pragma unroll
;                 for (int bj = 0; bj < 2; ++bj) { u32x2 wq[2];
; #pragma unroll
;                     for (int r2 = 0; r2 < 2; ++r2) { const int m = 2 * p2 + r2; f32x4 sa, sb;
; #pragma unroll
;                         for (int q = 0; q < 4; ++q) { sa[q] = (MRG8_SCALE / (W8_SCALE * AZ8_SCALE)) * t1[(gs[m][bj].x >> (8 * q)) & 255u]; sb[q] = (MRG8_SCALE / (W8_SCALE * AZ8_SCALE)) * t1[(gs[m][bj].y >> (8 * q)) & 255u]; }
;                         const f32x4 va = acc[ai][bj][m][0] * sa, vb = acc[ai][bj][m][1] * sb;
;                         wq[r2].x = pk4_fp8(va[0], va[1], va[2], va[3]); wq[r2].y = pk4_fp8(vb[0], vb[1], vb[2], vb[3]); }
;                     const size_t c = (size_t)(u.pn * 256 + bj * 128 + 32 * wc + 8 * fq);
;                     store_pair8(mrg, row0 * D + c, (row0 + 16) * D + c, wq[0], wq[1], (fq & 1) != 0); } }
	v_pk_mul_f32 v[98:99], v[98:99], s[92:93] op_sel_hi:[1,0]
	v_pk_mul_f32 v[96:97], v[96:97], s[92:93] op_sel_hi:[1,0]
	v_pk_mul_f32 v[90:91], v[90:91], v[98:99]
	v_pk_mul_f32 v[84:85], v[84:85], v[96:97]
	v_med3_f32 v0, v90, s53, v204
	v_med3_f32 v88, v91, s53, v204
	v_cvt_pk_fp8_f32 v94, v0, v88 op_sel:[0,0,1]
	v_med3_f32 v0, v84, s53, v204
	v_med3_f32 v84, v85, s53, v204
	v_mov_b32_e32 v95, v1
	v_cvt_pk_fp8_f32 v95, v0, v84
	s_waitcnt lgkmcnt(0)
	v_pk_mul_f32 v[104:105], v[104:105], s[92:93] op_sel_hi:[1,0]
	v_cndmask_b32_e32 v85, v103, v133, vcc
	v_pk_mul_f32 v[86:87], v[86:87], v[104:105]
	v_permlane16_swap_b32_e32 v92, v94
	v_med3_f32 v0, v86, s53, v204
	v_med3_f32 v84, v87, s53, v204
	v_cvt_pk_fp8_f32 v95, v0, v84 op_sel:[0,0,1]
	v_cndmask_b32_e32 v84, v102, v140, vcc
	v_lshl_add_u64 v[84:85], s[10:11], 0, v[84:85]
	v_and_b32_e32 v0, 0xff, v138
	v_permlane16_swap_b32_e32 v93, v95
	v_lshl_add_u64 v[86:87], v[84:85], 0, v[2:3]
	v_lshl_add_u32 v0, v0, 2, s2
	global_store_dwordx4 v[86:87], v[92:95], off sc1
	ds_read_b32 v86, v0
	v_and_b32_e32 v0, 0xff, v139
	v_lshl_add_u32 v0, v0, 2, s2
	ds_read_b32 v88, v0
	v_bfe_u32 v0, v138, 8, 8
	v_lshl_add_u32 v0, v0, 2, s2
	ds_read_b32 v87, v0
	v_bfe_u32 v0, v139, 8, 8
	v_lshl_add_u32 v0, v0, 2, s2
	ds_read_b32 v89, v0
	v_bfe_u32 v0, v138, 16, 8
	v_lshl_add_u32 v0, v0, 2, s2
	ds_read_b32 v90, v0
	v_bfe_u32 v0, v139, 16, 8
	v_lshl_add_u32 v0, v0, 2, s2
	ds_read_b32 v92, v0
	v_lshrrev_b32_e32 v0, 24, v138
	v_lshl_add_u32 v0, v0, 2, s2
	ds_read_b32 v91, v0
	s_waitcnt lgkmcnt(4)
	v_pk_mul_f32 v[86:87], v[86:87], s[92:93] op_sel_hi:[1,0]
	v_lshrrev_b32_e32 v0, 24, v139
	v_lshl_add_u32 v0, v0, 2, s2
	s_waitcnt lgkmcnt(3)
	v_pk_mul_f32 v[88:89], v[88:89], s[92:93] op_sel_hi:[1,0]
	v_pk_mul_f32 v[80:81], v[80:81], v[86:87]
	ds_read_b32 v93, v0
	v_pk_mul_f32 v[86:87], v[76:77], v[88:89]
	v_med3_f32 v0, v80, s53, v204
	v_med3_f32 v77, v81, s53, v204
	v_mov_b32_e32 v76, v1
	v_cvt_pk_fp8_f32 v76, v0, v77
	s_waitcnt lgkmcnt(1)
	v_pk_mul_f32 v[90:91], v[90:91], s[92:93] op_sel_hi:[1,0]
	v_med3_f32 v80, v87, s53, v204
	v_pk_mul_f32 v[82:83], v[82:83], v[90:91]
	s_waitcnt lgkmcnt(0)
	v_pk_mul_f32 v[92:93], v[92:93], s[92:93] op_sel_hi:[1,0]
	v_med3_f32 v0, v82, s53, v204
	v_med3_f32 v77, v83, s53, v204
	v_cvt_pk_fp8_f32 v76, v0, v77 op_sel:[0,0,1]
	v_med3_f32 v0, v86, s53, v204
	v_mov_b32_e32 v77, v1
	v_cvt_pk_fp8_f32 v77, v0, v80
	v_pk_mul_f32 v[78:79], v[78:79], v[92:93]
	s_mov_b32 s0, 0x20000
	v_med3_f32 v0, v78, s53, v204
	v_med3_f32 v78, v79, s53, v204
	v_cvt_pk_fp8_f32 v77, v0, v78 op_sel:[0,0,1]
	v_and_b32_e32 v0, 0xff, v136
	v_lshl_add_u32 v0, v0, 2, s2
	ds_read_b32 v78, v0
	v_and_b32_e32 v0, 0xff, v137
	v_lshl_add_u32 v0, v0, 2, s2
	ds_read_b32 v80, v0
	v_bfe_u32 v0, v136, 8, 8
	v_lshl_add_u32 v0, v0, 2, s2
	ds_read_b32 v79, v0
	v_bfe_u32 v0, v137, 8, 8
	v_lshl_add_u32 v0, v0, 2, s2
	ds_read_b32 v81, v0
	v_bfe_u32 v0, v136, 16, 8
	v_lshl_add_u32 v0, v0, 2, s2
	ds_read_b32 v82, v0
	v_bfe_u32 v0, v137, 16, 8
	v_lshl_add_u32 v0, v0, 2, s2
	ds_read_b32 v86, v0
	v_lshrrev_b32_e32 v0, 24, v136
	v_lshl_add_u32 v0, v0, 2, s2
	ds_read_b32 v83, v0
	s_waitcnt lgkmcnt(4)
	v_pk_mul_f32 v[78:79], v[78:79], s[92:93] op_sel_hi:[1,0]
	v_lshrrev_b32_e32 v0, 24, v137
	v_lshl_add_u32 v0, v0, 2, s2
	v_pk_mul_f32 v[72:73], v[72:73], v[78:79]
	ds_read_b32 v87, v0
	v_med3_f32 v0, v72, s53, v204
	v_med3_f32 v72, v73, s53, v204
	v_mov_b32_e32 v78, v1
	v_cvt_pk_fp8_f32 v78, v0, v72
	s_waitcnt lgkmcnt(1)
	v_pk_mul_f32 v[82:83], v[82:83], s[92:93] op_sel_hi:[1,0]
	v_pk_mul_f32 v[80:81], v[80:81], s[92:93] op_sel_hi:[1,0]
	v_pk_mul_f32 v[74:75], v[74:75], v[82:83]
	v_pk_mul_f32 v[68:69], v[68:69], v[80:81]
	v_med3_f32 v0, v74, s53, v204
	v_med3_f32 v72, v75, s53, v204
	v_cvt_pk_fp8_f32 v78, v0, v72 op_sel:[0,0,1]
	v_med3_f32 v0, v68, s53, v204
	v_med3_f32 v68, v69, s53, v204
	v_mov_b32_e32 v79, v1
	v_cvt_pk_fp8_f32 v79, v0, v68
	s_waitcnt lgkmcnt(0)
	v_pk_mul_f32 v[86:87], v[86:87], s[92:93] op_sel_hi:[1,0]
	v_permlane16_swap_b32_e32 v76, v78
	v_pk_mul_f32 v[70:71], v[70:71], v[86:87]
	v_lshl_add_u64 v[82:83], v[132:133], 0, s[80:81]
	v_med3_f32 v0, v70, s53, v204
	v_med3_f32 v68, v71, s53, v204
	v_cvt_pk_fp8_f32 v79, v0, v68 op_sel:[0,0,1]
	v_lshl_add_u64 v[68:69], v[84:85], 0, v[100:101]
	v_add_co_u32_e64 v70, s[6:7], s0, v134
	v_permlane16_swap_b32_e32 v77, v79
	global_store_dwordx4 v[68:69], v[76:79], off sc1
	v_addc_co_u32_e64 v71, s[6:7], 0, v135, s[6:7]
	v_lshl_add_u64 v[68:69], v[134:135], 0, s[80:81]
	global_load_dwordx2 v[86:87], v[70:71], off
	global_load_dwordx2 v[80:81], v[68:69], off offset:128
	s_mov_b32 s0, 0x24000
	v_add_co_u32_e64 v68, s[6:7], s0, v134
	s_mov_b32 s0, 0x28000
	s_nop 0
	v_addc_co_u32_e64 v69, s[6:7], 0, v135, s[6:7]
	global_load_dwordx2 v[88:89], v[68:69], off
	global_load_dwordx2 v[78:79], v[68:69], off offset:128
	v_add_co_u32_e64 v70, s[6:7], s0, v134
	v_lshl_add_u64 v[68:69], v[134:135], 0, s[68:69]
	s_nop 0
	v_addc_co_u32_e64 v71, s[6:7], 0, v135, s[6:7]
	s_mov_b32 s0, 0x2c000
	global_load_dwordx2 v[76:77], v[70:71], off
	s_nop 0
	global_load_dwordx2 v[70:71], v[68:69], off offset:128
	v_add_co_u32_e64 v68, s[6:7], s0, v134
	s_mov_b64 s[0:1], 0x23ff8
	s_nop 0
	v_addc_co_u32_e64 v69, s[6:7], 0, v135, s[6:7]
	global_load_dwordx2 v[74:75], v[68:69], off
	s_nop 0
	global_load_dwordx2 v[68:69], v[68:69], off offset:128
	v_lshl_add_u64 v[84:85], v[132:133], 0, s[0:1]
	s_mov_b64 s[0:1], 0x2bff8
	v_lshl_add_u64 v[72:73], v[132:133], 0, s[68:69]
	s_waitcnt vmcnt(7)
; DI unsigned pk4_fp8(float a, float b, float c, float d) { int r = 0; r = __builtin_amdgcn_cvt_pk_fp8_f32(sat8(a), sat8(b), r, false); r = __builtin_amdgcn_cvt_pk_fp8_f32(sat8(c), sat8(d), r, true); return (unsigned)r; }
;     DI void operator()(const f32x4 (&acc)[2][2][4][2], const Unit& u, int wr, int wc, int fr, int fq) const {
;     ...
;             for (int p2 = 0; p2 < 2; ++p2) { const size_t row0 = (size_t)u.pm * 256 + 128 * ai + 64 * wr + 32 * p2 + fr;
; #pragma unroll
;                 for (int bj = 0; bj < 2; ++bj) { u32x2 wq[2];
; #pragma unroll
;                     for (int r2 = 0; r2 < 2; ++r2) { const int m = 2 * p2 + r2; f32x4 sa, sb;
; #pragma unroll
;                         for (int q = 0; q < 4; ++q) { sa[q] = (MRG8_SCALE / (W8_SCALE * AZ8_SCALE)) * t1[(gs[m][bj].x >> (8 * q)) & 255u]; sb[q] = (MRG8_SCALE / (W8_SCALE * AZ8_SCALE)) * t1[(gs[m][bj].y >> (8 * q)) & 255u]; }
;                         const f32x4 va = acc[ai][bj][m][0] * sa, vb = acc[ai][bj][m][1] * sb;
;                         wq[r2].x = pk4_fp8(va[0], va[1], va[2], va[3]); wq[r2].y = pk4_fp8(vb[0], vb[1], vb[2], vb[3]); }
;                     const size_t c = (size_t)(u.pn * 256 + bj * 128 + 32 * wc + 8 * fq);
;                     store_pair8(mrg, row0 * D + c, (row0 + 16) * D + c, wq[0], wq[1], (fq & 1) != 0); } }
	v_and_b32_e32 v0, 0xff, v86
	v_lshl_add_u32 v0, v0, 2, s2
	ds_read_b32 v90, v0
	v_and_b32_e32 v0, 0xff, v87
	v_lshl_add_u32 v0, v0, 2, s2
	ds_read_b32 v92, v0
	v_bfe_u32 v0, v86, 8, 8
	v_lshl_add_u32 v0, v0, 2, s2
	ds_read_b32 v91, v0
	v_bfe_u32 v0, v87, 8, 8
	v_lshl_add_u32 v0, v0, 2, s2
	ds_read_b32 v93, v0
	v_bfe_u32 v0, v86, 16, 8
	v_lshl_add_u32 v0, v0, 2, s2
	ds_read_b32 v94, v0
	v_bfe_u32 v0, v87, 16, 8
	v_lshl_add_u32 v0, v0, 2, s2
	ds_read_b32 v96, v0
	v_lshrrev_b32_e32 v0, 24, v86
	v_lshl_add_u32 v0, v0, 2, s2
	ds_read_b32 v95, v0
	s_waitcnt lgkmcnt(4)
	v_pk_mul_f32 v[90:91], v[90:91], s[92:93] op_sel_hi:[1,0]
	v_lshrrev_b32_e32 v0, 24, v87
	v_lshl_add_u32 v0, v0, 2, s2
	s_waitcnt lgkmcnt(3)
	v_pk_mul_f32 v[86:87], v[92:93], s[92:93] op_sel_hi:[1,0]
	v_pk_mul_f32 v[64:65], v[64:65], v[90:91]
	ds_read_b32 v97, v0
	v_pk_mul_f32 v[86:87], v[60:61], v[86:87]
	v_med3_f32 v0, v64, s53, v204
	v_med3_f32 v61, v65, s53, v204
	v_mov_b32_e32 v60, v1
	v_cvt_pk_fp8_f32 v60, v0, v61
	s_waitcnt lgkmcnt(1)
	v_pk_mul_f32 v[94:95], v[94:95], s[92:93] op_sel_hi:[1,0]
	v_med3_f32 v64, v87, s53, v204
	v_pk_mul_f32 v[66:67], v[66:67], v[94:95]
	s_waitcnt lgkmcnt(0)
	v_pk_mul_f32 v[92:93], v[96:97], s[92:93] op_sel_hi:[1,0]
	v_med3_f32 v0, v66, s53, v204
	v_med3_f32 v61, v67, s53, v204
	v_cvt_pk_fp8_f32 v60, v0, v61 op_sel:[0,0,1]
	v_med3_f32 v0, v86, s53, v204
	v_mov_b32_e32 v61, v1
	v_cvt_pk_fp8_f32 v61, v0, v64
	v_pk_mul_f32 v[62:63], v[62:63], v[92:93]
	s_nop 0
	v_med3_f32 v0, v62, s53, v204
	v_med3_f32 v62, v63, s53, v204
	v_cvt_pk_fp8_f32 v61, v0, v62 op_sel:[0,0,1]
	s_waitcnt vmcnt(5)
	v_and_b32_e32 v0, 0xff, v88
	v_lshl_add_u32 v0, v0, 2, s2
	ds_read_b32 v62, v0
	v_and_b32_e32 v0, 0xff, v89
	v_lshl_add_u32 v0, v0, 2, s2
	ds_read_b32 v64, v0
	v_bfe_u32 v0, v88, 8, 8
	v_lshl_add_u32 v0, v0, 2, s2
	ds_read_b32 v63, v0
	v_bfe_u32 v0, v89, 8, 8
	v_lshl_add_u32 v0, v0, 2, s2
	ds_read_b32 v65, v0
	v_bfe_u32 v0, v88, 16, 8
	v_lshl_add_u32 v0, v0, 2, s2
	ds_read_b32 v66, v0
	v_bfe_u32 v0, v89, 16, 8
	v_lshl_add_u32 v0, v0, 2, s2
	ds_read_b32 v86, v0
	v_lshrrev_b32_e32 v0, 24, v88
	v_lshl_add_u32 v0, v0, 2, s2
	ds_read_b32 v67, v0
	s_waitcnt lgkmcnt(4)
	v_pk_mul_f32 v[62:63], v[62:63], s[92:93] op_sel_hi:[1,0]
	v_lshrrev_b32_e32 v0, 24, v89
	v_lshl_add_u32 v0, v0, 2, s2
	v_pk_mul_f32 v[56:57], v[56:57], v[62:63]
	ds_read_b32 v87, v0
	v_med3_f32 v0, v56, s53, v204
	v_med3_f32 v56, v57, s53, v204
	v_mov_b32_e32 v62, v1
	v_cvt_pk_fp8_f32 v62, v0, v56
	s_waitcnt lgkmcnt(1)
	v_pk_mul_f32 v[66:67], v[66:67], s[92:93] op_sel_hi:[1,0]
	v_pk_mul_f32 v[64:65], v[64:65], s[92:93] op_sel_hi:[1,0]
	v_pk_mul_f32 v[58:59], v[58:59], v[66:67]
	v_pk_mul_f32 v[52:53], v[52:53], v[64:65]
	v_med3_f32 v0, v58, s53, v204
	v_med3_f32 v56, v59, s53, v204
	v_cvt_pk_fp8_f32 v62, v0, v56 op_sel:[0,0,1]
	v_med3_f32 v0, v52, s53, v204
	v_med3_f32 v52, v53, s53, v204
	v_mov_b32_e32 v63, v1
	v_cvt_pk_fp8_f32 v63, v0, v52
	s_waitcnt lgkmcnt(0)
	v_pk_mul_f32 v[86:87], v[86:87], s[92:93] op_sel_hi:[1,0]
	v_cndmask_b32_e32 v53, v85, v83, vcc
	v_pk_mul_f32 v[54:55], v[54:55], v[86:87]
	v_permlane16_swap_b32_e32 v60, v62
	v_med3_f32 v0, v54, s53, v204
	v_med3_f32 v52, v55, s53, v204
	v_cvt_pk_fp8_f32 v63, v0, v52 op_sel:[0,0,1]
	v_cndmask_b32_e32 v52, v84, v82, vcc
	v_lshl_add_u64 v[52:53], s[10:11], 0, v[52:53]
	v_and_b32_e32 v0, 0xff, v80
	v_permlane16_swap_b32_e32 v61, v63
	v_lshl_add_u64 v[54:55], v[52:53], 0, v[2:3]
	v_lshl_add_u32 v0, v0, 2, s2
	global_store_dwordx4 v[54:55], v[60:63], off sc1
	ds_read_b32 v54, v0
	v_and_b32_e32 v0, 0xff, v81
	v_lshl_add_u32 v0, v0, 2, s2
	ds_read_b32 v56, v0
	v_bfe_u32 v0, v80, 8, 8
	v_lshl_add_u32 v0, v0, 2, s2
	ds_read_b32 v55, v0
	v_bfe_u32 v0, v81, 8, 8
	v_lshl_add_u32 v0, v0, 2, s2
	ds_read_b32 v57, v0
	v_bfe_u32 v0, v80, 16, 8
	v_lshl_add_u32 v0, v0, 2, s2
	ds_read_b32 v58, v0
	v_bfe_u32 v0, v81, 16, 8
	v_lshl_add_u32 v0, v0, 2, s2
	ds_read_b32 v60, v0
	v_lshrrev_b32_e32 v0, 24, v80
	v_lshl_add_u32 v0, v0, 2, s2
	ds_read_b32 v59, v0
	s_waitcnt lgkmcnt(4)
	v_pk_mul_f32 v[54:55], v[54:55], s[92:93] op_sel_hi:[1,0]
	v_lshrrev_b32_e32 v0, 24, v81
	v_lshl_add_u32 v0, v0, 2, s2
	s_waitcnt lgkmcnt(3)
	v_pk_mul_f32 v[56:57], v[56:57], s[92:93] op_sel_hi:[1,0]
	v_pk_mul_f32 v[48:49], v[48:49], v[54:55]
	ds_read_b32 v61, v0
	v_pk_mul_f32 v[54:55], v[44:45], v[56:57]
	v_med3_f32 v0, v48, s53, v204
	v_med3_f32 v45, v49, s53, v204
	v_mov_b32_e32 v44, v1
	v_cvt_pk_fp8_f32 v44, v0, v45
	s_waitcnt lgkmcnt(1)
	v_pk_mul_f32 v[58:59], v[58:59], s[92:93] op_sel_hi:[1,0]
	v_med3_f32 v48, v55, s53, v204
	v_pk_mul_f32 v[50:51], v[50:51], v[58:59]
	s_waitcnt lgkmcnt(0)
	v_pk_mul_f32 v[60:61], v[60:61], s[92:93] op_sel_hi:[1,0]
	v_med3_f32 v0, v50, s53, v204
	v_med3_f32 v45, v51, s53, v204
	v_cvt_pk_fp8_f32 v44, v0, v45 op_sel:[0,0,1]
	v_med3_f32 v0, v54, s53, v204
	v_mov_b32_e32 v45, v1
	v_cvt_pk_fp8_f32 v45, v0, v48
	v_pk_mul_f32 v[46:47], v[46:47], v[60:61]
	s_nop 0
	v_med3_f32 v0, v46, s53, v204
	v_med3_f32 v46, v47, s53, v204
	v_cvt_pk_fp8_f32 v45, v0, v46 op_sel:[0,0,1]
	s_waitcnt vmcnt(5)
	v_and_b32_e32 v0, 0xff, v78
	v_lshl_add_u32 v0, v0, 2, s2
	ds_read_b32 v46, v0
	v_and_b32_e32 v0, 0xff, v79
	v_lshl_add_u32 v0, v0, 2, s2
	ds_read_b32 v48, v0
	v_bfe_u32 v0, v78, 8, 8
	v_lshl_add_u32 v0, v0, 2, s2
	ds_read_b32 v47, v0
	v_bfe_u32 v0, v79, 8, 8
	v_lshl_add_u32 v0, v0, 2, s2
	ds_read_b32 v49, v0
	v_bfe_u32 v0, v78, 16, 8
	v_lshl_add_u32 v0, v0, 2, s2
	ds_read_b32 v50, v0
	v_bfe_u32 v0, v79, 16, 8
	v_lshl_add_u32 v0, v0, 2, s2
	ds_read_b32 v54, v0
	v_lshrrev_b32_e32 v0, 24, v78
	v_lshl_add_u32 v0, v0, 2, s2
	ds_read_b32 v51, v0
	s_waitcnt lgkmcnt(4)
; DI unsigned pk4_fp8(float a, float b, float c, float d) { int r = 0; r = __builtin_amdgcn_cvt_pk_fp8_f32(sat8(a), sat8(b), r, false); r = __builtin_amdgcn_cvt_pk_fp8_f32(sat8(c), sat8(d), r, true); return (unsigned)r; }
;     DI void operator()(const f32x4 (&acc)[2][2][4][2], const Unit& u, int wr, int wc, int fr, int fq) const {
;     ...
;             for (int p2 = 0; p2 < 2; ++p2) { const size_t row0 = (size_t)u.pm * 256 + 128 * ai + 64 * wr + 32 * p2 + fr;
; #pragma unroll
;                 for (int bj = 0; bj < 2; ++bj) { u32x2 wq[2];
; #pragma unroll
;                     for (int r2 = 0; r2 < 2; ++r2) { const int m = 2 * p2 + r2; f32x4 sa, sb;
; #pragma unroll
;                         for (int q = 0; q < 4; ++q) { sa[q] = (MRG8_SCALE / (W8_SCALE * AZ8_SCALE)) * t1[(gs[m][bj].x >> (8 * q)) & 255u]; sb[q] = (MRG8_SCALE / (W8_SCALE * AZ8_SCALE)) * t1[(gs[m][bj].y >> (8 * q)) & 255u]; }
;                         const f32x4 va = acc[ai][bj][m][0] * sa, vb = acc[ai][bj][m][1] * sb;
;                         wq[r2].x = pk4_fp8(va[0], va[1], va[2], va[3]); wq[r2].y = pk4_fp8(vb[0], vb[1], vb[2], vb[3]); }
;                     const size_t c = (size_t)(u.pn * 256 + bj * 128 + 32 * wc + 8 * fq);
;                     store_pair8(mrg, row0 * D + c, (row0 + 16) * D + c, wq[0], wq[1], (fq & 1) != 0); } }
	v_pk_mul_f32 v[46:47], v[46:47], s[92:93] op_sel_hi:[1,0]
	v_lshrrev_b32_e32 v0, 24, v79
	v_lshl_add_u32 v0, v0, 2, s2
	v_pk_mul_f32 v[40:41], v[40:41], v[46:47]
	ds_read_b32 v55, v0
	v_med3_f32 v0, v40, s53, v204
	v_med3_f32 v40, v41, s53, v204
	v_mov_b32_e32 v46, v1
	v_cvt_pk_fp8_f32 v46, v0, v40
	s_waitcnt lgkmcnt(1)
	v_pk_mul_f32 v[50:51], v[50:51], s[92:93] op_sel_hi:[1,0]
	v_pk_mul_f32 v[48:49], v[48:49], s[92:93] op_sel_hi:[1,0]
	v_pk_mul_f32 v[42:43], v[42:43], v[50:51]
	v_pk_mul_f32 v[36:37], v[36:37], v[48:49]
	v_med3_f32 v0, v42, s53, v204
	v_med3_f32 v40, v43, s53, v204
	v_cvt_pk_fp8_f32 v46, v0, v40 op_sel:[0,0,1]
	v_med3_f32 v0, v36, s53, v204
	v_med3_f32 v36, v37, s53, v204
	v_mov_b32_e32 v47, v1
	v_cvt_pk_fp8_f32 v47, v0, v36
	s_waitcnt lgkmcnt(0)
	v_pk_mul_f32 v[54:55], v[54:55], s[92:93] op_sel_hi:[1,0]
	v_permlane16_swap_b32_e32 v44, v46
	v_pk_mul_f32 v[38:39], v[38:39], v[54:55]
	s_nop 0
	v_med3_f32 v0, v38, s53, v204
	v_med3_f32 v36, v39, s53, v204
	v_cvt_pk_fp8_f32 v47, v0, v36 op_sel:[0,0,1]
	s_waitcnt vmcnt(4)
	v_and_b32_e32 v0, 0xff, v76
	v_lshl_add_u32 v0, v0, 2, s2
	ds_read_b32 v38, v0
	v_and_b32_e32 v0, 0xff, v77
	v_lshl_add_u32 v0, v0, 2, s2
	ds_read_b32 v40, v0
	v_bfe_u32 v0, v76, 8, 8
	v_lshl_add_u32 v0, v0, 2, s2
	ds_read_b32 v39, v0
	v_bfe_u32 v0, v77, 8, 8
	v_lshl_add_u32 v0, v0, 2, s2
	ds_read_b32 v41, v0
	v_bfe_u32 v0, v76, 16, 8
	v_lshl_add_u32 v0, v0, 2, s2
	ds_read_b32 v42, v0
	v_bfe_u32 v0, v77, 16, 8
	v_permlane16_swap_b32_e32 v45, v47
	v_lshl_add_u64 v[36:37], v[52:53], 0, v[100:101]
	v_lshl_add_u32 v0, v0, 2, s2
	global_store_dwordx4 v[36:37], v[44:47], off sc1
	ds_read_b32 v44, v0
	v_lshrrev_b32_e32 v0, 24, v76
	v_lshl_add_u32 v0, v0, 2, s2
	ds_read_b32 v43, v0
	s_waitcnt lgkmcnt(4)
	v_pk_mul_f32 v[38:39], v[38:39], s[92:93] op_sel_hi:[1,0]
	v_lshrrev_b32_e32 v0, 24, v77
	v_lshl_add_u32 v0, v0, 2, s2
	s_waitcnt lgkmcnt(3)
	v_pk_mul_f32 v[40:41], v[40:41], s[92:93] op_sel_hi:[1,0]
	v_pk_mul_f32 v[32:33], v[32:33], v[38:39]
	ds_read_b32 v45, v0
	v_pk_mul_f32 v[38:39], v[28:29], v[40:41]
	v_med3_f32 v0, v32, s53, v204
	v_med3_f32 v29, v33, s53, v204
	v_mov_b32_e32 v28, v1
	v_cvt_pk_fp8_f32 v28, v0, v29
	s_waitcnt lgkmcnt(1)
	v_pk_mul_f32 v[42:43], v[42:43], s[92:93] op_sel_hi:[1,0]
	v_med3_f32 v32, v39, s53, v204
	v_pk_mul_f32 v[34:35], v[34:35], v[42:43]
	s_waitcnt lgkmcnt(0)
	v_pk_mul_f32 v[44:45], v[44:45], s[92:93] op_sel_hi:[1,0]
	v_med3_f32 v0, v34, s53, v204
	v_med3_f32 v29, v35, s53, v204
	v_cvt_pk_fp8_f32 v28, v0, v29 op_sel:[0,0,1]
	v_med3_f32 v0, v38, s53, v204
	v_mov_b32_e32 v29, v1
	v_cvt_pk_fp8_f32 v29, v0, v32
	v_pk_mul_f32 v[30:31], v[30:31], v[44:45]
	v_lshl_add_u64 v[36:37], v[132:133], 0, s[0:1]
	v_med3_f32 v0, v30, s53, v204
	v_med3_f32 v30, v31, s53, v204
	v_cvt_pk_fp8_f32 v29, v0, v30 op_sel:[0,0,1]
	s_waitcnt vmcnt(3)
	v_and_b32_e32 v0, 0xff, v74
	v_lshl_add_u32 v0, v0, 2, s2
	ds_read_b32 v30, v0
	v_and_b32_e32 v0, 0xff, v75
	v_lshl_add_u32 v0, v0, 2, s2
	ds_read_b32 v32, v0
	v_bfe_u32 v0, v74, 8, 8
	v_lshl_add_u32 v0, v0, 2, s2
	ds_read_b32 v31, v0
	v_bfe_u32 v0, v75, 8, 8
	v_lshl_add_u32 v0, v0, 2, s2
	ds_read_b32 v33, v0
	v_bfe_u32 v0, v74, 16, 8
	v_lshl_add_u32 v0, v0, 2, s2
	ds_read_b32 v34, v0
	v_bfe_u32 v0, v75, 16, 8
	v_lshl_add_u32 v0, v0, 2, s2
	ds_read_b32 v38, v0
	v_lshrrev_b32_e32 v0, 24, v74
	v_lshl_add_u32 v0, v0, 2, s2
	ds_read_b32 v35, v0
	s_waitcnt lgkmcnt(4)
	v_pk_mul_f32 v[30:31], v[30:31], s[92:93] op_sel_hi:[1,0]
	v_lshrrev_b32_e32 v0, 24, v75
	v_lshl_add_u32 v0, v0, 2, s2
	v_pk_mul_f32 v[24:25], v[24:25], v[30:31]
	ds_read_b32 v39, v0
	v_med3_f32 v0, v24, s53, v204
	v_med3_f32 v24, v25, s53, v204
	v_mov_b32_e32 v30, v1
	v_cvt_pk_fp8_f32 v30, v0, v24
	s_waitcnt lgkmcnt(1)
	v_pk_mul_f32 v[34:35], v[34:35], s[92:93] op_sel_hi:[1,0]
	v_pk_mul_f32 v[32:33], v[32:33], s[92:93] op_sel_hi:[1,0]
	v_pk_mul_f32 v[26:27], v[26:27], v[34:35]
	v_pk_mul_f32 v[20:21], v[20:21], v[32:33]
	v_med3_f32 v0, v26, s53, v204
	v_med3_f32 v24, v27, s53, v204
	v_cvt_pk_fp8_f32 v30, v0, v24 op_sel:[0,0,1]
	v_med3_f32 v0, v20, s53, v204
	v_med3_f32 v20, v21, s53, v204
	v_mov_b32_e32 v31, v1
	v_cvt_pk_fp8_f32 v31, v0, v20
	s_waitcnt lgkmcnt(0)
; DI unsigned pk4_fp8(float a, float b, float c, float d) { int r = 0; r = __builtin_amdgcn_cvt_pk_fp8_f32(sat8(a), sat8(b), r, false); r = __builtin_amdgcn_cvt_pk_fp8_f32(sat8(c), sat8(d), r, true); return (unsigned)r; }
;     DI void operator()(const f32x4 (&acc)[2][2][4][2], const Unit& u, int wr, int wc, int fr, int fq) const {
;     ...
;             for (int p2 = 0; p2 < 2; ++p2) { const size_t row0 = (size_t)u.pm * 256 + 128 * ai + 64 * wr + 32 * p2 + fr;
; #pragma unroll
;                 for (int bj = 0; bj < 2; ++bj) { u32x2 wq[2];
; #pragma unroll
;                     for (int r2 = 0; r2 < 2; ++r2) { const int m = 2 * p2 + r2; f32x4 sa, sb;
; #pragma unroll
;                         for (int q = 0; q < 4; ++q) { sa[q] = (MRG8_SCALE / (W8_SCALE * AZ8_SCALE)) * t1[(gs[m][bj].x >> (8 * q)) & 255u]; sb[q] = (MRG8_SCALE / (W8_SCALE * AZ8_SCALE)) * t1[(gs[m][bj].y >> (8 * q)) & 255u]; }
;                         const f32x4 va = acc[ai][bj][m][0] * sa, vb = acc[ai][bj][m][1] * sb;
;                         wq[r2].x = pk4_fp8(va[0], va[1], va[2], va[3]); wq[r2].y = pk4_fp8(vb[0], vb[1], vb[2], vb[3]); }
;                     const size_t c = (size_t)(u.pn * 256 + bj * 128 + 32 * wc + 8 * fq);
;                     store_pair8(mrg, row0 * D + c, (row0 + 16) * D + c, wq[0], wq[1], (fq & 1) != 0); } }
	v_pk_mul_f32 v[38:39], v[38:39], s[92:93] op_sel_hi:[1,0]
	v_cndmask_b32_e32 v21, v37, v73, vcc
	v_pk_mul_f32 v[22:23], v[22:23], v[38:39]
	v_permlane16_swap_b32_e32 v28, v30
	v_med3_f32 v0, v22, s53, v204
	v_med3_f32 v20, v23, s53, v204
	v_cvt_pk_fp8_f32 v31, v0, v20 op_sel:[0,0,1]
	v_cndmask_b32_e32 v20, v36, v72, vcc
	v_lshl_add_u64 v[20:21], s[10:11], 0, v[20:21]
	v_and_b32_e32 v0, 0xff, v70
	v_permlane16_swap_b32_e32 v29, v31
	v_lshl_add_u64 v[2:3], v[20:21], 0, v[2:3]
	v_lshl_add_u32 v0, v0, 2, s2
	global_store_dwordx4 v[2:3], v[28:31], off sc1
	ds_read_b32 v2, v0
	v_and_b32_e32 v0, 0xff, v71
	v_lshl_add_u32 v0, v0, 2, s2
	ds_read_b32 v22, v0
	v_bfe_u32 v0, v70, 8, 8
	v_lshl_add_u32 v0, v0, 2, s2
	ds_read_b32 v3, v0
	v_bfe_u32 v0, v71, 8, 8
	v_lshl_add_u32 v0, v0, 2, s2
	ds_read_b32 v23, v0
	v_bfe_u32 v0, v70, 16, 8
	v_lshl_add_u32 v0, v0, 2, s2
	ds_read_b32 v24, v0
	v_bfe_u32 v0, v71, 16, 8
	v_lshl_add_u32 v0, v0, 2, s2
	ds_read_b32 v26, v0
	v_lshrrev_b32_e32 v0, 24, v70
	v_lshl_add_u32 v0, v0, 2, s2
	ds_read_b32 v25, v0
	s_waitcnt lgkmcnt(4)
	v_pk_mul_f32 v[2:3], v[2:3], s[92:93] op_sel_hi:[1,0]
	v_lshrrev_b32_e32 v0, 24, v71
	v_lshl_add_u32 v0, v0, 2, s2
	v_pk_mul_f32 v[2:3], v[16:17], v[2:3]
	ds_read_b32 v27, v0
	v_med3_f32 v0, v2, s53, v204
	v_med3_f32 v3, v3, s53, v204
	v_mov_b32_e32 v2, v1
	v_cvt_pk_fp8_f32 v2, v0, v3
	s_waitcnt lgkmcnt(1)
	v_pk_mul_f32 v[24:25], v[24:25], s[92:93] op_sel_hi:[1,0]
	v_pk_mul_f32 v[22:23], v[22:23], s[92:93] op_sel_hi:[1,0]
	v_pk_mul_f32 v[18:19], v[18:19], v[24:25]
	v_pk_mul_f32 v[12:13], v[12:13], v[22:23]
	v_med3_f32 v0, v18, s53, v204
	v_med3_f32 v3, v19, s53, v204
	v_cvt_pk_fp8_f32 v2, v0, v3 op_sel:[0,0,1]
	v_med3_f32 v0, v12, s53, v204
	v_med3_f32 v12, v13, s53, v204
	v_mov_b32_e32 v3, v1
	v_cvt_pk_fp8_f32 v3, v0, v12
	s_waitcnt lgkmcnt(0)
	v_pk_mul_f32 v[26:27], v[26:27], s[92:93] op_sel_hi:[1,0]
	s_andn2_b64 vcc, exec, s[4:5]
	v_pk_mul_f32 v[14:15], v[14:15], v[26:27]
	s_nop 0
	v_med3_f32 v0, v14, s53, v204
	v_med3_f32 v12, v15, s53, v204
	v_cvt_pk_fp8_f32 v3, v0, v12 op_sel:[0,0,1]
	s_waitcnt vmcnt(3)
	v_and_b32_e32 v0, 0xff, v68
	v_lshl_add_u32 v0, v0, 2, s2
	ds_read_b32 v12, v0
	v_and_b32_e32 v0, 0xff, v69
	v_lshl_add_u32 v0, v0, 2, s2
	ds_read_b32 v14, v0
	v_bfe_u32 v0, v68, 8, 8
	v_lshl_add_u32 v0, v0, 2, s2
	ds_read_b32 v13, v0
	v_bfe_u32 v0, v69, 8, 8
	v_lshl_add_u32 v0, v0, 2, s2
	ds_read_b32 v15, v0
	v_bfe_u32 v0, v68, 16, 8
	v_lshl_add_u32 v0, v0, 2, s2
	ds_read_b32 v16, v0
	v_bfe_u32 v0, v69, 16, 8
	v_lshl_add_u32 v0, v0, 2, s2
	ds_read_b32 v18, v0
	v_lshrrev_b32_e32 v0, 24, v68
	v_lshl_add_u32 v0, v0, 2, s2
	ds_read_b32 v17, v0
	s_waitcnt lgkmcnt(4)
	v_pk_mul_f32 v[12:13], v[12:13], s[92:93] op_sel_hi:[1,0]
	v_lshrrev_b32_e32 v0, 24, v69
	v_lshl_add_u32 v0, v0, 2, s2
	s_waitcnt lgkmcnt(3)
	v_pk_mul_f32 v[14:15], v[14:15], s[92:93] op_sel_hi:[1,0]
	v_pk_mul_f32 v[8:9], v[8:9], v[12:13]
	ds_read_b32 v19, v0
	v_pk_mul_f32 v[12:13], v[4:5], v[14:15]
	v_med3_f32 v0, v8, s53, v204
	v_med3_f32 v5, v9, s53, v204
	v_mov_b32_e32 v4, v1
	v_cvt_pk_fp8_f32 v4, v0, v5
	s_waitcnt lgkmcnt(1)
	v_pk_mul_f32 v[16:17], v[16:17], s[92:93] op_sel_hi:[1,0]
	v_med3_f32 v8, v13, s53, v204
	v_pk_mul_f32 v[10:11], v[10:11], v[16:17]
	s_waitcnt lgkmcnt(0)
	v_pk_mul_f32 v[18:19], v[18:19], s[92:93] op_sel_hi:[1,0]
	v_med3_f32 v0, v10, s53, v204
	v_med3_f32 v5, v11, s53, v204
	v_cvt_pk_fp8_f32 v4, v0, v5 op_sel:[0,0,1]
	v_med3_f32 v0, v12, s53, v204
	v_mov_b32_e32 v5, v1
	v_cvt_pk_fp8_f32 v5, v0, v8
	v_pk_mul_f32 v[6:7], v[6:7], v[18:19]
	v_permlane16_swap_b32_e32 v2, v4
	v_med3_f32 v0, v6, s53, v204
	v_med3_f32 v6, v7, s53, v204
	v_cvt_pk_fp8_f32 v5, v0, v6 op_sel:[0,0,1]
	v_lshl_add_u64 v[6:7], v[20:21], 0, v[100:101]
	s_mov_b64 s[2:3], -1
	v_permlane16_swap_b32_e32 v3, v5
	global_store_dwordx4 v[6:7], v[2:5], off sc1
	s_cbranch_vccnz .LBB0_897
	s_andn2_b64 vcc, exec, s[60:61]
	s_cbranch_vccnz .LBB0_896
	s_barrier
	s_branch .LBB0_896

; DI u32x4 pack8(const f32x4& a, const f32x4& b) { u32x4 w; w.x = pk2(a[0], a[1]); w.y = pk2(a[2], a[3]); w.z = pk2(b[0], b[1]); w.w = pk2(b[2], b[3]); return w; }
;     DI void operator()(const f32x4 (&acc)[2][2][4][2], const Unit& u, int wr, int wc, int fr, int fq) const {
;         EPI_ROWS_BEGIN
;             const size_t row = (size_t)u.pm * 256 + rt;
; #pragma unroll
;             for (int bj = 0; bj < 2; ++bj) *(u32x4*)(o + row * ldc + u.pn * 256 + bj * 128 + 32 * wc + 8 * fq) = pack8(acc[ai][bj][m][0] * sc, acc[ai][bj][m][1] * sc);
;         EPI_ROWS_END
.LBB0_975:
	s_mov_b32 s0, -1
	s_mov_b32 s13, s26
	s_ashr_i32 s21, s20, 31
	v_mbcnt_lo_u32_b32 v0, s0, 0
	v_mbcnt_hi_u32_b32 v0, s0, v0
	s_lshl_b32 s0, s13, 4
	s_andn2_b32 s0, s0, 63
	s_lshl_b64 s[2:3], s[20:21], 8
	v_and_or_b32 v130, v0, 15, s0
	v_ashrrev_i32_e32 v131, 31, v130
	s_lshl_b32 s0, s43, 8
	v_lshl_add_u64 v[138:139], s[2:3], 0, v[130:131]
	v_pk_mul_f32 v[126:127], v[126:127], s[96:97] op_sel_hi:[1,0]
	v_pk_mul_f32 v[122:123], v[122:123], s[96:97] op_sel_hi:[1,0]
	s_ashr_i32 s1, s0, 31
	v_ashrrev_i32_e32 v0, 1, v0
	v_pk_mul_f32 v[140:141], v[124:125], s[96:97] op_sel_hi:[1,0]
	v_cvt_pk_bf16_f32 v124, v126, v127
	v_cvt_pk_bf16_f32 v126, v122, v123
	v_lshlrev_b64 v[122:123], 11, v[138:139]
	v_and_b32_e32 v136, -8, v0
	v_lshl_add_u64 v[122:123], s[8:9], 0, v[122:123]
	s_lshl_b64 s[20:21], s[0:1], 1
	s_lshl_b32 s0, s13, 6
	v_ashrrev_i32_e32 v137, 31, v136
	v_pk_mul_f32 v[128:129], v[128:129], s[96:97] op_sel_hi:[1,0]
	v_lshl_add_u64 v[122:123], v[122:123], 0, s[20:21]
	s_and_b32 s58, s0, 0xc0
	v_cvt_pk_bf16_f32 v125, v128, v129
	v_lshl_add_u64 v[128:129], v[122:123], 0, s[58:59]
	v_lshlrev_b64 v[122:123], 1, v[136:137]
	v_cvt_pk_bf16_f32 v127, v140, v141
	v_lshl_add_u64 v[128:129], v[128:129], 0, v[122:123]
	global_store_dwordx4 v[128:129], v[124:127], off sc1
	v_pk_mul_f32 v[116:117], v[116:117], s[96:97] op_sel_hi:[1,0]
	v_pk_mul_f32 v[114:115], v[114:115], s[96:97] op_sel_hi:[1,0]
	v_pk_mul_f32 v[124:125], v[108:109], s[96:97] op_sel_hi:[1,0]
	v_pk_mul_f32 v[108:109], v[106:107], s[96:97] op_sel_hi:[1,0]
	v_cvt_pk_bf16_f32 v106, v114, v115
	v_cvt_pk_bf16_f32 v107, v116, v117
	v_cvt_pk_bf16_f32 v108, v108, v109
	v_cvt_pk_bf16_f32 v109, v124, v125
	global_store_dwordx4 v[128:129], v[106:109], off offset:256 sc1
	v_pk_mul_f32 v[110:111], v[110:111], s[96:97] op_sel_hi:[1,0]
	v_pk_mul_f32 v[112:113], v[112:113], s[96:97] op_sel_hi:[1,0]
	v_or_b32_e32 v106, 16, v130
	v_ashrrev_i32_e32 v107, 31, v106
	v_lshl_add_u64 v[114:115], s[2:3], 0, v[106:107]
	v_pk_mul_f32 v[108:109], v[120:121], s[96:97] op_sel_hi:[1,0]
	v_pk_mul_f32 v[106:107], v[118:119], s[96:97] op_sel_hi:[1,0]
	v_pk_mul_f32 v[100:101], v[100:101], s[96:97] op_sel_hi:[1,0]
	v_cvt_pk_bf16_f32 v106, v106, v107
	v_cvt_pk_bf16_f32 v107, v108, v109
	v_cvt_pk_bf16_f32 v108, v110, v111
	v_lshlrev_b64 v[110:111], 11, v[114:115]
	v_lshl_add_u64 v[110:111], s[8:9], 0, v[110:111]
	v_lshl_add_u64 v[110:111], v[110:111], 0, s[20:21]
	v_lshl_add_u64 v[110:111], v[110:111], 0, s[58:59]
	v_cvt_pk_bf16_f32 v109, v112, v113
	v_lshl_add_u64 v[110:111], v[110:111], 0, v[122:123]
	global_store_dwordx4 v[110:111], v[106:109], off sc1
	v_pk_mul_f32 v[98:99], v[98:99], s[96:97] op_sel_hi:[1,0]
	v_pk_mul_f32 v[94:95], v[94:95], s[96:97] op_sel_hi:[1,0]
	v_pk_mul_f32 v[106:107], v[92:93], s[96:97] op_sel_hi:[1,0]
	v_pk_mul_f32 v[92:93], v[90:91], s[96:97] op_sel_hi:[1,0]
	v_cvt_pk_bf16_f32 v90, v98, v99
	v_cvt_pk_bf16_f32 v91, v100, v101
	v_cvt_pk_bf16_f32 v92, v92, v93
	v_cvt_pk_bf16_f32 v93, v106, v107
	global_store_dwordx4 v[110:111], v[90:93], off offset:256 sc1
	v_pk_mul_f32 v[96:97], v[96:97], s[96:97] op_sel_hi:[1,0]
	v_pk_mul_f32 v[84:85], v[84:85], s[96:97] op_sel_hi:[1,0]
	v_or_b32_e32 v90, 32, v130
	v_ashrrev_i32_e32 v91, 31, v90
	v_lshl_add_u64 v[98:99], s[2:3], 0, v[90:91]
	v_pk_mul_f32 v[92:93], v[104:105], s[96:97] op_sel_hi:[1,0]
	v_pk_mul_f32 v[90:91], v[102:103], s[96:97] op_sel_hi:[1,0]
	v_pk_mul_f32 v[82:83], v[82:83], s[96:97] op_sel_hi:[1,0]
	v_cvt_pk_bf16_f32 v90, v90, v91
	v_cvt_pk_bf16_f32 v91, v92, v93
	v_cvt_pk_bf16_f32 v92, v94, v95
	v_lshlrev_b64 v[94:95], 11, v[98:99]
	v_lshl_add_u64 v[94:95], s[8:9], 0, v[94:95]
	v_lshl_add_u64 v[94:95], v[94:95], 0, s[20:21]
	v_lshl_add_u64 v[94:95], v[94:95], 0, s[58:59]
	v_cvt_pk_bf16_f32 v93, v96, v97
	v_lshl_add_u64 v[94:95], v[94:95], 0, v[122:123]
	global_store_dwordx4 v[94:95], v[90:93], off sc1
	v_pk_mul_f32 v[78:79], v[78:79], s[96:97] op_sel_hi:[1,0]
	v_pk_mul_f32 v[80:81], v[80:81], s[96:97] op_sel_hi:[1,0]
	v_pk_mul_f32 v[90:91], v[76:77], s[96:97] op_sel_hi:[1,0]
	v_pk_mul_f32 v[76:77], v[74:75], s[96:97] op_sel_hi:[1,0]
	v_cvt_pk_bf16_f32 v74, v82, v83
	v_cvt_pk_bf16_f32 v75, v84, v85
	v_cvt_pk_bf16_f32 v76, v76, v77
	v_cvt_pk_bf16_f32 v77, v90, v91
	global_store_dwordx4 v[94:95], v[74:77], off offset:256 sc1
	v_pk_mul_f32 v[72:73], v[72:73], s[96:97] op_sel_hi:[1,0]
	v_pk_mul_f32 v[70:71], v[70:71], s[96:97] op_sel_hi:[1,0]
	v_or_b32_e32 v74, 48, v130
	v_ashrrev_i32_e32 v75, 31, v74
	v_lshl_add_u64 v[82:83], s[2:3], 0, v[74:75]
	v_pk_mul_f32 v[76:77], v[88:89], s[96:97] op_sel_hi:[1,0]
	v_pk_mul_f32 v[74:75], v[86:87], s[96:97] op_sel_hi:[1,0]
	v_pk_mul_f32 v[62:63], v[62:63], s[96:97] op_sel_hi:[1,0]
	v_cvt_pk_bf16_f32 v74, v74, v75
	v_cvt_pk_bf16_f32 v75, v76, v77
	v_cvt_pk_bf16_f32 v76, v78, v79
	v_lshlrev_b64 v[78:79], 11, v[82:83]
	v_lshl_add_u64 v[78:79], s[8:9], 0, v[78:79]
	v_lshl_add_u64 v[78:79], v[78:79], 0, s[20:21]
	v_lshl_add_u64 v[78:79], v[78:79], 0, s[58:59]
	v_cvt_pk_bf16_f32 v77, v80, v81
	v_lshl_add_u64 v[78:79], v[78:79], 0, v[122:123]
	global_store_dwordx4 v[78:79], v[74:77], off sc1
; DI u32x4 pack8(const f32x4& a, const f32x4& b) { u32x4 w; w.x = pk2(a[0], a[1]); w.y = pk2(a[2], a[3]); w.z = pk2(b[0], b[1]); w.w = pk2(b[2], b[3]); return w; }
;     DI void operator()(const f32x4 (&acc)[2][2][4][2], const Unit& u, int wr, int wc, int fr, int fq) const {
;         EPI_ROWS_BEGIN
;             const size_t row = (size_t)u.pm * 256 + rt;
; #pragma unroll
;             for (int bj = 0; bj < 2; ++bj) *(u32x4*)(o + row * ldc + u.pn * 256 + bj * 128 + 32 * wc + 8 * fq) = pack8(acc[ai][bj][m][0] * sc, acc[ai][bj][m][1] * sc);
;         EPI_ROWS_END
	v_pk_mul_f32 v[64:65], v[64:65], s[96:97] op_sel_hi:[1,0]
	v_pk_mul_f32 v[52:53], v[52:53], s[96:97] op_sel_hi:[1,0]
	v_pk_mul_f32 v[74:75], v[68:69], s[96:97] op_sel_hi:[1,0]
	v_pk_mul_f32 v[68:69], v[66:67], s[96:97] op_sel_hi:[1,0]
	v_cvt_pk_bf16_f32 v66, v70, v71
	v_cvt_pk_bf16_f32 v67, v72, v73
	v_cvt_pk_bf16_f32 v68, v68, v69
	v_cvt_pk_bf16_f32 v69, v74, v75
	global_store_dwordx4 v[78:79], v[66:69], off offset:256 sc1
	v_pk_mul_f32 v[50:51], v[50:51], s[96:97] op_sel_hi:[1,0]
	v_pk_mul_f32 v[46:47], v[46:47], s[96:97] op_sel_hi:[1,0]
	v_add_u32_e32 v66, 0x80, v130
	v_ashrrev_i32_e32 v67, 31, v66
	v_lshl_add_u64 v[66:67], s[2:3], 0, v[66:67]
	v_pk_mul_f32 v[68:69], v[60:61], s[96:97] op_sel_hi:[1,0]
	v_pk_mul_f32 v[60:61], v[58:59], s[96:97] op_sel_hi:[1,0]
	v_cvt_pk_bf16_f32 v58, v62, v63
	v_lshlrev_b64 v[62:63], 11, v[66:67]
	v_lshl_add_u64 v[62:63], s[8:9], 0, v[62:63]
	v_lshl_add_u64 v[62:63], v[62:63], 0, s[20:21]
	v_lshl_add_u64 v[62:63], v[62:63], 0, s[58:59]
	v_cvt_pk_bf16_f32 v59, v64, v65
	v_cvt_pk_bf16_f32 v60, v60, v61
	v_cvt_pk_bf16_f32 v61, v68, v69
	v_lshl_add_u64 v[62:63], v[62:63], 0, v[122:123]
	global_store_dwordx4 v[62:63], v[58:61], off sc1
	v_pk_mul_f32 v[48:49], v[48:49], s[96:97] op_sel_hi:[1,0]
	v_pk_mul_f32 v[36:37], v[36:37], s[96:97] op_sel_hi:[1,0]
	v_pk_mul_f32 v[58:59], v[44:45], s[96:97] op_sel_hi:[1,0]
	v_pk_mul_f32 v[44:45], v[42:43], s[96:97] op_sel_hi:[1,0]
	v_cvt_pk_bf16_f32 v42, v50, v51
	v_cvt_pk_bf16_f32 v43, v52, v53
	v_cvt_pk_bf16_f32 v44, v44, v45
	v_cvt_pk_bf16_f32 v45, v58, v59
	global_store_dwordx4 v[62:63], v[42:45], off offset:256 sc1
	v_pk_mul_f32 v[34:35], v[34:35], s[96:97] op_sel_hi:[1,0]
	v_pk_mul_f32 v[30:31], v[30:31], s[96:97] op_sel_hi:[1,0]
	v_add_u32_e32 v42, 0x90, v130
	v_ashrrev_i32_e32 v43, 31, v42
	v_lshl_add_u64 v[50:51], s[2:3], 0, v[42:43]
	v_pk_mul_f32 v[44:45], v[56:57], s[96:97] op_sel_hi:[1,0]
	v_pk_mul_f32 v[42:43], v[54:55], s[96:97] op_sel_hi:[1,0]
	v_pk_mul_f32 v[32:33], v[32:33], s[96:97] op_sel_hi:[1,0]
	v_cvt_pk_bf16_f32 v42, v42, v43
	v_cvt_pk_bf16_f32 v43, v44, v45
	v_cvt_pk_bf16_f32 v44, v46, v47
	v_lshlrev_b64 v[46:47], 11, v[50:51]
	v_lshl_add_u64 v[46:47], s[8:9], 0, v[46:47]
	v_lshl_add_u64 v[46:47], v[46:47], 0, s[20:21]
	v_lshl_add_u64 v[46:47], v[46:47], 0, s[58:59]
	v_cvt_pk_bf16_f32 v45, v48, v49
	v_lshl_add_u64 v[46:47], v[46:47], 0, v[122:123]
	global_store_dwordx4 v[46:47], v[42:45], off sc1
	v_pk_mul_f32 v[20:21], v[20:21], s[96:97] op_sel_hi:[1,0]
	v_pk_mul_f32 v[18:19], v[18:19], s[96:97] op_sel_hi:[1,0]
	v_pk_mul_f32 v[42:43], v[28:29], s[96:97] op_sel_hi:[1,0]
	v_pk_mul_f32 v[28:29], v[26:27], s[96:97] op_sel_hi:[1,0]
	v_cvt_pk_bf16_f32 v26, v34, v35
	v_cvt_pk_bf16_f32 v27, v36, v37
	v_cvt_pk_bf16_f32 v28, v28, v29
	v_cvt_pk_bf16_f32 v29, v42, v43
	global_store_dwordx4 v[46:47], v[26:29], off offset:256 sc1
	v_pk_mul_f32 v[14:15], v[14:15], s[96:97] op_sel_hi:[1,0]
	v_pk_mul_f32 v[16:17], v[16:17], s[96:97] op_sel_hi:[1,0]
	v_add_u32_e32 v26, 0xa0, v130
	v_ashrrev_i32_e32 v27, 31, v26
	v_lshl_add_u64 v[34:35], s[2:3], 0, v[26:27]
	v_pk_mul_f32 v[28:29], v[40:41], s[96:97] op_sel_hi:[1,0]
	v_pk_mul_f32 v[26:27], v[38:39], s[96:97] op_sel_hi:[1,0]
	v_pk_mul_f32 v[8:9], v[8:9], s[96:97] op_sel_hi:[1,0]
	v_cvt_pk_bf16_f32 v26, v26, v27
	v_cvt_pk_bf16_f32 v27, v28, v29
	v_cvt_pk_bf16_f32 v28, v30, v31
	v_lshlrev_b64 v[30:31], 11, v[34:35]
	v_lshl_add_u64 v[30:31], s[8:9], 0, v[30:31]
	v_lshl_add_u64 v[30:31], v[30:31], 0, s[20:21]
	v_lshl_add_u64 v[30:31], v[30:31], 0, s[58:59]
	v_cvt_pk_bf16_f32 v29, v32, v33
	v_lshl_add_u64 v[30:31], v[30:31], 0, v[122:123]
	global_store_dwordx4 v[30:31], v[26:29], off sc1
	v_pk_mul_f32 v[6:7], v[6:7], s[96:97] op_sel_hi:[1,0]
	s_andn2_b64 vcc, exec, s[4:5]
	v_pk_mul_f32 v[26:27], v[12:13], s[96:97] op_sel_hi:[1,0]
	v_pk_mul_f32 v[12:13], v[10:11], s[96:97] op_sel_hi:[1,0]
	v_cvt_pk_bf16_f32 v10, v18, v19
	v_cvt_pk_bf16_f32 v11, v20, v21
	v_cvt_pk_bf16_f32 v12, v12, v13
	v_cvt_pk_bf16_f32 v13, v26, v27
	global_store_dwordx4 v[30:31], v[10:13], off offset:256 sc1
	s_nop 1
	v_add_u32_e32 v10, 0xb0, v130
	v_ashrrev_i32_e32 v11, 31, v10
	v_lshl_add_u64 v[18:19], s[2:3], 0, v[10:11]
	v_pk_mul_f32 v[12:13], v[24:25], s[96:97] op_sel_hi:[1,0]
	v_pk_mul_f32 v[10:11], v[22:23], s[96:97] op_sel_hi:[1,0]
	s_mov_b64 s[2:3], -1
	v_cvt_pk_bf16_f32 v10, v10, v11
	v_cvt_pk_bf16_f32 v11, v12, v13
	v_cvt_pk_bf16_f32 v12, v14, v15
	v_lshlrev_b64 v[14:15], 11, v[18:19]
	v_lshl_add_u64 v[14:15], s[8:9], 0, v[14:15]
	v_lshl_add_u64 v[14:15], v[14:15], 0, s[20:21]
	v_lshl_add_u64 v[14:15], v[14:15], 0, s[58:59]
	v_cvt_pk_bf16_f32 v13, v16, v17
	v_lshl_add_u64 v[14:15], v[14:15], 0, v[122:123]
	global_store_dwordx4 v[14:15], v[10:13], off sc1
	s_nop 1
	v_pk_mul_f32 v[10:11], v[4:5], s[96:97] op_sel_hi:[1,0]
	v_pk_mul_f32 v[4:5], v[2:3], s[96:97] op_sel_hi:[1,0]
	v_cvt_pk_bf16_f32 v2, v6, v7
	v_cvt_pk_bf16_f32 v3, v8, v9
	v_cvt_pk_bf16_f32 v4, v4, v5
	v_cvt_pk_bf16_f32 v5, v10, v11
	global_store_dwordx4 v[14:15], v[2:5], off offset:256 sc1
	s_cbranch_vccnz .LBB0_964
	s_andn2_b64 vcc, exec, s[6:7]
	s_cbranch_vccnz .LBB0_963
	s_barrier
	s_branch .LBB0_963

; #define LAS __attribute__((address_space(3)))
;     DI void operator()(const f32x4 (&acc)[2][2][4][2], const Unit& u, int wr, int wc, int fr, int fq) const {
;         int lrow = 64 * wr + fr; asm volatile("" : "+v"(lrow));
;         const int cj = u.pn * 128 + 32 * wc + 8 * fq; const LAS float* bb = bl + 32 * wc + 8 * fq;
;         const f32x4 bg0 = *(const LAS f32x4*)(bb), bg1 = *(const LAS f32x4*)(bb + 4), bu0 = *(const LAS f32x4*)(bb + 128), bu1 = *(const LAS f32x4*)(bb + 132);
;         unsigned char* abase = act + (size_t)u.pm * 256 * DFF;
;         constexpr float dq = 1.0f / (W8_SCALE * H8_SCALE * PROBE_KREP);
; #pragma unroll
;         for (int ai = 0; ai < 2; ++ai) { if (u.half == 2 - ai) continue;
;             u32x2 wprev = {0u, 0u}; const bool oddq = (fq & 1) != 0;
; #pragma unroll
;             for (int m = 0; m < 4; ++m) {
;             f32x4 g0 = acc[ai][0][m][0] * dq + bg0, g1 = acc[ai][0][m][1] * dq + bg1, u0 = acc[ai][1][m][0] * dq + bu0, u1 = acc[ai][1][m][1] * dq + bu1;
;             unsigned wv[2];
; #pragma unroll
;             for (int hv = 0; hv < 2; ++hv) { const f32x4 gq = hv ? g1 : g0, uq = hv ? u1 : u0; int r = 0;
; #pragma unroll
;                 for (int q = 0; q < 4; q += 2) {
;                     f32x2 g = {fminf(gq[q], 7.0f), fminf(gq[q + 1], 7.0f)};
;                     const f32x2 up = {fminf(fmaxf(uq[q], -7.0f), 7.0f), fminf(fmaxf(uq[q + 1], -7.0f), 7.0f)};
;                     f32x2 t = __builtin_elementwise_fma(up, (f32x2){ACT8_SCALE, ACT8_SCALE}, (f32x2){ACT8_SCALE, ACT8_SCALE}) * g;
;                     const f32x2 a = g * (f32x2){-1.702f * 1.4426950408889634f, -1.702f * 1.4426950408889634f};
;                     f32x2 e = {__builtin_amdgcn_exp2f(a[0]), __builtin_amdgcn_exp2f(a[1])}; e = e + (f32x2){1.0f, 1.0f};
;                     const f32x2 rc = {__builtin_amdgcn_rcpf(e[0]), __builtin_amdgcn_rcpf(e[1])};
;                     t = t * rc;
;                     r = q ? __builtin_amdgcn_cvt_pk_fp8_f32(t[0], t[1], r, true) : __builtin_amdgcn_cvt_pk_fp8_f32(t[0], t[1], r, false); }
;                 wv[hv] = (unsigned)r; }
.LBB0_1232:
	s_mov_b32 s0, -1
	s_mov_b32 s1, s56
	s_ashr_i32 s25, s24, 31
	v_mbcnt_lo_u32_b32 v0, s0, 0
	v_mbcnt_hi_u32_b32 v0, s0, v0
	s_lshl_b32 s0, s1, 4
	s_andn2_b32 s0, s0, 63
	s_nop 0
	v_and_or_b32 v23, v0, 15, s0
	s_lshl_b32 s0, s1, 5
	s_and_b32 s3, s0, 0x60
	s_lshl_b32 s0, s3, 2
	v_ashrrev_i32_e32 v18, 4, v0
	s_add_i32 s0, s0, 0
	v_lshl_add_u32 v0, v18, 5, s0
	v_add_u32_e32 v0, 0x21000, v0
	ds_read_b128 v[14:17], v0
	ds_read_b128 v[10:13], v0 offset:16
	ds_read_b128 v[6:9], v0 offset:512
	ds_read_b128 v[2:5], v0 offset:528
	s_lshl_b64 s[0:1], s[24:25], 18
	s_add_u32 s6, s97, s0
	s_addc_u32 s7, s62, s1
	v_and_b32_e32 v22, 1, v18
	s_or_b32 s0, s3, s2
	v_lshl_add_u32 v0, v18, 3, s0
	v_lshlrev_b32_e32 v18, 3, v22
	v_sub_u32_e32 v0, v0, v18
	s_and_b64 vcc, exec, s[28:29]
	v_lshlrev_b32_e32 v24, 14, v22
	v_lshlrev_b32_e32 v25, 10, v23
	s_cbranch_vccz .LBB0_1234
	s_waitcnt lgkmcnt(0)
	v_pk_fma_f32 v[32:33], v[182:183], s[52:53], v[6:7] op_sel_hi:[1,0,1]
	v_pk_fma_f32 v[18:19], v[190:191], s[52:53], v[14:15] op_sel_hi:[1,0,1]
	v_med3_f32 v32, v32, s93, v251
	v_med3_f32 v33, v33, s93, v251
	s_mov_b32 s0, 0x41000000
	v_min_f32_e32 v18, 0x40e00000, v18
	v_min_f32_e32 v19, 0x40e00000, v19
	v_pk_fma_f32 v[32:33], v[32:33], s[0:1], s[0:1] op_sel_hi:[1,0,0]
	s_mov_b32 s2, 0xc01d265f
	v_pk_mul_f32 v[32:33], v[18:19], v[32:33]
	v_pk_mul_f32 v[18:19], v[18:19], s[2:3] op_sel_hi:[1,0]
	v_pk_fma_f32 v[30:31], v[184:185], s[52:53], v[8:9] op_sel_hi:[1,0,1]
	v_exp_f32_e32 v18, v18
	v_exp_f32_e32 v19, v19
	v_pk_fma_f32 v[20:21], v[192:193], s[52:53], v[16:17] op_sel_hi:[1,0,1]
	v_med3_f32 v30, v30, s93, v251
	v_med3_f32 v31, v31, s93, v251
	v_min_f32_e32 v20, 0x40e00000, v20
	v_min_f32_e32 v21, 0x40e00000, v21
	v_pk_fma_f32 v[30:31], v[30:31], s[0:1], s[0:1] op_sel_hi:[1,0,0]
	v_pk_add_f32 v[18:19], v[18:19], 1.0 op_sel_hi:[1,0]
	v_pk_mul_f32 v[30:31], v[20:21], v[30:31]
	v_pk_mul_f32 v[20:21], v[20:21], s[2:3] op_sel_hi:[1,0]
	v_rcp_f32_e32 v18, v18
	v_exp_f32_e32 v20, v20
	v_exp_f32_e32 v21, v21
	v_rcp_f32_e32 v19, v19
	v_pk_fma_f32 v[28:29], v[186:187], s[52:53], v[10:11] op_sel_hi:[1,0,1]
	v_pk_fma_f32 v[36:37], v[178:179], s[52:53], v[2:3] op_sel_hi:[1,0,1]
	v_pk_add_f32 v[20:21], v[20:21], 1.0 op_sel_hi:[1,0]
	v_pk_mul_f32 v[32:33], v[32:33], v[18:19]
	v_mov_b32_e32 v18, v1
	v_rcp_f32_e32 v20, v20
	v_rcp_f32_e32 v21, v21
	v_cvt_pk_fp8_f32 v18, v32, v33
	v_pk_fma_f32 v[26:27], v[188:189], s[52:53], v[12:13] op_sel_hi:[1,0,1]
	v_pk_fma_f32 v[34:35], v[180:181], s[52:53], v[4:5] op_sel_hi:[1,0,1]
	v_pk_mul_f32 v[20:21], v[30:31], v[20:21]
	v_mov_b32_e32 v19, v1
	v_cvt_pk_fp8_f32 v18, v20, v21 op_sel:[0,0,1]
	v_min_f32_e32 v20, 0x40e00000, v28
	v_min_f32_e32 v21, 0x40e00000, v29
	v_med3_f32 v28, v36, s93, v251
	v_med3_f32 v29, v37, s93, v251
	v_pk_fma_f32 v[28:29], v[28:29], s[0:1], s[0:1] op_sel_hi:[1,0,0]
	v_pk_fma_f32 v[32:33], v[168:169], s[52:53], v[8:9] op_sel_hi:[1,0,1]
	v_pk_mul_f32 v[28:29], v[20:21], v[28:29]
	v_pk_mul_f32 v[20:21], v[20:21], s[2:3] op_sel_hi:[1,0]
	v_med3_f32 v32, v32, s93, v251
	v_exp_f32_e32 v20, v20
	v_exp_f32_e32 v21, v21
	v_med3_f32 v33, v33, s93, v251
	v_pk_fma_f32 v[32:33], v[32:33], s[0:1], s[0:1] op_sel_hi:[1,0,0]
	v_pk_fma_f32 v[30:31], v[170:171], s[52:53], v[10:11] op_sel_hi:[1,0,1]
	v_pk_add_f32 v[20:21], v[20:21], 1.0 op_sel_hi:[1,0]
	v_pk_fma_f32 v[38:39], v[162:163], s[52:53], v[2:3] op_sel_hi:[1,0,1]
	v_rcp_f32_e32 v20, v20
	v_rcp_f32_e32 v21, v21
	v_pk_fma_f32 v[36:37], v[164:165], s[52:53], v[4:5] op_sel_hi:[1,0,1]
	v_lshlrev_b32_e32 v22, 14, v22
	v_lshlrev_b32_e32 v23, 10, v23
	v_pk_mul_f32 v[20:21], v[28:29], v[20:21]
	v_pk_fma_f32 v[28:29], v[172:173], s[52:53], v[12:13] op_sel_hi:[1,0,1]
	v_cvt_pk_fp8_f32 v19, v20, v21
	v_min_f32_e32 v20, 0x40e00000, v26
	v_min_f32_e32 v21, 0x40e00000, v27
	v_med3_f32 v26, v34, s93, v251
	v_med3_f32 v27, v35, s93, v251
	v_pk_fma_f32 v[26:27], v[26:27], s[0:1], s[0:1] op_sel_hi:[1,0,0]
	v_pk_fma_f32 v[34:35], v[166:167], s[52:53], v[6:7] op_sel_hi:[1,0,1]
	v_pk_mul_f32 v[26:27], v[20:21], v[26:27]
	v_pk_mul_f32 v[20:21], v[20:21], s[2:3] op_sel_hi:[1,0]
	v_med3_f32 v34, v34, s93, v251
	v_exp_f32_e32 v20, v20
	v_exp_f32_e32 v21, v21
	v_med3_f32 v35, v35, s93, v251
	v_pk_fma_f32 v[34:35], v[34:35], s[0:1], s[0:1] op_sel_hi:[1,0,0]
	v_pk_add_f32 v[20:21], v[20:21], 1.0 op_sel_hi:[1,0]
	v_pk_fma_f32 v[40:41], v[130:131], s[52:53], v[2:3] op_sel_hi:[1,0,1]
	v_rcp_f32_e32 v20, v20
	v_rcp_f32_e32 v21, v21
	s_nop 0
	v_pk_mul_f32 v[20:21], v[26:27], v[20:21]
	s_nop 0
	v_cvt_pk_fp8_f32 v19, v20, v21 op_sel:[0,0,1]
	v_pk_fma_f32 v[20:21], v[174:175], s[52:53], v[14:15] op_sel_hi:[1,0,1]
	v_pk_fma_f32 v[26:27], v[176:177], s[52:53], v[16:17] op_sel_hi:[1,0,1]
	v_min_f32_e32 v20, 0x40e00000, v20
	v_min_f32_e32 v21, 0x40e00000, v21
	v_pk_mul_f32 v[34:35], v[20:21], v[34:35]
	v_pk_mul_f32 v[20:21], v[20:21], s[2:3] op_sel_hi:[1,0]
	v_min_f32_e32 v26, 0x40e00000, v26
	v_exp_f32_e32 v20, v20
	v_exp_f32_e32 v21, v21
	v_min_f32_e32 v27, 0x40e00000, v27
	v_pk_mul_f32 v[32:33], v[26:27], v[32:33]
	v_pk_mul_f32 v[26:27], v[26:27], s[2:3] op_sel_hi:[1,0]
	v_pk_add_f32 v[20:21], v[20:21], 1.0 op_sel_hi:[1,0]
	v_exp_f32_e32 v26, v26
	v_exp_f32_e32 v27, v27
	v_rcp_f32_e32 v20, v20
	v_rcp_f32_e32 v21, v21
	v_pk_add_f32 v[26:27], v[26:27], 1.0 op_sel_hi:[1,0]
	s_nop 0
	v_rcp_f32_e32 v26, v26
	v_pk_mul_f32 v[34:35], v[34:35], v[20:21]
	v_mov_b32_e32 v20, v1
	v_rcp_f32_e32 v27, v27
	v_cvt_pk_fp8_f32 v20, v34, v35
	v_mov_b32_e32 v21, v1
	v_pk_fma_f32 v[34:35], v[150:151], s[52:53], v[6:7] op_sel_hi:[1,0,1]
	v_pk_mul_f32 v[26:27], v[32:33], v[26:27]
	v_med3_f32 v34, v34, s93, v251
;     DI void operator()(const f32x4 (&acc)[2][2][4][2], const Unit& u, int wr, int wc, int fr, int fq) const {
;     ...
;         for (int ai = 0; ai < 2; ++ai) { if (u.half == 2 - ai) continue;
;             u32x2 wprev = {0u, 0u}; const bool oddq = (fq & 1) != 0;
; #pragma unroll
;             for (int m = 0; m < 4; ++m) {
;             f32x4 g0 = acc[ai][0][m][0] * dq + bg0, g1 = acc[ai][0][m][1] * dq + bg1, u0 = acc[ai][1][m][0] * dq + bu0, u1 = acc[ai][1][m][1] * dq + bu1;
;             unsigned wv[2];
; #pragma unroll
;             for (int hv = 0; hv < 2; ++hv) { const f32x4 gq = hv ? g1 : g0, uq = hv ? u1 : u0; int r = 0;
; #pragma unroll
;                 for (int q = 0; q < 4; q += 2) {
;                     f32x2 g = {fminf(gq[q], 7.0f), fminf(gq[q + 1], 7.0f)};
;                     const f32x2 up = {fminf(fmaxf(uq[q], -7.0f), 7.0f), fminf(fmaxf(uq[q + 1], -7.0f), 7.0f)};
;                     f32x2 t = __builtin_elementwise_fma(up, (f32x2){ACT8_SCALE, ACT8_SCALE}, (f32x2){ACT8_SCALE, ACT8_SCALE}) * g;
;                     const f32x2 a = g * (f32x2){-1.702f * 1.4426950408889634f, -1.702f * 1.4426950408889634f};
;                     f32x2 e = {__builtin_amdgcn_exp2f(a[0]), __builtin_amdgcn_exp2f(a[1])}; e = e + (f32x2){1.0f, 1.0f};
;                     const f32x2 rc = {__builtin_amdgcn_rcpf(e[0]), __builtin_amdgcn_rcpf(e[1])};
;                     t = t * rc;
;                     r = q ? __builtin_amdgcn_cvt_pk_fp8_f32(t[0], t[1], r, true) : __builtin_amdgcn_cvt_pk_fp8_f32(t[0], t[1], r, false); }
;                 wv[hv] = (unsigned)r; }
;             u32x2 w; w.x = wv[0]; w.y = wv[1];
;             if ((m & 1) == 0) wprev = w;
;             else {
;                 const auto rx = __builtin_amdgcn_permlane16_swap(wprev.x, w.x, false, false), ry = __builtin_amdgcn_permlane16_swap(wprev.y, w.y, false, false);
;                 u32x4 ww; ww.x = rx[0]; ww.y = ry[0]; ww.z = rx[1]; ww.w = ry[1];
;                 const unsigned off = (unsigned)((128 * ai + 16 * (m - 1 + (oddq ? 1 : 0)) + lrow) * DFF + cj - (oddq ? 8 : 0));
;                 *(u32x4*)(abase + off) = ww; }
;             asm volatile("" ::: "memory"); } }
	v_cvt_pk_fp8_f32 v20, v26, v27 op_sel:[0,0,1]
	v_min_f32_e32 v26, 0x40e00000, v30
	v_min_f32_e32 v27, 0x40e00000, v31
	v_med3_f32 v30, v38, s93, v251
	v_med3_f32 v31, v39, s93, v251
	v_pk_fma_f32 v[30:31], v[30:31], s[0:1], s[0:1] op_sel_hi:[1,0,0]
	v_permlane16_swap_b32_e32 v18, v20
	v_pk_mul_f32 v[30:31], v[26:27], v[30:31]
	v_pk_mul_f32 v[26:27], v[26:27], s[2:3] op_sel_hi:[1,0]
	v_med3_f32 v35, v35, s93, v251
	v_exp_f32_e32 v26, v26
	v_exp_f32_e32 v27, v27
	v_pk_fma_f32 v[34:35], v[34:35], s[0:1], s[0:1] op_sel_hi:[1,0,0]
	v_pk_fma_f32 v[32:33], v[152:153], s[52:53], v[8:9] op_sel_hi:[1,0,1]
	v_pk_fma_f32 v[38:39], v[146:147], s[52:53], v[2:3] op_sel_hi:[1,0,1]
	v_pk_add_f32 v[26:27], v[26:27], 1.0 op_sel_hi:[1,0]
	v_med3_f32 v32, v32, s93, v251
	v_rcp_f32_e32 v26, v26
	v_rcp_f32_e32 v27, v27
	v_med3_f32 v33, v33, s93, v251
	v_pk_fma_f32 v[32:33], v[32:33], s[0:1], s[0:1] op_sel_hi:[1,0,0]
	v_pk_mul_f32 v[26:27], v[30:31], v[26:27]
	s_nop 0
	v_cvt_pk_fp8_f32 v21, v26, v27
	v_min_f32_e32 v26, 0x40e00000, v28
	v_min_f32_e32 v27, 0x40e00000, v29
	v_med3_f32 v28, v36, s93, v251
	v_med3_f32 v29, v37, s93, v251
	v_pk_fma_f32 v[28:29], v[28:29], s[0:1], s[0:1] op_sel_hi:[1,0,0]
	v_pk_fma_f32 v[30:31], v[154:155], s[52:53], v[10:11] op_sel_hi:[1,0,1]
	v_pk_mul_f32 v[28:29], v[26:27], v[28:29]
	v_pk_mul_f32 v[26:27], v[26:27], s[2:3] op_sel_hi:[1,0]
	v_pk_fma_f32 v[36:37], v[148:149], s[52:53], v[4:5] op_sel_hi:[1,0,1]
	v_exp_f32_e32 v26, v26
	v_exp_f32_e32 v27, v27
	s_nop 0
	v_pk_add_f32 v[26:27], v[26:27], 1.0 op_sel_hi:[1,0]
	s_nop 0
	v_rcp_f32_e32 v26, v26
	v_rcp_f32_e32 v27, v27
	s_nop 0
	v_pk_mul_f32 v[26:27], v[28:29], v[26:27]
	s_nop 0
	v_cvt_pk_fp8_f32 v21, v26, v27 op_sel:[0,0,1]
	v_add3_u32 v26, v22, v23, v0
	v_pk_fma_f32 v[28:29], v[156:157], s[52:53], v[12:13] op_sel_hi:[1,0,1]
	v_permlane16_swap_b32_e32 v19, v21
	global_store_dwordx4 v26, v[18:21], s[6:7] sc1
	v_add_u32_e32 v26, 0x8000, v26
	s_nop 0
	v_pk_fma_f32 v[18:19], v[158:159], s[52:53], v[14:15] op_sel_hi:[1,0,1]
	v_pk_fma_f32 v[20:21], v[160:161], s[52:53], v[16:17] op_sel_hi:[1,0,1]
	v_min_f32_e32 v18, 0x40e00000, v18
	v_min_f32_e32 v19, 0x40e00000, v19
	v_pk_mul_f32 v[34:35], v[18:19], v[34:35]
	v_pk_mul_f32 v[18:19], v[18:19], s[2:3] op_sel_hi:[1,0]
	v_min_f32_e32 v20, 0x40e00000, v20
	v_exp_f32_e32 v18, v18
	v_exp_f32_e32 v19, v19
	v_min_f32_e32 v21, 0x40e00000, v21
	v_pk_mul_f32 v[32:33], v[20:21], v[32:33]
	v_pk_mul_f32 v[20:21], v[20:21], s[2:3] op_sel_hi:[1,0]
	v_pk_add_f32 v[18:19], v[18:19], 1.0 op_sel_hi:[1,0]
	v_exp_f32_e32 v20, v20
	v_exp_f32_e32 v21, v21
	v_rcp_f32_e32 v18, v18
	v_rcp_f32_e32 v19, v19
	v_pk_add_f32 v[20:21], v[20:21], 1.0 op_sel_hi:[1,0]
	s_nop 0
	v_rcp_f32_e32 v20, v20
	v_pk_mul_f32 v[34:35], v[34:35], v[18:19]
	v_mov_b32_e32 v18, v1
	v_rcp_f32_e32 v21, v21
	v_cvt_pk_fp8_f32 v18, v34, v35
	v_mov_b32_e32 v19, v1
	v_pk_fma_f32 v[34:35], v[136:137], s[52:53], v[8:9] op_sel_hi:[1,0,1]
	v_pk_mul_f32 v[20:21], v[32:33], v[20:21]
	v_med3_f32 v34, v34, s93, v251
	v_cvt_pk_fp8_f32 v18, v20, v21 op_sel:[0,0,1]
	v_min_f32_e32 v20, 0x40e00000, v30
	v_min_f32_e32 v21, 0x40e00000, v31
	v_med3_f32 v30, v38, s93, v251
	v_med3_f32 v31, v39, s93, v251
	v_pk_fma_f32 v[30:31], v[30:31], s[0:1], s[0:1] op_sel_hi:[1,0,0]
	v_med3_f32 v35, v35, s93, v251
	v_pk_mul_f32 v[30:31], v[20:21], v[30:31]
	v_pk_mul_f32 v[20:21], v[20:21], s[2:3] op_sel_hi:[1,0]
	v_pk_fma_f32 v[34:35], v[34:35], s[0:1], s[0:1] op_sel_hi:[1,0,0]
	v_exp_f32_e32 v20, v20
	v_exp_f32_e32 v21, v21
	v_pk_fma_f32 v[32:33], v[138:139], s[52:53], v[10:11] op_sel_hi:[1,0,1]
	v_pk_fma_f32 v[38:39], v[132:133], s[52:53], v[4:5] op_sel_hi:[1,0,1]
	v_pk_add_f32 v[20:21], v[20:21], 1.0 op_sel_hi:[1,0]
	s_nop 0
	v_rcp_f32_e32 v20, v20
	v_rcp_f32_e32 v21, v21
	s_nop 0
	v_pk_mul_f32 v[20:21], v[30:31], v[20:21]
	s_nop 0
	v_cvt_pk_fp8_f32 v19, v20, v21
	v_min_f32_e32 v20, 0x40e00000, v28
	v_min_f32_e32 v21, 0x40e00000, v29
	v_med3_f32 v28, v36, s93, v251
	v_med3_f32 v29, v37, s93, v251
	v_pk_fma_f32 v[28:29], v[28:29], s[0:1], s[0:1] op_sel_hi:[1,0,0]
	v_pk_fma_f32 v[36:37], v[134:135], s[52:53], v[6:7] op_sel_hi:[1,0,1]
	v_pk_mul_f32 v[28:29], v[20:21], v[28:29]
	v_pk_mul_f32 v[20:21], v[20:21], s[2:3] op_sel_hi:[1,0]
	v_med3_f32 v36, v36, s93, v251
	v_exp_f32_e32 v20, v20
	v_exp_f32_e32 v21, v21
	v_med3_f32 v37, v37, s93, v251
	v_pk_fma_f32 v[36:37], v[36:37], s[0:1], s[0:1] op_sel_hi:[1,0,0]
	v_pk_fma_f32 v[30:31], v[140:141], s[52:53], v[12:13] op_sel_hi:[1,0,1]
	v_pk_add_f32 v[20:21], v[20:21], 1.0 op_sel_hi:[1,0]
	s_nop 0
	v_rcp_f32_e32 v20, v20
	v_rcp_f32_e32 v21, v21
	s_nop 0
	v_pk_mul_f32 v[20:21], v[28:29], v[20:21]
	s_nop 0
	v_cvt_pk_fp8_f32 v19, v20, v21 op_sel:[0,0,1]
	v_pk_fma_f32 v[20:21], v[142:143], s[52:53], v[14:15] op_sel_hi:[1,0,1]
	v_pk_fma_f32 v[28:29], v[144:145], s[52:53], v[16:17] op_sel_hi:[1,0,1]
	v_min_f32_e32 v20, 0x40e00000, v20
	v_min_f32_e32 v21, 0x40e00000, v21
	v_pk_mul_f32 v[36:37], v[20:21], v[36:37]
	v_pk_mul_f32 v[20:21], v[20:21], s[2:3] op_sel_hi:[1,0]
	v_min_f32_e32 v28, 0x40e00000, v28
	v_exp_f32_e32 v20, v20
	v_exp_f32_e32 v21, v21
	v_min_f32_e32 v29, 0x40e00000, v29
	v_pk_mul_f32 v[34:35], v[28:29], v[34:35]
	v_pk_mul_f32 v[28:29], v[28:29], s[2:3] op_sel_hi:[1,0]
	v_pk_add_f32 v[20:21], v[20:21], 1.0 op_sel_hi:[1,0]
	v_exp_f32_e32 v28, v28
	v_exp_f32_e32 v29, v29
	v_rcp_f32_e32 v20, v20
	v_rcp_f32_e32 v21, v21
	v_pk_add_f32 v[28:29], v[28:29], 1.0 op_sel_hi:[1,0]
	s_nop 0
	v_rcp_f32_e32 v28, v28
	v_pk_mul_f32 v[36:37], v[36:37], v[20:21]
	v_mov_b32_e32 v20, v1
	v_rcp_f32_e32 v29, v29
	v_cvt_pk_fp8_f32 v20, v36, v37
	v_mov_b32_e32 v21, v1
	v_pk_mul_f32 v[28:29], v[34:35], v[28:29]
	s_nop 0
	v_cvt_pk_fp8_f32 v20, v28, v29 op_sel:[0,0,1]
	v_min_f32_e32 v28, 0x40e00000, v32
	v_min_f32_e32 v29, 0x40e00000, v33
	v_med3_f32 v32, v40, s93, v251
	v_med3_f32 v33, v41, s93, v251
	v_pk_fma_f32 v[32:33], v[32:33], s[0:1], s[0:1] op_sel_hi:[1,0,0]
	v_permlane16_swap_b32_e32 v18, v20
	v_pk_mul_f32 v[32:33], v[28:29], v[32:33]
	v_pk_mul_f32 v[28:29], v[28:29], s[2:3] op_sel_hi:[1,0]
	s_nop 0
	v_exp_f32_e32 v28, v28
	v_exp_f32_e32 v29, v29
	s_nop 0
	v_pk_add_f32 v[28:29], v[28:29], 1.0 op_sel_hi:[1,0]
	s_nop 0
	v_rcp_f32_e32 v28, v28
	v_rcp_f32_e32 v29, v29
	s_nop 0
	v_pk_mul_f32 v[28:29], v[32:33], v[28:29]
	s_nop 0
	v_cvt_pk_fp8_f32 v21, v28, v29
	v_min_f32_e32 v28, 0x40e00000, v30
	v_min_f32_e32 v29, 0x40e00000, v31
	v_med3_f32 v30, v38, s93, v251
	v_med3_f32 v31, v39, s93, v251
	v_pk_fma_f32 v[30:31], v[30:31], s[0:1], s[0:1] op_sel_hi:[1,0,0]
	s_nop 0
	v_pk_mul_f32 v[30:31], v[28:29], v[30:31]
	v_pk_mul_f32 v[28:29], v[28:29], s[2:3] op_sel_hi:[1,0]
	s_nop 0
	v_exp_f32_e32 v28, v28
	v_exp_f32_e32 v29, v29
	s_nop 0
	v_pk_add_f32 v[28:29], v[28:29], 1.0 op_sel_hi:[1,0]
	s_nop 0
	v_rcp_f32_e32 v28, v28
	v_rcp_f32_e32 v29, v29
	s_nop 0
	v_pk_mul_f32 v[28:29], v[30:31], v[28:29]
	s_nop 0
	v_cvt_pk_fp8_f32 v21, v28, v29 op_sel:[0,0,1]
	s_nop 1
	v_permlane16_swap_b32_e32 v19, v21
	global_store_dwordx4 v26, v[18:21], s[6:7] sc1
	s_cbranch_execz .LBB0_1235
;     DI void operator()(const f32x4 (&acc)[2][2][4][2], const Unit& u, int wr, int wc, int fr, int fq) const {
;     ...
;         for (int ai = 0; ai < 2; ++ai) { if (u.half == 2 - ai) continue;
;             u32x2 wprev = {0u, 0u}; const bool oddq = (fq & 1) != 0;
	s_branch .LBB0_1236

;     DI void operator()(const f32x4 (&acc)[2][2][4][2], const Unit& u, int wr, int wc, int fr, int fq) const {
;     ...
;         for (int ai = 0; ai < 2; ++ai) { if (u.half == 2 - ai) continue;
;             u32x2 wprev = {0u, 0u}; const bool oddq = (fq & 1) != 0;
; #pragma unroll
;             for (int m = 0; m < 4; ++m) {
;             f32x4 g0 = acc[ai][0][m][0] * dq + bg0, g1 = acc[ai][0][m][1] * dq + bg1, u0 = acc[ai][1][m][0] * dq + bu0, u1 = acc[ai][1][m][1] * dq + bu1;
;             unsigned wv[2];
; #pragma unroll
;             for (int hv = 0; hv < 2; ++hv) { const f32x4 gq = hv ? g1 : g0, uq = hv ? u1 : u0; int r = 0;
; #pragma unroll
;                 for (int q = 0; q < 4; q += 2) {
;                     f32x2 g = {fminf(gq[q], 7.0f), fminf(gq[q + 1], 7.0f)};
;                     const f32x2 up = {fminf(fmaxf(uq[q], -7.0f), 7.0f), fminf(fmaxf(uq[q + 1], -7.0f), 7.0f)};
;                     f32x2 t = __builtin_elementwise_fma(up, (f32x2){ACT8_SCALE, ACT8_SCALE}, (f32x2){ACT8_SCALE, ACT8_SCALE}) * g;
;                     const f32x2 a = g * (f32x2){-1.702f * 1.4426950408889634f, -1.702f * 1.4426950408889634f};
;                     f32x2 e = {__builtin_amdgcn_exp2f(a[0]), __builtin_amdgcn_exp2f(a[1])}; e = e + (f32x2){1.0f, 1.0f};
;                     const f32x2 rc = {__builtin_amdgcn_rcpf(e[0]), __builtin_amdgcn_rcpf(e[1])};
;                     t = t * rc;
;                     r = q ? __builtin_amdgcn_cvt_pk_fp8_f32(t[0], t[1], r, true) : __builtin_amdgcn_cvt_pk_fp8_f32(t[0], t[1], r, false); }
;                 wv[hv] = (unsigned)r; }
.LBB0_1236:
	s_andn2_b64 vcc, exec, s[22:23]
	s_cbranch_vccnz .LBB0_1238
	s_waitcnt lgkmcnt(0)
	v_pk_fma_f32 v[30:31], v[118:119], s[52:53], v[6:7] op_sel_hi:[1,0,1]
	v_pk_fma_f32 v[18:19], v[126:127], s[52:53], v[14:15] op_sel_hi:[1,0,1]
	v_med3_f32 v30, v30, s93, v251
	v_med3_f32 v31, v31, s93, v251
	s_mov_b32 s0, 0x41000000
	v_min_f32_e32 v18, 0x40e00000, v18
	v_min_f32_e32 v19, 0x40e00000, v19
	v_pk_fma_f32 v[30:31], v[30:31], s[0:1], s[0:1] op_sel_hi:[1,0,0]
	s_mov_b32 s2, 0xc01d265f
	v_pk_mul_f32 v[30:31], v[18:19], v[30:31]
	v_pk_mul_f32 v[18:19], v[18:19], s[2:3] op_sel_hi:[1,0]
	v_pk_fma_f32 v[28:29], v[120:121], s[52:53], v[8:9] op_sel_hi:[1,0,1]
	v_exp_f32_e32 v18, v18
	v_exp_f32_e32 v19, v19
	v_pk_fma_f32 v[20:21], v[128:129], s[52:53], v[16:17] op_sel_hi:[1,0,1]
	v_med3_f32 v28, v28, s93, v251
	v_med3_f32 v29, v29, s93, v251
	v_min_f32_e32 v20, 0x40e00000, v20
	v_min_f32_e32 v21, 0x40e00000, v21
	v_pk_fma_f32 v[28:29], v[28:29], s[0:1], s[0:1] op_sel_hi:[1,0,0]
	v_pk_add_f32 v[18:19], v[18:19], 1.0 op_sel_hi:[1,0]
	v_pk_mul_f32 v[28:29], v[20:21], v[28:29]
	v_pk_mul_f32 v[20:21], v[20:21], s[2:3] op_sel_hi:[1,0]
	v_rcp_f32_e32 v18, v18
	v_exp_f32_e32 v20, v20
	v_exp_f32_e32 v21, v21
	v_rcp_f32_e32 v19, v19
	v_pk_fma_f32 v[26:27], v[122:123], s[52:53], v[10:11] op_sel_hi:[1,0,1]
	v_pk_fma_f32 v[34:35], v[114:115], s[52:53], v[2:3] op_sel_hi:[1,0,1]
	v_pk_add_f32 v[20:21], v[20:21], 1.0 op_sel_hi:[1,0]
	v_pk_mul_f32 v[30:31], v[30:31], v[18:19]
	v_mov_b32_e32 v18, v1
	v_rcp_f32_e32 v20, v20
	v_rcp_f32_e32 v21, v21
	v_cvt_pk_fp8_f32 v18, v30, v31
	v_pk_fma_f32 v[24:25], v[124:125], s[52:53], v[12:13] op_sel_hi:[1,0,1]
	v_pk_fma_f32 v[32:33], v[116:117], s[52:53], v[4:5] op_sel_hi:[1,0,1]
	v_pk_mul_f32 v[20:21], v[28:29], v[20:21]
	v_mov_b32_e32 v19, v1
	v_cvt_pk_fp8_f32 v18, v20, v21 op_sel:[0,0,1]
	v_min_f32_e32 v20, 0x40e00000, v26
	v_min_f32_e32 v21, 0x40e00000, v27
	v_med3_f32 v26, v34, s93, v251
	v_med3_f32 v27, v35, s93, v251
	v_pk_fma_f32 v[26:27], v[26:27], s[0:1], s[0:1] op_sel_hi:[1,0,0]
	v_pk_fma_f32 v[30:31], v[104:105], s[52:53], v[8:9] op_sel_hi:[1,0,1]
	v_pk_mul_f32 v[26:27], v[20:21], v[26:27]
	v_pk_mul_f32 v[20:21], v[20:21], s[2:3] op_sel_hi:[1,0]
	v_med3_f32 v30, v30, s93, v251
	v_exp_f32_e32 v20, v20
	v_exp_f32_e32 v21, v21
	v_med3_f32 v31, v31, s93, v251
	v_pk_fma_f32 v[30:31], v[30:31], s[0:1], s[0:1] op_sel_hi:[1,0,0]
	v_pk_fma_f32 v[28:29], v[106:107], s[52:53], v[10:11] op_sel_hi:[1,0,1]
	v_pk_add_f32 v[20:21], v[20:21], 1.0 op_sel_hi:[1,0]
	v_pk_fma_f32 v[36:37], v[98:99], s[52:53], v[2:3] op_sel_hi:[1,0,1]
	v_rcp_f32_e32 v20, v20
	v_rcp_f32_e32 v21, v21
	v_pk_fma_f32 v[34:35], v[100:101], s[52:53], v[4:5] op_sel_hi:[1,0,1]
	v_add_u32_e32 v23, 0x20000, v23
	v_pk_mul_f32 v[20:21], v[26:27], v[20:21]
	v_pk_fma_f32 v[26:27], v[108:109], s[52:53], v[12:13] op_sel_hi:[1,0,1]
	v_cvt_pk_fp8_f32 v19, v20, v21
	v_min_f32_e32 v20, 0x40e00000, v24
	v_min_f32_e32 v21, 0x40e00000, v25
	v_med3_f32 v24, v32, s93, v251
	v_med3_f32 v25, v33, s93, v251
	v_pk_fma_f32 v[24:25], v[24:25], s[0:1], s[0:1] op_sel_hi:[1,0,0]
	v_pk_fma_f32 v[32:33], v[102:103], s[52:53], v[6:7] op_sel_hi:[1,0,1]
	v_pk_mul_f32 v[24:25], v[20:21], v[24:25]
	v_pk_mul_f32 v[20:21], v[20:21], s[2:3] op_sel_hi:[1,0]
	v_med3_f32 v32, v32, s93, v251
	v_exp_f32_e32 v20, v20
	v_exp_f32_e32 v21, v21
	v_med3_f32 v33, v33, s93, v251
	v_pk_fma_f32 v[32:33], v[32:33], s[0:1], s[0:1] op_sel_hi:[1,0,0]
	v_pk_add_f32 v[20:21], v[20:21], 1.0 op_sel_hi:[1,0]
	s_nop 0
	v_rcp_f32_e32 v20, v20
	v_rcp_f32_e32 v21, v21
	s_nop 0
	v_pk_mul_f32 v[20:21], v[24:25], v[20:21]
	s_nop 0
	v_cvt_pk_fp8_f32 v19, v20, v21 op_sel:[0,0,1]
	v_pk_fma_f32 v[20:21], v[110:111], s[52:53], v[14:15] op_sel_hi:[1,0,1]
	v_pk_fma_f32 v[24:25], v[112:113], s[52:53], v[16:17] op_sel_hi:[1,0,1]
	v_min_f32_e32 v20, 0x40e00000, v20
	v_min_f32_e32 v21, 0x40e00000, v21
	v_pk_mul_f32 v[32:33], v[20:21], v[32:33]
	v_pk_mul_f32 v[20:21], v[20:21], s[2:3] op_sel_hi:[1,0]
	v_min_f32_e32 v24, 0x40e00000, v24
	v_exp_f32_e32 v20, v20
	v_exp_f32_e32 v21, v21
	v_min_f32_e32 v25, 0x40e00000, v25
	v_pk_mul_f32 v[30:31], v[24:25], v[30:31]
	v_pk_mul_f32 v[24:25], v[24:25], s[2:3] op_sel_hi:[1,0]
	v_pk_add_f32 v[20:21], v[20:21], 1.0 op_sel_hi:[1,0]
	v_exp_f32_e32 v24, v24
	v_exp_f32_e32 v25, v25
	v_rcp_f32_e32 v20, v20
	v_rcp_f32_e32 v21, v21
	v_pk_add_f32 v[24:25], v[24:25], 1.0 op_sel_hi:[1,0]
	s_nop 0
	v_rcp_f32_e32 v24, v24
	v_pk_mul_f32 v[32:33], v[32:33], v[20:21]
	v_mov_b32_e32 v20, v1
	v_rcp_f32_e32 v25, v25
	v_cvt_pk_fp8_f32 v20, v32, v33
	v_mov_b32_e32 v21, v1
	v_pk_fma_f32 v[32:33], v[84:85], s[52:53], v[4:5] op_sel_hi:[1,0,1]
	v_pk_mul_f32 v[24:25], v[30:31], v[24:25]
	v_pk_fma_f32 v[30:31], v[86:87], s[52:53], v[6:7] op_sel_hi:[1,0,1]
	v_cvt_pk_fp8_f32 v20, v24, v25 op_sel:[0,0,1]
	v_min_f32_e32 v24, 0x40e00000, v28
	v_min_f32_e32 v25, 0x40e00000, v29
	v_med3_f32 v28, v36, s93, v251
	v_med3_f32 v29, v37, s93, v251
	v_pk_fma_f32 v[28:29], v[28:29], s[0:1], s[0:1] op_sel_hi:[1,0,0]
	v_permlane16_swap_b32_e32 v18, v20
	v_pk_mul_f32 v[28:29], v[24:25], v[28:29]
	v_pk_mul_f32 v[24:25], v[24:25], s[2:3] op_sel_hi:[1,0]
	v_med3_f32 v30, v30, s93, v251
	v_exp_f32_e32 v24, v24
	v_exp_f32_e32 v25, v25
	v_med3_f32 v31, v31, s93, v251
	v_pk_fma_f32 v[30:31], v[30:31], s[0:1], s[0:1] op_sel_hi:[1,0,0]
	v_pk_fma_f32 v[6:7], v[70:71], s[52:53], v[6:7] op_sel_hi:[1,0,1]
	v_pk_add_f32 v[24:25], v[24:25], 1.0 op_sel_hi:[1,0]
	v_med3_f32 v6, v6, s93, v251
	v_rcp_f32_e32 v24, v24
	v_rcp_f32_e32 v25, v25
	v_med3_f32 v7, v7, s93, v251
	v_pk_fma_f32 v[6:7], v[6:7], s[0:1], s[0:1] op_sel_hi:[1,0,0]
;     DI void operator()(const f32x4 (&acc)[2][2][4][2], const Unit& u, int wr, int wc, int fr, int fq) const {
;     ...
;         for (int ai = 0; ai < 2; ++ai) { if (u.half == 2 - ai) continue;
;             u32x2 wprev = {0u, 0u}; const bool oddq = (fq & 1) != 0;
; #pragma unroll
;             for (int m = 0; m < 4; ++m) {
;             f32x4 g0 = acc[ai][0][m][0] * dq + bg0, g1 = acc[ai][0][m][1] * dq + bg1, u0 = acc[ai][1][m][0] * dq + bu0, u1 = acc[ai][1][m][1] * dq + bu1;
;             unsigned wv[2];
; #pragma unroll
;             for (int hv = 0; hv < 2; ++hv) { const f32x4 gq = hv ? g1 : g0, uq = hv ? u1 : u0; int r = 0;
; #pragma unroll
;                 for (int q = 0; q < 4; q += 2) {
;                     f32x2 g = {fminf(gq[q], 7.0f), fminf(gq[q + 1], 7.0f)};
;                     const f32x2 up = {fminf(fmaxf(uq[q], -7.0f), 7.0f), fminf(fmaxf(uq[q + 1], -7.0f), 7.0f)};
;                     f32x2 t = __builtin_elementwise_fma(up, (f32x2){ACT8_SCALE, ACT8_SCALE}, (f32x2){ACT8_SCALE, ACT8_SCALE}) * g;
;                     const f32x2 a = g * (f32x2){-1.702f * 1.4426950408889634f, -1.702f * 1.4426950408889634f};
;                     f32x2 e = {__builtin_amdgcn_exp2f(a[0]), __builtin_amdgcn_exp2f(a[1])}; e = e + (f32x2){1.0f, 1.0f};
;                     const f32x2 rc = {__builtin_amdgcn_rcpf(e[0]), __builtin_amdgcn_rcpf(e[1])};
;                     t = t * rc;
;                     r = q ? __builtin_amdgcn_cvt_pk_fp8_f32(t[0], t[1], r, true) : __builtin_amdgcn_cvt_pk_fp8_f32(t[0], t[1], r, false); }
;                 wv[hv] = (unsigned)r; }
;             u32x2 w; w.x = wv[0]; w.y = wv[1];
;             if ((m & 1) == 0) wprev = w;
;             else {
;                 const auto rx = __builtin_amdgcn_permlane16_swap(wprev.x, w.x, false, false), ry = __builtin_amdgcn_permlane16_swap(wprev.y, w.y, false, false);
;                 u32x4 ww; ww.x = rx[0]; ww.y = ry[0]; ww.z = rx[1]; ww.w = ry[1];
;                 const unsigned off = (unsigned)((128 * ai + 16 * (m - 1 + (oddq ? 1 : 0)) + lrow) * DFF + cj - (oddq ? 8 : 0));
;                 *(u32x4*)(abase + off) = ww; }
;             asm volatile("" ::: "memory"); } }
	v_pk_fma_f32 v[4:5], v[68:69], s[52:53], v[4:5] op_sel_hi:[1,0,1]
	v_pk_mul_f32 v[24:25], v[28:29], v[24:25]
	v_pk_fma_f32 v[28:29], v[88:89], s[52:53], v[8:9] op_sel_hi:[1,0,1]
	v_cvt_pk_fp8_f32 v21, v24, v25
	v_min_f32_e32 v24, 0x40e00000, v26
	v_min_f32_e32 v25, 0x40e00000, v27
	v_med3_f32 v26, v34, s93, v251
	v_med3_f32 v27, v35, s93, v251
	v_pk_fma_f32 v[26:27], v[26:27], s[0:1], s[0:1] op_sel_hi:[1,0,0]
	v_med3_f32 v28, v28, s93, v251
	v_pk_mul_f32 v[26:27], v[24:25], v[26:27]
	v_pk_mul_f32 v[24:25], v[24:25], s[2:3] op_sel_hi:[1,0]
	v_med3_f32 v29, v29, s93, v251
	v_exp_f32_e32 v24, v24
	v_exp_f32_e32 v25, v25
	v_pk_fma_f32 v[28:29], v[28:29], s[0:1], s[0:1] op_sel_hi:[1,0,0]
	v_pk_fma_f32 v[34:35], v[82:83], s[52:53], v[2:3] op_sel_hi:[1,0,1]
	v_pk_fma_f32 v[8:9], v[72:73], s[52:53], v[8:9] op_sel_hi:[1,0,1]
	v_pk_add_f32 v[24:25], v[24:25], 1.0 op_sel_hi:[1,0]
	v_med3_f32 v8, v8, s93, v251
	v_rcp_f32_e32 v24, v24
	v_rcp_f32_e32 v25, v25
	v_med3_f32 v9, v9, s93, v251
	v_pk_fma_f32 v[8:9], v[8:9], s[0:1], s[0:1] op_sel_hi:[1,0,0]
	v_pk_fma_f32 v[2:3], v[66:67], s[52:53], v[2:3] op_sel_hi:[1,0,1]
	v_pk_mul_f32 v[24:25], v[26:27], v[24:25]
	v_pk_fma_f32 v[26:27], v[90:91], s[52:53], v[10:11] op_sel_hi:[1,0,1]
	v_cvt_pk_fp8_f32 v21, v24, v25 op_sel:[0,0,1]
	v_add3_u32 v24, v23, v0, v22
	v_pk_fma_f32 v[10:11], v[74:75], s[52:53], v[10:11] op_sel_hi:[1,0,1]
	v_med3_f32 v2, v2, s93, v251
	v_permlane16_swap_b32_e32 v19, v21
	global_store_dwordx4 v24, v[18:21], s[6:7] sc1
	v_pk_fma_f32 v[24:25], v[92:93], s[52:53], v[12:13] op_sel_hi:[1,0,1]
	v_med3_f32 v3, v3, s93, v251
	v_pk_fma_f32 v[18:19], v[94:95], s[52:53], v[14:15] op_sel_hi:[1,0,1]
	v_pk_fma_f32 v[20:21], v[96:97], s[52:53], v[16:17] op_sel_hi:[1,0,1]
	v_min_f32_e32 v18, 0x40e00000, v18
	v_min_f32_e32 v19, 0x40e00000, v19
	v_pk_mul_f32 v[30:31], v[18:19], v[30:31]
	v_pk_mul_f32 v[18:19], v[18:19], s[2:3] op_sel_hi:[1,0]
	v_min_f32_e32 v20, 0x40e00000, v20
	v_exp_f32_e32 v18, v18
	v_exp_f32_e32 v19, v19
	v_min_f32_e32 v21, 0x40e00000, v21
	v_pk_mul_f32 v[28:29], v[20:21], v[28:29]
	v_pk_mul_f32 v[20:21], v[20:21], s[2:3] op_sel_hi:[1,0]
	v_pk_add_f32 v[18:19], v[18:19], 1.0 op_sel_hi:[1,0]
	v_exp_f32_e32 v20, v20
	v_exp_f32_e32 v21, v21
	v_rcp_f32_e32 v18, v18
	v_rcp_f32_e32 v19, v19
	v_pk_fma_f32 v[14:15], v[78:79], s[52:53], v[14:15] op_sel_hi:[1,0,1]
	v_pk_add_f32 v[20:21], v[20:21], 1.0 op_sel_hi:[1,0]
	v_min_f32_e32 v14, 0x40e00000, v14
	v_pk_mul_f32 v[30:31], v[30:31], v[18:19]
	v_mov_b32_e32 v18, v1
	v_rcp_f32_e32 v20, v20
	v_rcp_f32_e32 v21, v21
	v_cvt_pk_fp8_f32 v18, v30, v31
	v_mov_b32_e32 v19, v1
	v_min_f32_e32 v15, 0x40e00000, v15
	v_pk_mul_f32 v[20:21], v[28:29], v[20:21]
	v_pk_mul_f32 v[6:7], v[14:15], v[6:7]
	v_cvt_pk_fp8_f32 v18, v20, v21 op_sel:[0,0,1]
	v_min_f32_e32 v20, 0x40e00000, v26
	v_min_f32_e32 v21, 0x40e00000, v27
	v_med3_f32 v26, v34, s93, v251
	v_med3_f32 v27, v35, s93, v251
	v_pk_fma_f32 v[26:27], v[26:27], s[0:1], s[0:1] op_sel_hi:[1,0,0]
	v_pk_mul_f32 v[14:15], v[14:15], s[2:3] op_sel_hi:[1,0]
	v_pk_mul_f32 v[26:27], v[20:21], v[26:27]
	v_pk_mul_f32 v[20:21], v[20:21], s[2:3] op_sel_hi:[1,0]
	v_exp_f32_e32 v14, v14
	v_exp_f32_e32 v20, v20
	v_exp_f32_e32 v21, v21
	v_exp_f32_e32 v15, v15
	v_pk_fma_f32 v[16:17], v[80:81], s[52:53], v[16:17] op_sel_hi:[1,0,1]
	v_pk_fma_f32 v[2:3], v[2:3], s[0:1], s[0:1] op_sel_hi:[1,0,0]
	v_pk_add_f32 v[20:21], v[20:21], 1.0 op_sel_hi:[1,0]
	v_pk_add_f32 v[14:15], v[14:15], 1.0 op_sel_hi:[1,0]
	v_rcp_f32_e32 v20, v20
	v_rcp_f32_e32 v21, v21
	v_rcp_f32_e32 v14, v14
	v_rcp_f32_e32 v15, v15
	v_pk_fma_f32 v[12:13], v[76:77], s[52:53], v[12:13] op_sel_hi:[1,0,1]
	v_pk_mul_f32 v[20:21], v[26:27], v[20:21]
	v_med3_f32 v4, v4, s93, v251
	v_cvt_pk_fp8_f32 v19, v20, v21
	v_min_f32_e32 v20, 0x40e00000, v24
	v_min_f32_e32 v21, 0x40e00000, v25
	v_med3_f32 v24, v32, s93, v251
	v_med3_f32 v25, v33, s93, v251
	v_pk_fma_f32 v[24:25], v[24:25], s[0:1], s[0:1] op_sel_hi:[1,0,0]
	v_pk_mul_f32 v[6:7], v[6:7], v[14:15]
	v_pk_mul_f32 v[24:25], v[20:21], v[24:25]
	v_pk_mul_f32 v[20:21], v[20:21], s[2:3] op_sel_hi:[1,0]
	v_med3_f32 v5, v5, s93, v251
	v_exp_f32_e32 v20, v20
	v_exp_f32_e32 v21, v21
	v_pk_fma_f32 v[4:5], v[4:5], s[0:1], s[0:1] op_sel_hi:[1,0,0]
	v_add_u32_e32 v0, v0, v22
	s_mov_b32 s0, 0x8000
	v_pk_add_f32 v[20:21], v[20:21], 1.0 op_sel_hi:[1,0]
	v_add3_u32 v0, v0, v23, s0
	v_rcp_f32_e32 v20, v20
	v_rcp_f32_e32 v21, v21
	s_nop 0
	v_pk_mul_f32 v[20:21], v[24:25], v[20:21]
	s_nop 0
	v_cvt_pk_fp8_f32 v19, v20, v21 op_sel:[0,0,1]
	v_mov_b32_e32 v20, v1
	v_cvt_pk_fp8_f32 v20, v6, v7
	v_min_f32_e32 v6, 0x40e00000, v16
	v_min_f32_e32 v7, 0x40e00000, v17
	v_pk_mul_f32 v[8:9], v[6:7], v[8:9]
	v_pk_mul_f32 v[6:7], v[6:7], s[2:3] op_sel_hi:[1,0]
	v_mov_b32_e32 v21, v1
	v_exp_f32_e32 v6, v6
	v_exp_f32_e32 v7, v7
	s_nop 0
	v_pk_add_f32 v[6:7], v[6:7], 1.0 op_sel_hi:[1,0]
	s_nop 0
	v_rcp_f32_e32 v6, v6
	v_rcp_f32_e32 v7, v7
	s_nop 0
	v_pk_mul_f32 v[6:7], v[8:9], v[6:7]
	s_nop 0
	v_cvt_pk_fp8_f32 v20, v6, v7 op_sel:[0,0,1]
	v_min_f32_e32 v6, 0x40e00000, v10
	v_min_f32_e32 v7, 0x40e00000, v11
	v_pk_mul_f32 v[2:3], v[6:7], v[2:3]
	v_pk_mul_f32 v[6:7], v[6:7], s[2:3] op_sel_hi:[1,0]
	v_permlane16_swap_b32_e32 v18, v20
	v_exp_f32_e32 v6, v6
	v_exp_f32_e32 v7, v7
	s_nop 0
	v_pk_add_f32 v[6:7], v[6:7], 1.0 op_sel_hi:[1,0]
	s_nop 0
	v_rcp_f32_e32 v6, v6
	v_rcp_f32_e32 v7, v7
	s_nop 0
	v_pk_mul_f32 v[2:3], v[2:3], v[6:7]
	s_nop 0
	v_cvt_pk_fp8_f32 v21, v2, v3
	v_min_f32_e32 v2, 0x40e00000, v12
	v_min_f32_e32 v3, 0x40e00000, v13
	v_pk_mul_f32 v[4:5], v[2:3], v[4:5]
	v_pk_mul_f32 v[2:3], v[2:3], s[2:3] op_sel_hi:[1,0]
	s_nop 0
	v_exp_f32_e32 v2, v2
	v_exp_f32_e32 v3, v3
	s_nop 0
	v_pk_add_f32 v[2:3], v[2:3], 1.0 op_sel_hi:[1,0]
	s_nop 0
	v_rcp_f32_e32 v2, v2
	v_rcp_f32_e32 v3, v3
	s_nop 0
	v_pk_mul_f32 v[2:3], v[4:5], v[2:3]
	s_nop 0
	v_cvt_pk_fp8_f32 v21, v2, v3 op_sel:[0,0,1]
	s_nop 1
	v_permlane16_swap_b32_e32 v19, v21
	global_store_dwordx4 v0, v[18:21], s[6:7] sc1
	s_and_b64 vcc, exec, s[4:5]
	s_mov_b64 s[2:3], -1
	s_cbranch_vccnz .LBB0_1201
	s_branch .LBB0_1239

; #define LAS __attribute__((address_space(3)))
;     DI void operator()(const f32x4 (&acc)[2][2][4][2], const Unit& u, int wr, int wc, int fr, int fq) const {
;         int lrow = 64 * wr + fr, cwl = 32 * wc + 8 * fq; asm volatile("" : "+v"(lrow), "+v"(cwl));
;         const int n = u.n; const int cw = u.pn * 256 + cwl;
;         const char* lb = (const char*)lists + (size_t)u.e * LIST_CAP * 8;
;         f32x4 bv[2][2];
; #pragma unroll
;         for (int bj = 0; bj < 2; ++bj) { const LAS float* bb = bl + cwl + bj * 128; bv[bj][0] = *(const LAS f32x4*)bb; bv[bj][1] = *(const LAS f32x4*)(bb + 4); }
;         constexpr float dq = 1.0f / (W8_SCALE * ACT8_SCALE);
; #pragma unroll
;         for (int ai = 0; ai < 2; ++ai) { if (u.half == 2 - ai) continue;
;             const bool oddq = (fq & 1) != 0;
; #pragma unroll
;             for (int p2 = 0; p2 < 2; ++p2) { u32x2 wq[2][2];
;                 const u32x2 en0 = *(const LAS u32x2*)((const LAS unsigned char*)entl + (128 * ai + 32 * p2 + lrow) * 8), en1 = *(const LAS u32x2*)((const LAS unsigned char*)entl + (128 * ai + 32 * p2 + 16 + lrow) * 8);
; #pragma unroll
;                 for (int r2 = 0; r2 < 2; ++r2) { const int m = 2 * p2 + r2; const float gs = __uint_as_float(r2 ? en1.y : en0.y) * YS8_SCALE;
;                     const f32x4 a0 = (acc[ai][0][m][0] * dq + bv[0][0]) * gs, a1 = (acc[ai][0][m][1] * dq + bv[0][1]) * gs, b0 = (acc[ai][1][m][0] * dq + bv[1][0]) * gs, b1 = (acc[ai][1][m][1] * dq + bv[1][1]) * gs;
;                     wq[r2][0].x = pk4_fp8(a0[0], a0[1], a0[2], a0[3]); wq[r2][0].y = pk4_fp8(a1[0], a1[1], a1[2], a1[3]); wq[r2][1].x = pk4_fp8(b0[0], b0[1], b0[2], b0[3]); wq[r2][1].y = pk4_fp8(b1[0], b1[1], b1[2], b1[3]); }
;                 const int msel = 2 * p2 + (oddq ? 1 : 0); const int li = u.j * 256 + 128 * ai + 16 * msel + lrow;
;                 char* dst = (char*)yslot + ((oddq ? en1.x : en0.x) * (unsigned)D + (unsigned)(cw - (oddq ? 8 : 0)));
; #pragma unroll
;                 for (int bj = 0; bj < 2; ++bj) { const auto rx = __builtin_amdgcn_permlane16_swap(wq[0][bj].x, wq[1][bj].x, false, false), ry = __builtin_amdgcn_permlane16_swap(wq[0][bj].y, wq[1][bj].y, false, false);
;                     u32x4 w; w.x = rx[0]; w.y = ry[0]; w.z = rx[1]; w.w = ry[1];
;                     if (li < n) *(u32x4*)(dst + 128 * bj) = w; } }
.LBB0_1328:
	s_mov_b32 s0, s39
	s_mov_b32 s1, -1
	s_and_b64 vcc, exec, s[4:5]
	v_mbcnt_lo_u32_b32 v0, s1, 0
	v_mbcnt_hi_u32_b32 v0, s1, v0
	s_lshl_b32 s1, s0, 4
	s_lshl_b32 s0, s0, 5
	s_andn2_b32 s1, s1, 63
	v_ashrrev_i32_e32 v18, 4, v0
	s_and_b32 s0, s0, 0x60
	v_and_or_b32 v0, v0, 15, s1
	v_lshl_add_u32 v19, v18, 3, s0
	v_and_b32_e32 v18, 1, v18
	v_lshl_add_u32 v2, v19, 2, 0
	v_add_u32_e32 v2, 0x21000, v2
	ds_read_b128 v[14:17], v2
	ds_read_b128 v[10:13], v2 offset:16
	ds_read_b128 v[6:9], v2 offset:512
	ds_read_b128 v[2:5], v2 offset:528
	v_add_u32_e32 v19, s2, v19
	v_cmp_eq_u32_e64 s[6:7], 0, v18
	v_lshl_add_u32 v31, v18, 4, v0
	v_lshlrev_b32_e32 v18, 3, v18
	v_sub_u32_e32 v28, v19, v18
	v_lshlrev_b32_e32 v30, 3, v0
	s_mov_b64 s[2:3], -1
	v_add_u32_e32 v29, s17, v31
	v_readlane_b32 s72, v253, 25
	v_readlane_b32 s73, v253, 26
	s_cbranch_vccnz .LBB0_1339
	v_add_u32_e32 v0, 0, v30
	v_add_u32_e32 v0, 0x20700, v0
	s_waitcnt lgkmcnt(0)
	ds_read2_b64 v[32:35], v0 offset1:16
	v_pk_fma_f32 v[18:19], v[192:193], s[50:51], v[16:17] op_sel_hi:[1,0,1]
	v_pk_fma_f32 v[20:21], v[190:191], s[50:51], v[14:15] op_sel_hi:[1,0,1]
	v_pk_fma_f32 v[22:23], v[188:189], s[50:51], v[12:13] op_sel_hi:[1,0,1]
	v_pk_fma_f32 v[38:39], v[178:179], s[50:51], v[10:11] op_sel_hi:[1,0,1]
	s_waitcnt lgkmcnt(0)
	v_mul_f32_e32 v26, 0x42800000, v33
	v_pk_mul_f32 v[24:25], v[18:19], v[26:27] op_sel_hi:[1,0]
	v_pk_mul_f32 v[18:19], v[20:21], v[26:27] op_sel_hi:[1,0]
	v_pk_fma_f32 v[20:21], v[186:187], s[50:51], v[10:11] op_sel_hi:[1,0,1]
	v_med3_f32 v0, v18, s53, v204
	v_pk_mul_f32 v[20:21], v[20:21], v[26:27] op_sel_hi:[1,0]
	v_med3_f32 v19, v19, s53, v204
	v_mov_b32_e32 v18, v1
	v_cvt_pk_fp8_f32 v18, v0, v19
	v_med3_f32 v20, v20, s53, v204
	v_med3_f32 v21, v21, s53, v204
	v_mov_b32_e32 v19, v1
	v_cvt_pk_fp8_f32 v19, v20, v21
	v_pk_mul_f32 v[22:23], v[22:23], v[26:27] op_sel_hi:[1,0]
	v_med3_f32 v0, v24, s53, v204
	v_med3_f32 v24, v25, s53, v204
	v_cvt_pk_fp8_f32 v18, v0, v24 op_sel:[0,0,1]
	v_med3_f32 v0, v22, s53, v204
	v_med3_f32 v20, v23, s53, v204
	v_cvt_pk_fp8_f32 v19, v0, v20 op_sel:[0,0,1]
	v_mul_f32_e32 v22, 0x42800000, v35
	v_pk_fma_f32 v[20:21], v[184:185], s[50:51], v[16:17] op_sel_hi:[1,0,1]
	v_pk_fma_f32 v[24:25], v[182:183], s[50:51], v[14:15] op_sel_hi:[1,0,1]
	v_pk_mul_f32 v[36:37], v[20:21], v[22:23] op_sel_hi:[1,0]
	v_pk_mul_f32 v[20:21], v[24:25], v[22:23] op_sel_hi:[1,0]
	v_pk_mul_f32 v[38:39], v[38:39], v[22:23] op_sel_hi:[1,0]
	v_med3_f32 v0, v20, s53, v204
	v_med3_f32 v21, v21, s53, v204
	v_mov_b32_e32 v20, v1
	v_cvt_pk_fp8_f32 v20, v0, v21
	v_med3_f32 v27, v38, s53, v204
	v_med3_f32 v33, v39, s53, v204
	v_mov_b32_e32 v21, v1
	v_cvt_pk_fp8_f32 v21, v27, v33
	v_pk_fma_f32 v[24:25], v[180:181], s[50:51], v[12:13] op_sel_hi:[1,0,1]
	v_med3_f32 v0, v36, s53, v204
	v_pk_mul_f32 v[24:25], v[24:25], v[22:23] op_sel_hi:[1,0]
	v_med3_f32 v23, v37, s53, v204
	v_cvt_pk_fp8_f32 v20, v0, v23 op_sel:[0,0,1]
	v_med3_f32 v0, v24, s53, v204
	v_med3_f32 v23, v25, s53, v204
	v_cvt_pk_fp8_f32 v21, v0, v23 op_sel:[0,0,1]
	v_cndmask_b32_e64 v0, v34, v32, s[6:7]
	v_lshl_add_u32 v0, v0, 10, v28
	v_lshl_add_u64 v[24:25], s[10:11], 0, v[0:1]
	v_cmp_gt_i32_e32 vcc, s70, v29
	v_permlane16_swap_b32_e32 v18, v20
	v_permlane16_swap_b32_e32 v19, v21
	s_and_saveexec_b64 s[2:3], vcc
	s_cbranch_execz .LBB0_1331
	global_store_dwordx4 v[24:25], v[18:21], off sc1
.LBB0_1331:
	s_or_b64 exec, exec, s[2:3]
	v_mov_b32_e32 v27, v26
	v_pk_fma_f32 v[18:19], v[176:177], s[50:51], v[8:9] op_sel_hi:[1,0,1]
	v_pk_fma_f32 v[20:21], v[174:175], s[50:51], v[6:7] op_sel_hi:[1,0,1]
	v_mov_b32_e32 v32, v26
	v_mov_b32_e32 v33, v26
	v_pk_mul_f32 v[34:35], v[18:19], v[32:33]
	v_pk_mul_f32 v[18:19], v[20:21], v[26:27]
	v_pk_fma_f32 v[36:37], v[170:171], s[50:51], v[2:3] op_sel_hi:[1,0,1]
	v_med3_f32 v0, v18, s53, v204
	v_pk_mul_f32 v[26:27], v[36:37], v[26:27]
	v_med3_f32 v19, v19, s53, v204
	v_mov_b32_e32 v18, v1
	v_cvt_pk_fp8_f32 v18, v0, v19
	v_med3_f32 v26, v26, s53, v204
	v_med3_f32 v27, v27, s53, v204
	v_mov_b32_e32 v19, v1
	v_cvt_pk_fp8_f32 v19, v26, v27
	v_pk_fma_f32 v[20:21], v[172:173], s[50:51], v[4:5] op_sel_hi:[1,0,1]
	v_med3_f32 v0, v34, s53, v204
	v_pk_mul_f32 v[20:21], v[20:21], v[32:33]
	v_med3_f32 v32, v35, s53, v204
	v_cvt_pk_fp8_f32 v18, v0, v32 op_sel:[0,0,1]
	v_med3_f32 v0, v20, s53, v204
	v_med3_f32 v20, v21, s53, v204
	v_mov_b32_e32 v23, v22
	v_cvt_pk_fp8_f32 v19, v0, v20 op_sel:[0,0,1]
	v_pk_fma_f32 v[20:21], v[168:169], s[50:51], v[8:9] op_sel_hi:[1,0,1]
	v_pk_fma_f32 v[26:27], v[166:167], s[50:51], v[6:7] op_sel_hi:[1,0,1]
	v_mov_b32_e32 v32, v22
	v_mov_b32_e32 v33, v22
	v_pk_mul_f32 v[34:35], v[20:21], v[32:33]
	v_pk_mul_f32 v[20:21], v[26:27], v[22:23]
	v_pk_fma_f32 v[36:37], v[162:163], s[50:51], v[2:3] op_sel_hi:[1,0,1]
	v_med3_f32 v0, v20, s53, v204
	v_pk_mul_f32 v[22:23], v[36:37], v[22:23]
	v_med3_f32 v21, v21, s53, v204
	v_mov_b32_e32 v20, v1
	v_cvt_pk_fp8_f32 v20, v0, v21
	v_med3_f32 v22, v22, s53, v204
	v_med3_f32 v23, v23, s53, v204
	v_mov_b32_e32 v21, v1
	v_cvt_pk_fp8_f32 v21, v22, v23
	v_pk_fma_f32 v[26:27], v[164:165], s[50:51], v[4:5] op_sel_hi:[1,0,1]
	v_med3_f32 v0, v34, s53, v204
	v_pk_mul_f32 v[26:27], v[26:27], v[32:33]
	v_med3_f32 v32, v35, s53, v204
	v_cvt_pk_fp8_f32 v20, v0, v32 op_sel:[0,0,1]
	v_med3_f32 v0, v26, s53, v204
	v_med3_f32 v22, v27, s53, v204
	v_cvt_pk_fp8_f32 v21, v0, v22 op_sel:[0,0,1]
	v_permlane16_swap_b32_e32 v18, v20
	s_nop 0
	v_permlane16_swap_b32_e32 v19, v21
	s_and_saveexec_b64 s[2:3], vcc
	s_cbranch_execz .LBB0_1333
	global_store_dwordx4 v[24:25], v[18:21], off offset:128 sc1
; #define LAS __attribute__((address_space(3)))
; DI unsigned pk4_fp8(float a, float b, float c, float d) { int r = 0; r = __builtin_amdgcn_cvt_pk_fp8_f32(sat8(a), sat8(b), r, false); r = __builtin_amdgcn_cvt_pk_fp8_f32(sat8(c), sat8(d), r, true); return (unsigned)r; }
;     DI void operator()(const f32x4 (&acc)[2][2][4][2], const Unit& u, int wr, int wc, int fr, int fq) const {
;     ...
;         for (int ai = 0; ai < 2; ++ai) { if (u.half == 2 - ai) continue;
;             const bool oddq = (fq & 1) != 0;
; #pragma unroll
;             for (int p2 = 0; p2 < 2; ++p2) { u32x2 wq[2][2];
;                 const u32x2 en0 = *(const LAS u32x2*)((const LAS unsigned char*)entl + (128 * ai + 32 * p2 + lrow) * 8), en1 = *(const LAS u32x2*)((const LAS unsigned char*)entl + (128 * ai + 32 * p2 + 16 + lrow) * 8);
; #pragma unroll
;                 for (int r2 = 0; r2 < 2; ++r2) { const int m = 2 * p2 + r2; const float gs = __uint_as_float(r2 ? en1.y : en0.y) * YS8_SCALE;
;                     const f32x4 a0 = (acc[ai][0][m][0] * dq + bv[0][0]) * gs, a1 = (acc[ai][0][m][1] * dq + bv[0][1]) * gs, b0 = (acc[ai][1][m][0] * dq + bv[1][0]) * gs, b1 = (acc[ai][1][m][1] * dq + bv[1][1]) * gs;
;                     wq[r2][0].x = pk4_fp8(a0[0], a0[1], a0[2], a0[3]); wq[r2][0].y = pk4_fp8(a1[0], a1[1], a1[2], a1[3]); wq[r2][1].x = pk4_fp8(b0[0], b0[1], b0[2], b0[3]); wq[r2][1].y = pk4_fp8(b1[0], b1[1], b1[2], b1[3]); }
;                 const int msel = 2 * p2 + (oddq ? 1 : 0); const int li = u.j * 256 + 128 * ai + 16 * msel + lrow;
;                 char* dst = (char*)yslot + ((oddq ? en1.x : en0.x) * (unsigned)D + (unsigned)(cw - (oddq ? 8 : 0)));
; #pragma unroll
;                 for (int bj = 0; bj < 2; ++bj) { const auto rx = __builtin_amdgcn_permlane16_swap(wq[0][bj].x, wq[1][bj].x, false, false), ry = __builtin_amdgcn_permlane16_swap(wq[0][bj].y, wq[1][bj].y, false, false);
;                     u32x4 w; w.x = rx[0]; w.y = ry[0]; w.z = rx[1]; w.w = ry[1];
;                     if (li < n) *(u32x4*)(dst + 128 * bj) = w; } }
.LBB0_1333:
	s_or_b64 exec, exec, s[2:3]
	s_add_i32 s0, 0, 0x20700
	v_add_u32_e32 v0, s0, v30
	ds_read2_b64 v[32:35], v0 offset0:32 offset1:48
	v_pk_fma_f32 v[18:19], v[160:161], s[50:51], v[16:17] op_sel_hi:[1,0,1]
	v_pk_fma_f32 v[20:21], v[158:159], s[50:51], v[14:15] op_sel_hi:[1,0,1]
	v_pk_fma_f32 v[22:23], v[156:157], s[50:51], v[12:13] op_sel_hi:[1,0,1]
	v_pk_fma_f32 v[38:39], v[146:147], s[50:51], v[10:11] op_sel_hi:[1,0,1]
	s_waitcnt lgkmcnt(0)
	v_mul_f32_e32 v26, 0x42800000, v33
	v_pk_mul_f32 v[24:25], v[18:19], v[26:27] op_sel_hi:[1,0]
	v_pk_mul_f32 v[18:19], v[20:21], v[26:27] op_sel_hi:[1,0]
	v_pk_fma_f32 v[20:21], v[154:155], s[50:51], v[10:11] op_sel_hi:[1,0,1]
	v_med3_f32 v0, v18, s53, v204
	v_pk_mul_f32 v[20:21], v[20:21], v[26:27] op_sel_hi:[1,0]
	v_med3_f32 v19, v19, s53, v204
	v_mov_b32_e32 v18, v1
	v_cvt_pk_fp8_f32 v18, v0, v19
	v_med3_f32 v20, v20, s53, v204
	v_med3_f32 v21, v21, s53, v204
	v_mov_b32_e32 v19, v1
	v_cvt_pk_fp8_f32 v19, v20, v21
	v_pk_mul_f32 v[22:23], v[22:23], v[26:27] op_sel_hi:[1,0]
	v_med3_f32 v0, v24, s53, v204
	v_med3_f32 v24, v25, s53, v204
	v_cvt_pk_fp8_f32 v18, v0, v24 op_sel:[0,0,1]
	v_med3_f32 v0, v22, s53, v204
	v_med3_f32 v20, v23, s53, v204
	v_cvt_pk_fp8_f32 v19, v0, v20 op_sel:[0,0,1]
	v_mul_f32_e32 v22, 0x42800000, v35
	v_pk_fma_f32 v[20:21], v[152:153], s[50:51], v[16:17] op_sel_hi:[1,0,1]
	v_pk_fma_f32 v[24:25], v[150:151], s[50:51], v[14:15] op_sel_hi:[1,0,1]
	v_pk_mul_f32 v[36:37], v[20:21], v[22:23] op_sel_hi:[1,0]
	v_pk_mul_f32 v[20:21], v[24:25], v[22:23] op_sel_hi:[1,0]
	v_pk_mul_f32 v[38:39], v[38:39], v[22:23] op_sel_hi:[1,0]
	v_med3_f32 v0, v20, s53, v204
	v_med3_f32 v21, v21, s53, v204
	v_mov_b32_e32 v20, v1
	v_cvt_pk_fp8_f32 v20, v0, v21
	v_med3_f32 v27, v38, s53, v204
	v_med3_f32 v33, v39, s53, v204
	v_mov_b32_e32 v21, v1
	v_cvt_pk_fp8_f32 v21, v27, v33
	v_pk_fma_f32 v[24:25], v[148:149], s[50:51], v[12:13] op_sel_hi:[1,0,1]
	v_med3_f32 v0, v36, s53, v204
	v_pk_mul_f32 v[24:25], v[24:25], v[22:23] op_sel_hi:[1,0]
	v_med3_f32 v23, v37, s53, v204
	v_cvt_pk_fp8_f32 v20, v0, v23 op_sel:[0,0,1]
	v_med3_f32 v0, v24, s53, v204
	v_med3_f32 v23, v25, s53, v204
	v_cvt_pk_fp8_f32 v21, v0, v23 op_sel:[0,0,1]
	v_cndmask_b32_e64 v0, v34, v32, s[6:7]
	v_add3_u32 v23, v31, s17, 32
	v_lshl_add_u32 v0, v0, 10, v28
	v_lshl_add_u64 v[24:25], s[10:11], 0, v[0:1]
	v_cmp_gt_i32_e32 vcc, s70, v23
	v_permlane16_swap_b32_e32 v18, v20
	v_permlane16_swap_b32_e32 v19, v21
	s_and_saveexec_b64 s[2:3], vcc
	s_cbranch_execz .LBB0_1335
	global_store_dwordx4 v[24:25], v[18:21], off sc1
.LBB0_1335:
	s_or_b64 exec, exec, s[2:3]
	v_mov_b32_e32 v27, v26
	v_pk_fma_f32 v[18:19], v[144:145], s[50:51], v[8:9] op_sel_hi:[1,0,1]
	v_pk_fma_f32 v[20:21], v[142:143], s[50:51], v[6:7] op_sel_hi:[1,0,1]
	v_mov_b32_e32 v32, v26
	v_mov_b32_e32 v33, v26
	v_pk_mul_f32 v[34:35], v[18:19], v[32:33]
	v_pk_mul_f32 v[18:19], v[20:21], v[26:27]
	v_pk_fma_f32 v[36:37], v[138:139], s[50:51], v[2:3] op_sel_hi:[1,0,1]
	v_med3_f32 v0, v18, s53, v204
	v_pk_mul_f32 v[26:27], v[36:37], v[26:27]
	v_med3_f32 v19, v19, s53, v204
	v_mov_b32_e32 v18, v1
	v_cvt_pk_fp8_f32 v18, v0, v19
	v_med3_f32 v26, v26, s53, v204
	v_med3_f32 v27, v27, s53, v204
	v_mov_b32_e32 v19, v1
	v_cvt_pk_fp8_f32 v19, v26, v27
	v_pk_fma_f32 v[20:21], v[140:141], s[50:51], v[4:5] op_sel_hi:[1,0,1]
	v_med3_f32 v0, v34, s53, v204
	v_pk_mul_f32 v[20:21], v[20:21], v[32:33]
	v_med3_f32 v31, v35, s53, v204
	v_cvt_pk_fp8_f32 v18, v0, v31 op_sel:[0,0,1]
	v_med3_f32 v0, v20, s53, v204
	v_med3_f32 v20, v21, s53, v204
	v_mov_b32_e32 v23, v22
	v_cvt_pk_fp8_f32 v19, v0, v20 op_sel:[0,0,1]
	v_pk_fma_f32 v[20:21], v[136:137], s[50:51], v[8:9] op_sel_hi:[1,0,1]
	v_pk_fma_f32 v[26:27], v[134:135], s[50:51], v[6:7] op_sel_hi:[1,0,1]
	v_mov_b32_e32 v32, v22
	v_mov_b32_e32 v33, v22
	v_pk_mul_f32 v[34:35], v[20:21], v[32:33]
	v_pk_mul_f32 v[20:21], v[26:27], v[22:23]
	v_pk_fma_f32 v[36:37], v[130:131], s[50:51], v[2:3] op_sel_hi:[1,0,1]
	v_med3_f32 v0, v20, s53, v204
	v_pk_mul_f32 v[22:23], v[36:37], v[22:23]
	v_med3_f32 v21, v21, s53, v204
	v_mov_b32_e32 v20, v1
	v_cvt_pk_fp8_f32 v20, v0, v21
	v_med3_f32 v22, v22, s53, v204
	v_med3_f32 v23, v23, s53, v204
	v_mov_b32_e32 v21, v1
	v_cvt_pk_fp8_f32 v21, v22, v23
	v_pk_fma_f32 v[26:27], v[132:133], s[50:51], v[4:5] op_sel_hi:[1,0,1]
	v_med3_f32 v0, v34, s53, v204
	v_pk_mul_f32 v[26:27], v[26:27], v[32:33]
	v_med3_f32 v31, v35, s53, v204
	v_cvt_pk_fp8_f32 v20, v0, v31 op_sel:[0,0,1]
	v_med3_f32 v0, v26, s53, v204
	v_med3_f32 v22, v27, s53, v204
	v_cvt_pk_fp8_f32 v21, v0, v22 op_sel:[0,0,1]
	v_permlane16_swap_b32_e32 v18, v20
	s_nop 0
	v_permlane16_swap_b32_e32 v19, v21
	s_and_saveexec_b64 s[2:3], vcc
	s_cbranch_execz .LBB0_1337
	global_store_dwordx4 v[24:25], v[18:21], off offset:128 sc1

; #define LAS __attribute__((address_space(3)))
; DI unsigned pk4_fp8(float a, float b, float c, float d) { int r = 0; r = __builtin_amdgcn_cvt_pk_fp8_f32(sat8(a), sat8(b), r, false); r = __builtin_amdgcn_cvt_pk_fp8_f32(sat8(c), sat8(d), r, true); return (unsigned)r; }
;     DI void operator()(const f32x4 (&acc)[2][2][4][2], const Unit& u, int wr, int wc, int fr, int fq) const {
;     ...
;         for (int ai = 0; ai < 2; ++ai) { if (u.half == 2 - ai) continue;
;             const bool oddq = (fq & 1) != 0;
; #pragma unroll
;             for (int p2 = 0; p2 < 2; ++p2) { u32x2 wq[2][2];
;                 const u32x2 en0 = *(const LAS u32x2*)((const LAS unsigned char*)entl + (128 * ai + 32 * p2 + lrow) * 8), en1 = *(const LAS u32x2*)((const LAS unsigned char*)entl + (128 * ai + 32 * p2 + 16 + lrow) * 8);
; #pragma unroll
;                 for (int r2 = 0; r2 < 2; ++r2) { const int m = 2 * p2 + r2; const float gs = __uint_as_float(r2 ? en1.y : en0.y) * YS8_SCALE;
;                     const f32x4 a0 = (acc[ai][0][m][0] * dq + bv[0][0]) * gs, a1 = (acc[ai][0][m][1] * dq + bv[0][1]) * gs, b0 = (acc[ai][1][m][0] * dq + bv[1][0]) * gs, b1 = (acc[ai][1][m][1] * dq + bv[1][1]) * gs;
;                     wq[r2][0].x = pk4_fp8(a0[0], a0[1], a0[2], a0[3]); wq[r2][0].y = pk4_fp8(a1[0], a1[1], a1[2], a1[3]); wq[r2][1].x = pk4_fp8(b0[0], b0[1], b0[2], b0[3]); wq[r2][1].y = pk4_fp8(b1[0], b1[1], b1[2], b1[3]); }
;                 const int msel = 2 * p2 + (oddq ? 1 : 0); const int li = u.j * 256 + 128 * ai + 16 * msel + lrow;
;                 char* dst = (char*)yslot + ((oddq ? en1.x : en0.x) * (unsigned)D + (unsigned)(cw - (oddq ? 8 : 0)));
; #pragma unroll
;                 for (int bj = 0; bj < 2; ++bj) { const auto rx = __builtin_amdgcn_permlane16_swap(wq[0][bj].x, wq[1][bj].x, false, false), ry = __builtin_amdgcn_permlane16_swap(wq[0][bj].y, wq[1][bj].y, false, false);
;                     u32x4 w; w.x = rx[0]; w.y = ry[0]; w.z = rx[1]; w.w = ry[1];
;                     if (li < n) *(u32x4*)(dst + 128 * bj) = w; } }
.LBB0_1340:
	s_add_i32 s0, 0, 0x20700
	v_add_u32_e32 v30, s0, v30
	s_waitcnt lgkmcnt(0)
	ds_read2_b64 v[32:35], v30 offset0:128 offset1:144
	v_pk_fma_f32 v[18:19], v[128:129], s[50:51], v[16:17] op_sel_hi:[1,0,1]
	v_pk_fma_f32 v[20:21], v[126:127], s[50:51], v[14:15] op_sel_hi:[1,0,1]
	v_pk_fma_f32 v[22:23], v[124:125], s[50:51], v[12:13] op_sel_hi:[1,0,1]
	v_pk_fma_f32 v[38:39], v[114:115], s[50:51], v[10:11] op_sel_hi:[1,0,1]
	s_waitcnt lgkmcnt(0)
	v_mul_f32_e32 v26, 0x42800000, v33
	v_pk_mul_f32 v[24:25], v[18:19], v[26:27] op_sel_hi:[1,0]
	v_pk_mul_f32 v[18:19], v[20:21], v[26:27] op_sel_hi:[1,0]
	v_pk_fma_f32 v[20:21], v[122:123], s[50:51], v[10:11] op_sel_hi:[1,0,1]
	v_med3_f32 v0, v18, s53, v204
	v_pk_mul_f32 v[20:21], v[20:21], v[26:27] op_sel_hi:[1,0]
	v_med3_f32 v19, v19, s53, v204
	v_mov_b32_e32 v18, v1
	v_cvt_pk_fp8_f32 v18, v0, v19
	v_med3_f32 v20, v20, s53, v204
	v_med3_f32 v21, v21, s53, v204
	v_mov_b32_e32 v19, v1
	v_cvt_pk_fp8_f32 v19, v20, v21
	v_pk_mul_f32 v[22:23], v[22:23], v[26:27] op_sel_hi:[1,0]
	v_med3_f32 v0, v24, s53, v204
	v_med3_f32 v24, v25, s53, v204
	v_cvt_pk_fp8_f32 v18, v0, v24 op_sel:[0,0,1]
	v_med3_f32 v0, v22, s53, v204
	v_med3_f32 v20, v23, s53, v204
	v_cvt_pk_fp8_f32 v19, v0, v20 op_sel:[0,0,1]
	v_mul_f32_e32 v22, 0x42800000, v35
	v_pk_fma_f32 v[20:21], v[120:121], s[50:51], v[16:17] op_sel_hi:[1,0,1]
	v_pk_fma_f32 v[24:25], v[118:119], s[50:51], v[14:15] op_sel_hi:[1,0,1]
	v_pk_mul_f32 v[36:37], v[20:21], v[22:23] op_sel_hi:[1,0]
	v_pk_mul_f32 v[20:21], v[24:25], v[22:23] op_sel_hi:[1,0]
	v_pk_mul_f32 v[38:39], v[38:39], v[22:23] op_sel_hi:[1,0]
	v_med3_f32 v0, v20, s53, v204
	v_med3_f32 v21, v21, s53, v204
	v_mov_b32_e32 v20, v1
	v_cvt_pk_fp8_f32 v20, v0, v21
	v_med3_f32 v27, v38, s53, v204
	v_med3_f32 v31, v39, s53, v204
	v_mov_b32_e32 v21, v1
	v_cvt_pk_fp8_f32 v21, v27, v31
	v_pk_fma_f32 v[24:25], v[116:117], s[50:51], v[12:13] op_sel_hi:[1,0,1]
	v_med3_f32 v0, v36, s53, v204
	v_pk_mul_f32 v[24:25], v[24:25], v[22:23] op_sel_hi:[1,0]
	v_med3_f32 v23, v37, s53, v204
	v_cvt_pk_fp8_f32 v20, v0, v23 op_sel:[0,0,1]
	v_med3_f32 v0, v24, s53, v204
	v_med3_f32 v23, v25, s53, v204
	v_cvt_pk_fp8_f32 v21, v0, v23 op_sel:[0,0,1]
	v_cndmask_b32_e64 v0, v34, v32, s[6:7]
	v_add_u32_e32 v23, 0x80, v29
	v_lshl_add_u32 v0, v0, 10, v28
	v_lshl_add_u64 v[24:25], s[10:11], 0, v[0:1]
	v_cmp_gt_i32_e32 vcc, s70, v23
	v_permlane16_swap_b32_e32 v18, v20
	v_permlane16_swap_b32_e32 v19, v21
	s_and_saveexec_b64 s[2:3], vcc
	s_cbranch_execz .LBB0_1342
	global_store_dwordx4 v[24:25], v[18:21], off sc1
.LBB0_1342:
	s_or_b64 exec, exec, s[2:3]
	v_mov_b32_e32 v27, v26
	v_pk_fma_f32 v[18:19], v[112:113], s[50:51], v[8:9] op_sel_hi:[1,0,1]
	v_pk_fma_f32 v[20:21], v[110:111], s[50:51], v[6:7] op_sel_hi:[1,0,1]
	v_mov_b32_e32 v32, v26
	v_mov_b32_e32 v33, v26
	v_pk_mul_f32 v[34:35], v[18:19], v[32:33]
	v_pk_mul_f32 v[18:19], v[20:21], v[26:27]
	v_pk_fma_f32 v[36:37], v[106:107], s[50:51], v[2:3] op_sel_hi:[1,0,1]
	v_med3_f32 v0, v18, s53, v204
	v_pk_mul_f32 v[26:27], v[36:37], v[26:27]
	v_med3_f32 v19, v19, s53, v204
	v_mov_b32_e32 v18, v1
	v_cvt_pk_fp8_f32 v18, v0, v19
	v_med3_f32 v26, v26, s53, v204
	v_med3_f32 v27, v27, s53, v204
	v_mov_b32_e32 v19, v1
	v_cvt_pk_fp8_f32 v19, v26, v27
	v_pk_fma_f32 v[20:21], v[108:109], s[50:51], v[4:5] op_sel_hi:[1,0,1]
	v_med3_f32 v0, v34, s53, v204
	v_pk_mul_f32 v[20:21], v[20:21], v[32:33]
	v_med3_f32 v31, v35, s53, v204
	v_cvt_pk_fp8_f32 v18, v0, v31 op_sel:[0,0,1]
	v_med3_f32 v0, v20, s53, v204
	v_med3_f32 v20, v21, s53, v204
	v_mov_b32_e32 v23, v22
	v_cvt_pk_fp8_f32 v19, v0, v20 op_sel:[0,0,1]
	v_pk_fma_f32 v[20:21], v[104:105], s[50:51], v[8:9] op_sel_hi:[1,0,1]
	v_pk_fma_f32 v[26:27], v[102:103], s[50:51], v[6:7] op_sel_hi:[1,0,1]
	v_mov_b32_e32 v32, v22
	v_mov_b32_e32 v33, v22
	v_pk_mul_f32 v[34:35], v[20:21], v[32:33]
	v_pk_mul_f32 v[20:21], v[26:27], v[22:23]
	v_pk_fma_f32 v[36:37], v[98:99], s[50:51], v[2:3] op_sel_hi:[1,0,1]
	v_med3_f32 v0, v20, s53, v204
	v_pk_mul_f32 v[22:23], v[36:37], v[22:23]
	v_med3_f32 v21, v21, s53, v204
	v_mov_b32_e32 v20, v1
	v_cvt_pk_fp8_f32 v20, v0, v21
	v_med3_f32 v22, v22, s53, v204
	v_med3_f32 v23, v23, s53, v204
	v_mov_b32_e32 v21, v1
	v_cvt_pk_fp8_f32 v21, v22, v23
	v_pk_fma_f32 v[26:27], v[100:101], s[50:51], v[4:5] op_sel_hi:[1,0,1]
	v_med3_f32 v0, v34, s53, v204
	v_pk_mul_f32 v[26:27], v[26:27], v[32:33]
	v_med3_f32 v31, v35, s53, v204
	v_cvt_pk_fp8_f32 v20, v0, v31 op_sel:[0,0,1]
	v_med3_f32 v0, v26, s53, v204
	v_med3_f32 v22, v27, s53, v204
	v_cvt_pk_fp8_f32 v21, v0, v22 op_sel:[0,0,1]
	v_permlane16_swap_b32_e32 v18, v20
	s_nop 0
	v_permlane16_swap_b32_e32 v19, v21
	s_and_saveexec_b64 s[2:3], vcc
	s_cbranch_execz .LBB0_1344
	global_store_dwordx4 v[24:25], v[18:21], off offset:128 sc1
; #define LAS __attribute__((address_space(3)))
; DI unsigned pk4_fp8(float a, float b, float c, float d) { int r = 0; r = __builtin_amdgcn_cvt_pk_fp8_f32(sat8(a), sat8(b), r, false); r = __builtin_amdgcn_cvt_pk_fp8_f32(sat8(c), sat8(d), r, true); return (unsigned)r; }
;     DI void operator()(const f32x4 (&acc)[2][2][4][2], const Unit& u, int wr, int wc, int fr, int fq) const {
;     ...
;         for (int ai = 0; ai < 2; ++ai) { if (u.half == 2 - ai) continue;
;             const bool oddq = (fq & 1) != 0;
; #pragma unroll
;             for (int p2 = 0; p2 < 2; ++p2) { u32x2 wq[2][2];
;                 const u32x2 en0 = *(const LAS u32x2*)((const LAS unsigned char*)entl + (128 * ai + 32 * p2 + lrow) * 8), en1 = *(const LAS u32x2*)((const LAS unsigned char*)entl + (128 * ai + 32 * p2 + 16 + lrow) * 8);
; #pragma unroll
;                 for (int r2 = 0; r2 < 2; ++r2) { const int m = 2 * p2 + r2; const float gs = __uint_as_float(r2 ? en1.y : en0.y) * YS8_SCALE;
;                     const f32x4 a0 = (acc[ai][0][m][0] * dq + bv[0][0]) * gs, a1 = (acc[ai][0][m][1] * dq + bv[0][1]) * gs, b0 = (acc[ai][1][m][0] * dq + bv[1][0]) * gs, b1 = (acc[ai][1][m][1] * dq + bv[1][1]) * gs;
;                     wq[r2][0].x = pk4_fp8(a0[0], a0[1], a0[2], a0[3]); wq[r2][0].y = pk4_fp8(a1[0], a1[1], a1[2], a1[3]); wq[r2][1].x = pk4_fp8(b0[0], b0[1], b0[2], b0[3]); wq[r2][1].y = pk4_fp8(b1[0], b1[1], b1[2], b1[3]); }
;                 const int msel = 2 * p2 + (oddq ? 1 : 0); const int li = u.j * 256 + 128 * ai + 16 * msel + lrow;
;                 char* dst = (char*)yslot + ((oddq ? en1.x : en0.x) * (unsigned)D + (unsigned)(cw - (oddq ? 8 : 0)));
; #pragma unroll
;                 for (int bj = 0; bj < 2; ++bj) { const auto rx = __builtin_amdgcn_permlane16_swap(wq[0][bj].x, wq[1][bj].x, false, false), ry = __builtin_amdgcn_permlane16_swap(wq[0][bj].y, wq[1][bj].y, false, false);
;                     u32x4 w; w.x = rx[0]; w.y = ry[0]; w.z = rx[1]; w.w = ry[1];
;                     if (li < n) *(u32x4*)(dst + 128 * bj) = w; } }
.LBB0_1344:
	s_or_b64 exec, exec, s[2:3]
	ds_read2_b64 v[30:33], v30 offset0:160 offset1:176
	v_pk_fma_f32 v[18:19], v[96:97], s[50:51], v[16:17] op_sel_hi:[1,0,1]
	v_pk_fma_f32 v[20:21], v[94:95], s[50:51], v[14:15] op_sel_hi:[1,0,1]
	v_pk_fma_f32 v[22:23], v[92:93], s[50:51], v[12:13] op_sel_hi:[1,0,1]
	v_pk_fma_f32 v[14:15], v[86:87], s[50:51], v[14:15] op_sel_hi:[1,0,1]
	s_waitcnt lgkmcnt(0)
	v_mul_f32_e32 v24, 0x42800000, v31
	v_pk_mul_f32 v[26:27], v[18:19], v[24:25] op_sel_hi:[1,0]
	v_pk_mul_f32 v[18:19], v[20:21], v[24:25] op_sel_hi:[1,0]
	v_pk_fma_f32 v[20:21], v[90:91], s[50:51], v[10:11] op_sel_hi:[1,0,1]
	v_med3_f32 v0, v18, s53, v204
	v_med3_f32 v19, v19, s53, v204
	v_mov_b32_e32 v18, v1
	v_pk_mul_f32 v[20:21], v[20:21], v[24:25] op_sel_hi:[1,0]
	v_cvt_pk_fp8_f32 v18, v0, v19
	v_med3_f32 v20, v20, s53, v204
	v_med3_f32 v21, v21, s53, v204
	v_mov_b32_e32 v19, v1
	v_cvt_pk_fp8_f32 v19, v20, v21
	v_pk_mul_f32 v[22:23], v[22:23], v[24:25] op_sel_hi:[1,0]
	v_med3_f32 v0, v26, s53, v204
	v_med3_f32 v25, v27, s53, v204
	v_cvt_pk_fp8_f32 v18, v0, v25 op_sel:[0,0,1]
	v_med3_f32 v0, v22, s53, v204
	v_mul_f32_e32 v22, 0x42800000, v33
	v_med3_f32 v20, v23, s53, v204
	v_pk_mul_f32 v[14:15], v[14:15], v[22:23] op_sel_hi:[1,0]
	v_pk_fma_f32 v[10:11], v[82:83], s[50:51], v[10:11] op_sel_hi:[1,0,1]
	v_cvt_pk_fp8_f32 v19, v0, v20 op_sel:[0,0,1]
	v_pk_mul_f32 v[10:11], v[10:11], v[22:23] op_sel_hi:[1,0]
	v_med3_f32 v0, v14, s53, v204
	v_med3_f32 v14, v15, s53, v204
	v_mov_b32_e32 v20, v1
	v_cvt_pk_fp8_f32 v20, v0, v14
	v_med3_f32 v10, v10, s53, v204
	v_med3_f32 v11, v11, s53, v204
	v_mov_b32_e32 v21, v1
	v_pk_fma_f32 v[16:17], v[88:89], s[50:51], v[16:17] op_sel_hi:[1,0,1]
	v_cvt_pk_fp8_f32 v21, v10, v11
	v_pk_mul_f32 v[16:17], v[16:17], v[22:23] op_sel_hi:[1,0]
	v_pk_fma_f32 v[12:13], v[84:85], s[50:51], v[12:13] op_sel_hi:[1,0,1]
	v_med3_f32 v0, v16, s53, v204
	v_pk_mul_f32 v[12:13], v[12:13], v[22:23] op_sel_hi:[1,0]
	v_med3_f32 v14, v17, s53, v204
	v_cvt_pk_fp8_f32 v20, v0, v14 op_sel:[0,0,1]
	v_med3_f32 v0, v12, s53, v204
	v_med3_f32 v10, v13, s53, v204
	v_cvt_pk_fp8_f32 v21, v0, v10 op_sel:[0,0,1]
	v_cndmask_b32_e64 v0, v32, v30, s[6:7]
	v_add_u32_e32 v10, 0xa0, v29
	v_lshl_add_u32 v0, v0, 10, v28
	v_lshl_add_u64 v[14:15], s[10:11], 0, v[0:1]
	v_cmp_gt_i32_e32 vcc, s70, v10
	v_permlane16_swap_b32_e32 v18, v20
	v_permlane16_swap_b32_e32 v19, v21
	s_and_saveexec_b64 s[2:3], vcc
	s_cbranch_execz .LBB0_1346
	global_store_dwordx4 v[14:15], v[18:21], off sc1
.LBB0_1346:
	s_or_b64 exec, exec, s[2:3]
	v_mov_b32_e32 v25, v24
	v_pk_fma_f32 v[10:11], v[80:81], s[50:51], v[8:9] op_sel_hi:[1,0,1]
	v_pk_fma_f32 v[12:13], v[78:79], s[50:51], v[6:7] op_sel_hi:[1,0,1]
	v_mov_b32_e32 v16, v24
	v_mov_b32_e32 v17, v24
	v_pk_mul_f32 v[18:19], v[10:11], v[16:17]
	v_pk_mul_f32 v[10:11], v[12:13], v[24:25]
	v_pk_fma_f32 v[12:13], v[76:77], s[50:51], v[4:5] op_sel_hi:[1,0,1]
	v_pk_fma_f32 v[20:21], v[74:75], s[50:51], v[2:3] op_sel_hi:[1,0,1]
	v_pk_mul_f32 v[12:13], v[12:13], v[16:17]
	v_pk_mul_f32 v[16:17], v[20:21], v[24:25]
	v_med3_f32 v0, v10, s53, v204
	v_med3_f32 v11, v11, s53, v204
	v_mov_b32_e32 v10, v1
	v_cvt_pk_fp8_f32 v10, v0, v11
	v_med3_f32 v16, v16, s53, v204
	v_med3_f32 v17, v17, s53, v204
	v_mov_b32_e32 v11, v1
	v_cvt_pk_fp8_f32 v11, v16, v17
	v_med3_f32 v0, v18, s53, v204
	v_med3_f32 v18, v19, s53, v204
	v_mov_b32_e32 v23, v22
	v_cvt_pk_fp8_f32 v10, v0, v18 op_sel:[0,0,1]
	v_med3_f32 v0, v12, s53, v204
	v_med3_f32 v12, v13, s53, v204
	v_pk_fma_f32 v[6:7], v[70:71], s[50:51], v[6:7] op_sel_hi:[1,0,1]
	v_cvt_pk_fp8_f32 v11, v0, v12 op_sel:[0,0,1]
	v_pk_fma_f32 v[8:9], v[72:73], s[50:51], v[8:9] op_sel_hi:[1,0,1]
	v_mov_b32_e32 v12, v22
	v_mov_b32_e32 v13, v22
	v_pk_mul_f32 v[6:7], v[6:7], v[22:23]
	v_pk_fma_f32 v[4:5], v[68:69], s[50:51], v[4:5] op_sel_hi:[1,0,1]
	v_pk_fma_f32 v[2:3], v[66:67], s[50:51], v[2:3] op_sel_hi:[1,0,1]
	v_pk_mul_f32 v[8:9], v[8:9], v[12:13]
	v_pk_mul_f32 v[4:5], v[4:5], v[12:13]
	v_pk_mul_f32 v[2:3], v[2:3], v[22:23]
	v_med3_f32 v0, v6, s53, v204
	v_med3_f32 v6, v7, s53, v204
	v_mov_b32_e32 v12, v1
	v_cvt_pk_fp8_f32 v12, v0, v6
	v_med3_f32 v2, v2, s53, v204
	v_med3_f32 v3, v3, s53, v204
	v_mov_b32_e32 v13, v1
	v_cvt_pk_fp8_f32 v13, v2, v3
	v_med3_f32 v0, v8, s53, v204
	v_med3_f32 v6, v9, s53, v204
	v_cvt_pk_fp8_f32 v12, v0, v6 op_sel:[0,0,1]
	v_med3_f32 v0, v4, s53, v204
	v_med3_f32 v2, v5, s53, v204
	v_cvt_pk_fp8_f32 v13, v0, v2 op_sel:[0,0,1]
	v_permlane16_swap_b32_e32 v10, v12
	s_nop 0
	v_permlane16_swap_b32_e32 v11, v13
	s_and_saveexec_b64 s[2:3], vcc
	s_cbranch_execz .LBB0_1348
	global_store_dwordx4 v[14:15], v[10:13], off offset:128 sc1
